# static s_setprio 1 for waves 4-7 in GEMM phases, per-phase prio flips deleted (on top of v6)
# baseline (speedup 1.0000x reference)
.LBB0_434:
	s_cmpk_lt_u32 s92, 0x100
	s_cbranch_scc1 .Lsprio_1
	s_setprio 1

.LBB0_451:
	ds_read_b128 v[128:131], v182
	ds_read_b128 v[132:135], v182 offset:1024
	ds_read_b128 v[136:139], v182 offset:2048
	ds_read_b128 v[140:143], v182 offset:3072
	s_add_u32 s20, s18, 0x80
	s_addc_u32 s21, s19, 0
	s_cmp_eq_u32 s51, 28
	s_cselect_b32 s23, s45, s21
	s_cselect_b32 s22, s46, s20
	s_cselect_b32 s21, s47, s50
	s_cselect_b32 s20, s48, s49
	v_lshl_add_u64 v[214:215], s[18:19], 0, v[158:159]
	s_add_i32 m0, s30, 0xc000
	ds_read_b128 v[160:163], v183
	ds_read_b128 v[186:189], v183 offset:1024
	ds_read_b128 v[190:193], v183 offset:2048
	ds_read_b128 v[194:197], v183 offset:3072
	ds_read_b128 v[198:201], v183 offset:4096
	ds_read_b128 v[202:205], v183 offset:5120
	ds_read_b128 v[206:209], v183 offset:6144
	ds_read_b128 v[210:213], v183 offset:7168
	global_load_lds_dwordx4 v[214:215], off
	v_lshl_add_u64 v[214:215], s[18:19], 0, v[156:157]
	s_add_i32 m0, s30, 0xe000
	s_nop 0
	global_load_lds_dwordx4 v[214:215], off
	s_waitcnt lgkmcnt(8)
	s_barrier
	s_waitcnt lgkmcnt(0)
	s_waitcnt lgkmcnt(0)
	v_mfma_f32_16x16x32_bf16 v[124:127], v[128:131], v[160:163], v[124:127]
	v_mfma_f32_16x16x32_bf16 v[120:123], v[136:139], v[160:163], v[120:123]
	v_mfma_f32_16x16x32_bf16 v[116:119], v[128:131], v[190:193], v[116:119]
	v_mfma_f32_16x16x32_bf16 v[112:115], v[136:139], v[190:193], v[112:115]
	v_mfma_f32_16x16x32_bf16 v[108:111], v[128:131], v[198:201], v[108:111]
	v_mfma_f32_16x16x32_bf16 v[100:103], v[136:139], v[198:201], v[100:103]
	v_mfma_f32_16x16x32_bf16 v[92:95], v[128:131], v[206:209], v[92:95]
	v_mfma_f32_16x16x32_bf16 v[80:83], v[136:139], v[206:209], v[80:83]
	v_mfma_f32_16x16x32_bf16 v[124:127], v[132:135], v[186:189], v[124:127]
	v_mfma_f32_16x16x32_bf16 v[120:123], v[140:143], v[186:189], v[120:123]
	v_mfma_f32_16x16x32_bf16 v[116:119], v[132:135], v[194:197], v[116:119]
	v_mfma_f32_16x16x32_bf16 v[112:115], v[140:143], v[194:197], v[112:115]
	v_mfma_f32_16x16x32_bf16 v[108:111], v[132:135], v[202:205], v[108:111]
	v_mfma_f32_16x16x32_bf16 v[100:103], v[140:143], v[202:205], v[100:103]
	v_mfma_f32_16x16x32_bf16 v[92:95], v[132:135], v[210:213], v[92:95]
	v_mfma_f32_16x16x32_bf16 v[80:83], v[140:143], v[210:213], v[80:83]
	s_barrier
	s_add_i32 s52, s38, s29
	v_lshl_add_u64 v[230:231], s[20:21], 0, v[144:145]
	s_mov_b32 m0, s52
	ds_read_b128 v[214:217], v184
	ds_read_b128 v[218:221], v184 offset:1024
	ds_read_b128 v[222:225], v184 offset:2048
	ds_read_b128 v[226:229], v184 offset:3072
	global_load_lds_dwordx4 v[230:231], off
	v_lshl_add_u64 v[232:233], s[20:21], 0, v[146:147]
	s_add_i32 m0, s52, 0x2000
	s_nop 0
	global_load_lds_dwordx4 v[232:233], off
	s_barrier
	s_waitcnt lgkmcnt(0)
	s_waitcnt lgkmcnt(0)
	v_mfma_f32_16x16x32_bf16 v[104:107], v[214:217], v[160:163], v[104:107]
	v_mfma_f32_16x16x32_bf16 v[96:99], v[222:225], v[160:163], v[96:99]
	v_mfma_f32_16x16x32_bf16 v[88:91], v[214:217], v[190:193], v[88:91]
	v_mfma_f32_16x16x32_bf16 v[84:87], v[222:225], v[190:193], v[84:87]
	v_mfma_f32_16x16x32_bf16 v[76:79], v[214:217], v[198:201], v[76:79]
	v_mfma_f32_16x16x32_bf16 v[72:75], v[222:225], v[198:201], v[72:75]
	v_mfma_f32_16x16x32_bf16 v[68:71], v[214:217], v[206:209], v[68:71]
	v_mfma_f32_16x16x32_bf16 v[64:67], v[222:225], v[206:209], v[64:67]
	v_mfma_f32_16x16x32_bf16 v[104:107], v[218:221], v[186:189], v[104:107]
	v_mfma_f32_16x16x32_bf16 v[96:99], v[226:229], v[186:189], v[96:99]
	v_mfma_f32_16x16x32_bf16 v[88:91], v[218:221], v[194:197], v[88:91]
	v_mfma_f32_16x16x32_bf16 v[84:87], v[226:229], v[194:197], v[84:87]
	v_mfma_f32_16x16x32_bf16 v[76:79], v[218:221], v[202:205], v[76:79]
	v_mfma_f32_16x16x32_bf16 v[72:75], v[226:229], v[202:205], v[72:75]
	v_mfma_f32_16x16x32_bf16 v[68:71], v[218:221], v[210:213], v[68:71]
	v_mfma_f32_16x16x32_bf16 v[64:67], v[226:229], v[210:213], v[64:67]
	s_mov_b32 m0, s30
	v_lshl_add_u64 v[234:235], s[22:23], 0, v[148:149]
	s_barrier
	ds_read_b128 v[160:163], v183 offset:16384
	ds_read_b128 v[186:189], v183 offset:17408
	ds_read_b128 v[190:193], v183 offset:18432
	ds_read_b128 v[194:197], v183 offset:19456
	ds_read_b128 v[198:201], v183 offset:20480
	ds_read_b128 v[202:205], v183 offset:21504
	ds_read_b128 v[206:209], v183 offset:22528
	ds_read_b128 v[210:213], v183 offset:23552
	global_load_lds_dwordx4 v[234:235], off
	v_lshl_add_u64 v[236:237], s[22:23], 0, v[150:151]
	s_mov_b32 m0, s31
	s_nop 0
	global_load_lds_dwordx4 v[236:237], off
	s_barrier
	s_waitcnt lgkmcnt(0)
	s_waitcnt lgkmcnt(0)
	v_mfma_f32_16x16x32_bf16 v[60:63], v[128:131], v[160:163], v[60:63]
	v_mfma_f32_16x16x32_bf16 v[56:59], v[136:139], v[160:163], v[56:59]
	v_mfma_f32_16x16x32_bf16 v[48:51], v[128:131], v[190:193], v[48:51]
	v_mfma_f32_16x16x32_bf16 v[40:43], v[136:139], v[190:193], v[40:43]
	v_mfma_f32_16x16x32_bf16 v[32:35], v[128:131], v[198:201], v[32:35]
	v_mfma_f32_16x16x32_bf16 v[24:27], v[136:139], v[198:201], v[24:27]
	v_mfma_f32_16x16x32_bf16 v[16:19], v[128:131], v[206:209], v[16:19]
	v_mfma_f32_16x16x32_bf16 v[8:11], v[136:139], v[206:209], v[8:11]
	v_mfma_f32_16x16x32_bf16 v[60:63], v[132:135], v[186:189], v[60:63]
	v_mfma_f32_16x16x32_bf16 v[56:59], v[140:143], v[186:189], v[56:59]
	v_mfma_f32_16x16x32_bf16 v[48:51], v[132:135], v[194:197], v[48:51]
	v_mfma_f32_16x16x32_bf16 v[40:43], v[140:143], v[194:197], v[40:43]
	v_mfma_f32_16x16x32_bf16 v[32:35], v[132:135], v[202:205], v[32:35]
	v_mfma_f32_16x16x32_bf16 v[24:27], v[140:143], v[202:205], v[24:27]
	v_mfma_f32_16x16x32_bf16 v[16:19], v[132:135], v[210:213], v[16:19]
	v_mfma_f32_16x16x32_bf16 v[8:11], v[140:143], v[210:213], v[8:11]
	s_barrier
	s_add_u32 s52, s20, 0x80000
	s_addc_u32 s53, s21, 0
	s_add_i32 s54, s39, s29
	v_lshl_add_u64 v[128:129], s[52:53], 0, v[144:145]
	s_mov_b32 m0, s54
	s_nop 0
	global_load_lds_dwordx4 v[128:129], off
	v_lshl_add_u64 v[128:129], s[52:53], 0, v[146:147]
	s_add_i32 m0, s54, 0x2000
	s_nop 0
	global_load_lds_dwordx4 v[128:129], off
	s_waitcnt vmcnt(6)
	s_barrier
	v_mfma_f32_16x16x32_bf16 v[52:55], v[214:217], v[160:163], v[52:55]
	v_mfma_f32_16x16x32_bf16 v[44:47], v[222:225], v[160:163], v[44:47]
	v_mfma_f32_16x16x32_bf16 v[36:39], v[214:217], v[190:193], v[36:39]
	v_mfma_f32_16x16x32_bf16 v[28:31], v[222:225], v[190:193], v[28:31]
	v_mfma_f32_16x16x32_bf16 v[20:23], v[214:217], v[198:201], v[20:23]
	v_mfma_f32_16x16x32_bf16 v[12:15], v[222:225], v[198:201], v[12:15]
	v_mfma_f32_16x16x32_bf16 v[4:7], v[214:217], v[206:209], v[4:7]
	v_mfma_f32_16x16x32_bf16 v[0:3], v[222:225], v[206:209], v[0:3]
	v_mfma_f32_16x16x32_bf16 v[52:55], v[218:221], v[186:189], v[52:55]
	v_mfma_f32_16x16x32_bf16 v[44:47], v[226:229], v[186:189], v[44:47]
	v_mfma_f32_16x16x32_bf16 v[36:39], v[218:221], v[194:197], v[36:39]
	v_mfma_f32_16x16x32_bf16 v[28:31], v[226:229], v[194:197], v[28:31]
	v_mfma_f32_16x16x32_bf16 v[20:23], v[218:221], v[202:205], v[20:23]
	v_mfma_f32_16x16x32_bf16 v[12:15], v[226:229], v[202:205], v[12:15]
	v_mfma_f32_16x16x32_bf16 v[4:7], v[218:221], v[210:213], v[4:7]
	v_mfma_f32_16x16x32_bf16 v[0:3], v[226:229], v[210:213], v[0:3]
	s_add_i32 s52, 0, 0x18000
	v_add_u32_e32 v140, s52, v180
	s_barrier
	ds_read_b128 v[128:131], v140
	ds_read_b128 v[132:135], v140 offset:1024
	ds_read_b128 v[136:139], v140 offset:2048
	ds_read_b128 v[140:143], v140 offset:3072
	s_mov_b32 m0, s33
	v_lshl_add_u64 v[214:215], s[22:23], 0, v[152:153]
	ds_read_b128 v[160:163], v183 offset:32768
	ds_read_b128 v[186:189], v183 offset:33792
	ds_read_b128 v[190:193], v183 offset:34816
	ds_read_b128 v[194:197], v183 offset:35840
	ds_read_b128 v[198:201], v183 offset:36864
	ds_read_b128 v[202:205], v183 offset:37888
	ds_read_b128 v[206:209], v183 offset:38912
	ds_read_b128 v[210:213], v183 offset:39936
	global_load_lds_dwordx4 v[214:215], off
	v_lshl_add_u64 v[214:215], s[22:23], 0, v[154:155]
	s_mov_b32 m0, s34
	s_nop 0
	global_load_lds_dwordx4 v[214:215], off
	s_waitcnt lgkmcnt(8)
	s_barrier
	s_waitcnt lgkmcnt(0)
	s_waitcnt lgkmcnt(0)
	v_mfma_f32_16x16x32_bf16 v[124:127], v[128:131], v[160:163], v[124:127]
	v_mfma_f32_16x16x32_bf16 v[120:123], v[136:139], v[160:163], v[120:123]
	v_mfma_f32_16x16x32_bf16 v[116:119], v[128:131], v[190:193], v[116:119]
	v_mfma_f32_16x16x32_bf16 v[112:115], v[136:139], v[190:193], v[112:115]
	v_mfma_f32_16x16x32_bf16 v[108:111], v[128:131], v[198:201], v[108:111]
	v_mfma_f32_16x16x32_bf16 v[100:103], v[136:139], v[198:201], v[100:103]
	v_mfma_f32_16x16x32_bf16 v[92:95], v[128:131], v[206:209], v[92:95]
	v_mfma_f32_16x16x32_bf16 v[80:83], v[136:139], v[206:209], v[80:83]
	v_mfma_f32_16x16x32_bf16 v[124:127], v[132:135], v[186:189], v[124:127]
	v_mfma_f32_16x16x32_bf16 v[120:123], v[140:143], v[186:189], v[120:123]
	v_mfma_f32_16x16x32_bf16 v[116:119], v[132:135], v[194:197], v[116:119]
	v_mfma_f32_16x16x32_bf16 v[112:115], v[140:143], v[194:197], v[112:115]
	v_mfma_f32_16x16x32_bf16 v[108:111], v[132:135], v[202:205], v[108:111]
	v_mfma_f32_16x16x32_bf16 v[100:103], v[140:143], v[202:205], v[100:103]
	v_mfma_f32_16x16x32_bf16 v[92:95], v[132:135], v[210:213], v[92:95]
	v_mfma_f32_16x16x32_bf16 v[80:83], v[140:143], v[210:213], v[80:83]
	s_barrier
	s_add_i32 s22, 0, 0x1c000
	s_add_i32 s23, s52, s29
	v_add_u32_e32 v185, s22, v180
	v_lshl_add_u64 v[230:231], v[230:231], 0, s[0:1]
	s_mov_b32 m0, s23
	ds_read_b128 v[214:217], v185
	ds_read_b128 v[218:221], v185 offset:1024
	ds_read_b128 v[222:225], v185 offset:2048
	ds_read_b128 v[226:229], v185 offset:3072
	global_load_lds_dwordx4 v[230:231], off
	v_lshl_add_u64 v[230:231], v[232:233], 0, s[0:1]
	s_add_i32 m0, s23, 0x2000
	s_nop 0
	global_load_lds_dwordx4 v[230:231], off
	s_barrier
	s_waitcnt lgkmcnt(0)
	s_waitcnt lgkmcnt(0)
	v_mfma_f32_16x16x32_bf16 v[104:107], v[214:217], v[160:163], v[104:107]
	v_mfma_f32_16x16x32_bf16 v[96:99], v[222:225], v[160:163], v[96:99]
	v_mfma_f32_16x16x32_bf16 v[88:91], v[214:217], v[190:193], v[88:91]
	v_mfma_f32_16x16x32_bf16 v[84:87], v[222:225], v[190:193], v[84:87]
	v_mfma_f32_16x16x32_bf16 v[76:79], v[214:217], v[198:201], v[76:79]
	v_mfma_f32_16x16x32_bf16 v[72:75], v[222:225], v[198:201], v[72:75]
	v_mfma_f32_16x16x32_bf16 v[68:71], v[214:217], v[206:209], v[68:71]
	v_mfma_f32_16x16x32_bf16 v[64:67], v[222:225], v[206:209], v[64:67]
	v_mfma_f32_16x16x32_bf16 v[104:107], v[218:221], v[186:189], v[104:107]
	v_mfma_f32_16x16x32_bf16 v[96:99], v[226:229], v[186:189], v[96:99]
	v_mfma_f32_16x16x32_bf16 v[88:91], v[218:221], v[194:197], v[88:91]
	v_mfma_f32_16x16x32_bf16 v[84:87], v[226:229], v[194:197], v[84:87]
	v_mfma_f32_16x16x32_bf16 v[76:79], v[218:221], v[202:205], v[76:79]
	v_mfma_f32_16x16x32_bf16 v[72:75], v[226:229], v[202:205], v[72:75]
	v_mfma_f32_16x16x32_bf16 v[68:71], v[218:221], v[210:213], v[68:71]
	v_mfma_f32_16x16x32_bf16 v[64:67], v[226:229], v[210:213], v[64:67]
	s_mov_b32 m0, s36
	v_lshl_add_u64 v[230:231], v[234:235], 0, s[0:1]
	s_barrier
	ds_read_b128 v[160:163], v183 offset:49152
	ds_read_b128 v[186:189], v183 offset:50176
	ds_read_b128 v[190:193], v183 offset:51200
	ds_read_b128 v[194:197], v183 offset:52224
	ds_read_b128 v[198:201], v183 offset:53248
	ds_read_b128 v[202:205], v183 offset:54272
	ds_read_b128 v[206:209], v183 offset:55296
	ds_read_b128 v[210:213], v183 offset:56320
	global_load_lds_dwordx4 v[230:231], off
	v_lshl_add_u64 v[230:231], v[236:237], 0, s[0:1]
	s_mov_b32 m0, s37
	s_nop 0
	global_load_lds_dwordx4 v[230:231], off
	s_barrier
	s_waitcnt lgkmcnt(0)
	s_waitcnt lgkmcnt(0)
	v_mfma_f32_16x16x32_bf16 v[60:63], v[128:131], v[160:163], v[60:63]
	v_mfma_f32_16x16x32_bf16 v[56:59], v[136:139], v[160:163], v[56:59]
	v_mfma_f32_16x16x32_bf16 v[48:51], v[128:131], v[190:193], v[48:51]
	v_mfma_f32_16x16x32_bf16 v[40:43], v[136:139], v[190:193], v[40:43]
	v_mfma_f32_16x16x32_bf16 v[32:35], v[128:131], v[198:201], v[32:35]
	v_mfma_f32_16x16x32_bf16 v[24:27], v[136:139], v[198:201], v[24:27]
	v_mfma_f32_16x16x32_bf16 v[16:19], v[128:131], v[206:209], v[16:19]
	v_mfma_f32_16x16x32_bf16 v[8:11], v[136:139], v[206:209], v[8:11]
	v_mfma_f32_16x16x32_bf16 v[60:63], v[132:135], v[186:189], v[60:63]
	v_mfma_f32_16x16x32_bf16 v[56:59], v[140:143], v[186:189], v[56:59]
	v_mfma_f32_16x16x32_bf16 v[48:51], v[132:135], v[194:197], v[48:51]
	v_mfma_f32_16x16x32_bf16 v[40:43], v[140:143], v[194:197], v[40:43]
	v_mfma_f32_16x16x32_bf16 v[32:35], v[132:135], v[202:205], v[32:35]
	v_mfma_f32_16x16x32_bf16 v[24:27], v[140:143], v[202:205], v[24:27]
	v_mfma_f32_16x16x32_bf16 v[16:19], v[132:135], v[210:213], v[16:19]
	v_mfma_f32_16x16x32_bf16 v[8:11], v[140:143], v[210:213], v[8:11]
	s_barrier
	s_add_u32 s20, s20, 0x80080
	s_addc_u32 s21, s21, 0
	s_add_i32 s22, s22, s29
	v_lshl_add_u64 v[128:129], s[20:21], 0, v[144:145]
	s_mov_b32 m0, s22
	s_nop 0
	global_load_lds_dwordx4 v[128:129], off
	v_lshl_add_u64 v[128:129], s[20:21], 0, v[146:147]
	s_add_i32 m0, s22, 0x2000
	s_nop 0
	global_load_lds_dwordx4 v[128:129], off
	s_waitcnt vmcnt(6)
	s_barrier
	v_mfma_f32_16x16x32_bf16 v[52:55], v[214:217], v[160:163], v[52:55]
	v_mfma_f32_16x16x32_bf16 v[44:47], v[222:225], v[160:163], v[44:47]
	v_mfma_f32_16x16x32_bf16 v[36:39], v[214:217], v[190:193], v[36:39]
	v_mfma_f32_16x16x32_bf16 v[28:31], v[222:225], v[190:193], v[28:31]
	v_mfma_f32_16x16x32_bf16 v[20:23], v[214:217], v[198:201], v[20:23]
	v_mfma_f32_16x16x32_bf16 v[12:15], v[222:225], v[198:201], v[12:15]
	v_mfma_f32_16x16x32_bf16 v[4:7], v[214:217], v[206:209], v[4:7]
	v_mfma_f32_16x16x32_bf16 v[0:3], v[222:225], v[206:209], v[0:3]
	v_mfma_f32_16x16x32_bf16 v[52:55], v[218:221], v[186:189], v[52:55]
	v_mfma_f32_16x16x32_bf16 v[44:47], v[226:229], v[186:189], v[44:47]
	v_mfma_f32_16x16x32_bf16 v[36:39], v[218:221], v[194:197], v[36:39]
	v_mfma_f32_16x16x32_bf16 v[28:31], v[226:229], v[194:197], v[28:31]
	v_mfma_f32_16x16x32_bf16 v[20:23], v[218:221], v[202:205], v[20:23]
	v_mfma_f32_16x16x32_bf16 v[12:15], v[226:229], v[202:205], v[12:15]
	v_mfma_f32_16x16x32_bf16 v[4:7], v[218:221], v[210:213], v[4:7]
	v_mfma_f32_16x16x32_bf16 v[0:3], v[226:229], v[210:213], v[0:3]
	s_add_i32 s51, s51, 2
	s_add_u32 s18, s18, 0x100
	s_addc_u32 s19, s19, 0
	s_add_u32 s49, s49, 0x100
	s_addc_u32 s50, s50, 0
	s_cmp_gt_u32 s51, 29
	s_barrier
	s_cbranch_scc0 .LBB0_451
	v_lshl_or_b32 v162, s44, 8, v181
	v_ashrrev_i32_e32 v163, 31, v162
	v_lshl_add_u64 v[128:129], v[162:163], 2, s[8:9]
	global_load_dwordx4 v[140:143], v[128:129], off
	global_load_dwordx4 v[136:139], v[128:129], off offset:16
	global_load_dwordx4 v[132:135], v[128:129], off offset:512
	s_nop 0
	global_load_dwordx4 v[128:131], v[128:129], off offset:528
	v_lshl_add_u32 v185, s43, 8, v179
	v_mov_b64_e32 v[160:161], s[6:7]
	v_mad_i64_i32 v[186:187], s[18:19], v185, s40, v[160:161]
	v_lshlrev_b64 v[162:163], 1, v[162:163]
	v_or_b32_e32 v188, 16, v185
	v_lshl_add_u64 v[186:187], v[186:187], 0, v[162:163]
	v_mad_i64_i32 v[188:189], s[18:19], v188, s40, v[160:161]
	v_or_b32_e32 v190, 32, v185
	v_lshl_add_u64 v[188:189], v[188:189], 0, v[162:163]
	v_mad_i64_i32 v[190:191], s[18:19], v190, s40, v[160:161]
	v_or_b32_e32 v192, 48, v185
	v_lshl_add_u64 v[190:191], v[190:191], 0, v[162:163]
	v_mad_i64_i32 v[192:193], s[18:19], v192, s40, v[160:161]
	v_lshl_add_u64 v[192:193], v[192:193], 0, v[162:163]
	s_and_b64 vcc, exec, s[14:15]
	s_mov_b32 s44, s42
	s_mov_b32 s43, s41
	s_mov_b64 s[20:21], s[16:17]
	s_waitcnt vmcnt(0)
	v_pk_add_f32 v[124:125], v[124:125], v[140:141]
	v_pk_add_f32 v[126:127], v[126:127], v[142:143]
	v_pk_add_f32 v[122:123], v[122:123], v[138:139]
	v_pk_add_f32 v[196:197], v[64:65], v[128:129]
	v_cvt_pk_bf16_f32 v64, v124, v125
	v_pk_add_f32 v[120:121], v[120:121], v[136:137]
	v_pk_add_f32 v[104:105], v[104:105], v[132:133]
	v_pk_add_f32 v[194:195], v[66:67], v[130:131]
	v_cvt_pk_bf16_f32 v65, v126, v127
	v_cvt_pk_bf16_f32 v66, v120, v121
	v_cvt_pk_bf16_f32 v67, v122, v123
	global_store_dwordx4 v[186:187], v[64:67], off
	v_pk_add_f32 v[106:107], v[106:107], v[134:135]
	v_pk_add_f32 v[98:99], v[98:99], v[130:131]
	v_cvt_pk_bf16_f32 v64, v104, v105
	v_pk_add_f32 v[96:97], v[96:97], v[128:129]
	v_pk_add_f32 v[116:117], v[116:117], v[140:141]
	v_cvt_pk_bf16_f32 v65, v106, v107
	v_cvt_pk_bf16_f32 v66, v96, v97
	v_cvt_pk_bf16_f32 v67, v98, v99
	global_store_dwordx4 v[186:187], v[64:67], off offset:256
	v_pk_add_f32 v[118:119], v[118:119], v[142:143]
	v_pk_add_f32 v[114:115], v[114:115], v[138:139]
	v_cvt_pk_bf16_f32 v64, v116, v117
	v_pk_add_f32 v[112:113], v[112:113], v[136:137]
	v_pk_add_f32 v[88:89], v[88:89], v[132:133]
	v_cvt_pk_bf16_f32 v65, v118, v119
	v_cvt_pk_bf16_f32 v66, v112, v113
	v_cvt_pk_bf16_f32 v67, v114, v115
	global_store_dwordx4 v[188:189], v[64:67], off
	v_pk_add_f32 v[90:91], v[90:91], v[134:135]
	v_pk_add_f32 v[86:87], v[86:87], v[130:131]
	v_cvt_pk_bf16_f32 v64, v88, v89
	v_pk_add_f32 v[84:85], v[84:85], v[128:129]
	v_pk_add_f32 v[108:109], v[108:109], v[140:141]
	v_cvt_pk_bf16_f32 v65, v90, v91
	v_cvt_pk_bf16_f32 v66, v84, v85
	v_cvt_pk_bf16_f32 v67, v86, v87
	global_store_dwordx4 v[188:189], v[64:67], off offset:256
	v_pk_add_f32 v[110:111], v[110:111], v[142:143]
	v_pk_add_f32 v[102:103], v[102:103], v[138:139]
	v_cvt_pk_bf16_f32 v64, v108, v109
	v_pk_add_f32 v[100:101], v[100:101], v[136:137]
	v_pk_add_f32 v[76:77], v[76:77], v[132:133]
	v_cvt_pk_bf16_f32 v65, v110, v111
	v_cvt_pk_bf16_f32 v66, v100, v101
	v_cvt_pk_bf16_f32 v67, v102, v103
	global_store_dwordx4 v[190:191], v[64:67], off
	v_pk_add_f32 v[78:79], v[78:79], v[134:135]
	v_pk_add_f32 v[74:75], v[74:75], v[130:131]
	v_cvt_pk_bf16_f32 v64, v76, v77
	v_pk_add_f32 v[72:73], v[72:73], v[128:129]
	v_pk_add_f32 v[92:93], v[92:93], v[140:141]
	v_cvt_pk_bf16_f32 v65, v78, v79
	v_cvt_pk_bf16_f32 v66, v72, v73
	v_cvt_pk_bf16_f32 v67, v74, v75
	global_store_dwordx4 v[190:191], v[64:67], off offset:256
	v_pk_add_f32 v[94:95], v[94:95], v[142:143]
	v_pk_add_f32 v[82:83], v[82:83], v[138:139]
	v_cvt_pk_bf16_f32 v64, v92, v93
	v_pk_add_f32 v[80:81], v[80:81], v[136:137]
	v_pk_add_f32 v[68:69], v[68:69], v[132:133]
	v_cvt_pk_bf16_f32 v65, v94, v95
	v_cvt_pk_bf16_f32 v66, v80, v81
	v_cvt_pk_bf16_f32 v67, v82, v83
	global_store_dwordx4 v[192:193], v[64:67], off
	v_pk_add_f32 v[70:71], v[70:71], v[134:135]
	v_pk_add_f32 v[62:63], v[62:63], v[142:143]
	v_cvt_pk_bf16_f32 v64, v68, v69
	v_cvt_pk_bf16_f32 v65, v70, v71
	v_cvt_pk_bf16_f32 v66, v196, v197
	v_cvt_pk_bf16_f32 v67, v194, v195
	global_store_dwordx4 v[192:193], v[64:67], off offset:256
	v_pk_add_f32 v[60:61], v[60:61], v[140:141]
	v_pk_add_f32 v[52:53], v[52:53], v[132:133]
	v_add_u32_e32 v64, 0x80, v185
	v_mad_i64_i32 v[64:65], s[18:19], v64, s40, v[160:161]
	v_lshl_add_u64 v[64:65], v[64:65], 0, v[162:163]
	v_pk_add_f32 v[66:67], v[58:59], v[138:139]
	v_pk_add_f32 v[58:59], v[56:57], v[136:137]
	v_cvt_pk_bf16_f32 v56, v60, v61
	v_cvt_pk_bf16_f32 v57, v62, v63
	v_pk_add_f32 v[54:55], v[54:55], v[134:135]
	v_cvt_pk_bf16_f32 v58, v58, v59
	v_cvt_pk_bf16_f32 v59, v66, v67
	global_store_dwordx4 v[64:65], v[56:59], off
	v_pk_add_f32 v[48:49], v[48:49], v[140:141]
	v_pk_add_f32 v[36:37], v[36:37], v[132:133]
	v_pk_add_f32 v[56:57], v[46:47], v[130:131]
	v_pk_add_f32 v[46:47], v[44:45], v[128:129]
	v_cvt_pk_bf16_f32 v44, v52, v53
	v_cvt_pk_bf16_f32 v45, v54, v55
	v_pk_add_f32 v[38:39], v[38:39], v[134:135]
	v_cvt_pk_bf16_f32 v46, v46, v47
	v_cvt_pk_bf16_f32 v47, v56, v57
	global_store_dwordx4 v[64:65], v[44:47], off offset:256
	v_pk_add_f32 v[32:33], v[32:33], v[140:141]
	v_pk_add_f32 v[20:21], v[20:21], v[132:133]
	v_add_u32_e32 v44, 0x90, v185
	v_mad_i64_i32 v[44:45], s[18:19], v44, s40, v[160:161]
	v_lshl_add_u64 v[44:45], v[44:45], 0, v[162:163]
	v_pk_add_f32 v[46:47], v[50:51], v[142:143]
	v_pk_add_f32 v[50:51], v[42:43], v[138:139]
	v_pk_add_f32 v[42:43], v[40:41], v[136:137]
	v_cvt_pk_bf16_f32 v40, v48, v49
	v_cvt_pk_bf16_f32 v41, v46, v47
	v_pk_add_f32 v[22:23], v[22:23], v[134:135]
	v_cvt_pk_bf16_f32 v42, v42, v43
	v_cvt_pk_bf16_f32 v43, v50, v51
	global_store_dwordx4 v[44:45], v[40:43], off
	v_pk_add_f32 v[16:17], v[16:17], v[140:141]
	v_pk_add_f32 v[6:7], v[6:7], v[134:135]
	v_pk_add_f32 v[40:41], v[30:31], v[130:131]
	v_pk_add_f32 v[30:31], v[28:29], v[128:129]
	v_cvt_pk_bf16_f32 v28, v36, v37
	v_cvt_pk_bf16_f32 v29, v38, v39
	v_pk_add_f32 v[4:5], v[4:5], v[132:133]
	v_cvt_pk_bf16_f32 v30, v30, v31
	v_cvt_pk_bf16_f32 v31, v40, v41
	global_store_dwordx4 v[44:45], v[28:31], off offset:256
	s_nop 1
	v_add_u32_e32 v28, 0xa0, v185
	v_mad_i64_i32 v[28:29], s[18:19], v28, s40, v[160:161]
	v_lshl_add_u64 v[28:29], v[28:29], 0, v[162:163]
	v_pk_add_f32 v[30:31], v[34:35], v[142:143]
	v_pk_add_f32 v[34:35], v[26:27], v[138:139]
	v_pk_add_f32 v[26:27], v[24:25], v[136:137]
	v_cvt_pk_bf16_f32 v24, v32, v33
	v_cvt_pk_bf16_f32 v25, v30, v31
	s_nop 0
	v_cvt_pk_bf16_f32 v26, v26, v27
	v_cvt_pk_bf16_f32 v27, v34, v35
	global_store_dwordx4 v[28:29], v[24:27], off
	s_nop 1
	v_pk_add_f32 v[24:25], v[14:15], v[130:131]
	v_pk_add_f32 v[14:15], v[12:13], v[128:129]
	v_cvt_pk_bf16_f32 v12, v20, v21
	v_cvt_pk_bf16_f32 v13, v22, v23
	s_nop 0
	v_cvt_pk_bf16_f32 v14, v14, v15
	v_cvt_pk_bf16_f32 v15, v24, v25
	global_store_dwordx4 v[28:29], v[12:15], off offset:256
	s_nop 1
	v_add_u32_e32 v12, 0xb0, v185
	v_mad_i64_i32 v[12:13], s[18:19], v12, s40, v[160:161]
	v_lshl_add_u64 v[12:13], v[12:13], 0, v[162:163]
	v_pk_add_f32 v[14:15], v[18:19], v[142:143]
	v_pk_add_f32 v[18:19], v[10:11], v[138:139]
	v_pk_add_f32 v[10:11], v[8:9], v[136:137]
	v_cvt_pk_bf16_f32 v8, v16, v17
	v_cvt_pk_bf16_f32 v9, v14, v15
	s_mov_b64 s[18:19], s[12:13]
	v_cvt_pk_bf16_f32 v10, v10, v11
	v_cvt_pk_bf16_f32 v11, v18, v19
	global_store_dwordx4 v[12:13], v[8:11], off
	s_nop 1
	v_pk_add_f32 v[8:9], v[2:3], v[130:131]
	v_pk_add_f32 v[2:3], v[0:1], v[128:129]
	v_cvt_pk_bf16_f32 v0, v4, v5
	v_cvt_pk_bf16_f32 v1, v6, v7
	s_nop 0
	v_cvt_pk_bf16_f32 v2, v2, v3
	v_cvt_pk_bf16_f32 v3, v8, v9
	global_store_dwordx4 v[12:13], v[0:3], off offset:256
	s_cbranch_vccz .LBB0_445
	s_waitcnt vmcnt(0)
	s_cmpk_gt_u32 s24, 0xff
	s_cbranch_scc1 .LBB0_455
	s_barrier

.LBB0_472:
	ds_read_b128 v[0:3], v181
	ds_read_b128 v[4:7], v185
	ds_read_b128 v[8:11], v186
	ds_read_b128 v[12:15], v187
	s_add_u32 s20, s18, 0x80
	s_addc_u32 s21, s19, 0
	s_cmp_eq_u32 s60, 12
	s_cselect_b32 s23, s54, s21
	s_cselect_b32 s22, s55, s20
	s_cselect_b32 s21, s56, s59
	s_cselect_b32 s20, s57, s58
	v_lshl_add_u64 v[162:163], s[18:19], 0, v[160:161]
	s_add_i32 m0, s26, 0xc000
	ds_read_b128 v[166:169], v198
	ds_read_b128 v[170:173], v198 offset:1024
	ds_read_b128 v[202:205], v198 offset:2048
	ds_read_b128 v[206:209], v198 offset:3072
	ds_read_b128 v[210:213], v198 offset:4096
	ds_read_b128 v[214:217], v198 offset:5120
	ds_read_b128 v[218:221], v198 offset:6144
	ds_read_b128 v[222:225], v198 offset:7168
	global_load_lds_dwordx4 v[162:163], off
	v_lshl_add_u64 v[162:163], s[18:19], 0, v[158:159]
	s_add_i32 m0, s26, 0xe000
	s_nop 0
	global_load_lds_dwordx4 v[162:163], off
	s_waitcnt lgkmcnt(8)
	s_barrier
	s_waitcnt lgkmcnt(0)
	s_waitcnt lgkmcnt(0)
	v_mfma_scale_f32_16x16x128_f8f6f4 v[140:143], v[0:7], v[166:173], v[140:143], v199, v200 op_sel_hi:[0,0,0]
	v_mfma_scale_f32_16x16x128_f8f6f4 v[136:139], v[8:15], v[166:173], v[136:139], v199, v200 op_sel_hi:[0,0,0]
	v_mfma_scale_f32_16x16x128_f8f6f4 v[132:135], v[0:7], v[202:209], v[132:135], v199, v200 op_sel_hi:[0,0,0]
	v_mfma_scale_f32_16x16x128_f8f6f4 v[128:131], v[8:15], v[202:209], v[128:131], v199, v200 op_sel_hi:[0,0,0]
	v_mfma_scale_f32_16x16x128_f8f6f4 v[124:127], v[0:7], v[210:217], v[124:127], v199, v200 op_sel_hi:[0,0,0]
	v_mfma_scale_f32_16x16x128_f8f6f4 v[116:119], v[8:15], v[210:217], v[116:119], v199, v200 op_sel_hi:[0,0,0]
	v_mfma_scale_f32_16x16x128_f8f6f4 v[108:111], v[0:7], v[218:225], v[108:111], v199, v200 op_sel_hi:[0,0,0]
	v_mfma_scale_f32_16x16x128_f8f6f4 v[100:103], v[8:15], v[218:225], v[100:103], v199, v200 op_sel_hi:[0,0,0]
	s_barrier
	s_mov_b32 m0, s27
	v_lshl_add_u64 v[162:163], s[20:21], 0, v[144:145]
	ds_read_b128 v[226:229], v182
	ds_read_b128 v[230:233], v188
	ds_read_b128 v[234:237], v189
	ds_read_b128 v[238:241], v190
	global_load_lds_dwordx4 v[162:163], off
	v_lshl_add_u64 v[164:165], s[20:21], 0, v[146:147]
	s_mov_b32 m0, s28
	s_nop 0
	global_load_lds_dwordx4 v[164:165], off
	s_barrier
	s_waitcnt lgkmcnt(0)
	s_waitcnt lgkmcnt(0)
	v_mfma_scale_f32_16x16x128_f8f6f4 v[120:123], v[226:233], v[166:173], v[120:123], v199, v200 op_sel_hi:[0,0,0]
	v_mfma_scale_f32_16x16x128_f8f6f4 v[112:115], v[234:241], v[166:173], v[112:115], v199, v200 op_sel_hi:[0,0,0]
	v_mfma_scale_f32_16x16x128_f8f6f4 v[104:107], v[226:233], v[202:209], v[104:107], v199, v200 op_sel_hi:[0,0,0]
	v_mfma_scale_f32_16x16x128_f8f6f4 v[96:99], v[234:241], v[202:209], v[96:99], v199, v200 op_sel_hi:[0,0,0]
	v_mfma_scale_f32_16x16x128_f8f6f4 v[92:95], v[226:233], v[210:217], v[92:95], v199, v200 op_sel_hi:[0,0,0]
	v_mfma_scale_f32_16x16x128_f8f6f4 v[88:91], v[234:241], v[210:217], v[88:91], v199, v200 op_sel_hi:[0,0,0]
	v_mfma_scale_f32_16x16x128_f8f6f4 v[84:87], v[226:233], v[218:225], v[84:87], v199, v200 op_sel_hi:[0,0,0]
	v_mfma_scale_f32_16x16x128_f8f6f4 v[80:83], v[234:241], v[218:225], v[80:83], v199, v200 op_sel_hi:[0,0,0]
	s_mov_b32 m0, s26
	v_lshl_add_u64 v[166:167], s[22:23], 0, v[148:149]
	s_barrier
	ds_read_b128 v[170:173], v198 offset:16384
	ds_read_b128 v[174:177], v198 offset:17408
	ds_read_b128 v[202:205], v198 offset:18432
	ds_read_b128 v[206:209], v198 offset:19456
	ds_read_b128 v[210:213], v198 offset:20480
	ds_read_b128 v[214:217], v198 offset:21504
	ds_read_b128 v[218:221], v198 offset:22528
	ds_read_b128 v[222:225], v198 offset:23552
	global_load_lds_dwordx4 v[166:167], off
	v_lshl_add_u64 v[168:169], s[22:23], 0, v[150:151]
	s_mov_b32 m0, s29
	s_nop 0
	global_load_lds_dwordx4 v[168:169], off
	s_barrier
	s_waitcnt lgkmcnt(0)
	s_waitcnt lgkmcnt(0)
	v_mfma_scale_f32_16x16x128_f8f6f4 v[76:79], v[0:7], v[170:177], v[76:79], v199, v200 op_sel_hi:[0,0,0]
	v_mfma_scale_f32_16x16x128_f8f6f4 v[72:75], v[8:15], v[170:177], v[72:75], v199, v200 op_sel_hi:[0,0,0]
	v_mfma_scale_f32_16x16x128_f8f6f4 v[64:67], v[0:7], v[202:209], v[64:67], v199, v200 op_sel_hi:[0,0,0]
	v_mfma_scale_f32_16x16x128_f8f6f4 v[56:59], v[8:15], v[202:209], v[56:59], v199, v200 op_sel_hi:[0,0,0]
	v_mfma_scale_f32_16x16x128_f8f6f4 v[48:51], v[0:7], v[210:217], v[48:51], v199, v200 op_sel_hi:[0,0,0]
	v_mfma_scale_f32_16x16x128_f8f6f4 v[40:43], v[8:15], v[210:217], v[40:43], v199, v200 op_sel_hi:[0,0,0]
	v_mfma_scale_f32_16x16x128_f8f6f4 v[32:35], v[0:7], v[218:225], v[32:35], v199, v200 op_sel_hi:[0,0,0]
	v_mfma_scale_f32_16x16x128_f8f6f4 v[24:27], v[8:15], v[218:225], v[24:27], v199, v200 op_sel_hi:[0,0,0]
	s_barrier
	s_add_u32 s62, s20, 0x40000
	s_addc_u32 s63, s21, 0
	s_mov_b32 m0, s30
	v_lshl_add_u64 v[0:1], s[62:63], 0, v[144:145]
	global_load_lds_dwordx4 v[0:1], off
	v_lshl_add_u64 v[0:1], s[62:63], 0, v[146:147]
	s_mov_b32 m0, s31
	s_nop 0
	global_load_lds_dwordx4 v[0:1], off
	s_waitcnt vmcnt(6)
	s_barrier
	v_mfma_scale_f32_16x16x128_f8f6f4 v[68:71], v[226:233], v[170:177], v[68:71], v199, v200 op_sel_hi:[0,0,0]
	v_mfma_scale_f32_16x16x128_f8f6f4 v[60:63], v[234:241], v[170:177], v[60:63], v199, v200 op_sel_hi:[0,0,0]
	v_mfma_scale_f32_16x16x128_f8f6f4 v[52:55], v[226:233], v[202:209], v[52:55], v199, v200 op_sel_hi:[0,0,0]
	v_mfma_scale_f32_16x16x128_f8f6f4 v[44:47], v[234:241], v[202:209], v[44:47], v199, v200 op_sel_hi:[0,0,0]
	v_mfma_scale_f32_16x16x128_f8f6f4 v[36:39], v[226:233], v[210:217], v[36:39], v199, v200 op_sel_hi:[0,0,0]
	v_mfma_scale_f32_16x16x128_f8f6f4 v[28:31], v[234:241], v[210:217], v[28:31], v199, v200 op_sel_hi:[0,0,0]
	v_mfma_scale_f32_16x16x128_f8f6f4 v[20:23], v[226:233], v[218:225], v[20:23], v199, v200 op_sel_hi:[0,0,0]
	v_mfma_scale_f32_16x16x128_f8f6f4 v[16:19], v[234:241], v[218:225], v[16:19], v199, v200 op_sel_hi:[0,0,0]
	s_barrier
	ds_read_b128 v[0:3], v183
	ds_read_b128 v[4:7], v191
	ds_read_b128 v[8:11], v192
	ds_read_b128 v[12:15], v193
	s_mov_b32 m0, s33
	v_lshl_add_u64 v[178:179], s[22:23], 0, v[152:153]
	ds_read_b128 v[170:173], v198 offset:32768
	ds_read_b128 v[174:177], v198 offset:33792
	ds_read_b128 v[202:205], v198 offset:34816
	ds_read_b128 v[206:209], v198 offset:35840
	ds_read_b128 v[210:213], v198 offset:36864
	ds_read_b128 v[214:217], v198 offset:37888
	ds_read_b128 v[218:221], v198 offset:38912
	ds_read_b128 v[222:225], v198 offset:39936
	global_load_lds_dwordx4 v[178:179], off
	v_lshl_add_u64 v[178:179], s[22:23], 0, v[154:155]
	s_mov_b32 m0, s34
	s_nop 0
	global_load_lds_dwordx4 v[178:179], off
	s_waitcnt lgkmcnt(8)
	s_barrier
	s_waitcnt lgkmcnt(0)
	s_waitcnt lgkmcnt(0)
	v_mfma_scale_f32_16x16x128_f8f6f4 v[140:143], v[0:7], v[170:177], v[140:143], v199, v200 op_sel_hi:[0,0,0]
	v_mfma_scale_f32_16x16x128_f8f6f4 v[136:139], v[8:15], v[170:177], v[136:139], v199, v200 op_sel_hi:[0,0,0]
	v_mfma_scale_f32_16x16x128_f8f6f4 v[132:135], v[0:7], v[202:209], v[132:135], v199, v200 op_sel_hi:[0,0,0]
	v_mfma_scale_f32_16x16x128_f8f6f4 v[128:131], v[8:15], v[202:209], v[128:131], v199, v200 op_sel_hi:[0,0,0]
	v_mfma_scale_f32_16x16x128_f8f6f4 v[124:127], v[0:7], v[210:217], v[124:127], v199, v200 op_sel_hi:[0,0,0]
	v_mfma_scale_f32_16x16x128_f8f6f4 v[116:119], v[8:15], v[210:217], v[116:119], v199, v200 op_sel_hi:[0,0,0]
	v_mfma_scale_f32_16x16x128_f8f6f4 v[108:111], v[0:7], v[218:225], v[108:111], v199, v200 op_sel_hi:[0,0,0]
	v_mfma_scale_f32_16x16x128_f8f6f4 v[100:103], v[8:15], v[218:225], v[100:103], v199, v200 op_sel_hi:[0,0,0]
	s_barrier
	s_mov_b32 m0, s40
	v_lshl_add_u64 v[162:163], v[162:163], 0, s[10:11]
	ds_read_b128 v[226:229], v184
	ds_read_b128 v[230:233], v194
	ds_read_b128 v[234:237], v195
	ds_read_b128 v[238:241], v196
	global_load_lds_dwordx4 v[162:163], off
	v_lshl_add_u64 v[162:163], v[164:165], 0, s[10:11]
	s_mov_b32 m0, s41
	s_nop 0
	global_load_lds_dwordx4 v[162:163], off
	s_barrier
	s_waitcnt lgkmcnt(0)
	s_waitcnt lgkmcnt(0)
	v_mfma_scale_f32_16x16x128_f8f6f4 v[120:123], v[226:233], v[170:177], v[120:123], v199, v200 op_sel_hi:[0,0,0]
	v_mfma_scale_f32_16x16x128_f8f6f4 v[112:115], v[234:241], v[170:177], v[112:115], v199, v200 op_sel_hi:[0,0,0]
	v_mfma_scale_f32_16x16x128_f8f6f4 v[104:107], v[226:233], v[202:209], v[104:107], v199, v200 op_sel_hi:[0,0,0]
	v_mfma_scale_f32_16x16x128_f8f6f4 v[96:99], v[234:241], v[202:209], v[96:99], v199, v200 op_sel_hi:[0,0,0]
	v_mfma_scale_f32_16x16x128_f8f6f4 v[92:95], v[226:233], v[210:217], v[92:95], v199, v200 op_sel_hi:[0,0,0]
	v_mfma_scale_f32_16x16x128_f8f6f4 v[88:91], v[234:241], v[210:217], v[88:91], v199, v200 op_sel_hi:[0,0,0]
	v_mfma_scale_f32_16x16x128_f8f6f4 v[84:87], v[226:233], v[218:225], v[84:87], v199, v200 op_sel_hi:[0,0,0]
	v_mfma_scale_f32_16x16x128_f8f6f4 v[80:83], v[234:241], v[218:225], v[80:83], v199, v200 op_sel_hi:[0,0,0]
	s_mov_b32 m0, s42
	v_lshl_add_u64 v[162:163], v[166:167], 0, s[10:11]
	s_barrier
	ds_read_b128 v[170:173], v198 offset:49152
	ds_read_b128 v[174:177], v198 offset:50176
	ds_read_b128 v[202:205], v198 offset:51200
	ds_read_b128 v[206:209], v198 offset:52224
	ds_read_b128 v[210:213], v198 offset:53248
	ds_read_b128 v[214:217], v198 offset:54272
	ds_read_b128 v[218:221], v198 offset:55296
	ds_read_b128 v[222:225], v198 offset:56320
	global_load_lds_dwordx4 v[162:163], off
	v_lshl_add_u64 v[162:163], v[168:169], 0, s[10:11]
	s_mov_b32 m0, s43
	s_nop 0
	global_load_lds_dwordx4 v[162:163], off
	s_barrier
	s_waitcnt lgkmcnt(0)
	s_waitcnt lgkmcnt(0)
	v_mfma_scale_f32_16x16x128_f8f6f4 v[76:79], v[0:7], v[170:177], v[76:79], v199, v200 op_sel_hi:[0,0,0]
	v_mfma_scale_f32_16x16x128_f8f6f4 v[72:75], v[8:15], v[170:177], v[72:75], v199, v200 op_sel_hi:[0,0,0]
	v_mfma_scale_f32_16x16x128_f8f6f4 v[64:67], v[0:7], v[202:209], v[64:67], v199, v200 op_sel_hi:[0,0,0]
	v_mfma_scale_f32_16x16x128_f8f6f4 v[56:59], v[8:15], v[202:209], v[56:59], v199, v200 op_sel_hi:[0,0,0]
	v_mfma_scale_f32_16x16x128_f8f6f4 v[48:51], v[0:7], v[210:217], v[48:51], v199, v200 op_sel_hi:[0,0,0]
	v_mfma_scale_f32_16x16x128_f8f6f4 v[40:43], v[8:15], v[210:217], v[40:43], v199, v200 op_sel_hi:[0,0,0]
	v_mfma_scale_f32_16x16x128_f8f6f4 v[32:35], v[0:7], v[218:225], v[32:35], v199, v200 op_sel_hi:[0,0,0]
	v_mfma_scale_f32_16x16x128_f8f6f4 v[24:27], v[8:15], v[218:225], v[24:27], v199, v200 op_sel_hi:[0,0,0]
	s_barrier
	s_add_u32 s20, s20, 0x40080
	s_addc_u32 s21, s21, 0
	s_mov_b32 m0, s44
	v_lshl_add_u64 v[0:1], s[20:21], 0, v[144:145]
	global_load_lds_dwordx4 v[0:1], off
	v_lshl_add_u64 v[0:1], s[20:21], 0, v[146:147]
	s_mov_b32 m0, s45
	s_nop 0
	global_load_lds_dwordx4 v[0:1], off
	s_waitcnt vmcnt(6)
	s_barrier
	v_mfma_scale_f32_16x16x128_f8f6f4 v[68:71], v[226:233], v[170:177], v[68:71], v199, v200 op_sel_hi:[0,0,0]
	v_mfma_scale_f32_16x16x128_f8f6f4 v[60:63], v[234:241], v[170:177], v[60:63], v199, v200 op_sel_hi:[0,0,0]
	v_mfma_scale_f32_16x16x128_f8f6f4 v[52:55], v[226:233], v[202:209], v[52:55], v199, v200 op_sel_hi:[0,0,0]
	v_mfma_scale_f32_16x16x128_f8f6f4 v[44:47], v[234:241], v[202:209], v[44:47], v199, v200 op_sel_hi:[0,0,0]
	v_mfma_scale_f32_16x16x128_f8f6f4 v[36:39], v[226:233], v[210:217], v[36:39], v199, v200 op_sel_hi:[0,0,0]
	v_mfma_scale_f32_16x16x128_f8f6f4 v[28:31], v[234:241], v[210:217], v[28:31], v199, v200 op_sel_hi:[0,0,0]
	v_mfma_scale_f32_16x16x128_f8f6f4 v[20:23], v[226:233], v[218:225], v[20:23], v199, v200 op_sel_hi:[0,0,0]
	v_mfma_scale_f32_16x16x128_f8f6f4 v[16:19], v[234:241], v[218:225], v[16:19], v199, v200 op_sel_hi:[0,0,0]
	s_add_i32 s60, s60, 2
	s_add_u32 s18, s18, 0x100
	s_addc_u32 s19, s19, 0
	s_add_u32 s58, s58, 0x100
	s_addc_u32 s59, s59, 0
	s_cmp_gt_u32 s60, 13
	s_barrier
	s_cbranch_scc0 .LBB0_472
	s_nop 15
	s_nop 15
	s_lshl_b32 s18, s53, 8
	v_add_u32_e32 v176, s18, v180
	s_cmp_lg_u32 s52, 0
	v_or_b32_e32 v174, 16, v176
	v_or_b32_e32 v172, 32, v176
	v_or_b32_e32 v170, 48, v176
	v_add_u32_e32 v168, 0x80, v176
	v_add_u32_e32 v166, 0x90, v176
	v_add_u32_e32 v164, 0xa0, v176
	v_add_u32_e32 v162, 0xb0, v176
	s_cbranch_scc0 .LBB0_475
	v_ashrrev_i32_e32 v177, 31, v176
	v_lshl_add_u64 v[0:1], v[176:177], 2, s[8:9]
	v_add_co_u32_e32 v0, vcc, 0x7000, v0
	s_ashr_i32 s18, s51, 3
	s_nop 0
	v_addc_co_u32_e32 v1, vcc, 0, v1, vcc
	global_load_dword v4, v[0:1], off offset:1024
	global_load_dword v6, v[0:1], off offset:1088
	global_load_dword v8, v[0:1], off offset:1152
	global_load_dword v10, v[0:1], off offset:1216
	v_mad_i64_i32 v[2:3], s[20:21], s18, v201, v[176:177]
	v_lshlrev_b64 v[2:3], 12, v[2:3]
	v_lshl_add_u64 v[178:179], s[0:1], 0, v[2:3]
	global_load_dword v202, v[0:1], off offset:1536
	global_load_dword v204, v[0:1], off offset:1600
	global_load_dword v2, v[0:1], off offset:1664
	s_nop 0
	global_load_dword v0, v[0:1], off offset:1728
	s_lshl_b32 s19, s51, 8
	s_and_b32 s19, s19, 0x700
	v_ashrrev_i32_e32 v175, 31, v174
	v_or_b32_e32 v5, s19, v197
	v_mad_i64_i32 v[12:13], s[20:21], s18, v201, v[174:175]
	v_lshlrev_b32_e32 v156, 1, v5
	v_ashrrev_i32_e32 v173, 31, v172
	v_lshlrev_b64 v[12:13], 12, v[12:13]
	v_lshl_add_u64 v[178:179], v[178:179], 0, v[156:157]
	v_mad_i64_i32 v[14:15], s[20:21], s18, v201, v[172:173]
	v_lshl_add_u64 v[12:13], s[0:1], 0, v[12:13]
	v_lshlrev_b64 v[14:15], 12, v[14:15]
	v_lshl_add_u64 v[12:13], v[12:13], 0, v[156:157]
	v_lshl_add_u64 v[14:15], s[0:1], 0, v[14:15]
	v_lshl_add_u64 v[14:15], v[14:15], 0, v[156:157]
	v_ashrrev_i32_e32 v171, 31, v170
	v_ashrrev_i32_e32 v169, 31, v168
	v_ashrrev_i32_e32 v167, 31, v166
	v_ashrrev_i32_e32 v165, 31, v164
	v_ashrrev_i32_e32 v163, 31, v162
	s_waitcnt vmcnt(0)
	v_pk_add_f32 v[206:207], v[142:143], v[4:5] op_sel_hi:[1,0]
	v_pk_add_f32 v[208:209], v[140:141], v[4:5] op_sel_hi:[1,0]
	v_pk_add_f32 v[210:211], v[138:139], v[4:5] op_sel_hi:[1,0]
	v_pk_add_f32 v[212:213], v[136:137], v[4:5] op_sel_hi:[1,0]
	v_pk_add_f32 v[214:215], v[122:123], v[4:5] op_sel_hi:[1,0]
	v_pk_add_f32 v[216:217], v[120:121], v[4:5] op_sel_hi:[1,0]
	v_pk_add_f32 v[218:219], v[114:115], v[4:5] op_sel_hi:[1,0]
	v_pk_add_f32 v[220:221], v[112:113], v[4:5] op_sel_hi:[1,0]
	v_cvt_pk_bf16_f32 v4, v208, v209
	v_cvt_pk_bf16_f32 v5, v206, v207
	v_pk_add_f32 v[222:223], v[134:135], v[6:7] op_sel_hi:[1,0]
	v_pk_add_f32 v[224:225], v[132:133], v[6:7] op_sel_hi:[1,0]
	v_pk_add_f32 v[226:227], v[130:131], v[6:7] op_sel_hi:[1,0]
	v_pk_add_f32 v[228:229], v[128:129], v[6:7] op_sel_hi:[1,0]
	v_pk_add_f32 v[230:231], v[106:107], v[6:7] op_sel_hi:[1,0]
	v_pk_add_f32 v[232:233], v[104:105], v[6:7] op_sel_hi:[1,0]
	v_pk_add_f32 v[234:235], v[98:99], v[6:7] op_sel_hi:[1,0]
	v_pk_add_f32 v[236:237], v[96:97], v[6:7] op_sel_hi:[1,0]
	v_cvt_pk_bf16_f32 v6, v212, v213
	v_cvt_pk_bf16_f32 v7, v210, v211
	global_store_dwordx4 v[178:179], v[4:7], off
	v_pk_add_f32 v[238:239], v[126:127], v[8:9] op_sel_hi:[1,0]
	v_pk_add_f32 v[240:241], v[124:125], v[8:9] op_sel_hi:[1,0]
	v_cvt_pk_bf16_f32 v4, v216, v217
	v_cvt_pk_bf16_f32 v5, v214, v215
	v_cvt_pk_bf16_f32 v6, v220, v221
	v_cvt_pk_bf16_f32 v7, v218, v219
	global_store_dwordx4 v[178:179], v[4:7], off offset:256
	v_pk_add_f32 v[242:243], v[118:119], v[8:9] op_sel_hi:[1,0]
	v_pk_add_f32 v[244:245], v[116:117], v[8:9] op_sel_hi:[1,0]
	v_cvt_pk_bf16_f32 v4, v224, v225
	v_cvt_pk_bf16_f32 v5, v222, v223
	v_cvt_pk_bf16_f32 v6, v228, v229
	v_cvt_pk_bf16_f32 v7, v226, v227
	global_store_dwordx4 v[12:13], v[4:7], off
	v_pk_add_f32 v[246:247], v[94:95], v[8:9] op_sel_hi:[1,0]
	v_pk_add_f32 v[248:249], v[92:93], v[8:9] op_sel_hi:[1,0]
	v_cvt_pk_bf16_f32 v4, v232, v233
	v_cvt_pk_bf16_f32 v5, v230, v231
	v_cvt_pk_bf16_f32 v6, v236, v237
	v_cvt_pk_bf16_f32 v7, v234, v235
	global_store_dwordx4 v[12:13], v[4:7], off offset:256
	v_pk_add_f32 v[250:251], v[90:91], v[8:9] op_sel_hi:[1,0]
	v_pk_add_f32 v[8:9], v[88:89], v[8:9] op_sel_hi:[1,0]
	v_cvt_pk_bf16_f32 v4, v240, v241
	v_cvt_pk_bf16_f32 v5, v238, v239
	v_cvt_pk_bf16_f32 v6, v244, v245
	v_cvt_pk_bf16_f32 v7, v242, v243
	global_store_dwordx4 v[14:15], v[4:7], off
	v_pk_add_f32 v[12:13], v[102:103], v[10:11] op_sel_hi:[1,0]
	s_nop 0
	v_cvt_pk_bf16_f32 v4, v248, v249
	v_cvt_pk_bf16_f32 v5, v246, v247
	v_cvt_pk_bf16_f32 v6, v8, v9
	v_cvt_pk_bf16_f32 v7, v250, v251
	global_store_dwordx4 v[14:15], v[4:7], off offset:256
	v_pk_add_f32 v[14:15], v[100:101], v[10:11] op_sel_hi:[1,0]
	s_nop 0
	v_mad_i64_i32 v[4:5], s[20:21], s18, v201, v[170:171]
	v_lshlrev_b64 v[4:5], 12, v[4:5]
	v_lshl_add_u64 v[4:5], s[0:1], 0, v[4:5]
	v_lshl_add_u64 v[8:9], v[4:5], 0, v[156:157]
	v_pk_add_f32 v[4:5], v[108:109], v[10:11] op_sel_hi:[1,0]
	v_pk_add_f32 v[6:7], v[110:111], v[10:11] op_sel_hi:[1,0]
	v_cvt_pk_bf16_f32 v4, v4, v5
	s_nop 0
	v_cvt_pk_bf16_f32 v5, v6, v7
	v_cvt_pk_bf16_f32 v6, v14, v15
	v_cvt_pk_bf16_f32 v7, v12, v13
	global_store_dwordx4 v[8:9], v[4:7], off
	v_pk_add_f32 v[12:13], v[82:83], v[10:11] op_sel_hi:[1,0]
	s_nop 0
	v_pk_add_f32 v[4:5], v[84:85], v[10:11] op_sel_hi:[1,0]
	v_pk_add_f32 v[6:7], v[86:87], v[10:11] op_sel_hi:[1,0]
	v_cvt_pk_bf16_f32 v4, v4, v5
	v_pk_add_f32 v[10:11], v[80:81], v[10:11] op_sel_hi:[1,0]
	v_cvt_pk_bf16_f32 v5, v6, v7
	s_nop 0
	v_cvt_pk_bf16_f32 v6, v10, v11
	v_cvt_pk_bf16_f32 v7, v12, v13
	global_store_dwordx4 v[8:9], v[4:7], off offset:256
	v_pk_add_f32 v[10:11], v[74:75], v[202:203] op_sel_hi:[1,0]
	v_pk_add_f32 v[12:13], v[72:73], v[202:203] op_sel_hi:[1,0]
	v_mad_i64_i32 v[4:5], s[20:21], s18, v201, v[168:169]
	v_lshlrev_b64 v[4:5], 12, v[4:5]
	v_lshl_add_u64 v[4:5], s[0:1], 0, v[4:5]
	v_lshl_add_u64 v[8:9], v[4:5], 0, v[156:157]
	v_pk_add_f32 v[4:5], v[76:77], v[202:203] op_sel_hi:[1,0]
	v_pk_add_f32 v[6:7], v[78:79], v[202:203] op_sel_hi:[1,0]
	v_cvt_pk_bf16_f32 v4, v4, v5
	s_nop 0
	v_cvt_pk_bf16_f32 v5, v6, v7
	v_cvt_pk_bf16_f32 v6, v12, v13
	v_cvt_pk_bf16_f32 v7, v10, v11
	global_store_dwordx4 v[8:9], v[4:7], off
	v_pk_add_f32 v[10:11], v[62:63], v[202:203] op_sel_hi:[1,0]
	v_pk_add_f32 v[12:13], v[60:61], v[202:203] op_sel_hi:[1,0]
	v_pk_add_f32 v[4:5], v[68:69], v[202:203] op_sel_hi:[1,0]
	v_pk_add_f32 v[6:7], v[70:71], v[202:203] op_sel_hi:[1,0]
	v_cvt_pk_bf16_f32 v4, v4, v5
	s_nop 0
	v_cvt_pk_bf16_f32 v5, v6, v7
	v_cvt_pk_bf16_f32 v6, v12, v13
	v_cvt_pk_bf16_f32 v7, v10, v11
	global_store_dwordx4 v[8:9], v[4:7], off offset:256
	v_pk_add_f32 v[10:11], v[58:59], v[204:205] op_sel_hi:[1,0]
	v_pk_add_f32 v[12:13], v[56:57], v[204:205] op_sel_hi:[1,0]
	v_mad_i64_i32 v[4:5], s[20:21], s18, v201, v[166:167]
	v_lshlrev_b64 v[4:5], 12, v[4:5]
	v_lshl_add_u64 v[4:5], s[0:1], 0, v[4:5]
	v_lshl_add_u64 v[8:9], v[4:5], 0, v[156:157]
	v_pk_add_f32 v[4:5], v[64:65], v[204:205] op_sel_hi:[1,0]
	v_pk_add_f32 v[6:7], v[66:67], v[204:205] op_sel_hi:[1,0]
	v_cvt_pk_bf16_f32 v4, v4, v5
	s_nop 0
	v_cvt_pk_bf16_f32 v5, v6, v7
	v_cvt_pk_bf16_f32 v6, v12, v13
	v_cvt_pk_bf16_f32 v7, v10, v11
	global_store_dwordx4 v[8:9], v[4:7], off
	v_pk_add_f32 v[10:11], v[46:47], v[204:205] op_sel_hi:[1,0]
	v_pk_add_f32 v[12:13], v[44:45], v[204:205] op_sel_hi:[1,0]
	v_pk_add_f32 v[4:5], v[52:53], v[204:205] op_sel_hi:[1,0]
	v_pk_add_f32 v[6:7], v[54:55], v[204:205] op_sel_hi:[1,0]
	v_cvt_pk_bf16_f32 v4, v4, v5
	s_nop 0
	v_cvt_pk_bf16_f32 v5, v6, v7
	v_cvt_pk_bf16_f32 v6, v12, v13
	v_cvt_pk_bf16_f32 v7, v10, v11
	global_store_dwordx4 v[8:9], v[4:7], off offset:256
	v_pk_add_f32 v[10:11], v[42:43], v[2:3] op_sel_hi:[1,0]
	v_pk_add_f32 v[12:13], v[40:41], v[2:3] op_sel_hi:[1,0]
	v_mad_i64_i32 v[4:5], s[20:21], s18, v201, v[164:165]
	v_lshlrev_b64 v[4:5], 12, v[4:5]
	v_lshl_add_u64 v[4:5], s[0:1], 0, v[4:5]
	v_lshl_add_u64 v[8:9], v[4:5], 0, v[156:157]
	v_pk_add_f32 v[6:7], v[50:51], v[2:3] op_sel_hi:[1,0]
	v_pk_add_f32 v[4:5], v[48:49], v[2:3] op_sel_hi:[1,0]
	s_nop 0
	v_cvt_pk_bf16_f32 v4, v4, v5
	v_cvt_pk_bf16_f32 v5, v6, v7
	v_cvt_pk_bf16_f32 v6, v12, v13
	v_cvt_pk_bf16_f32 v7, v10, v11
	global_store_dwordx4 v[8:9], v[4:7], off
	v_pk_add_f32 v[10:11], v[30:31], v[2:3] op_sel_hi:[1,0]
	v_pk_add_f32 v[12:13], v[28:29], v[2:3] op_sel_hi:[1,0]
	v_pk_add_f32 v[4:5], v[38:39], v[2:3] op_sel_hi:[1,0]
	v_pk_add_f32 v[6:7], v[36:37], v[2:3] op_sel_hi:[1,0]
	s_nop 0
	v_cvt_pk_bf16_f32 v2, v6, v7
	v_cvt_pk_bf16_f32 v3, v4, v5
	v_cvt_pk_bf16_f32 v4, v12, v13
	v_cvt_pk_bf16_f32 v5, v10, v11
	global_store_dwordx4 v[8:9], v[2:5], off offset:256
	v_pk_add_f32 v[6:7], v[26:27], v[0:1] op_sel_hi:[1,0]
	v_pk_add_f32 v[8:9], v[24:25], v[0:1] op_sel_hi:[1,0]
	v_mad_i64_i32 v[2:3], s[18:19], s18, v201, v[162:163]
	v_lshlrev_b64 v[2:3], 12, v[2:3]
	v_lshl_add_u64 v[2:3], s[0:1], 0, v[2:3]
	v_lshl_add_u64 v[178:179], v[2:3], 0, v[156:157]
	v_pk_add_f32 v[2:3], v[32:33], v[0:1] op_sel_hi:[1,0]
	v_pk_add_f32 v[4:5], v[34:35], v[0:1] op_sel_hi:[1,0]
	v_cvt_pk_bf16_f32 v2, v2, v3
	s_nop 0
	v_cvt_pk_bf16_f32 v3, v4, v5
	v_cvt_pk_bf16_f32 v4, v8, v9
	v_cvt_pk_bf16_f32 v5, v6, v7
	global_store_dwordx4 v[178:179], v[2:5], off
	v_pk_add_f32 v[6:7], v[18:19], v[0:1] op_sel_hi:[1,0]
	v_pk_add_f32 v[8:9], v[16:17], v[0:1] op_sel_hi:[1,0]
	v_pk_add_f32 v[2:3], v[22:23], v[0:1] op_sel_hi:[1,0]
	v_pk_add_f32 v[4:5], v[20:21], v[0:1] op_sel_hi:[1,0]
	s_nop 0
	v_cvt_pk_bf16_f32 v0, v4, v5
	v_cvt_pk_bf16_f32 v1, v2, v3
	v_cvt_pk_bf16_f32 v2, v8, v9
	v_cvt_pk_bf16_f32 v3, v6, v7
	s_cbranch_execnz .LBB0_465
	s_branch .LBB0_464

.LBB0_533:
	s_setprio 0
	s_cmp_lt_i32 s82, 5
	s_mov_b64 s[4:5], s[86:87]
	s_mov_b32 s8, 0
	s_cselect_b64 s[6:7], -1, 0
	s_and_b64 s[24:25], s[6:7], s[0:1]
	v_mbcnt_lo_u32_b32 v0, -1, s8
	v_mbcnt_hi_u32_b32 v0, -1, v0
	v_or_b32_e32 v0, s92, v0
	s_andn2_b64 vcc, exec, s[24:25]
	s_cbranch_vccnz .LBB0_542
	v_lshl_add_u32 v90, s2, 9, v0
	s_mov_b32 s0, 0x240000
	v_cmp_gt_i32_e32 vcc, s0, v90
	s_mov_b64 s[8:9], s[86:87]
	s_and_saveexec_b64 s[0:1], vcc
	s_cbranch_execz .LBB0_541
	s_load_dwordx2 s[10:11], s[4:5], 0x138
	v_lshlrev_b32_e32 v0, 3, v0
	s_load_dwordx4 s[4:7], s[8:9], 0x50
	v_and_b32_e32 v0, 0x3f8, v0
	v_lshlrev_b32_e32 v80, 1, v0
	v_mov_b32_e32 v81, 0
	s_waitcnt lgkmcnt(0)
	v_lshl_add_u64 v[82:83], s[10:11], 0, v[80:81]
	v_lshlrev_b32_e32 v80, 2, v0
	v_lshl_add_u64 v[48:49], s[4:5], 0, v[80:81]
	s_mov_b64 s[8:9], 0x1000
	v_lshl_add_u64 v[16:17], v[48:49], 0, s[8:9]
	s_movk_i32 s8, 0x2000
	v_add_co_u32_e32 v18, vcc, s8, v48
	s_mov_b64 s[8:9], 0x2000
	v_lshl_add_u64 v[20:21], v[48:49], 0, s[8:9]
	s_mov_b64 s[8:9], 0x3000
	v_addc_co_u32_e32 v19, vcc, 0, v49, vcc
	v_lshl_add_u64 v[32:33], v[48:49], 0, s[8:9]
	s_movk_i32 s8, 0x4000
	v_add_co_u32_e32 v34, vcc, s8, v48
	s_mov_b64 s[8:9], 0x4000
	v_lshl_add_u64 v[36:37], v[48:49], 0, s[8:9]
	s_mov_b64 s[8:9], 0x5000
	v_addc_co_u32_e32 v35, vcc, 0, v49, vcc
	v_lshl_add_u64 v[50:51], v[48:49], 0, s[8:9]
	s_movk_i32 s8, 0x6000
	v_add_co_u32_e32 v52, vcc, s8, v48
	s_mov_b64 s[8:9], 0x6000
	v_lshl_add_u64 v[54:55], v[48:49], 0, s[8:9]
	s_mov_b64 s[8:9], 0x7000
	v_addc_co_u32_e32 v53, vcc, 0, v49, vcc
	v_lshl_add_u64 v[84:85], v[48:49], 0, s[8:9]
	s_mov_b32 s8, 0x8000
	v_add_co_u32_e32 v86, vcc, s8, v48
	s_mov_b64 s[8:9], 0x8000
	s_nop 0
	v_addc_co_u32_e32 v87, vcc, 0, v49, vcc
	global_load_dwordx4 v[0:3], v[18:19], off offset:-4096
	global_load_dwordx4 v[4:7], v[18:19], off
	global_load_dwordx4 v[8:11], v[16:17], off offset:16
	global_load_dwordx4 v[12:15], v[20:21], off offset:16
	s_nop 0
	global_load_dwordx4 v[16:19], v[34:35], off offset:-4096
	global_load_dwordx4 v[20:23], v[34:35], off
	global_load_dwordx4 v[24:27], v[32:33], off offset:16
	global_load_dwordx4 v[28:31], v[36:37], off offset:16
	s_nop 0
	global_load_dwordx4 v[32:35], v[52:53], off offset:-4096
	global_load_dwordx4 v[36:39], v[52:53], off
	global_load_dwordx4 v[40:43], v[50:51], off offset:16
	global_load_dwordx4 v[44:47], v[54:55], off offset:16
	v_lshl_add_u64 v[88:89], v[48:49], 0, s[8:9]
	global_load_dwordx4 v[48:51], v[86:87], off offset:-4096
	global_load_dwordx4 v[52:55], v[86:87], off
	global_load_dwordx4 v[56:59], v[84:85], off offset:16
	global_load_dwordx4 v[60:63], v[88:89], off offset:16
	global_load_dwordx4 v[64:67], v80, s[4:5] offset:16
	global_load_dwordx4 v[68:71], v80, s[6:7] offset:16
	global_load_dwordx4 v[72:75], v80, s[4:5]
	global_load_dwordx4 v[76:79], v80, s[6:7]
	s_mov_b64 s[4:5], 0x4fb00000
	v_lshl_add_u64 v[84:85], v[82:83], 0, s[4:5]
	s_mov_b64 s[4:5], 0x34e00000
	v_lshl_add_u64 v[86:87], v[82:83], 0, s[4:5]
	s_lshl_b32 s28, s3, 9
	s_mov_b64 s[26:27], 0
	s_movk_i32 s29, 0x3fff
	s_movk_i32 s30, 0x3a00
	s_mov_b32 s31, 0x23ffff
	s_branch .LBB0_537

.LBB0_601:
	s_lshl_b32 s24, s62, 7
	s_lshl_b32 s22, s63, 8
	s_and_b32 s24, s24, 0xffffff00
	s_ashr_i32 s23, s22, 31
	s_ashr_i32 s25, s24, 31
	s_lshl_b64 s[22:23], s[22:23], 11
	s_lshl_b64 s[24:25], s[24:25], 1
	s_add_u32 s22, s36, s22
	s_addc_u32 s23, s37, s23
	s_add_u32 s22, s22, s24
	s_addc_u32 s23, s23, s25
	s_and_b64 s[24:25], s[26:27], exec
	ds_read_b128 v[4:7], v56
	ds_read_b128 v[8:11], v56 offset:1024
	ds_read_b128 v[12:15], v56 offset:2048
	ds_read_b128 v[16:19], v56 offset:3072
	s_cselect_b32 s31, s23, s35
	s_cselect_b32 s30, s22, s34
	s_lshl_b32 s24, s62, 8
	s_ashr_i32 s25, s24, 31
	s_lshl_b64 s[24:25], s[24:25], 9
	s_add_u32 s24, s38, s24
	s_addc_u32 s25, s39, s25
	s_and_b64 s[26:27], s[26:27], exec
	s_cselect_b32 s27, s25, s29
	s_cselect_b32 s26, s24, s28
	v_lshl_add_u64 v[0:1], s[34:35], 0, v[48:49]
	s_mov_b32 m0, s47
	v_lshl_add_u64 v[2:3], v[0:1], 0, s[6:7]
	ds_read_b128 v[20:23], v57
	ds_read_b128 v[24:27], v57 offset:1024
	ds_read_b128 v[28:31], v57 offset:2048
	ds_read_b128 v[32:35], v57 offset:3072
	ds_read_b128 v[36:39], v57 offset:4096
	ds_read_b128 v[62:65], v57 offset:5120
	ds_read_b128 v[66:69], v57 offset:6144
	ds_read_b128 v[70:73], v57 offset:7168
	global_load_lds_dwordx4 v[2:3], off
	v_lshl_add_u64 v[2:3], s[34:35], 0, v[50:51]
	v_lshl_add_u64 v[52:53], v[2:3], 0, s[6:7]
	s_mov_b32 m0, s48
	s_nop 0
	global_load_lds_dwordx4 v[52:53], off
	s_waitcnt lgkmcnt(8)
	s_barrier
	s_waitcnt lgkmcnt(0)
	s_waitcnt lgkmcnt(0)
	v_mfma_f32_16x16x32_bf16 v[74:77], v[4:7], v[20:23], 0
	v_mfma_f32_16x16x32_bf16 v[78:81], v[12:15], v[20:23], 0
	v_mfma_f32_16x16x32_bf16 v[82:85], v[4:7], v[28:31], 0
	v_mfma_f32_16x16x32_bf16 v[86:89], v[12:15], v[28:31], 0
	v_mfma_f32_16x16x32_bf16 v[90:93], v[4:7], v[36:39], 0
	v_mfma_f32_16x16x32_bf16 v[94:97], v[12:15], v[36:39], 0
	v_mfma_f32_16x16x32_bf16 v[98:101], v[4:7], v[66:69], 0
	v_mfma_f32_16x16x32_bf16 v[102:105], v[12:15], v[66:69], 0
	v_mfma_f32_16x16x32_bf16 v[74:77], v[8:11], v[24:27], v[74:77]
	v_mfma_f32_16x16x32_bf16 v[78:81], v[16:19], v[24:27], v[78:81]
	v_mfma_f32_16x16x32_bf16 v[82:85], v[8:11], v[32:35], v[82:85]
	v_mfma_f32_16x16x32_bf16 v[86:89], v[16:19], v[32:35], v[86:89]
	v_mfma_f32_16x16x32_bf16 v[90:93], v[8:11], v[62:65], v[90:93]
	v_mfma_f32_16x16x32_bf16 v[94:97], v[16:19], v[62:65], v[94:97]
	v_mfma_f32_16x16x32_bf16 v[98:101], v[8:11], v[70:73], v[98:101]
	v_mfma_f32_16x16x32_bf16 v[102:105], v[16:19], v[70:73], v[102:105]
	s_barrier
	v_lshl_add_u64 v[52:53], s[28:29], 0, v[42:43]
	s_mov_b32 m0, s49
	v_lshl_add_u64 v[122:123], v[52:53], 0, s[8:9]
	v_lshl_add_u64 v[218:219], s[28:29], 0, v[40:41]
	ds_read_b128 v[106:109], v58
	ds_read_b128 v[110:113], v58 offset:1024
	ds_read_b128 v[114:117], v58 offset:2048
	ds_read_b128 v[118:121], v58 offset:3072
	global_load_lds_dwordx4 v[122:123], off
	v_lshl_add_u64 v[122:123], v[218:219], 0, s[8:9]
	s_mov_b32 m0, s50
	s_nop 0
	global_load_lds_dwordx4 v[122:123], off
	s_barrier
	s_waitcnt lgkmcnt(0)
	s_waitcnt lgkmcnt(0)
	v_mfma_f32_16x16x32_bf16 v[122:125], v[106:109], v[20:23], 0
	v_mfma_f32_16x16x32_bf16 v[20:23], v[114:117], v[20:23], 0
	v_mfma_f32_16x16x32_bf16 v[122:125], v[110:113], v[24:27], v[122:125]
	v_mfma_f32_16x16x32_bf16 v[20:23], v[118:121], v[24:27], v[20:23]
	v_mfma_f32_16x16x32_bf16 v[24:27], v[106:109], v[28:31], 0
	v_mfma_f32_16x16x32_bf16 v[28:31], v[114:117], v[28:31], 0
	v_mfma_f32_16x16x32_bf16 v[24:27], v[110:113], v[32:35], v[24:27]
	v_mfma_f32_16x16x32_bf16 v[28:31], v[118:121], v[32:35], v[28:31]
	v_mfma_f32_16x16x32_bf16 v[32:35], v[106:109], v[36:39], 0
	v_mfma_f32_16x16x32_bf16 v[36:39], v[114:117], v[36:39], 0
	v_mfma_f32_16x16x32_bf16 v[32:35], v[110:113], v[62:65], v[32:35]
	v_mfma_f32_16x16x32_bf16 v[36:39], v[118:121], v[62:65], v[36:39]
	v_mfma_f32_16x16x32_bf16 v[62:65], v[106:109], v[66:69], 0
	v_mfma_f32_16x16x32_bf16 v[66:69], v[114:117], v[66:69], 0
	v_mfma_f32_16x16x32_bf16 v[62:65], v[110:113], v[70:73], v[62:65]
	v_mfma_f32_16x16x32_bf16 v[66:69], v[118:121], v[70:73], v[66:69]
	v_lshl_add_u64 v[220:221], s[34:35], 0, v[44:45]
	s_mov_b32 m0, s41
	v_lshl_add_u64 v[154:155], v[220:221], 0, s[8:9]
	v_lshl_add_u64 v[222:223], s[34:35], 0, v[46:47]
	s_barrier
	ds_read_b128 v[70:73], v57 offset:16384
	ds_read_b128 v[126:129], v57 offset:17408
	ds_read_b128 v[130:133], v57 offset:18432
	ds_read_b128 v[134:137], v57 offset:19456
	ds_read_b128 v[138:141], v57 offset:20480
	ds_read_b128 v[142:145], v57 offset:21504
	ds_read_b128 v[146:149], v57 offset:22528
	ds_read_b128 v[150:153], v57 offset:23552
	global_load_lds_dwordx4 v[154:155], off
	v_lshl_add_u64 v[154:155], v[222:223], 0, s[8:9]
	s_mov_b32 m0, s42
	s_nop 0
	global_load_lds_dwordx4 v[154:155], off
	s_barrier
	s_waitcnt lgkmcnt(0)
	s_waitcnt lgkmcnt(0)
	v_mfma_f32_16x16x32_bf16 v[154:157], v[4:7], v[70:73], 0
	v_mfma_f32_16x16x32_bf16 v[162:165], v[4:7], v[130:133], 0
	v_mfma_f32_16x16x32_bf16 v[170:173], v[4:7], v[138:141], 0
	v_mfma_f32_16x16x32_bf16 v[4:7], v[4:7], v[146:149], 0
	v_mfma_f32_16x16x32_bf16 v[154:157], v[8:11], v[126:129], v[154:157]
	v_mfma_f32_16x16x32_bf16 v[158:161], v[12:15], v[70:73], 0
	v_mfma_f32_16x16x32_bf16 v[162:165], v[8:11], v[134:137], v[162:165]
	v_mfma_f32_16x16x32_bf16 v[166:169], v[12:15], v[130:133], 0
	v_mfma_f32_16x16x32_bf16 v[170:173], v[8:11], v[142:145], v[170:173]
	v_mfma_f32_16x16x32_bf16 v[174:177], v[12:15], v[138:141], 0
	v_mfma_f32_16x16x32_bf16 v[4:7], v[8:11], v[150:153], v[4:7]
	v_mfma_f32_16x16x32_bf16 v[8:11], v[12:15], v[146:149], 0
	v_mfma_f32_16x16x32_bf16 v[158:161], v[16:19], v[126:129], v[158:161]
	v_mfma_f32_16x16x32_bf16 v[166:169], v[16:19], v[134:137], v[166:169]
	v_mfma_f32_16x16x32_bf16 v[174:177], v[16:19], v[142:145], v[174:177]
	v_mfma_f32_16x16x32_bf16 v[8:11], v[16:19], v[150:153], v[8:11]
	s_barrier
	s_add_u32 s34, s28, 0x10100
	s_addc_u32 s35, s29, 0
	s_mov_b32 m0, s51
	v_lshl_add_u64 v[12:13], s[34:35], 0, v[42:43]
	global_load_lds_dwordx4 v[12:13], off
	v_lshl_add_u64 v[12:13], s[34:35], 0, v[40:41]
	s_mov_b32 m0, s52
	s_nop 0
	global_load_lds_dwordx4 v[12:13], off
	s_waitcnt vmcnt(6)
	s_barrier
	v_mfma_f32_16x16x32_bf16 v[12:15], v[106:109], v[70:73], 0
	v_mfma_f32_16x16x32_bf16 v[16:19], v[114:117], v[70:73], 0
	v_mfma_f32_16x16x32_bf16 v[12:15], v[110:113], v[126:129], v[12:15]
	v_mfma_f32_16x16x32_bf16 v[16:19], v[118:121], v[126:129], v[16:19]
	v_mfma_f32_16x16x32_bf16 v[70:73], v[106:109], v[130:133], 0
	v_mfma_f32_16x16x32_bf16 v[126:129], v[114:117], v[130:133], 0
	v_mfma_f32_16x16x32_bf16 v[130:133], v[106:109], v[138:141], 0
	v_mfma_f32_16x16x32_bf16 v[106:109], v[106:109], v[146:149], 0
	v_mfma_f32_16x16x32_bf16 v[70:73], v[110:113], v[134:137], v[70:73]
	v_mfma_f32_16x16x32_bf16 v[126:129], v[118:121], v[134:137], v[126:129]
	v_mfma_f32_16x16x32_bf16 v[130:133], v[110:113], v[142:145], v[130:133]
	v_mfma_f32_16x16x32_bf16 v[134:137], v[114:117], v[138:141], 0
	v_mfma_f32_16x16x32_bf16 v[106:109], v[110:113], v[150:153], v[106:109]
	v_mfma_f32_16x16x32_bf16 v[110:113], v[114:117], v[146:149], 0
	v_mfma_f32_16x16x32_bf16 v[134:137], v[118:121], v[142:145], v[134:137]
	v_mfma_f32_16x16x32_bf16 v[110:113], v[118:121], v[150:153], v[110:113]
	s_barrier
	ds_read_b128 v[114:117], v59
	ds_read_b128 v[118:121], v59 offset:1024
	ds_read_b128 v[138:141], v59 offset:2048
	ds_read_b128 v[142:145], v59 offset:3072
	s_mov_b32 m0, s43
	v_lshl_add_u64 v[202:203], v[0:1], 0, s[8:9]
	ds_read_b128 v[146:149], v57 offset:32768
	ds_read_b128 v[150:153], v57 offset:33792
	ds_read_b128 v[178:181], v57 offset:34816
	ds_read_b128 v[182:185], v57 offset:35840
	ds_read_b128 v[186:189], v57 offset:36864
	ds_read_b128 v[190:193], v57 offset:37888
	ds_read_b128 v[194:197], v57 offset:38912
	ds_read_b128 v[198:201], v57 offset:39936
	global_load_lds_dwordx4 v[202:203], off
	v_lshl_add_u64 v[202:203], v[2:3], 0, s[8:9]
	s_mov_b32 m0, s44
	s_nop 0
	global_load_lds_dwordx4 v[202:203], off
	s_waitcnt lgkmcnt(8)
	s_barrier
	s_waitcnt lgkmcnt(0)
	s_waitcnt lgkmcnt(0)
	v_mfma_f32_16x16x32_bf16 v[74:77], v[114:117], v[146:149], v[74:77]
	v_mfma_f32_16x16x32_bf16 v[78:81], v[138:141], v[146:149], v[78:81]
	v_mfma_f32_16x16x32_bf16 v[82:85], v[114:117], v[178:181], v[82:85]
	v_mfma_f32_16x16x32_bf16 v[86:89], v[138:141], v[178:181], v[86:89]
	v_mfma_f32_16x16x32_bf16 v[90:93], v[114:117], v[186:189], v[90:93]
	v_mfma_f32_16x16x32_bf16 v[94:97], v[138:141], v[186:189], v[94:97]
	v_mfma_f32_16x16x32_bf16 v[98:101], v[114:117], v[194:197], v[98:101]
	v_mfma_f32_16x16x32_bf16 v[102:105], v[138:141], v[194:197], v[102:105]
	v_mfma_f32_16x16x32_bf16 v[74:77], v[118:121], v[150:153], v[74:77]
	v_mfma_f32_16x16x32_bf16 v[78:81], v[142:145], v[150:153], v[78:81]
	v_mfma_f32_16x16x32_bf16 v[82:85], v[118:121], v[182:185], v[82:85]
	v_mfma_f32_16x16x32_bf16 v[86:89], v[142:145], v[182:185], v[86:89]
	v_mfma_f32_16x16x32_bf16 v[90:93], v[118:121], v[190:193], v[90:93]
	v_mfma_f32_16x16x32_bf16 v[94:97], v[142:145], v[190:193], v[94:97]
	v_mfma_f32_16x16x32_bf16 v[98:101], v[118:121], v[198:201], v[98:101]
	v_mfma_f32_16x16x32_bf16 v[102:105], v[142:145], v[198:201], v[102:105]
	s_barrier
	s_mov_b32 m0, s57
	v_lshl_add_u64 v[52:53], v[52:53], 0, s[10:11]
	ds_read_b128 v[202:205], v60
	ds_read_b128 v[206:209], v60 offset:1024
	ds_read_b128 v[210:213], v60 offset:2048
	ds_read_b128 v[214:217], v60 offset:3072
	global_load_lds_dwordx4 v[52:53], off
	v_lshl_add_u64 v[52:53], v[218:219], 0, s[10:11]
	s_mov_b32 m0, s58
	s_nop 0
	global_load_lds_dwordx4 v[52:53], off
	s_barrier
	s_waitcnt lgkmcnt(0)
	s_waitcnt lgkmcnt(0)
	v_mfma_f32_16x16x32_bf16 v[122:125], v[202:205], v[146:149], v[122:125]
	v_mfma_f32_16x16x32_bf16 v[20:23], v[210:213], v[146:149], v[20:23]
	v_mfma_f32_16x16x32_bf16 v[24:27], v[202:205], v[178:181], v[24:27]
	v_mfma_f32_16x16x32_bf16 v[28:31], v[210:213], v[178:181], v[28:31]
	v_mfma_f32_16x16x32_bf16 v[32:35], v[202:205], v[186:189], v[32:35]
	v_mfma_f32_16x16x32_bf16 v[36:39], v[210:213], v[186:189], v[36:39]
	v_mfma_f32_16x16x32_bf16 v[62:65], v[202:205], v[194:197], v[62:65]
	v_mfma_f32_16x16x32_bf16 v[66:69], v[210:213], v[194:197], v[66:69]
	v_mfma_f32_16x16x32_bf16 v[122:125], v[206:209], v[150:153], v[122:125]
	v_mfma_f32_16x16x32_bf16 v[20:23], v[214:217], v[150:153], v[20:23]
	v_mfma_f32_16x16x32_bf16 v[24:27], v[206:209], v[182:185], v[24:27]
	v_mfma_f32_16x16x32_bf16 v[28:31], v[214:217], v[182:185], v[28:31]
	v_mfma_f32_16x16x32_bf16 v[32:35], v[206:209], v[190:193], v[32:35]
	v_mfma_f32_16x16x32_bf16 v[36:39], v[214:217], v[190:193], v[36:39]
	v_mfma_f32_16x16x32_bf16 v[62:65], v[206:209], v[198:201], v[62:65]
	v_mfma_f32_16x16x32_bf16 v[66:69], v[214:217], v[198:201], v[66:69]
	s_mov_b32 m0, s45
	v_lshl_add_u64 v[52:53], v[220:221], 0, s[10:11]
	s_barrier
	ds_read_b128 v[146:149], v57 offset:49152
	ds_read_b128 v[150:153], v57 offset:50176
	ds_read_b128 v[178:181], v57 offset:51200
	ds_read_b128 v[182:185], v57 offset:52224
	ds_read_b128 v[186:189], v57 offset:53248
	ds_read_b128 v[190:193], v57 offset:54272
	ds_read_b128 v[194:197], v57 offset:55296
	ds_read_b128 v[198:201], v57 offset:56320
	global_load_lds_dwordx4 v[52:53], off
	v_lshl_add_u64 v[52:53], v[222:223], 0, s[10:11]
	s_mov_b32 m0, s46
	s_nop 0
	global_load_lds_dwordx4 v[52:53], off
	s_barrier
	s_waitcnt lgkmcnt(0)
	s_waitcnt lgkmcnt(0)
	v_mfma_f32_16x16x32_bf16 v[154:157], v[114:117], v[146:149], v[154:157]
	v_mfma_f32_16x16x32_bf16 v[158:161], v[138:141], v[146:149], v[158:161]
	v_mfma_f32_16x16x32_bf16 v[162:165], v[114:117], v[178:181], v[162:165]
	v_mfma_f32_16x16x32_bf16 v[166:169], v[138:141], v[178:181], v[166:169]
	v_mfma_f32_16x16x32_bf16 v[170:173], v[114:117], v[186:189], v[170:173]
	v_mfma_f32_16x16x32_bf16 v[174:177], v[138:141], v[186:189], v[174:177]
	v_mfma_f32_16x16x32_bf16 v[4:7], v[114:117], v[194:197], v[4:7]
	v_mfma_f32_16x16x32_bf16 v[8:11], v[138:141], v[194:197], v[8:11]
	v_mfma_f32_16x16x32_bf16 v[154:157], v[118:121], v[150:153], v[154:157]
	v_mfma_f32_16x16x32_bf16 v[158:161], v[142:145], v[150:153], v[158:161]
	v_mfma_f32_16x16x32_bf16 v[162:165], v[118:121], v[182:185], v[162:165]
	v_mfma_f32_16x16x32_bf16 v[166:169], v[142:145], v[182:185], v[166:169]
	v_mfma_f32_16x16x32_bf16 v[170:173], v[118:121], v[190:193], v[170:173]
	v_mfma_f32_16x16x32_bf16 v[174:177], v[142:145], v[190:193], v[174:177]
	v_mfma_f32_16x16x32_bf16 v[4:7], v[118:121], v[198:201], v[4:7]
	v_mfma_f32_16x16x32_bf16 v[8:11], v[142:145], v[198:201], v[8:11]
	s_barrier
	s_add_u32 s28, s28, 0x10180
	s_addc_u32 s29, s29, 0
	s_mov_b32 m0, s59
	v_lshl_add_u64 v[52:53], s[28:29], 0, v[42:43]
	global_load_lds_dwordx4 v[52:53], off
	v_lshl_add_u64 v[52:53], s[28:29], 0, v[40:41]
	s_mov_b32 m0, s60
	s_nop 0
	global_load_lds_dwordx4 v[52:53], off
	s_waitcnt vmcnt(6)
	s_barrier
	v_mfma_f32_16x16x32_bf16 v[12:15], v[202:205], v[146:149], v[12:15]
	v_mfma_f32_16x16x32_bf16 v[16:19], v[210:213], v[146:149], v[16:19]
	v_mfma_f32_16x16x32_bf16 v[70:73], v[202:205], v[178:181], v[70:73]
	v_mfma_f32_16x16x32_bf16 v[114:117], v[210:213], v[178:181], v[126:129]
	v_mfma_f32_16x16x32_bf16 v[118:121], v[202:205], v[186:189], v[130:133]
	v_mfma_f32_16x16x32_bf16 v[126:129], v[210:213], v[186:189], v[134:137]
	v_mfma_f32_16x16x32_bf16 v[106:109], v[202:205], v[194:197], v[106:109]
	v_mfma_f32_16x16x32_bf16 v[110:113], v[210:213], v[194:197], v[110:113]
	v_mfma_f32_16x16x32_bf16 v[12:15], v[206:209], v[150:153], v[12:15]
	v_mfma_f32_16x16x32_bf16 v[16:19], v[214:217], v[150:153], v[16:19]
	v_mfma_f32_16x16x32_bf16 v[70:73], v[206:209], v[182:185], v[70:73]
	v_mfma_f32_16x16x32_bf16 v[114:117], v[214:217], v[182:185], v[114:117]
	v_mfma_f32_16x16x32_bf16 v[118:121], v[206:209], v[190:193], v[118:121]
	v_mfma_f32_16x16x32_bf16 v[126:129], v[214:217], v[190:193], v[126:129]
	v_mfma_f32_16x16x32_bf16 v[106:109], v[206:209], v[198:201], v[106:109]
	v_mfma_f32_16x16x32_bf16 v[110:113], v[214:217], v[198:201], v[110:113]
	s_barrier
	ds_read_b128 v[130:133], v56
	ds_read_b128 v[134:137], v56 offset:1024
	ds_read_b128 v[138:141], v56 offset:2048
	ds_read_b128 v[142:145], v56 offset:3072
	s_mov_b32 m0, s47
	v_lshl_add_u64 v[0:1], v[0:1], 0, s[10:11]
	ds_read_b128 v[146:149], v57
	ds_read_b128 v[150:153], v57 offset:1024
	ds_read_b128 v[178:181], v57 offset:2048
	ds_read_b128 v[182:185], v57 offset:3072
	ds_read_b128 v[186:189], v57 offset:4096
	ds_read_b128 v[190:193], v57 offset:5120
	ds_read_b128 v[194:197], v57 offset:6144
	ds_read_b128 v[198:201], v57 offset:7168
	global_load_lds_dwordx4 v[0:1], off
	v_lshl_add_u64 v[0:1], v[2:3], 0, s[10:11]
	s_mov_b32 m0, s48
	s_nop 0
	global_load_lds_dwordx4 v[0:1], off
	s_waitcnt lgkmcnt(8)
	s_barrier
	s_waitcnt lgkmcnt(0)
	s_waitcnt lgkmcnt(0)
	v_mfma_f32_16x16x32_bf16 v[0:3], v[130:133], v[146:149], v[74:77]
	v_mfma_f32_16x16x32_bf16 v[74:77], v[138:141], v[146:149], v[78:81]
	v_mfma_f32_16x16x32_bf16 v[78:81], v[130:133], v[178:181], v[82:85]
	v_mfma_f32_16x16x32_bf16 v[82:85], v[138:141], v[178:181], v[86:89]
	v_mfma_f32_16x16x32_bf16 v[86:89], v[130:133], v[186:189], v[90:93]
	v_mfma_f32_16x16x32_bf16 v[90:93], v[138:141], v[186:189], v[94:97]
	v_mfma_f32_16x16x32_bf16 v[94:97], v[130:133], v[194:197], v[98:101]
	v_mfma_f32_16x16x32_bf16 v[98:101], v[138:141], v[194:197], v[102:105]
	v_mfma_f32_16x16x32_bf16 v[0:3], v[134:137], v[150:153], v[0:3]
	v_mfma_f32_16x16x32_bf16 v[74:77], v[142:145], v[150:153], v[74:77]
	v_mfma_f32_16x16x32_bf16 v[78:81], v[134:137], v[182:185], v[78:81]
	v_mfma_f32_16x16x32_bf16 v[82:85], v[142:145], v[182:185], v[82:85]
	v_mfma_f32_16x16x32_bf16 v[86:89], v[134:137], v[190:193], v[86:89]
	v_mfma_f32_16x16x32_bf16 v[90:93], v[142:145], v[190:193], v[90:93]
	v_mfma_f32_16x16x32_bf16 v[94:97], v[134:137], v[198:201], v[94:97]
	v_mfma_f32_16x16x32_bf16 v[98:101], v[142:145], v[198:201], v[98:101]
	s_barrier
	s_mov_b32 m0, s49
	v_lshl_add_u64 v[52:53], s[26:27], 0, v[42:43]
	ds_read_b128 v[102:105], v58
	ds_read_b128 v[202:205], v58 offset:1024
	ds_read_b128 v[206:209], v58 offset:2048
	ds_read_b128 v[210:213], v58 offset:3072
	global_load_lds_dwordx4 v[52:53], off
	v_lshl_add_u64 v[218:219], s[26:27], 0, v[40:41]
	s_mov_b32 m0, s50
	s_nop 0
	global_load_lds_dwordx4 v[218:219], off
	s_barrier
	s_waitcnt lgkmcnt(0)
	s_waitcnt lgkmcnt(0)
	v_mfma_f32_16x16x32_bf16 v[122:125], v[102:105], v[146:149], v[122:125]
	v_mfma_f32_16x16x32_bf16 v[20:23], v[206:209], v[146:149], v[20:23]
	v_mfma_f32_16x16x32_bf16 v[24:27], v[102:105], v[178:181], v[24:27]
	v_mfma_f32_16x16x32_bf16 v[28:31], v[206:209], v[178:181], v[28:31]
	v_mfma_f32_16x16x32_bf16 v[32:35], v[102:105], v[186:189], v[32:35]
	v_mfma_f32_16x16x32_bf16 v[36:39], v[206:209], v[186:189], v[36:39]
	v_mfma_f32_16x16x32_bf16 v[62:65], v[102:105], v[194:197], v[62:65]
	v_mfma_f32_16x16x32_bf16 v[66:69], v[206:209], v[194:197], v[66:69]
	v_mfma_f32_16x16x32_bf16 v[122:125], v[202:205], v[150:153], v[122:125]
	v_mfma_f32_16x16x32_bf16 v[20:23], v[210:213], v[150:153], v[20:23]
	v_mfma_f32_16x16x32_bf16 v[24:27], v[202:205], v[182:185], v[24:27]
	v_mfma_f32_16x16x32_bf16 v[28:31], v[210:213], v[182:185], v[28:31]
	v_mfma_f32_16x16x32_bf16 v[32:35], v[202:205], v[190:193], v[32:35]
	v_mfma_f32_16x16x32_bf16 v[36:39], v[210:213], v[190:193], v[36:39]
	v_mfma_f32_16x16x32_bf16 v[62:65], v[202:205], v[198:201], v[62:65]
	v_mfma_f32_16x16x32_bf16 v[66:69], v[210:213], v[198:201], v[66:69]
	s_mov_b32 m0, s41
	v_lshl_add_u64 v[234:235], s[30:31], 0, v[44:45]
	s_barrier
	ds_read_b128 v[146:149], v57 offset:16384
	ds_read_b128 v[150:153], v57 offset:17408
	ds_read_b128 v[178:181], v57 offset:18432
	ds_read_b128 v[182:185], v57 offset:19456
	ds_read_b128 v[186:189], v57 offset:20480
	ds_read_b128 v[190:193], v57 offset:21504
	ds_read_b128 v[194:197], v57 offset:22528
	ds_read_b128 v[198:201], v57 offset:23552
	global_load_lds_dwordx4 v[234:235], off
	v_lshl_add_u64 v[236:237], s[30:31], 0, v[46:47]
	s_mov_b32 m0, s42
	s_nop 0
	global_load_lds_dwordx4 v[236:237], off
	s_barrier
	s_waitcnt lgkmcnt(0)
	s_waitcnt lgkmcnt(0)
	v_mfma_f32_16x16x32_bf16 v[154:157], v[130:133], v[146:149], v[154:157]
	v_mfma_f32_16x16x32_bf16 v[158:161], v[138:141], v[146:149], v[158:161]
	v_mfma_f32_16x16x32_bf16 v[162:165], v[130:133], v[178:181], v[162:165]
	v_mfma_f32_16x16x32_bf16 v[166:169], v[138:141], v[178:181], v[166:169]
	v_mfma_f32_16x16x32_bf16 v[170:173], v[130:133], v[186:189], v[170:173]
	v_mfma_f32_16x16x32_bf16 v[174:177], v[138:141], v[186:189], v[174:177]
	v_mfma_f32_16x16x32_bf16 v[4:7], v[130:133], v[194:197], v[4:7]
	v_mfma_f32_16x16x32_bf16 v[8:11], v[138:141], v[194:197], v[8:11]
	v_mfma_f32_16x16x32_bf16 v[154:157], v[134:137], v[150:153], v[154:157]
	v_mfma_f32_16x16x32_bf16 v[158:161], v[142:145], v[150:153], v[158:161]
	v_mfma_f32_16x16x32_bf16 v[162:165], v[134:137], v[182:185], v[162:165]
	v_mfma_f32_16x16x32_bf16 v[166:169], v[142:145], v[182:185], v[166:169]
	v_mfma_f32_16x16x32_bf16 v[170:173], v[134:137], v[190:193], v[170:173]
	v_mfma_f32_16x16x32_bf16 v[174:177], v[142:145], v[190:193], v[174:177]
	v_mfma_f32_16x16x32_bf16 v[4:7], v[134:137], v[198:201], v[4:7]
	v_mfma_f32_16x16x32_bf16 v[8:11], v[142:145], v[198:201], v[8:11]
	s_barrier
	s_add_u32 s28, s26, 0x10000
	s_addc_u32 s29, s27, 0
	s_mov_b32 m0, s51
	v_lshl_add_u64 v[130:131], s[28:29], 0, v[42:43]
	global_load_lds_dwordx4 v[130:131], off
	v_lshl_add_u64 v[130:131], s[28:29], 0, v[40:41]
	s_mov_b32 m0, s52
	s_nop 0
	global_load_lds_dwordx4 v[130:131], off
	s_waitcnt vmcnt(6)
	s_barrier
	v_mfma_f32_16x16x32_bf16 v[16:19], v[206:209], v[146:149], v[16:19]
	v_mfma_f32_16x16x32_bf16 v[130:133], v[210:213], v[150:153], v[16:19]
	v_mfma_f32_16x16x32_bf16 v[16:19], v[102:105], v[178:181], v[70:73]
	v_mfma_f32_16x16x32_bf16 v[70:73], v[202:205], v[182:185], v[16:19]
	v_mfma_f32_16x16x32_bf16 v[16:19], v[206:209], v[178:181], v[114:117]
	v_mfma_f32_16x16x32_bf16 v[114:117], v[210:213], v[182:185], v[16:19]
	v_mfma_f32_16x16x32_bf16 v[16:19], v[102:105], v[186:189], v[118:121]
	v_mfma_f32_16x16x32_bf16 v[118:121], v[202:205], v[190:193], v[16:19]
	v_mfma_f32_16x16x32_bf16 v[16:19], v[206:209], v[186:189], v[126:129]
	v_mfma_f32_16x16x32_bf16 v[126:129], v[210:213], v[190:193], v[16:19]
	v_mfma_f32_16x16x32_bf16 v[16:19], v[102:105], v[194:197], v[106:109]
	v_mfma_f32_16x16x32_bf16 v[12:15], v[102:105], v[146:149], v[12:15]
	v_mfma_f32_16x16x32_bf16 v[102:105], v[202:205], v[198:201], v[16:19]
	v_mfma_f32_16x16x32_bf16 v[16:19], v[206:209], v[194:197], v[110:113]
	v_mfma_f32_16x16x32_bf16 v[12:15], v[202:205], v[150:153], v[12:15]
	v_mfma_f32_16x16x32_bf16 v[106:109], v[210:213], v[198:201], v[16:19]
	s_barrier
	ds_read_b128 v[110:113], v59
	ds_read_b128 v[134:137], v59 offset:1024
	ds_read_b128 v[138:141], v59 offset:2048
	ds_read_b128 v[142:145], v59 offset:3072
	s_mov_b32 m0, s43
	v_lshl_add_u64 v[198:199], s[30:31], 0, v[48:49]
	ds_read_b128 v[16:19], v57 offset:32768
	ds_read_b128 v[146:149], v57 offset:33792
	ds_read_b128 v[150:153], v57 offset:34816
	ds_read_b128 v[178:181], v57 offset:35840
	ds_read_b128 v[182:185], v57 offset:36864
	ds_read_b128 v[186:189], v57 offset:37888
	ds_read_b128 v[190:193], v57 offset:38912
	ds_read_b128 v[194:197], v57 offset:39936
	global_load_lds_dwordx4 v[198:199], off
	v_lshl_add_u64 v[198:199], s[30:31], 0, v[50:51]
	s_mov_b32 m0, s44
	s_nop 0
	global_load_lds_dwordx4 v[198:199], off
	s_waitcnt lgkmcnt(8)
	s_barrier
	s_waitcnt lgkmcnt(0)
	s_waitcnt lgkmcnt(0)
	v_mfma_f32_16x16x32_bf16 v[0:3], v[110:113], v[16:19], v[0:3]
	v_mfma_f32_16x16x32_bf16 v[198:201], v[134:137], v[146:149], v[0:3]
	v_mfma_f32_16x16x32_bf16 v[0:3], v[138:141], v[16:19], v[74:77]
	v_mfma_f32_16x16x32_bf16 v[74:77], v[142:145], v[146:149], v[0:3]
	v_mfma_f32_16x16x32_bf16 v[0:3], v[110:113], v[150:153], v[78:81]
	v_mfma_f32_16x16x32_bf16 v[78:81], v[134:137], v[178:181], v[0:3]
	v_mfma_f32_16x16x32_bf16 v[0:3], v[138:141], v[150:153], v[82:85]
	v_mfma_f32_16x16x32_bf16 v[82:85], v[142:145], v[178:181], v[0:3]
	v_mfma_f32_16x16x32_bf16 v[0:3], v[110:113], v[182:185], v[86:89]
	v_mfma_f32_16x16x32_bf16 v[86:89], v[134:137], v[186:189], v[0:3]
	v_mfma_f32_16x16x32_bf16 v[0:3], v[138:141], v[182:185], v[90:93]
	v_mfma_f32_16x16x32_bf16 v[90:93], v[142:145], v[186:189], v[0:3]
	v_mfma_f32_16x16x32_bf16 v[0:3], v[110:113], v[190:193], v[94:97]
	v_mfma_f32_16x16x32_bf16 v[94:97], v[134:137], v[194:197], v[0:3]
	v_mfma_f32_16x16x32_bf16 v[0:3], v[138:141], v[190:193], v[98:101]
	v_mfma_f32_16x16x32_bf16 v[98:101], v[142:145], v[194:197], v[0:3]
	s_barrier
	s_mov_b32 m0, s57
	s_nop 3
	v_lshl_add_u64 v[0:1], v[52:53], 0, s[6:7]
	ds_read_b128 v[202:205], v60
	ds_read_b128 v[206:209], v60 offset:1024
	ds_read_b128 v[210:213], v60 offset:2048
	ds_read_b128 v[214:217], v60 offset:3072
	global_load_lds_dwordx4 v[0:1], off
	v_lshl_add_u64 v[0:1], v[218:219], 0, s[6:7]
	s_mov_b32 m0, s58
	s_nop 0
	global_load_lds_dwordx4 v[0:1], off
	s_barrier
	s_waitcnt lgkmcnt(0)
	s_waitcnt lgkmcnt(0)
	v_mfma_f32_16x16x32_bf16 v[0:3], v[202:205], v[16:19], v[122:125]
	v_mfma_f32_16x16x32_bf16 v[122:125], v[206:209], v[146:149], v[0:3]
	v_mfma_f32_16x16x32_bf16 v[0:3], v[210:213], v[16:19], v[20:23]
	v_mfma_f32_16x16x32_bf16 v[146:149], v[214:217], v[146:149], v[0:3]
	v_mfma_f32_16x16x32_bf16 v[0:3], v[202:205], v[150:153], v[24:27]
	v_mfma_f32_16x16x32_bf16 v[218:221], v[206:209], v[178:181], v[0:3]
	v_mfma_f32_16x16x32_bf16 v[0:3], v[210:213], v[150:153], v[28:31]
	v_mfma_f32_16x16x32_bf16 v[150:153], v[214:217], v[178:181], v[0:3]
	v_mfma_f32_16x16x32_bf16 v[0:3], v[202:205], v[182:185], v[32:35]
	v_mfma_f32_16x16x32_bf16 v[178:181], v[206:209], v[186:189], v[0:3]
	v_mfma_f32_16x16x32_bf16 v[0:3], v[210:213], v[182:185], v[36:39]
	v_mfma_f32_16x16x32_bf16 v[182:185], v[214:217], v[186:189], v[0:3]
	v_mfma_f32_16x16x32_bf16 v[0:3], v[202:205], v[190:193], v[62:65]
	v_mfma_f32_16x16x32_bf16 v[62:65], v[206:209], v[194:197], v[0:3]
	v_mfma_f32_16x16x32_bf16 v[0:3], v[210:213], v[190:193], v[66:69]
	v_mfma_f32_16x16x32_bf16 v[66:69], v[214:217], v[194:197], v[0:3]
	s_mov_b32 m0, s45
	s_nop 4
	v_lshl_add_u64 v[0:1], v[234:235], 0, s[6:7]
	s_barrier
	ds_read_b128 v[24:27], v57 offset:49152
	ds_read_b128 v[28:31], v57 offset:50176
	ds_read_b128 v[186:189], v57 offset:51200
	ds_read_b128 v[190:193], v57 offset:52224
	ds_read_b128 v[194:197], v57 offset:53248
	ds_read_b128 v[222:225], v57 offset:54272
	ds_read_b128 v[226:229], v57 offset:55296
	ds_read_b128 v[230:233], v57 offset:56320
	global_load_lds_dwordx4 v[0:1], off
	v_lshl_add_u64 v[0:1], v[236:237], 0, s[6:7]
	s_mov_b32 m0, s46
	s_nop 0
	global_load_lds_dwordx4 v[0:1], off
	s_barrier
	s_waitcnt lgkmcnt(0)
	s_waitcnt lgkmcnt(0)
	v_mfma_f32_16x16x32_bf16 v[0:3], v[110:113], v[24:27], v[154:157]
	v_mfma_f32_16x16x32_bf16 v[154:157], v[134:137], v[28:31], v[0:3]
	v_mfma_f32_16x16x32_bf16 v[0:3], v[138:141], v[24:27], v[158:161]
	v_mfma_f32_16x16x32_bf16 v[158:161], v[142:145], v[28:31], v[0:3]
	v_mfma_f32_16x16x32_bf16 v[0:3], v[110:113], v[186:189], v[162:165]
	v_mfma_f32_16x16x32_bf16 v[36:39], v[134:137], v[190:193], v[0:3]
	v_mfma_f32_16x16x32_bf16 v[0:3], v[138:141], v[186:189], v[166:169]
	v_mfma_f32_16x16x32_bf16 v[32:35], v[142:145], v[190:193], v[0:3]
	v_mfma_f32_16x16x32_bf16 v[0:3], v[110:113], v[194:197], v[170:173]
	v_mfma_f32_16x16x32_bf16 v[20:23], v[134:137], v[222:225], v[0:3]
	v_mfma_f32_16x16x32_bf16 v[0:3], v[138:141], v[194:197], v[174:177]
	v_mfma_f32_16x16x32_bf16 v[16:19], v[142:145], v[222:225], v[0:3]
	v_mfma_f32_16x16x32_bf16 v[0:3], v[110:113], v[226:229], v[4:7]
	v_mfma_f32_16x16x32_bf16 v[4:7], v[134:137], v[230:233], v[0:3]
	v_mfma_f32_16x16x32_bf16 v[0:3], v[138:141], v[226:229], v[8:11]
	v_mfma_f32_16x16x32_bf16 v[0:3], v[142:145], v[230:233], v[0:3]
	s_barrier
	s_add_u32 s26, s26, 0x10080
	s_addc_u32 s27, s27, 0
	s_mov_b32 m0, s59
	v_lshl_add_u64 v[8:9], s[26:27], 0, v[42:43]
	global_load_lds_dwordx4 v[8:9], off
	v_lshl_add_u64 v[8:9], s[26:27], 0, v[40:41]
	s_mov_b32 m0, s60
	s_nop 0
	global_load_lds_dwordx4 v[8:9], off
	s_waitcnt vmcnt(6)
	s_barrier
	v_mfma_f32_16x16x32_bf16 v[8:11], v[202:205], v[24:27], v[12:15]
	v_mfma_f32_16x16x32_bf16 v[110:113], v[206:209], v[28:31], v[8:11]
	v_mfma_f32_16x16x32_bf16 v[8:11], v[210:213], v[24:27], v[130:133]
	v_mfma_f32_16x16x32_bf16 v[130:133], v[214:217], v[28:31], v[8:11]
	v_mfma_f32_16x16x32_bf16 v[8:11], v[202:205], v[186:189], v[70:73]
	v_mfma_f32_16x16x32_bf16 v[70:73], v[206:209], v[190:193], v[8:11]
	v_mfma_f32_16x16x32_bf16 v[8:11], v[210:213], v[186:189], v[114:117]
	v_mfma_f32_16x16x32_bf16 v[114:117], v[214:217], v[190:193], v[8:11]
	v_mfma_f32_16x16x32_bf16 v[8:11], v[202:205], v[194:197], v[118:121]
	v_mfma_f32_16x16x32_bf16 v[28:31], v[206:209], v[222:225], v[8:11]
	v_mfma_f32_16x16x32_bf16 v[8:11], v[210:213], v[194:197], v[126:129]
	v_mfma_f32_16x16x32_bf16 v[24:27], v[214:217], v[222:225], v[8:11]
	v_mfma_f32_16x16x32_bf16 v[8:11], v[202:205], v[226:229], v[102:105]
	v_mfma_f32_16x16x32_bf16 v[12:15], v[206:209], v[230:233], v[8:11]
	v_mfma_f32_16x16x32_bf16 v[8:11], v[210:213], v[226:229], v[106:109]
	v_mfma_f32_16x16x32_bf16 v[8:11], v[214:217], v[230:233], v[8:11]
	s_nop 0
	v_lshl_add_u32 v106, s65, 8, v54
	v_lshl_or_b32 v52, s64, 8, v55
	v_ashrrev_i32_e32 v107, 31, v106
	v_ashrrev_i32_e32 v53, 31, v52
	v_lshlrev_b64 v[102:103], 12, v[106:107]
	v_lshl_add_u64 v[102:103], s[4:5], 0, v[102:103]
	v_lshlrev_b64 v[108:109], 1, v[52:53]
	v_lshl_add_u64 v[52:53], v[102:103], 0, v[108:109]
	s_barrier
	v_cvt_pk_bf16_f32 v102, v198, v199
	v_cvt_pk_bf16_f32 v103, v200, v201
	v_cvt_pk_bf16_f32 v104, v74, v75
	v_cvt_pk_bf16_f32 v105, v76, v77
	global_store_dwordx4 v[52:53], v[102:105], off
	v_cvt_pk_bf16_f32 v74, v122, v123
	v_cvt_pk_bf16_f32 v75, v124, v125
	v_cvt_pk_bf16_f32 v76, v146, v147
	v_cvt_pk_bf16_f32 v77, v148, v149
	global_store_dwordx4 v[52:53], v[74:77], off offset:256
	s_mov_b32 s64, s62
	s_mov_b32 s65, s63
	v_or_b32_e32 v74, 16, v106
	v_ashrrev_i32_e32 v75, 31, v74
	v_lshlrev_b64 v[74:75], 12, v[74:75]
	v_lshl_add_u64 v[74:75], s[4:5], 0, v[74:75]
	v_lshl_add_u64 v[102:103], v[74:75], 0, v[108:109]
	v_cvt_pk_bf16_f32 v74, v78, v79
	v_cvt_pk_bf16_f32 v75, v80, v81
	v_cvt_pk_bf16_f32 v76, v82, v83
	v_cvt_pk_bf16_f32 v77, v84, v85
	global_store_dwordx4 v[102:103], v[74:77], off
	s_mov_b64 s[28:29], s[24:25]
	s_mov_b64 s[34:35], s[22:23]
	v_cvt_pk_bf16_f32 v74, v218, v219
	v_cvt_pk_bf16_f32 v75, v220, v221
	v_cvt_pk_bf16_f32 v76, v150, v151
	v_cvt_pk_bf16_f32 v77, v152, v153
	global_store_dwordx4 v[102:103], v[74:77], off offset:256
	s_nop 1
	v_or_b32_e32 v74, 32, v106
	v_ashrrev_i32_e32 v75, 31, v74
	v_lshlrev_b64 v[74:75], 12, v[74:75]
	v_lshl_add_u64 v[74:75], s[4:5], 0, v[74:75]
	v_lshl_add_u64 v[78:79], v[74:75], 0, v[108:109]
	v_cvt_pk_bf16_f32 v74, v86, v87
	v_cvt_pk_bf16_f32 v75, v88, v89
	v_cvt_pk_bf16_f32 v76, v90, v91
	v_cvt_pk_bf16_f32 v77, v92, v93
	global_store_dwordx4 v[78:79], v[74:77], off
	s_nop 1
	v_cvt_pk_bf16_f32 v74, v178, v179
	v_cvt_pk_bf16_f32 v75, v180, v181
	v_cvt_pk_bf16_f32 v76, v182, v183
	v_cvt_pk_bf16_f32 v77, v184, v185
	global_store_dwordx4 v[78:79], v[74:77], off offset:256
	s_nop 1
	v_or_b32_e32 v74, 48, v106
	v_ashrrev_i32_e32 v75, 31, v74
	v_lshlrev_b64 v[74:75], 12, v[74:75]
	v_lshl_add_u64 v[74:75], s[4:5], 0, v[74:75]
	v_lshl_add_u64 v[78:79], v[74:75], 0, v[108:109]
	v_cvt_pk_bf16_f32 v74, v94, v95
	v_cvt_pk_bf16_f32 v75, v96, v97
	v_cvt_pk_bf16_f32 v76, v98, v99
	v_cvt_pk_bf16_f32 v77, v100, v101
	global_store_dwordx4 v[78:79], v[74:77], off
	v_cvt_pk_bf16_f32 v62, v62, v63
	v_cvt_pk_bf16_f32 v63, v64, v65
	v_cvt_pk_bf16_f32 v64, v66, v67
	v_cvt_pk_bf16_f32 v65, v68, v69
	v_add_co_u32_e32 v68, vcc, s53, v52
	global_store_dwordx4 v[78:79], v[62:65], off offset:256
	v_lshl_add_u64 v[66:67], v[52:53], 0, s[12:13]
	v_addc_co_u32_e32 v69, vcc, 0, v53, vcc
	v_cvt_pk_bf16_f32 v62, v154, v155
	v_cvt_pk_bf16_f32 v63, v156, v157
	v_cvt_pk_bf16_f32 v64, v158, v159
	v_cvt_pk_bf16_f32 v65, v160, v161
	global_store_dwordx4 v[68:69], v[62:65], off
	s_nop 1
	v_cvt_pk_bf16_f32 v62, v110, v111
	v_cvt_pk_bf16_f32 v63, v112, v113
	v_cvt_pk_bf16_f32 v64, v130, v131
	v_cvt_pk_bf16_f32 v65, v132, v133
	global_store_dwordx4 v[66:67], v[62:65], off offset:256
	v_cvt_pk_bf16_f32 v36, v36, v37
	v_cvt_pk_bf16_f32 v37, v38, v39
	v_cvt_pk_bf16_f32 v38, v32, v33
	v_add_co_u32_e32 v32, vcc, s54, v52
	s_nop 0
	v_lshl_add_u64 v[62:63], v[52:53], 0, s[14:15]
	v_addc_co_u32_e32 v33, vcc, 0, v53, vcc
	v_cvt_pk_bf16_f32 v39, v34, v35
	global_store_dwordx4 v[32:33], v[36:39], off
	v_cvt_pk_bf16_f32 v32, v70, v71
	v_cvt_pk_bf16_f32 v33, v72, v73
	v_cvt_pk_bf16_f32 v34, v114, v115
	v_cvt_pk_bf16_f32 v35, v116, v117
	global_store_dwordx4 v[62:63], v[32:35], off offset:256
	v_cvt_pk_bf16_f32 v20, v20, v21
	v_cvt_pk_bf16_f32 v21, v22, v23
	v_cvt_pk_bf16_f32 v22, v16, v17
	v_add_co_u32_e32 v16, vcc, s55, v52
	s_nop 0
	v_lshl_add_u64 v[32:33], v[52:53], 0, s[16:17]
	v_addc_co_u32_e32 v17, vcc, 0, v53, vcc
	v_cvt_pk_bf16_f32 v23, v18, v19
	global_store_dwordx4 v[16:17], v[20:23], off
	v_cvt_pk_bf16_f32 v16, v28, v29
	v_cvt_pk_bf16_f32 v17, v30, v31
	v_cvt_pk_bf16_f32 v18, v24, v25
	v_cvt_pk_bf16_f32 v19, v26, v27
	global_store_dwordx4 v[32:33], v[16:19], off offset:256
	v_cvt_pk_bf16_f32 v4, v4, v5
	v_cvt_pk_bf16_f32 v5, v6, v7
	v_cvt_pk_bf16_f32 v6, v0, v1
	v_add_co_u32_e32 v0, vcc, s56, v52
	s_nop 0
	v_lshl_add_u64 v[16:17], v[52:53], 0, s[18:19]
	v_addc_co_u32_e32 v1, vcc, 0, v53, vcc
	s_andn2_b64 vcc, exec, s[20:21]
	v_cvt_pk_bf16_f32 v7, v2, v3
	global_store_dwordx4 v[0:1], v[4:7], off
	v_cvt_pk_bf16_f32 v0, v12, v13
	v_cvt_pk_bf16_f32 v1, v14, v15
	v_cvt_pk_bf16_f32 v2, v8, v9
	v_cvt_pk_bf16_f32 v3, v10, v11
	global_store_dwordx4 v[16:17], v[0:3], off offset:256
	s_cbranch_vccz .LBB0_604

.LBB0_661:
	s_setprio 0
	s_mov_b64 s[0:1], s[86:87]
	s_mov_b32 s8, 0
	s_cmp_lt_i32 s82, 7
	s_cselect_b64 s[6:7], -1, 0
	v_mbcnt_lo_u32_b32 v0, -1, s8
	v_mbcnt_hi_u32_b32 v0, -1, v0
	v_or_b32_e32 v0, s92, v0
	s_and_b64 s[4:5], s[6:7], s[4:5]
	s_andn2_b64 vcc, exec, s[4:5]
	v_readfirstlane_b32 s6, v0
	s_cbranch_vccnz .LBB0_959
	s_cmpk_gt_i32 s2, 0xff
	v_writelane_b32 v255, s4, 0
	s_nop 1
	v_writelane_b32 v255, s5, 1
	v_writelane_b32 v255, s92, 2
	v_writelane_b32 v255, s90, 3
	s_nop 1
	v_writelane_b32 v255, s91, 4
	v_writelane_b32 v255, s85, 5
	v_writelane_b32 v255, s88, 6
	s_nop 1
	v_writelane_b32 v255, s89, 7
	v_writelane_b32 v255, s80, 8
	s_nop 1
	v_writelane_b32 v255, s81, 9
	v_writelane_b32 v255, s82, 10
	v_writelane_b32 v255, s83, 11
	v_writelane_b32 v255, s86, 12
	s_nop 1
	v_writelane_b32 v255, s87, 13
	s_cbranch_scc1 .LBB0_742
	s_load_dwordx2 s[0:1], s[0:1], 0x138
	s_ashr_i32 s7, s6, 6
	v_lshlrev_b32_e32 v9, 3, v0
	v_and_b32_e32 v5, 15, v0
	v_ashrrev_i32_e32 v148, 3, v0
	s_waitcnt lgkmcnt(0)
	s_add_u32 s90, s0, 0x34e00000
	s_addc_u32 s91, s1, 0
	s_add_u32 s4, s0, 0x51f00000
	v_writelane_b32 v255, s4, 14
	s_addc_u32 s4, s1, 0
	v_writelane_b32 v255, s4, 15
	s_add_u32 s0, s0, 0x56700000
	v_writelane_b32 v255, s0, 16
	s_addc_u32 s0, s1, 0
	v_writelane_b32 v255, s0, 17
	s_movk_i32 s0, 0x2940
	v_cmp_gt_i32_e64 s[0:1], s0, v0
	s_cmp_gt_u32 s6, 63
	s_cselect_b64 s[92:93], -1, 0
	v_writelane_b32 v255, s0, 18
	s_cmp_lt_u32 s6, 64
	v_and_b32_e32 v4, 56, v9
	v_writelane_b32 v255, s1, 19
	s_movk_i32 s1, 0x480
	v_cmp_gt_i32_e64 s[8:9], s1, v0
	s_movk_i32 s0, 0x90
	v_mul_lo_u32 v10, v148, s0
	v_writelane_b32 v255, s8, 20
	v_lshlrev_b32_e32 v11, 1, v4
	v_bfe_u32 v7, v0, 4, 2
	v_writelane_b32 v255, s9, 21
	s_cselect_b64 s[8:9], -1, 0
	s_lshl_b32 s11, s7, 4
	s_add_i32 s10, 0, 0x10800
	s_add_i32 s1, 0, 0x1f500
	s_and_b32 s11, s11, 48
	s_add_i32 s33, 0, 0x12c00
	s_add_i32 s12, 0, 0x1d100
	s_cmp_lt_i32 s7, 4
	v_or_b32_e32 v153, s11, v5
	v_mov_b32_e32 v15, s12
	s_cselect_b64 s[96:97], -1, 0
	v_add3_u32 v150, s10, v10, v11
	v_mul_u32_u24_e32 v10, 0x90, v4
	v_lshlrev_b32_e32 v11, 1, v148
	v_and_b32_e32 v13, 48, v0
	v_mad_u32_u24 v15, v153, s0, v15
	v_mul_lo_u32 v8, v0, s0
	v_add3_u32 v151, s1, v10, v11
	v_lshlrev_b32_e32 v10, 2, v7
	v_add_u32_e32 v14, 0, v13
	v_add_u32_e32 v156, v15, v13
	v_add_u32_e32 v13, s1, v13
	s_and_b64 s[0:1], s[96:97], exec
	v_or_b32_e32 v152, s11, v10
	s_cselect_b32 s79, 0, 32
	s_cselect_b32 s44, 16, 48
	s_add_i32 s0, 0, 0x23200
	v_and_b32_e32 v116, 0xf8, v9
	v_add_u32_e32 v1, 0x200, v0
	v_add_u32_e32 v2, 0x400, v0
	v_add_u32_e32 v3, 0x600, v0
	v_lshlrev_b32_e32 v11, 3, v7
	v_lshl_add_u32 v157, v152, 2, s0
	v_lshlrev_b32_e32 v158, 5, v7
	v_bfe_u32 v7, v0, 2, 2
	s_and_b32 s0, s6, 0xffffffc0
	v_ashrrev_i32_e32 v144, 5, v0
	v_ashrrev_i32_e32 v145, 5, v1
	v_ashrrev_i32_e32 v146, 5, v2
	v_ashrrev_i32_e32 v147, 5, v3
	v_lshl_add_u32 v6, v116, 1, 0
	v_add_u32_e32 v12, s33, v11
	s_movk_i32 s7, 0x210
	v_or_b32_e32 v7, v11, v7
	s_add_i32 s1, s0, 0
	v_and_b32_e32 v9, 24, v9
	v_add_u32_e32 v9, s1, v9
	v_add_u32_e32 v159, s0, v12
	v_mad_u64_u32 v[120:121], s[0:1], v144, s7, v[6:7]
	v_mad_u64_u32 v[122:123], s[0:1], v145, s7, v[6:7]
	v_mad_u64_u32 v[124:125], s[0:1], v146, s7, v[6:7]
	v_mad_u64_u32 v[126:127], s[0:1], v147, s7, v[6:7]
	s_ashr_i32 s0, s6, 3
	s_andn2_b32 s0, s0, 31
	s_or_b32 s1, s0, 16
	v_add_u32_e32 v155, v12, v11
	v_cmp_eq_u32_e32 vcc, 0, v5
	v_or_b32_e32 v6, s0, v5
	v_or_b32_e32 v11, s1, v5
	v_or_b32_e32 v125, s79, v5
	v_or_b32_e32 v127, s44, v5
	v_mul_u32_u24_e32 v160, 0x210, v5
	v_mul_u32_u24_e32 v17, 0x90, v5
	v_or_b32_e32 v18, 16, v5
	v_or_b32_e32 v161, 0x800, v5
	v_max_i32_e32 v5, 0x280, v0
	v_writelane_b32 v255, s8, 22
	v_or_b32_e32 v121, s0, v10
	v_sub_u32_e32 v5, v5, v0
	v_writelane_b32 v255, s9, 23
	v_mad_u32_u24 v154, v153, s7, v14
	v_mul_lo_u32 v6, v6, s7
	v_mul_lo_u32 v11, v11, s7
	v_cmp_ge_i32_e64 s[6:7], v121, v153
	v_add_u32_e32 v5, 0x1ff, v5
	v_lshrrev_b32_e32 v19, 9, v5
	v_writelane_b32 v255, s6, 24
	s_movk_i32 s0, 0x5ff
	v_or_b32_e32 v10, s1, v10
	v_writelane_b32 v255, s7, 25
	v_add_u32_e32 v20, 1, v19
	v_add_u32_e32 v19, -3, v19
	v_cmp_lt_u32_e64 s[0:1], s0, v5
	v_lshrrev_b32_e32 v21, 2, v19
	v_add_u32_e32 v22, 1, v21
	v_writelane_b32 v255, s0, 26
	v_or_b32_e32 v12, 1, v121
	v_and_b32_e32 v23, 3, v22
	v_writelane_b32 v255, s1, 27
	v_cmp_lt_u32_e64 s[0:1], 11, v19
	v_cmp_ge_i32_e64 s[14:15], v12, v153
	v_or_b32_e32 v12, 2, v121
	v_writelane_b32 v255, s0, 28
	v_cmp_ge_i32_e64 s[18:19], v12, v153
	v_cmp_le_i32_e64 s[20:21], v12, v153
	v_writelane_b32 v255, s1, 29
	v_cmp_ne_u32_e64 s[0:1], 0, v23
	v_or_b32_e32 v12, 3, v121
	v_and_b32_e32 v5, 0xfffffc, v20
	v_writelane_b32 v255, s0, 30
	v_add_u32_e32 v177, s10, v8
	v_mbcnt_lo_u32_b32 v8, -1, 0
	v_and_b32_e32 v117, 63, v0
	v_cmp_ge_i32_e64 s[22:23], v12, v153
	v_cmp_le_i32_e64 s[24:25], v12, v153
	v_or_b32_e32 v12, 1, v10
	v_writelane_b32 v255, s1, 31
	v_cmp_ne_u32_e64 s[0:1], v20, v5
	v_mbcnt_hi_u32_b32 v8, -1, v8
	v_cmp_ge_i32_e64 s[26:27], v10, v153
	v_cmp_le_i32_e64 s[28:29], v10, v153
	v_cmp_ge_i32_e64 s[30:31], v12, v153
	v_cmp_lt_i32_e64 s[34:35], v10, v153
	v_or_b32_e32 v12, 2, v10
	v_or_b32_e32 v10, 3, v10
	v_lshl_add_u32 v162, v5, 9, v0
	v_writelane_b32 v255, s0, 32
	v_lshlrev_b32_e32 v165, 1, v0
	v_add_u16_e32 v5, 1, v21
	v_and_or_b32 v8, v8, 64, v117
	v_mov_b32_e32 v119, 0
	v_lshl_add_u32 v123, v121, 1, v15
	v_cmp_ge_i32_e64 s[36:37], v12, v153
	v_cmp_le_i32_e64 s[38:39], v12, v153
	v_cmp_ge_i32_e64 s[40:41], v10, v153
	v_cmp_le_i32_e64 s[42:43], v10, v153
	v_mul_u32_u24_e32 v10, 0x210, v125
	v_mul_u32_u24_e32 v12, 0x210, v127
	v_mul_u32_u24_e32 v15, 0x90, v125
	v_mul_u32_u24_e32 v16, 0x90, v127
	v_mul_u32_u24_e32 v7, 0x210, v7
	v_mul_u32_u24_e32 v18, 0x210, v18
	v_writelane_b32 v255, s1, 33
	v_add_u32_e32 v166, 0, v165
	v_and_b32_e32 v5, 3, v5
	v_lshlrev_b32_e32 v128, 1, v4
	s_add_i32 s0, 0, 0x22700
	v_lshlrev_b32_e32 v8, 2, v8
	v_cmp_gt_i32_e64 s[4:5], 64, v0
	v_bitop3_b32 v149, v0, 63, v0 bitop3:0xc
	s_mov_b32 s80, 0
	v_cmp_eq_u32_e64 s[8:9], 0, v117
	s_and_b64 s[86:87], s[96:97], vcc
	v_cmp_le_i32_e64 s[12:13], v121, v153
	v_cmp_lt_i32_e64 s[16:17], v121, v153
	v_add_u32_e32 v163, 0xfffffe00, v0
	v_lshl_add_u32 v164, v0, 2, s33
	v_add_u32_e32 v167, 0x21900, v166
	v_and_b32_e32 v168, 0x7ffffffc, v22
	v_lshlrev_b32_e32 v169, 12, v5
	s_movk_i32 s45, 0x3a00
	s_mov_b64 s[84:85], 0x3800
	s_mov_b32 s33, 0xbfb8aa3b
	s_mov_b32 s76, 0x3f2aaaab
	v_mov_b32_e32 v170, 0x3ecc95a3
	s_mov_b32 s77, 0x3f317218
	s_mov_b32 s78, 0x7f800000
	s_mov_b32 s74, 0x33800000
	v_mov_b32_e32 v171, 0xff800000
	v_writelane_b32 v255, s0, 34
	v_add_u32_e32 v172, v14, v6
	v_add_u32_e32 v173, v14, v11
	v_add_u32_e32 v174, v9, v7
	v_add_u32_e32 v175, v13, v17
	s_mov_b32 s75, 0xc3e00000
	v_add_u32_e32 v176, v159, v18
	v_mov_b32_e32 v4, 0x3f80
	v_mov_b32_e32 v5, v119
	v_mov_b32_e32 v6, v119
	v_mov_b32_e32 v7, v119
	v_xor_b32_e32 v178, 0xfc, v8
	v_mov_b32_e32 v130, 0x3f317218
	v_mov_b32_e32 v179, 0x7f800000
	v_mov_b32_e32 v180, 0x7fc00000
	v_add_u32_e32 v181, v155, v10
	v_add_u32_e32 v182, v155, v12
	v_add_u32_e32 v183, v13, v15
	v_add_u32_e32 v184, v13, v16
	v_mov_b32_e32 v185, 0x43e00000
	s_mov_b32 s6, s2
	s_branch .LBB0_665

.LBB0_1025:
	ds_read_b128 v[0:3], v186
	ds_read_b128 v[4:7], v190
	ds_read_b128 v[8:11], v191
	ds_read_b128 v[12:15], v192
	s_add_u32 s34, s30, 0x80
	s_addc_u32 s35, s31, 0
	s_cmp_eq_u32 s65, 12
	s_cselect_b32 s37, s21, s35
	s_cselect_b32 s36, s61, s34
	s_cselect_b32 s35, s23, s64
	s_cselect_b32 s34, s62, s63
	v_lshl_add_u64 v[160:161], s[30:31], 0, v[158:159]
	s_add_i32 m0, s29, 0xc000
	ds_read_b128 v[206:209], v203
	ds_read_b128 v[210:213], v203 offset:1024
	ds_read_b128 v[214:217], v203 offset:2048
	ds_read_b128 v[218:221], v203 offset:3072
	ds_read_b128 v[222:225], v203 offset:4096
	ds_read_b128 v[226:229], v203 offset:5120
	ds_read_b128 v[230:233], v203 offset:6144
	ds_read_b128 v[234:237], v203 offset:7168
	global_load_lds_dwordx4 v[160:161], off
	v_lshl_add_u64 v[160:161], s[30:31], 0, v[156:157]
	s_add_i32 m0, s29, 0xe000
	s_nop 0
	global_load_lds_dwordx4 v[160:161], off
	s_waitcnt lgkmcnt(8)
	s_barrier
	s_waitcnt lgkmcnt(0)
	s_waitcnt lgkmcnt(0)
	v_mfma_scale_f32_16x16x128_f8f6f4 v[140:143], v[0:7], v[206:213], v[140:143], v204, v205 op_sel_hi:[0,0,0]
	v_mfma_scale_f32_16x16x128_f8f6f4 v[136:139], v[8:15], v[206:213], v[136:139], v204, v205 op_sel_hi:[0,0,0]
	v_mfma_scale_f32_16x16x128_f8f6f4 v[132:135], v[0:7], v[214:221], v[132:135], v204, v205 op_sel_hi:[0,0,0]
	v_mfma_scale_f32_16x16x128_f8f6f4 v[128:131], v[8:15], v[214:221], v[128:131], v204, v205 op_sel_hi:[0,0,0]
	v_mfma_scale_f32_16x16x128_f8f6f4 v[124:127], v[0:7], v[222:229], v[124:127], v204, v205 op_sel_hi:[0,0,0]
	v_mfma_scale_f32_16x16x128_f8f6f4 v[120:123], v[8:15], v[222:229], v[120:123], v204, v205 op_sel_hi:[0,0,0]
	v_mfma_scale_f32_16x16x128_f8f6f4 v[116:119], v[0:7], v[230:237], v[116:119], v204, v205 op_sel_hi:[0,0,0]
	v_mfma_scale_f32_16x16x128_f8f6f4 v[112:115], v[8:15], v[230:237], v[112:115], v204, v205 op_sel_hi:[0,0,0]
	s_barrier
	s_mov_b32 m0, s45
	v_lshl_add_u64 v[160:161], s[34:35], 0, v[144:145]
	ds_read_b128 v[238:241], v187
	ds_read_b128 v[242:245], v193
	ds_read_b128 v[246:249], v194
	ds_read_b128 v[250:253], v195
	global_load_lds_dwordx4 v[160:161], off
	v_lshl_add_u64 v[162:163], s[34:35], 0, v[146:147]
	s_mov_b32 m0, s46
	s_nop 0
	global_load_lds_dwordx4 v[162:163], off
	s_barrier
	s_waitcnt lgkmcnt(0)
	s_waitcnt lgkmcnt(0)
	v_mfma_scale_f32_16x16x128_f8f6f4 v[108:111], v[238:245], v[206:213], v[108:111], v204, v205 op_sel_hi:[0,0,0]
	v_mfma_scale_f32_16x16x128_f8f6f4 v[104:107], v[246:253], v[206:213], v[104:107], v204, v205 op_sel_hi:[0,0,0]
	v_mfma_scale_f32_16x16x128_f8f6f4 v[100:103], v[238:245], v[214:221], v[100:103], v204, v205 op_sel_hi:[0,0,0]
	v_mfma_scale_f32_16x16x128_f8f6f4 v[96:99], v[246:253], v[214:221], v[96:99], v204, v205 op_sel_hi:[0,0,0]
	v_mfma_scale_f32_16x16x128_f8f6f4 v[92:95], v[238:245], v[222:229], v[92:95], v204, v205 op_sel_hi:[0,0,0]
	v_mfma_scale_f32_16x16x128_f8f6f4 v[88:91], v[246:253], v[222:229], v[88:91], v204, v205 op_sel_hi:[0,0,0]
	v_mfma_scale_f32_16x16x128_f8f6f4 v[84:87], v[238:245], v[230:237], v[84:87], v204, v205 op_sel_hi:[0,0,0]
	v_mfma_scale_f32_16x16x128_f8f6f4 v[80:83], v[246:253], v[230:237], v[80:83], v204, v205 op_sel_hi:[0,0,0]
	s_mov_b32 m0, s29
	v_lshl_add_u64 v[164:165], s[36:37], 0, v[148:149]
	s_barrier
	ds_read_b128 v[206:209], v203 offset:16384
	ds_read_b128 v[210:213], v203 offset:17408
	ds_read_b128 v[214:217], v203 offset:18432
	ds_read_b128 v[218:221], v203 offset:19456
	ds_read_b128 v[222:225], v203 offset:20480
	ds_read_b128 v[226:229], v203 offset:21504
	ds_read_b128 v[230:233], v203 offset:22528
	ds_read_b128 v[234:237], v203 offset:23552
	global_load_lds_dwordx4 v[164:165], off
	v_lshl_add_u64 v[166:167], s[36:37], 0, v[150:151]
	s_mov_b32 m0, s47
	s_nop 0
	global_load_lds_dwordx4 v[166:167], off
	s_barrier
	s_waitcnt lgkmcnt(0)
	s_waitcnt lgkmcnt(0)
	v_mfma_scale_f32_16x16x128_f8f6f4 v[76:79], v[0:7], v[206:213], v[76:79], v204, v205 op_sel_hi:[0,0,0]
	v_mfma_scale_f32_16x16x128_f8f6f4 v[72:75], v[8:15], v[206:213], v[72:75], v204, v205 op_sel_hi:[0,0,0]
	v_mfma_scale_f32_16x16x128_f8f6f4 v[68:71], v[0:7], v[214:221], v[68:71], v204, v205 op_sel_hi:[0,0,0]
	v_mfma_scale_f32_16x16x128_f8f6f4 v[64:67], v[8:15], v[214:221], v[64:67], v204, v205 op_sel_hi:[0,0,0]
	v_mfma_scale_f32_16x16x128_f8f6f4 v[60:63], v[0:7], v[222:229], v[60:63], v204, v205 op_sel_hi:[0,0,0]
	v_mfma_scale_f32_16x16x128_f8f6f4 v[56:59], v[8:15], v[222:229], v[56:59], v204, v205 op_sel_hi:[0,0,0]
	v_mfma_scale_f32_16x16x128_f8f6f4 v[52:55], v[0:7], v[230:237], v[52:55], v204, v205 op_sel_hi:[0,0,0]
	v_mfma_scale_f32_16x16x128_f8f6f4 v[48:51], v[8:15], v[230:237], v[48:51], v204, v205 op_sel_hi:[0,0,0]
	s_barrier
	s_add_u32 s66, s34, 0x40000
	s_addc_u32 s67, s35, 0
	s_mov_b32 m0, s48
	v_lshl_add_u64 v[0:1], s[66:67], 0, v[144:145]
	global_load_lds_dwordx4 v[0:1], off
	v_lshl_add_u64 v[0:1], s[66:67], 0, v[146:147]
	s_mov_b32 m0, s49
	s_nop 0
	global_load_lds_dwordx4 v[0:1], off
	s_waitcnt vmcnt(6)
	s_barrier
	v_mfma_scale_f32_16x16x128_f8f6f4 v[44:47], v[238:245], v[206:213], v[44:47], v204, v205 op_sel_hi:[0,0,0]
	v_mfma_scale_f32_16x16x128_f8f6f4 v[40:43], v[246:253], v[206:213], v[40:43], v204, v205 op_sel_hi:[0,0,0]
	v_mfma_scale_f32_16x16x128_f8f6f4 v[36:39], v[238:245], v[214:221], v[36:39], v204, v205 op_sel_hi:[0,0,0]
	v_mfma_scale_f32_16x16x128_f8f6f4 v[32:35], v[246:253], v[214:221], v[32:35], v204, v205 op_sel_hi:[0,0,0]
	v_mfma_scale_f32_16x16x128_f8f6f4 v[28:31], v[238:245], v[222:229], v[28:31], v204, v205 op_sel_hi:[0,0,0]
	v_mfma_scale_f32_16x16x128_f8f6f4 v[24:27], v[246:253], v[222:229], v[24:27], v204, v205 op_sel_hi:[0,0,0]
	v_mfma_scale_f32_16x16x128_f8f6f4 v[20:23], v[238:245], v[230:237], v[20:23], v204, v205 op_sel_hi:[0,0,0]
	v_mfma_scale_f32_16x16x128_f8f6f4 v[16:19], v[246:253], v[230:237], v[16:19], v204, v205 op_sel_hi:[0,0,0]
	s_barrier
	ds_read_b128 v[0:3], v188
	ds_read_b128 v[4:7], v196
	ds_read_b128 v[8:11], v197
	ds_read_b128 v[12:15], v198
	s_mov_b32 m0, s50
	v_lshl_add_u64 v[168:169], s[36:37], 0, v[152:153]
	ds_read_b128 v[206:209], v203 offset:32768
	ds_read_b128 v[210:213], v203 offset:33792
	ds_read_b128 v[214:217], v203 offset:34816
	ds_read_b128 v[218:221], v203 offset:35840
	ds_read_b128 v[222:225], v203 offset:36864
	ds_read_b128 v[226:229], v203 offset:37888
	ds_read_b128 v[230:233], v203 offset:38912
	ds_read_b128 v[234:237], v203 offset:39936
	global_load_lds_dwordx4 v[168:169], off
	v_lshl_add_u64 v[168:169], s[36:37], 0, v[154:155]
	s_mov_b32 m0, s51
	s_nop 0
	global_load_lds_dwordx4 v[168:169], off
	s_waitcnt lgkmcnt(8)
	s_barrier
	s_waitcnt lgkmcnt(0)
	s_waitcnt lgkmcnt(0)
	v_mfma_scale_f32_16x16x128_f8f6f4 v[140:143], v[0:7], v[206:213], v[140:143], v204, v205 op_sel_hi:[0,0,0]
	v_mfma_scale_f32_16x16x128_f8f6f4 v[136:139], v[8:15], v[206:213], v[136:139], v204, v205 op_sel_hi:[0,0,0]
	v_mfma_scale_f32_16x16x128_f8f6f4 v[132:135], v[0:7], v[214:221], v[132:135], v204, v205 op_sel_hi:[0,0,0]
	v_mfma_scale_f32_16x16x128_f8f6f4 v[128:131], v[8:15], v[214:221], v[128:131], v204, v205 op_sel_hi:[0,0,0]
	v_mfma_scale_f32_16x16x128_f8f6f4 v[124:127], v[0:7], v[222:229], v[124:127], v204, v205 op_sel_hi:[0,0,0]
	v_mfma_scale_f32_16x16x128_f8f6f4 v[120:123], v[8:15], v[222:229], v[120:123], v204, v205 op_sel_hi:[0,0,0]
	v_mfma_scale_f32_16x16x128_f8f6f4 v[116:119], v[0:7], v[230:237], v[116:119], v204, v205 op_sel_hi:[0,0,0]
	v_mfma_scale_f32_16x16x128_f8f6f4 v[112:115], v[8:15], v[230:237], v[112:115], v204, v205 op_sel_hi:[0,0,0]
	s_barrier
	s_mov_b32 m0, s53
	v_lshl_add_u64 v[160:161], v[160:161], 0, s[0:1]
	ds_read_b128 v[238:241], v189
	ds_read_b128 v[242:245], v199
	ds_read_b128 v[246:249], v200
	ds_read_b128 v[250:253], v201
	global_load_lds_dwordx4 v[160:161], off
	v_lshl_add_u64 v[160:161], v[162:163], 0, s[0:1]
	s_mov_b32 m0, s54
	s_nop 0
	global_load_lds_dwordx4 v[160:161], off
	s_barrier
	s_waitcnt lgkmcnt(0)
	s_waitcnt lgkmcnt(0)
	v_mfma_scale_f32_16x16x128_f8f6f4 v[108:111], v[238:245], v[206:213], v[108:111], v204, v205 op_sel_hi:[0,0,0]
	v_mfma_scale_f32_16x16x128_f8f6f4 v[104:107], v[246:253], v[206:213], v[104:107], v204, v205 op_sel_hi:[0,0,0]
	v_mfma_scale_f32_16x16x128_f8f6f4 v[100:103], v[238:245], v[214:221], v[100:103], v204, v205 op_sel_hi:[0,0,0]
	v_mfma_scale_f32_16x16x128_f8f6f4 v[96:99], v[246:253], v[214:221], v[96:99], v204, v205 op_sel_hi:[0,0,0]
	v_mfma_scale_f32_16x16x128_f8f6f4 v[92:95], v[238:245], v[222:229], v[92:95], v204, v205 op_sel_hi:[0,0,0]
	v_mfma_scale_f32_16x16x128_f8f6f4 v[88:91], v[246:253], v[222:229], v[88:91], v204, v205 op_sel_hi:[0,0,0]
	v_mfma_scale_f32_16x16x128_f8f6f4 v[84:87], v[238:245], v[230:237], v[84:87], v204, v205 op_sel_hi:[0,0,0]
	v_mfma_scale_f32_16x16x128_f8f6f4 v[80:83], v[246:253], v[230:237], v[80:83], v204, v205 op_sel_hi:[0,0,0]
	s_mov_b32 m0, s55
	v_lshl_add_u64 v[160:161], v[164:165], 0, s[0:1]
	s_barrier
	ds_read_b128 v[206:209], v203 offset:49152
	ds_read_b128 v[210:213], v203 offset:50176
	ds_read_b128 v[214:217], v203 offset:51200
	ds_read_b128 v[218:221], v203 offset:52224
	ds_read_b128 v[222:225], v203 offset:53248
	ds_read_b128 v[226:229], v203 offset:54272
	ds_read_b128 v[230:233], v203 offset:55296
	ds_read_b128 v[234:237], v203 offset:56320
	global_load_lds_dwordx4 v[160:161], off
	v_lshl_add_u64 v[160:161], v[166:167], 0, s[0:1]
	s_mov_b32 m0, s56
	s_nop 0
	global_load_lds_dwordx4 v[160:161], off
	s_barrier
	s_waitcnt lgkmcnt(0)
	s_waitcnt lgkmcnt(0)
	v_mfma_scale_f32_16x16x128_f8f6f4 v[76:79], v[0:7], v[206:213], v[76:79], v204, v205 op_sel_hi:[0,0,0]
	v_mfma_scale_f32_16x16x128_f8f6f4 v[72:75], v[8:15], v[206:213], v[72:75], v204, v205 op_sel_hi:[0,0,0]
	v_mfma_scale_f32_16x16x128_f8f6f4 v[68:71], v[0:7], v[214:221], v[68:71], v204, v205 op_sel_hi:[0,0,0]
	v_mfma_scale_f32_16x16x128_f8f6f4 v[64:67], v[8:15], v[214:221], v[64:67], v204, v205 op_sel_hi:[0,0,0]
	v_mfma_scale_f32_16x16x128_f8f6f4 v[60:63], v[0:7], v[222:229], v[60:63], v204, v205 op_sel_hi:[0,0,0]
	v_mfma_scale_f32_16x16x128_f8f6f4 v[56:59], v[8:15], v[222:229], v[56:59], v204, v205 op_sel_hi:[0,0,0]
	v_mfma_scale_f32_16x16x128_f8f6f4 v[52:55], v[0:7], v[230:237], v[52:55], v204, v205 op_sel_hi:[0,0,0]
	v_mfma_scale_f32_16x16x128_f8f6f4 v[48:51], v[8:15], v[230:237], v[48:51], v204, v205 op_sel_hi:[0,0,0]
	s_barrier
	s_add_u32 s34, s34, 0x40080
	s_addc_u32 s35, s35, 0
	s_mov_b32 m0, s57
	v_lshl_add_u64 v[0:1], s[34:35], 0, v[144:145]
	global_load_lds_dwordx4 v[0:1], off
	v_lshl_add_u64 v[0:1], s[34:35], 0, v[146:147]
	s_mov_b32 m0, s58
	s_nop 0
	global_load_lds_dwordx4 v[0:1], off
	s_waitcnt vmcnt(6)
	s_barrier
	v_mfma_scale_f32_16x16x128_f8f6f4 v[44:47], v[238:245], v[206:213], v[44:47], v204, v205 op_sel_hi:[0,0,0]
	v_mfma_scale_f32_16x16x128_f8f6f4 v[40:43], v[246:253], v[206:213], v[40:43], v204, v205 op_sel_hi:[0,0,0]
	v_mfma_scale_f32_16x16x128_f8f6f4 v[36:39], v[238:245], v[214:221], v[36:39], v204, v205 op_sel_hi:[0,0,0]
	v_mfma_scale_f32_16x16x128_f8f6f4 v[32:35], v[246:253], v[214:221], v[32:35], v204, v205 op_sel_hi:[0,0,0]
	v_mfma_scale_f32_16x16x128_f8f6f4 v[28:31], v[238:245], v[222:229], v[28:31], v204, v205 op_sel_hi:[0,0,0]
	v_mfma_scale_f32_16x16x128_f8f6f4 v[24:27], v[246:253], v[222:229], v[24:27], v204, v205 op_sel_hi:[0,0,0]
	v_mfma_scale_f32_16x16x128_f8f6f4 v[20:23], v[238:245], v[230:237], v[20:23], v204, v205 op_sel_hi:[0,0,0]
	v_mfma_scale_f32_16x16x128_f8f6f4 v[16:19], v[246:253], v[230:237], v[16:19], v204, v205 op_sel_hi:[0,0,0]
	s_add_i32 s65, s65, 2
	s_add_u32 s30, s30, 0x100
	s_addc_u32 s31, s31, 0
	s_add_u32 s63, s63, 0x100
	s_addc_u32 s64, s64, 0
	s_cmp_gt_u32 s65, 13
	s_barrier
	s_cbranch_scc0 .LBB0_1025
	v_lshl_add_u32 v6, s28, 8, v185
	v_lshl_or_b32 v10, s60, 8, v202
	v_mov_b64_e32 v[8:9], s[8:9]
	v_ashrrev_i32_e32 v11, 31, v10
	v_mad_i64_i32 v[0:1], s[30:31], v6, s59, v[8:9]
	v_lshl_add_u64 v[12:13], v[0:1], 0, s[16:17]
	v_lshlrev_b64 v[4:5], 1, v[10:11]
	s_nop 15
	s_nop 15
	v_lshl_add_u64 v[0:1], v[12:13], 0, v[4:5]
	global_load_dwordx4 v[206:209], v[0:1], off
	v_or_b32_e32 v218, 16, v6
	v_mad_i64_i32 v[0:1], s[30:31], v218, s59, v[8:9]
	v_lshl_add_u64 v[14:15], v[0:1], 0, s[16:17]
	v_lshl_add_u64 v[0:1], v[14:15], 0, v[4:5]
	global_load_dwordx4 v[210:213], v[0:1], off
	v_or_b32_e32 v168, 32, v6
	v_ashrrev_i32_e32 v7, 31, v6
	v_or_b32_e32 v162, 48, v6
	v_mad_i64_i32 v[0:1], s[30:31], v168, s59, v[8:9]
	v_mad_i64_i32 v[2:3], s[30:31], v162, s59, v[8:9]
	v_lshlrev_b64 v[160:161], 12, v[6:7]
	v_lshl_add_u64 v[166:167], v[0:1], 0, s[16:17]
	v_lshl_add_u64 v[164:165], v[2:3], 0, s[16:17]
	v_lshl_add_u64 v[0:1], s[6:7], 0, v[160:161]
	v_lshl_add_u64 v[2:3], v[166:167], 0, v[4:5]
	v_lshl_add_u64 v[220:221], v[164:165], 0, v[4:5]
	v_lshl_add_u64 v[160:161], v[0:1], 0, v[4:5]
	global_load_dwordx4 v[214:217], v[2:3], off
	s_nop 0
	global_load_dwordx4 v[0:3], v[220:221], off
	v_ashrrev_i32_e32 v219, 31, v218
	v_ashrrev_i32_e32 v169, 31, v168
	v_ashrrev_i32_e32 v163, 31, v162
	s_and_b64 vcc, exec, s[18:19]
	s_mov_b32 s60, s22
	s_mov_b32 s28, s20
	s_mov_b64 s[34:35], s[26:27]
	s_waitcnt vmcnt(0)
	v_lshlrev_b32_e32 v7, 16, v206
	v_and_b32_e32 v11, 0xffff0000, v206
	v_lshlrev_b32_e32 v206, 16, v207
	v_and_b32_e32 v207, 0xffff0000, v207
	v_lshlrev_b32_e32 v220, 16, v208
	v_and_b32_e32 v208, 0xffff0000, v208
	v_lshlrev_b32_e32 v221, 16, v209
	v_and_b32_e32 v209, 0xffff0000, v209
	v_mul_f32_e32 v7, 0xbfb8aa3b, v7
	v_mul_f32_e32 v11, 0xbfb8aa3b, v11
	v_mul_f32_e32 v206, 0xbfb8aa3b, v206
	v_mul_f32_e32 v207, 0xbfb8aa3b, v207
	v_mul_f32_e32 v220, 0xbfb8aa3b, v220
	v_mul_f32_e32 v208, 0xbfb8aa3b, v208
	v_mul_f32_e32 v221, 0xbfb8aa3b, v221
	v_mul_f32_e32 v209, 0xbfb8aa3b, v209
	v_exp_f32_e32 v7, v7
	v_exp_f32_e32 v11, v11
	v_exp_f32_e32 v206, v206
	v_exp_f32_e32 v207, v207
	v_exp_f32_e32 v220, v220
	v_exp_f32_e32 v208, v208
	v_exp_f32_e32 v221, v221
	v_exp_f32_e32 v209, v209
	v_lshlrev_b32_e32 v222, 16, v210
	v_and_b32_e32 v210, 0xffff0000, v210
	v_lshlrev_b32_e32 v223, 16, v211
	v_mul_f32_e32 v222, 0xbfb8aa3b, v222
	v_mul_f32_e32 v210, 0xbfb8aa3b, v210
	v_mul_f32_e32 v223, 0xbfb8aa3b, v223
	v_exp_f32_e32 v224, v222
	v_exp_f32_e32 v210, v210
	v_exp_f32_e32 v226, v223
	v_add_f32_e32 v7, 1.0, v7
	v_add_f32_e32 v11, 1.0, v11
	v_add_f32_e32 v222, 1.0, v206
	v_add_f32_e32 v223, 1.0, v207
	v_add_f32_e32 v220, 1.0, v220
	v_add_f32_e32 v225, 1.0, v208
	v_add_f32_e32 v227, 1.0, v221
	v_add_f32_e32 v228, 1.0, v209
	v_rcp_f32_e32 v206, v7
	v_rcp_f32_e32 v207, v11
	v_rcp_f32_e32 v208, v222
	v_rcp_f32_e32 v209, v223
	v_rcp_f32_e32 v220, v220
	v_rcp_f32_e32 v221, v225
	v_rcp_f32_e32 v222, v227
	v_rcp_f32_e32 v223, v228
	v_add_f32_e32 v11, 1.0, v210
	v_rcp_f32_e32 v225, v11
	v_pk_mul_f32 v[140:141], v[140:141], v[206:207]
	v_pk_mul_f32 v[206:207], v[138:139], v[222:223]
	v_pk_mul_f32 v[138:139], v[136:137], v[220:221]
	v_cvt_pk_bf16_f32 v136, v140, v141
	v_and_b32_e32 v11, 0xffff0000, v211
	v_pk_mul_f32 v[142:143], v[142:143], v[208:209]
	v_mul_f32_e32 v11, 0xbfb8aa3b, v11
	v_cvt_pk_bf16_f32 v137, v142, v143
	v_cvt_pk_bf16_f32 v138, v138, v139
	v_cvt_pk_bf16_f32 v139, v206, v207
	global_store_dwordx4 v[160:161], v[136:139], off
	v_exp_f32_e32 v11, v11
	v_add_f32_e32 v7, 1.0, v224
	v_lshlrev_b32_e32 v136, 16, v212
	v_mul_f32_e32 v136, 0xbfb8aa3b, v136
	v_exp_f32_e32 v138, v136
	v_rcp_f32_e32 v224, v7
	v_add_f32_e32 v7, 1.0, v226
	v_rcp_f32_e32 v136, v7
	v_add_f32_e32 v7, 1.0, v11
	v_rcp_f32_e32 v137, v7
	v_add_f32_e32 v7, 1.0, v138
	v_rcp_f32_e32 v138, v7
	v_and_b32_e32 v7, 0xffff0000, v212
	v_lshlrev_b32_e32 v11, 16, v213
	v_mul_f32_e32 v7, 0xbfb8aa3b, v7
	v_mul_f32_e32 v11, 0xbfb8aa3b, v11
	v_and_b32_e32 v139, 0xffff0000, v213
	v_exp_f32_e32 v7, v7
	v_exp_f32_e32 v11, v11
	v_mul_f32_e32 v139, 0xbfb8aa3b, v139
	v_exp_f32_e32 v139, v139
	v_add_f32_e32 v7, 1.0, v7
	v_add_f32_e32 v11, 1.0, v11
	v_rcp_f32_e32 v140, v11
	v_add_f32_e32 v11, 1.0, v139
	v_rcp_f32_e32 v139, v7
	v_rcp_f32_e32 v141, v11
	v_pk_mul_f32 v[132:133], v[132:133], v[224:225]
	v_pk_mul_f32 v[134:135], v[134:135], v[136:137]
	v_pk_mul_f32 v[128:129], v[128:129], v[138:139]
	v_pk_mul_f32 v[136:137], v[130:131], v[140:141]
	v_cvt_pk_bf16_f32 v130, v132, v133
	v_cvt_pk_bf16_f32 v131, v134, v135
	v_cvt_pk_bf16_f32 v132, v128, v129
	v_lshlrev_b64 v[128:129], 12, v[218:219]
	v_lshlrev_b32_e32 v7, 16, v214
	v_lshl_add_u64 v[128:129], s[6:7], 0, v[128:129]
	v_mul_f32_e32 v7, 0xbfb8aa3b, v7
	v_lshl_add_u64 v[128:129], v[128:129], 0, v[4:5]
	v_and_b32_e32 v11, 0xffff0000, v214
	v_cvt_pk_bf16_f32 v133, v136, v137
	v_exp_f32_e32 v7, v7
	global_store_dwordx4 v[128:129], v[130:133], off
	v_mul_f32_e32 v11, 0xbfb8aa3b, v11
	v_exp_f32_e32 v11, v11
	v_lshlrev_b32_e32 v130, 16, v215
	v_mul_f32_e32 v130, 0xbfb8aa3b, v130
	v_exp_f32_e32 v132, v130
	v_add_f32_e32 v7, 1.0, v7
	v_rcp_f32_e32 v130, v7
	v_add_f32_e32 v7, 1.0, v11
	v_and_b32_e32 v11, 0xffff0000, v215
	v_rcp_f32_e32 v131, v7
	v_add_f32_e32 v7, 1.0, v132
	v_mul_f32_e32 v11, 0xbfb8aa3b, v11
	v_lshlrev_b32_e32 v132, 16, v216
	v_exp_f32_e32 v11, v11
	v_mul_f32_e32 v132, 0xbfb8aa3b, v132
	v_exp_f32_e32 v134, v132
	v_rcp_f32_e32 v132, v7
	v_add_f32_e32 v7, 1.0, v11
	v_rcp_f32_e32 v133, v7
	v_add_f32_e32 v7, 1.0, v134
	v_rcp_f32_e32 v134, v7
	v_and_b32_e32 v7, 0xffff0000, v216
	v_lshlrev_b32_e32 v11, 16, v217
	v_mul_f32_e32 v7, 0xbfb8aa3b, v7
	v_mul_f32_e32 v11, 0xbfb8aa3b, v11
	v_and_b32_e32 v135, 0xffff0000, v217
	v_exp_f32_e32 v7, v7
	v_exp_f32_e32 v11, v11
	v_mul_f32_e32 v135, 0xbfb8aa3b, v135
	v_exp_f32_e32 v135, v135
	v_add_f32_e32 v7, 1.0, v7
	v_add_f32_e32 v11, 1.0, v11
	v_rcp_f32_e32 v136, v11
	v_add_f32_e32 v11, 1.0, v135
	v_rcp_f32_e32 v135, v7
	v_rcp_f32_e32 v137, v11
	v_lshlrev_b32_e32 v7, 16, v0
	v_mul_f32_e32 v7, 0xbfb8aa3b, v7
	v_exp_f32_e32 v7, v7
	v_pk_mul_f32 v[124:125], v[124:125], v[130:131]
	v_pk_mul_f32 v[120:121], v[120:121], v[134:135]
	v_pk_mul_f32 v[126:127], v[126:127], v[132:133]
	v_pk_mul_f32 v[130:131], v[122:123], v[136:137]
	v_cvt_pk_bf16_f32 v122, v124, v125
	v_cvt_pk_bf16_f32 v123, v126, v127
	v_cvt_pk_bf16_f32 v124, v120, v121
	v_lshlrev_b64 v[120:121], 12, v[168:169]
	v_lshl_add_u64 v[120:121], s[6:7], 0, v[120:121]
	v_lshl_add_u64 v[120:121], v[120:121], 0, v[4:5]
	v_add_f32_e32 v7, 1.0, v7
	v_cvt_pk_bf16_f32 v125, v130, v131
	global_store_dwordx4 v[120:121], v[122:125], off
	v_and_b32_e32 v0, 0xffff0000, v0
	v_mul_f32_e32 v0, 0xbfb8aa3b, v0
	v_rcp_f32_e32 v122, v7
	v_lshlrev_b32_e32 v7, 16, v2
	v_mul_f32_e32 v7, 0xbfb8aa3b, v7
	v_exp_f32_e32 v7, v7
	v_lshlrev_b32_e32 v11, 16, v1
	v_and_b32_e32 v2, 0xffff0000, v2
	v_exp_f32_e32 v0, v0
	v_add_f32_e32 v7, 1.0, v7
	v_rcp_f32_e32 v124, v7
	v_lshlrev_b32_e32 v7, 16, v3
	v_and_b32_e32 v3, 0xffff0000, v3
	v_mul_f32_e32 v11, 0xbfb8aa3b, v11
	v_and_b32_e32 v1, 0xffff0000, v1
	v_mul_f32_e32 v2, 0xbfb8aa3b, v2
	v_mul_f32_e32 v7, 0xbfb8aa3b, v7
	v_mul_f32_e32 v3, 0xbfb8aa3b, v3
	v_exp_f32_e32 v11, v11
	v_mul_f32_e32 v1, 0xbfb8aa3b, v1
	v_exp_f32_e32 v2, v2
	v_exp_f32_e32 v7, v7
	v_exp_f32_e32 v3, v3
	v_exp_f32_e32 v1, v1
	v_add_f32_e32 v0, 1.0, v0
	v_rcp_f32_e32 v123, v0
	v_add_f32_e32 v0, 1.0, v11
	v_add_f32_e32 v11, 1.0, v2
	v_add_f32_e32 v2, 1.0, v7
	v_add_f32_e32 v3, 1.0, v3
	v_add_f32_e32 v1, 1.0, v1
	v_rcp_f32_e32 v2, v2
	v_rcp_f32_e32 v3, v3
	v_rcp_f32_e32 v125, v11
	v_rcp_f32_e32 v0, v0
	v_rcp_f32_e32 v1, v1
	v_pk_mul_f32 v[114:115], v[114:115], v[2:3]
	v_pk_mul_f32 v[2:3], v[112:113], v[124:125]
	v_lshlrev_b64 v[112:113], 12, v[162:163]
	v_pk_mul_f32 v[118:119], v[118:119], v[0:1]
	v_pk_mul_f32 v[0:1], v[116:117], v[122:123]
	v_lshl_add_u64 v[112:113], s[6:7], 0, v[112:113]
	v_cvt_pk_bf16_f32 v0, v0, v1
	v_lshl_add_u64 v[112:113], v[112:113], 0, v[4:5]
	v_cvt_pk_bf16_f32 v1, v118, v119
	v_cvt_pk_bf16_f32 v2, v2, v3
	v_cvt_pk_bf16_f32 v3, v114, v115
	global_store_dwordx4 v[112:113], v[0:3], off
	s_nop 1
	v_or_b32_e32 v0, 0x80, v10
	v_ashrrev_i32_e32 v1, 31, v0
	v_lshlrev_b64 v[10:11], 1, v[0:1]
	v_lshl_add_u64 v[0:1], v[12:13], 0, v[10:11]
	global_load_dwordx4 v[114:117], v[0:1], off
	v_lshl_add_u64 v[0:1], v[14:15], 0, v[10:11]
	global_load_dwordx4 v[12:15], v[0:1], off
	v_lshl_add_u64 v[0:1], v[166:167], 0, v[10:11]
	s_waitcnt vmcnt(0)
	v_lshlrev_b32_e32 v2, 16, v114
	v_mul_f32_e32 v2, 0xbfb8aa3b, v2
	v_exp_f32_e32 v7, v2
	v_lshl_add_u64 v[2:3], v[164:165], 0, v[10:11]
	global_load_dwordx4 v[122:125], v[0:1], off
	s_nop 0
	global_load_dwordx4 v[0:3], v[2:3], off
	v_and_b32_e32 v114, 0xffff0000, v114
	v_mul_f32_e32 v114, 0xbfb8aa3b, v114
	v_exp_f32_e32 v114, v114
	v_lshlrev_b32_e32 v118, 16, v115
	v_add_f32_e32 v7, 1.0, v7
	v_mul_f32_e32 v118, 0xbfb8aa3b, v118
	v_exp_f32_e32 v126, v118
	v_rcp_f32_e32 v118, v7
	v_add_f32_e32 v7, 1.0, v114
	v_and_b32_e32 v114, 0xffff0000, v115
	v_mul_f32_e32 v114, 0xbfb8aa3b, v114
	v_exp_f32_e32 v115, v114
	v_lshlrev_b32_e32 v114, 16, v116
	v_mul_f32_e32 v114, 0xbfb8aa3b, v114
	v_rcp_f32_e32 v119, v7
	v_add_f32_e32 v7, 1.0, v126
	v_exp_f32_e32 v126, v114
	v_rcp_f32_e32 v114, v7
	v_add_f32_e32 v7, 1.0, v115
	v_rcp_f32_e32 v115, v7
	v_add_f32_e32 v7, 1.0, v126
	v_rcp_f32_e32 v126, v7
	v_and_b32_e32 v7, 0xffff0000, v116
	v_lshlrev_b32_e32 v116, 16, v117
	v_and_b32_e32 v117, 0xffff0000, v117
	v_mul_f32_e32 v7, 0xbfb8aa3b, v7
	v_mul_f32_e32 v116, 0xbfb8aa3b, v116
	v_mul_f32_e32 v117, 0xbfb8aa3b, v117
	v_exp_f32_e32 v7, v7
	v_exp_f32_e32 v116, v116
	v_exp_f32_e32 v117, v117
	v_pk_mul_f32 v[110:111], v[110:111], v[114:115]
	v_add_f32_e32 v7, 1.0, v7
	v_add_f32_e32 v116, 1.0, v116
	v_add_f32_e32 v117, 1.0, v117
	v_rcp_f32_e32 v116, v116
	v_rcp_f32_e32 v117, v117
	v_rcp_f32_e32 v127, v7
	v_lshlrev_b32_e32 v7, 16, v12
	v_mul_f32_e32 v7, 0xbfb8aa3b, v7
	v_and_b32_e32 v12, 0xffff0000, v12
	v_exp_f32_e32 v7, v7
	v_mul_f32_e32 v12, 0xbfb8aa3b, v12
	v_exp_f32_e32 v12, v12
	v_pk_mul_f32 v[108:109], v[108:109], v[118:119]
	v_pk_mul_f32 v[114:115], v[106:107], v[116:117]
	v_pk_mul_f32 v[106:107], v[104:105], v[126:127]
	v_cvt_pk_bf16_f32 v104, v108, v109
	v_cvt_pk_bf16_f32 v105, v110, v111
	v_add_f32_e32 v7, 1.0, v7
	v_cvt_pk_bf16_f32 v106, v106, v107
	v_cvt_pk_bf16_f32 v107, v114, v115
	global_store_dwordx4 v[160:161], v[104:107], off offset:256
	s_nop 1
	v_lshlrev_b32_e32 v104, 16, v13
	v_mul_f32_e32 v104, 0xbfb8aa3b, v104
	v_exp_f32_e32 v106, v104
	v_rcp_f32_e32 v104, v7
	v_add_f32_e32 v7, 1.0, v12
	v_and_b32_e32 v12, 0xffff0000, v13
	v_mul_f32_e32 v12, 0xbfb8aa3b, v12
	v_exp_f32_e32 v13, v12
	v_lshlrev_b32_e32 v12, 16, v14
	v_mul_f32_e32 v12, 0xbfb8aa3b, v12
	v_rcp_f32_e32 v105, v7
	v_add_f32_e32 v7, 1.0, v106
	v_exp_f32_e32 v106, v12
	v_rcp_f32_e32 v12, v7
	v_add_f32_e32 v7, 1.0, v13
	v_rcp_f32_e32 v13, v7
	v_add_f32_e32 v7, 1.0, v106
	v_rcp_f32_e32 v106, v7
	v_and_b32_e32 v7, 0xffff0000, v14
	v_lshlrev_b32_e32 v14, 16, v15
	v_and_b32_e32 v15, 0xffff0000, v15
	v_mul_f32_e32 v7, 0xbfb8aa3b, v7
	v_mul_f32_e32 v14, 0xbfb8aa3b, v14
	v_mul_f32_e32 v15, 0xbfb8aa3b, v15
	v_exp_f32_e32 v7, v7
	v_exp_f32_e32 v14, v14
	v_exp_f32_e32 v15, v15
	v_pk_mul_f32 v[102:103], v[102:103], v[12:13]
	v_add_f32_e32 v7, 1.0, v7
	v_add_f32_e32 v14, 1.0, v14
	v_add_f32_e32 v15, 1.0, v15
	v_rcp_f32_e32 v14, v14
	v_rcp_f32_e32 v15, v15
	v_rcp_f32_e32 v107, v7
	v_pk_mul_f32 v[12:13], v[100:101], v[104:105]
	s_waitcnt vmcnt(0)
	v_lshlrev_b32_e32 v7, 16, v122
	v_pk_mul_f32 v[98:99], v[98:99], v[14:15]
	v_pk_mul_f32 v[14:15], v[96:97], v[106:107]
	v_cvt_pk_bf16_f32 v12, v12, v13
	v_cvt_pk_bf16_f32 v13, v102, v103
	v_mul_f32_e32 v7, 0xbfb8aa3b, v7
	v_cvt_pk_bf16_f32 v14, v14, v15
	v_cvt_pk_bf16_f32 v15, v98, v99
	global_store_dwordx4 v[128:129], v[12:15], off offset:256
	v_exp_f32_e32 v7, v7
	v_lshlrev_b32_e32 v97, 16, v125
	v_and_b32_e32 v12, 0xffff0000, v122
	v_mul_f32_e32 v12, 0xbfb8aa3b, v12
	v_exp_f32_e32 v13, v12
	v_lshlrev_b32_e32 v12, 16, v123
	v_mul_f32_e32 v12, 0xbfb8aa3b, v12
	v_exp_f32_e32 v14, v12
	v_add_f32_e32 v7, 1.0, v7
	v_rcp_f32_e32 v12, v7
	v_add_f32_e32 v7, 1.0, v13
	v_rcp_f32_e32 v13, v7
	v_add_f32_e32 v7, 1.0, v14
	v_and_b32_e32 v14, 0xffff0000, v123
	v_mul_f32_e32 v14, 0xbfb8aa3b, v14
	v_exp_f32_e32 v15, v14
	v_lshlrev_b32_e32 v14, 16, v124
	v_mul_f32_e32 v14, 0xbfb8aa3b, v14
	v_exp_f32_e32 v96, v14
	v_rcp_f32_e32 v14, v7
	v_add_f32_e32 v7, 1.0, v15
	v_rcp_f32_e32 v15, v7
	v_add_f32_e32 v7, 1.0, v96
	v_rcp_f32_e32 v96, v7
	v_and_b32_e32 v7, 0xffff0000, v124
	v_mul_f32_e32 v97, 0xbfb8aa3b, v97
	v_and_b32_e32 v98, 0xffff0000, v125
	v_mul_f32_e32 v7, 0xbfb8aa3b, v7
	v_exp_f32_e32 v97, v97
	v_mul_f32_e32 v98, 0xbfb8aa3b, v98
	v_exp_f32_e32 v7, v7
	v_exp_f32_e32 v99, v98
	v_add_f32_e32 v97, 1.0, v97
	v_rcp_f32_e32 v98, v97
	v_add_f32_e32 v7, 1.0, v7
	v_add_f32_e32 v97, 1.0, v99
	v_rcp_f32_e32 v99, v97
	v_rcp_f32_e32 v97, v7
	v_lshlrev_b32_e32 v7, 16, v0
	v_mul_f32_e32 v7, 0xbfb8aa3b, v7
	v_exp_f32_e32 v7, v7
	v_pk_mul_f32 v[12:13], v[92:93], v[12:13]
	v_pk_mul_f32 v[14:15], v[94:95], v[14:15]
	v_cvt_pk_bf16_f32 v12, v12, v13
	v_pk_mul_f32 v[90:91], v[90:91], v[98:99]
	v_pk_mul_f32 v[88:89], v[88:89], v[96:97]
	v_cvt_pk_bf16_f32 v13, v14, v15
	v_add_f32_e32 v7, 1.0, v7
	v_cvt_pk_bf16_f32 v14, v88, v89
	v_cvt_pk_bf16_f32 v15, v90, v91
	global_store_dwordx4 v[120:121], v[12:15], off offset:256
	v_and_b32_e32 v0, 0xffff0000, v0
	v_mul_f32_e32 v0, 0xbfb8aa3b, v0
	v_lshlrev_b32_e32 v12, 16, v1
	v_mul_f32_e32 v12, 0xbfb8aa3b, v12
	v_exp_f32_e32 v14, v12
	v_rcp_f32_e32 v12, v7
	v_lshlrev_b32_e32 v7, 16, v2
	v_mul_f32_e32 v7, 0xbfb8aa3b, v7
	v_exp_f32_e32 v0, v0
	v_exp_f32_e32 v7, v7
	v_and_b32_e32 v1, 0xffff0000, v1
	v_mul_f32_e32 v1, 0xbfb8aa3b, v1
	v_add_f32_e32 v0, 1.0, v0
	v_add_f32_e32 v7, 1.0, v7
	v_rcp_f32_e32 v13, v0
	v_add_f32_e32 v0, 1.0, v14
	v_rcp_f32_e32 v14, v7
	v_and_b32_e32 v2, 0xffff0000, v2
	v_lshlrev_b32_e32 v7, 16, v3
	v_and_b32_e32 v3, 0xffff0000, v3
	v_exp_f32_e32 v1, v1
	v_mul_f32_e32 v2, 0xbfb8aa3b, v2
	v_mul_f32_e32 v7, 0xbfb8aa3b, v7
	v_mul_f32_e32 v3, 0xbfb8aa3b, v3
	v_exp_f32_e32 v2, v2
	v_exp_f32_e32 v7, v7
	v_exp_f32_e32 v3, v3
	v_add_f32_e32 v1, 1.0, v1
	v_rcp_f32_e32 v0, v0
	v_rcp_f32_e32 v1, v1
	v_add_f32_e32 v15, 1.0, v2
	v_add_f32_e32 v2, 1.0, v7
	v_add_f32_e32 v3, 1.0, v3
	v_rcp_f32_e32 v2, v2
	v_rcp_f32_e32 v3, v3
	v_rcp_f32_e32 v15, v15
	v_pk_mul_f32 v[86:87], v[86:87], v[0:1]
	v_pk_mul_f32 v[0:1], v[84:85], v[12:13]
	v_pk_mul_f32 v[12:13], v[82:83], v[2:3]
	v_pk_mul_f32 v[2:3], v[80:81], v[14:15]
	v_cvt_pk_bf16_f32 v0, v0, v1
	v_cvt_pk_bf16_f32 v1, v86, v87
	v_add_u32_e32 v98, 0x80, v6
	v_cvt_pk_bf16_f32 v2, v2, v3
	v_cvt_pk_bf16_f32 v3, v12, v13
	global_store_dwordx4 v[112:113], v[0:3], off offset:256
	v_add_u32_e32 v100, 0x90, v6
	v_add_u32_e32 v82, 0xb0, v6
	v_mad_i64_i32 v[0:1], s[30:31], v98, s59, v[8:9]
	v_lshl_add_u64 v[12:13], v[0:1], 0, s[16:17]
	v_lshl_add_u64 v[0:1], v[12:13], 0, v[4:5]
	global_load_dwordx4 v[86:89], v[0:1], off
	v_mad_i64_i32 v[0:1], s[30:31], v100, s59, v[8:9]
	v_lshl_add_u64 v[14:15], v[0:1], 0, s[16:17]
	v_lshl_add_u64 v[0:1], v[14:15], 0, v[4:5]
	global_load_dwordx4 v[90:93], v[0:1], off
	v_add_u32_e32 v84, 0xa0, v6
	v_mad_i64_i32 v[2:3], s[30:31], v82, s59, v[8:9]
	v_mad_i64_i32 v[0:1], s[30:31], v84, s59, v[8:9]
	v_lshl_add_u64 v[6:7], v[2:3], 0, s[16:17]
	v_lshl_add_u64 v[80:81], v[0:1], 0, s[16:17]
	v_lshl_add_u64 v[0:1], v[80:81], 0, v[4:5]
	v_ashrrev_i32_e32 v99, 31, v98
	v_ashrrev_i32_e32 v101, 31, v100
	v_ashrrev_i32_e32 v85, 31, v84
	v_ashrrev_i32_e32 v83, 31, v82
	s_mov_b64 s[30:31], s[24:25]
	s_waitcnt vmcnt(0)
	v_lshlrev_b32_e32 v2, 16, v86
	v_mul_f32_e32 v2, 0xbfb8aa3b, v2
	v_exp_f32_e32 v8, v2
	v_lshl_add_u64 v[2:3], v[6:7], 0, v[4:5]
	global_load_dwordx4 v[94:97], v[0:1], off
	s_nop 0
	global_load_dwordx4 v[0:3], v[2:3], off
	v_and_b32_e32 v9, 0xffff0000, v86
	v_lshlrev_b32_e32 v102, 16, v88
	v_and_b32_e32 v88, 0xffff0000, v88
	v_lshlrev_b32_e32 v103, 16, v89
	v_and_b32_e32 v89, 0xffff0000, v89
	v_mul_f32_e32 v9, 0xbfb8aa3b, v9
	v_lshlrev_b32_e32 v86, 16, v87
	v_and_b32_e32 v87, 0xffff0000, v87
	v_mul_f32_e32 v102, 0xbfb8aa3b, v102
	v_mul_f32_e32 v88, 0xbfb8aa3b, v88
	v_mul_f32_e32 v103, 0xbfb8aa3b, v103
	v_mul_f32_e32 v89, 0xbfb8aa3b, v89
	v_exp_f32_e32 v9, v9
	v_mul_f32_e32 v86, 0xbfb8aa3b, v86
	v_mul_f32_e32 v87, 0xbfb8aa3b, v87
	v_exp_f32_e32 v102, v102
	v_exp_f32_e32 v88, v88
	v_exp_f32_e32 v103, v103
	v_exp_f32_e32 v89, v89
	v_exp_f32_e32 v86, v86
	v_exp_f32_e32 v87, v87
	v_add_f32_e32 v8, 1.0, v8
	v_add_f32_e32 v9, 1.0, v9
	v_add_f32_e32 v102, 1.0, v102
	v_add_f32_e32 v104, 1.0, v88
	v_add_f32_e32 v88, 1.0, v103
	v_add_f32_e32 v89, 1.0, v89
	v_rcp_f32_e32 v8, v8
	v_rcp_f32_e32 v9, v9
	v_add_f32_e32 v86, 1.0, v86
	v_add_f32_e32 v87, 1.0, v87
	v_rcp_f32_e32 v102, v102
	v_rcp_f32_e32 v88, v88
	v_rcp_f32_e32 v89, v89
	v_rcp_f32_e32 v103, v104
	v_rcp_f32_e32 v86, v86
	v_rcp_f32_e32 v87, v87
	v_pk_mul_f32 v[8:9], v[76:77], v[8:9]
	v_pk_mul_f32 v[76:77], v[74:75], v[88:89]
	v_pk_mul_f32 v[74:75], v[72:73], v[102:103]
	v_pk_mul_f32 v[78:79], v[78:79], v[86:87]
	v_cvt_pk_bf16_f32 v72, v8, v9
	v_lshlrev_b64 v[8:9], 12, v[98:99]
	v_cvt_pk_bf16_f32 v73, v78, v79
	v_cvt_pk_bf16_f32 v74, v74, v75
	v_cvt_pk_bf16_f32 v75, v76, v77
	v_lshlrev_b32_e32 v76, 16, v90
	v_mul_f32_e32 v76, 0xbfb8aa3b, v76
	v_lshl_add_u64 v[8:9], s[6:7], 0, v[8:9]
	v_exp_f32_e32 v76, v76
	v_lshl_add_u64 v[8:9], v[8:9], 0, v[4:5]
	global_store_dwordx4 v[8:9], v[72:75], off
	v_lshlrev_b32_e32 v78, 16, v93
	v_and_b32_e32 v79, 0xffff0000, v93
	v_lshlrev_b32_e32 v74, 16, v91
	v_and_b32_e32 v75, 0xffff0000, v91
	v_and_b32_e32 v73, 0xffff0000, v90
	v_mul_f32_e32 v74, 0xbfb8aa3b, v74
	v_mul_f32_e32 v75, 0xbfb8aa3b, v75
	v_mul_f32_e32 v73, 0xbfb8aa3b, v73
	v_exp_f32_e32 v74, v74
	v_exp_f32_e32 v75, v75
	v_mul_f32_e32 v78, 0xbfb8aa3b, v78
	v_mul_f32_e32 v79, 0xbfb8aa3b, v79
	v_add_f32_e32 v72, 1.0, v76
	v_exp_f32_e32 v73, v73
	v_lshlrev_b32_e32 v76, 16, v92
	v_and_b32_e32 v77, 0xffff0000, v92
	v_exp_f32_e32 v78, v78
	v_exp_f32_e32 v79, v79
	v_mul_f32_e32 v76, 0xbfb8aa3b, v76
	v_mul_f32_e32 v77, 0xbfb8aa3b, v77
	v_exp_f32_e32 v76, v76
	v_exp_f32_e32 v77, v77
	v_add_f32_e32 v74, 1.0, v74
	v_add_f32_e32 v75, 1.0, v75
	v_add_f32_e32 v73, 1.0, v73
	v_rcp_f32_e32 v74, v74
	v_rcp_f32_e32 v75, v75
	v_add_f32_e32 v78, 1.0, v78
	v_add_f32_e32 v79, 1.0, v79
	v_rcp_f32_e32 v72, v72
	v_rcp_f32_e32 v73, v73
	v_rcp_f32_e32 v78, v78
	v_rcp_f32_e32 v79, v79
	v_add_f32_e32 v76, 1.0, v76
	v_add_f32_e32 v77, 1.0, v77
	v_rcp_f32_e32 v76, v76
	v_rcp_f32_e32 v77, v77
	v_pk_mul_f32 v[70:71], v[70:71], v[74:75]
	v_pk_mul_f32 v[68:69], v[68:69], v[72:73]
	v_pk_mul_f32 v[72:73], v[66:67], v[78:79]
	v_cvt_pk_bf16_f32 v66, v68, v69
	v_cvt_pk_bf16_f32 v67, v70, v71
	s_waitcnt vmcnt(0)
	v_lshlrev_b32_e32 v70, 16, v94
	v_mul_f32_e32 v70, 0xbfb8aa3b, v70
	v_pk_mul_f32 v[64:65], v[64:65], v[76:77]
	v_exp_f32_e32 v70, v70
	v_cvt_pk_bf16_f32 v68, v64, v65
	v_lshlrev_b64 v[64:65], 12, v[100:101]
	v_lshl_add_u64 v[64:65], s[6:7], 0, v[64:65]
	v_lshl_add_u64 v[64:65], v[64:65], 0, v[4:5]
	v_cvt_pk_bf16_f32 v69, v72, v73
	global_store_dwordx4 v[64:65], v[66:69], off
	v_and_b32_e32 v71, 0xffff0000, v96
	v_mul_f32_e32 v71, 0xbfb8aa3b, v71
	v_add_f32_e32 v66, 1.0, v70
	v_and_b32_e32 v67, 0xffff0000, v94
	v_lshlrev_b32_e32 v70, 16, v96
	v_mul_f32_e32 v67, 0xbfb8aa3b, v67
	v_lshlrev_b32_e32 v68, 16, v95
	v_and_b32_e32 v69, 0xffff0000, v95
	v_mul_f32_e32 v70, 0xbfb8aa3b, v70
	v_lshlrev_b32_e32 v72, 16, v97
	v_and_b32_e32 v73, 0xffff0000, v97
	v_exp_f32_e32 v67, v67
	v_mul_f32_e32 v68, 0xbfb8aa3b, v68
	v_mul_f32_e32 v69, 0xbfb8aa3b, v69
	v_exp_f32_e32 v70, v70
	v_exp_f32_e32 v71, v71
	v_mul_f32_e32 v72, 0xbfb8aa3b, v72
	v_mul_f32_e32 v73, 0xbfb8aa3b, v73
	v_exp_f32_e32 v68, v68
	v_exp_f32_e32 v69, v69
	v_exp_f32_e32 v72, v72
	v_exp_f32_e32 v73, v73
	v_add_f32_e32 v67, 1.0, v67
	v_add_f32_e32 v70, 1.0, v70
	v_add_f32_e32 v71, 1.0, v71
	v_rcp_f32_e32 v66, v66
	v_rcp_f32_e32 v67, v67
	v_add_f32_e32 v68, 1.0, v68
	v_add_f32_e32 v69, 1.0, v69
	v_rcp_f32_e32 v70, v70
	v_add_f32_e32 v72, 1.0, v72
	v_add_f32_e32 v73, 1.0, v73
	v_rcp_f32_e32 v71, v71
	v_rcp_f32_e32 v68, v68
	v_rcp_f32_e32 v69, v69
	v_rcp_f32_e32 v72, v72
	v_rcp_f32_e32 v73, v73
	v_pk_mul_f32 v[60:61], v[60:61], v[66:67]
	v_pk_mul_f32 v[56:57], v[56:57], v[70:71]
	v_pk_mul_f32 v[62:63], v[62:63], v[68:69]
	v_pk_mul_f32 v[66:67], v[58:59], v[72:73]
	v_cvt_pk_bf16_f32 v58, v60, v61
	v_cvt_pk_bf16_f32 v59, v62, v63
	v_cvt_pk_bf16_f32 v60, v56, v57
	v_lshlrev_b64 v[56:57], 12, v[84:85]
	v_lshl_add_u64 v[56:57], s[6:7], 0, v[56:57]
	v_lshlrev_b32_e32 v62, 16, v0
	v_lshl_add_u64 v[56:57], v[56:57], 0, v[4:5]
	v_and_b32_e32 v0, 0xffff0000, v0
	v_cvt_pk_bf16_f32 v61, v66, v67
	global_store_dwordx4 v[56:57], v[58:61], off
	v_mul_f32_e32 v0, 0xbfb8aa3b, v0
	v_exp_f32_e32 v0, v0
	v_lshlrev_b32_e32 v59, 16, v1
	v_mul_f32_e32 v59, 0xbfb8aa3b, v59
	v_exp_f32_e32 v60, v59
	v_add_f32_e32 v0, 1.0, v0
	v_rcp_f32_e32 v59, v0
	v_lshlrev_b32_e32 v61, 16, v3
	v_add_f32_e32 v0, 1.0, v60
	v_lshlrev_b32_e32 v60, 16, v2
	v_and_b32_e32 v2, 0xffff0000, v2
	v_and_b32_e32 v3, 0xffff0000, v3
	v_mul_f32_e32 v62, 0xbfb8aa3b, v62
	v_mul_f32_e32 v60, 0xbfb8aa3b, v60
	v_mul_f32_e32 v2, 0xbfb8aa3b, v2
	v_mul_f32_e32 v61, 0xbfb8aa3b, v61
	v_mul_f32_e32 v3, 0xbfb8aa3b, v3
	v_exp_f32_e32 v62, v62
	v_and_b32_e32 v1, 0xffff0000, v1
	v_exp_f32_e32 v60, v60
	v_exp_f32_e32 v2, v2
	v_exp_f32_e32 v61, v61
	v_exp_f32_e32 v3, v3
	v_mul_f32_e32 v1, 0xbfb8aa3b, v1
	v_exp_f32_e32 v1, v1
	v_add_f32_e32 v58, 1.0, v62
	v_add_f32_e32 v60, 1.0, v60
	v_add_f32_e32 v62, 1.0, v2
	v_add_f32_e32 v2, 1.0, v61
	v_add_f32_e32 v3, 1.0, v3
	v_rcp_f32_e32 v60, v60
	v_rcp_f32_e32 v2, v2
	v_rcp_f32_e32 v3, v3
	v_rcp_f32_e32 v61, v62
	v_add_f32_e32 v1, 1.0, v1
	v_rcp_f32_e32 v58, v58
	v_rcp_f32_e32 v0, v0
	v_rcp_f32_e32 v1, v1
	v_pk_mul_f32 v[50:51], v[50:51], v[2:3]
	v_pk_mul_f32 v[2:3], v[48:49], v[60:61]
	v_lshlrev_b64 v[48:49], 12, v[82:83]
	v_lshl_add_u64 v[48:49], s[6:7], 0, v[48:49]
	v_pk_mul_f32 v[54:55], v[54:55], v[0:1]
	v_pk_mul_f32 v[0:1], v[52:53], v[58:59]
	v_lshl_add_u64 v[4:5], v[48:49], 0, v[4:5]
	v_cvt_pk_bf16_f32 v0, v0, v1
	v_cvt_pk_bf16_f32 v1, v54, v55
	v_cvt_pk_bf16_f32 v2, v2, v3
	v_cvt_pk_bf16_f32 v3, v50, v51
	global_store_dwordx4 v[4:5], v[0:3], off
	s_nop 1
	v_lshl_add_u64 v[0:1], v[12:13], 0, v[10:11]
	global_load_dwordx4 v[48:51], v[0:1], off
	v_lshl_add_u64 v[0:1], v[14:15], 0, v[10:11]
	global_load_dwordx4 v[12:15], v[0:1], off
	v_lshl_add_u64 v[0:1], v[80:81], 0, v[10:11]
	s_waitcnt vmcnt(0)
	v_lshlrev_b32_e32 v2, 16, v48
	v_mul_f32_e32 v2, 0xbfb8aa3b, v2
	v_exp_f32_e32 v58, v2
	v_lshl_add_u64 v[2:3], v[6:7], 0, v[10:11]
	global_load_dwordx4 v[52:55], v[0:1], off
	s_nop 0
	global_load_dwordx4 v[0:3], v[2:3], off
	v_and_b32_e32 v7, 0xffff0000, v48
	v_lshlrev_b32_e32 v10, 16, v49
	v_and_b32_e32 v11, 0xffff0000, v49
	v_lshlrev_b32_e32 v48, 16, v50
	v_and_b32_e32 v49, 0xffff0000, v50
	v_lshlrev_b32_e32 v50, 16, v51
	v_and_b32_e32 v51, 0xffff0000, v51
	v_mul_f32_e32 v7, 0xbfb8aa3b, v7
	v_mul_f32_e32 v48, 0xbfb8aa3b, v48
	v_mul_f32_e32 v49, 0xbfb8aa3b, v49
	v_mul_f32_e32 v50, 0xbfb8aa3b, v50
	v_mul_f32_e32 v51, 0xbfb8aa3b, v51
	v_exp_f32_e32 v7, v7
	v_mul_f32_e32 v10, 0xbfb8aa3b, v10
	v_mul_f32_e32 v11, 0xbfb8aa3b, v11
	v_exp_f32_e32 v48, v48
	v_exp_f32_e32 v49, v49
	v_exp_f32_e32 v50, v50
	v_exp_f32_e32 v51, v51
	v_exp_f32_e32 v10, v10
	v_exp_f32_e32 v11, v11
	v_add_f32_e32 v6, 1.0, v58
	v_add_f32_e32 v7, 1.0, v7
	v_add_f32_e32 v48, 1.0, v48
	v_add_f32_e32 v49, 1.0, v49
	v_add_f32_e32 v50, 1.0, v50
	v_add_f32_e32 v51, 1.0, v51
	v_rcp_f32_e32 v6, v6
	v_rcp_f32_e32 v7, v7
	v_add_f32_e32 v10, 1.0, v10
	v_add_f32_e32 v11, 1.0, v11
	v_rcp_f32_e32 v48, v48
	v_rcp_f32_e32 v50, v50
	v_rcp_f32_e32 v51, v51
	v_rcp_f32_e32 v49, v49
	v_rcp_f32_e32 v10, v10
	v_rcp_f32_e32 v11, v11
	v_pk_mul_f32 v[6:7], v[44:45], v[6:7]
	v_pk_mul_f32 v[44:45], v[42:43], v[50:51]
	v_pk_mul_f32 v[42:43], v[40:41], v[48:49]
	v_pk_mul_f32 v[10:11], v[46:47], v[10:11]
	v_cvt_pk_bf16_f32 v40, v6, v7
	v_lshlrev_b32_e32 v6, 16, v12
	v_cvt_pk_bf16_f32 v41, v10, v11
	v_cvt_pk_bf16_f32 v42, v42, v43
	v_cvt_pk_bf16_f32 v43, v44, v45
	global_store_dwordx4 v[8:9], v[40:43], off offset:256
	v_and_b32_e32 v7, 0xffff0000, v12
	v_lshlrev_b32_e32 v8, 16, v13
	v_and_b32_e32 v9, 0xffff0000, v13
	v_mul_f32_e32 v6, 0xbfb8aa3b, v6
	v_mul_f32_e32 v7, 0xbfb8aa3b, v7
	v_mul_f32_e32 v8, 0xbfb8aa3b, v8
	v_mul_f32_e32 v9, 0xbfb8aa3b, v9
	v_exp_f32_e32 v6, v6
	v_exp_f32_e32 v7, v7
	v_exp_f32_e32 v8, v8
	v_exp_f32_e32 v9, v9
	v_lshlrev_b32_e32 v10, 16, v14
	v_and_b32_e32 v11, 0xffff0000, v14
	v_lshlrev_b32_e32 v12, 16, v15
	v_and_b32_e32 v13, 0xffff0000, v15
	v_mul_f32_e32 v10, 0xbfb8aa3b, v10
	v_mul_f32_e32 v11, 0xbfb8aa3b, v11
	v_mul_f32_e32 v12, 0xbfb8aa3b, v12
	v_mul_f32_e32 v13, 0xbfb8aa3b, v13
	v_exp_f32_e32 v10, v10
	v_exp_f32_e32 v11, v11
	v_exp_f32_e32 v12, v12
	v_exp_f32_e32 v13, v13
	v_add_f32_e32 v6, 1.0, v6
	v_add_f32_e32 v7, 1.0, v7
	v_add_f32_e32 v8, 1.0, v8
	v_add_f32_e32 v9, 1.0, v9
	v_rcp_f32_e32 v6, v6
	v_rcp_f32_e32 v7, v7
	v_rcp_f32_e32 v8, v8
	v_rcp_f32_e32 v9, v9
	v_add_f32_e32 v10, 1.0, v10
	v_add_f32_e32 v11, 1.0, v11
	v_add_f32_e32 v12, 1.0, v12
	v_add_f32_e32 v13, 1.0, v13
	v_rcp_f32_e32 v10, v10
	v_rcp_f32_e32 v12, v12
	v_rcp_f32_e32 v13, v13
	v_rcp_f32_e32 v11, v11
	v_pk_mul_f32 v[8:9], v[38:39], v[8:9]
	v_pk_mul_f32 v[6:7], v[36:37], v[6:7]
	v_pk_mul_f32 v[12:13], v[34:35], v[12:13]
	v_cvt_pk_bf16_f32 v6, v6, v7
	v_cvt_pk_bf16_f32 v7, v8, v9
	s_waitcnt vmcnt(0)
	v_lshlrev_b32_e32 v8, 16, v52
	v_mul_f32_e32 v8, 0xbfb8aa3b, v8
	v_pk_mul_f32 v[10:11], v[32:33], v[10:11]
	v_exp_f32_e32 v14, v8
	v_cvt_pk_bf16_f32 v8, v10, v11
	v_cvt_pk_bf16_f32 v9, v12, v13
	global_store_dwordx4 v[64:65], v[6:9], off offset:256
	v_lshlrev_b32_e32 v10, 16, v54
	v_and_b32_e32 v11, 0xffff0000, v54
	v_and_b32_e32 v7, 0xffff0000, v52
	v_lshlrev_b32_e32 v8, 16, v53
	v_and_b32_e32 v9, 0xffff0000, v53
	v_mul_f32_e32 v7, 0xbfb8aa3b, v7
	v_mul_f32_e32 v8, 0xbfb8aa3b, v8
	v_mul_f32_e32 v9, 0xbfb8aa3b, v9
	v_exp_f32_e32 v7, v7
	v_exp_f32_e32 v8, v8
	v_exp_f32_e32 v9, v9
	v_lshlrev_b32_e32 v12, 16, v55
	v_and_b32_e32 v13, 0xffff0000, v55
	v_mul_f32_e32 v10, 0xbfb8aa3b, v10
	v_mul_f32_e32 v11, 0xbfb8aa3b, v11
	v_mul_f32_e32 v12, 0xbfb8aa3b, v12
	v_mul_f32_e32 v13, 0xbfb8aa3b, v13
	v_exp_f32_e32 v10, v10
	v_exp_f32_e32 v11, v11
	v_exp_f32_e32 v12, v12
	v_exp_f32_e32 v13, v13
	v_add_f32_e32 v6, 1.0, v14
	v_add_f32_e32 v7, 1.0, v7
	v_add_f32_e32 v8, 1.0, v8
	v_add_f32_e32 v9, 1.0, v9
	v_rcp_f32_e32 v6, v6
	v_rcp_f32_e32 v7, v7
	v_rcp_f32_e32 v8, v8
	v_rcp_f32_e32 v9, v9
	v_add_f32_e32 v10, 1.0, v10
	v_add_f32_e32 v11, 1.0, v11
	v_add_f32_e32 v12, 1.0, v12
	v_add_f32_e32 v13, 1.0, v13
	v_rcp_f32_e32 v10, v10
	v_rcp_f32_e32 v12, v12
	v_rcp_f32_e32 v13, v13
	v_rcp_f32_e32 v11, v11
	v_pk_mul_f32 v[8:9], v[30:31], v[8:9]
	v_pk_mul_f32 v[6:7], v[28:29], v[6:7]
	v_pk_mul_f32 v[12:13], v[26:27], v[12:13]
	v_cvt_pk_bf16_f32 v6, v6, v7
	v_cvt_pk_bf16_f32 v7, v8, v9
	v_lshlrev_b32_e32 v8, 16, v0
	v_mul_f32_e32 v8, 0xbfb8aa3b, v8
	v_and_b32_e32 v0, 0xffff0000, v0
	v_pk_mul_f32 v[10:11], v[24:25], v[10:11]
	v_exp_f32_e32 v14, v8
	v_cvt_pk_bf16_f32 v8, v10, v11
	v_cvt_pk_bf16_f32 v9, v12, v13
	global_store_dwordx4 v[56:57], v[6:9], off offset:256
	v_mul_f32_e32 v0, 0xbfb8aa3b, v0
	v_exp_f32_e32 v0, v0
	v_lshlrev_b32_e32 v7, 16, v1
	v_mul_f32_e32 v7, 0xbfb8aa3b, v7
	v_exp_f32_e32 v8, v7
	v_add_f32_e32 v0, 1.0, v0
	v_rcp_f32_e32 v7, v0
	v_and_b32_e32 v1, 0xffff0000, v1
	v_add_f32_e32 v0, 1.0, v8
	v_lshlrev_b32_e32 v8, 16, v2
	v_and_b32_e32 v2, 0xffff0000, v2
	v_lshlrev_b32_e32 v9, 16, v3
	v_and_b32_e32 v3, 0xffff0000, v3
	v_mul_f32_e32 v1, 0xbfb8aa3b, v1
	v_mul_f32_e32 v8, 0xbfb8aa3b, v8
	v_mul_f32_e32 v2, 0xbfb8aa3b, v2
	v_mul_f32_e32 v9, 0xbfb8aa3b, v9
	v_mul_f32_e32 v3, 0xbfb8aa3b, v3
	v_exp_f32_e32 v1, v1
	v_exp_f32_e32 v8, v8
	v_exp_f32_e32 v2, v2
	v_exp_f32_e32 v9, v9
	v_exp_f32_e32 v3, v3
	v_add_f32_e32 v6, 1.0, v14
	v_add_f32_e32 v1, 1.0, v1
	v_add_f32_e32 v8, 1.0, v8
	v_add_f32_e32 v10, 1.0, v2
	v_add_f32_e32 v2, 1.0, v9
	v_add_f32_e32 v3, 1.0, v3
	v_rcp_f32_e32 v6, v6
	v_rcp_f32_e32 v0, v0
	v_rcp_f32_e32 v1, v1
	v_rcp_f32_e32 v8, v8
	v_rcp_f32_e32 v2, v2
	v_rcp_f32_e32 v3, v3
	v_rcp_f32_e32 v9, v10
	v_pk_mul_f32 v[10:11], v[22:23], v[0:1]
	v_pk_mul_f32 v[0:1], v[20:21], v[6:7]
	v_pk_mul_f32 v[6:7], v[18:19], v[2:3]
	v_pk_mul_f32 v[2:3], v[16:17], v[8:9]
	v_cvt_pk_bf16_f32 v0, v0, v1
	v_cvt_pk_bf16_f32 v1, v10, v11
	s_nop 0
	v_cvt_pk_bf16_f32 v2, v2, v3
	v_cvt_pk_bf16_f32 v3, v6, v7
	global_store_dwordx4 v[4:5], v[0:3], off offset:256
	s_cbranch_vccz .LBB0_1018
	s_waitcnt vmcnt(0)
	s_cmpk_gt_u32 s33, 0xff
	s_cbranch_scc1 .LBB0_1029
	s_barrier

.LBB0_1041:
	ds_read_b128 v[0:3], v193
	ds_read_b128 v[4:7], v197
	ds_read_b128 v[8:11], v198
	ds_read_b128 v[12:15], v199
	s_add_u32 s28, s26, 0x80
	s_addc_u32 s29, s27, 0
	s_cmp_eq_u32 s59, 4
	s_cselect_b32 s31, s19, s29
	s_cselect_b32 s30, s55, s28
	s_cselect_b32 s29, s21, s58
	s_cselect_b32 s28, s56, s57
	v_lshl_add_u64 v[160:161], s[26:27], 0, v[158:159]
	s_add_i32 m0, s1, 0xc000
	ds_read_b128 v[164:167], v210
	ds_read_b128 v[168:171], v210 offset:1024
	ds_read_b128 v[172:175], v210 offset:2048
	ds_read_b128 v[176:179], v210 offset:3072
	ds_read_b128 v[180:183], v210 offset:4096
	ds_read_b128 v[184:187], v210 offset:5120
	ds_read_b128 v[214:217], v210 offset:6144
	ds_read_b128 v[218:221], v210 offset:7168
	global_load_lds_dwordx4 v[160:161], off
	v_lshl_add_u64 v[160:161], s[26:27], 0, v[156:157]
	s_add_i32 m0, s1, 0xe000
	s_nop 0
	global_load_lds_dwordx4 v[160:161], off
	s_waitcnt lgkmcnt(8)
	s_barrier
	s_waitcnt lgkmcnt(0)
	s_waitcnt lgkmcnt(0)
	v_mfma_scale_f32_16x16x128_f8f6f4 v[140:143], v[0:7], v[164:171], v[140:143], v211, v212 op_sel_hi:[0,0,0]
	v_mfma_scale_f32_16x16x128_f8f6f4 v[136:139], v[8:15], v[164:171], v[136:139], v211, v212 op_sel_hi:[0,0,0]
	v_mfma_scale_f32_16x16x128_f8f6f4 v[132:135], v[0:7], v[172:179], v[132:135], v211, v212 op_sel_hi:[0,0,0]
	v_mfma_scale_f32_16x16x128_f8f6f4 v[128:131], v[8:15], v[172:179], v[128:131], v211, v212 op_sel_hi:[0,0,0]
	v_mfma_scale_f32_16x16x128_f8f6f4 v[124:127], v[0:7], v[180:187], v[124:127], v211, v212 op_sel_hi:[0,0,0]
	v_mfma_scale_f32_16x16x128_f8f6f4 v[120:123], v[8:15], v[180:187], v[120:123], v211, v212 op_sel_hi:[0,0,0]
	v_mfma_scale_f32_16x16x128_f8f6f4 v[116:119], v[0:7], v[214:221], v[116:119], v211, v212 op_sel_hi:[0,0,0]
	v_mfma_scale_f32_16x16x128_f8f6f4 v[112:115], v[8:15], v[214:221], v[112:115], v211, v212 op_sel_hi:[0,0,0]
	s_barrier
	s_mov_b32 m0, s38
	v_lshl_add_u64 v[160:161], s[28:29], 0, v[144:145]
	ds_read_b128 v[222:225], v194
	ds_read_b128 v[226:229], v200
	ds_read_b128 v[230:233], v201
	ds_read_b128 v[234:237], v202
	global_load_lds_dwordx4 v[160:161], off
	v_lshl_add_u64 v[162:163], s[28:29], 0, v[146:147]
	s_mov_b32 m0, s39
	s_nop 0
	global_load_lds_dwordx4 v[162:163], off
	s_barrier
	s_waitcnt lgkmcnt(0)
	s_waitcnt lgkmcnt(0)
	v_mfma_scale_f32_16x16x128_f8f6f4 v[108:111], v[222:229], v[164:171], v[108:111], v211, v212 op_sel_hi:[0,0,0]
	v_mfma_scale_f32_16x16x128_f8f6f4 v[104:107], v[230:237], v[164:171], v[104:107], v211, v212 op_sel_hi:[0,0,0]
	v_mfma_scale_f32_16x16x128_f8f6f4 v[100:103], v[222:229], v[172:179], v[100:103], v211, v212 op_sel_hi:[0,0,0]
	v_mfma_scale_f32_16x16x128_f8f6f4 v[96:99], v[230:237], v[172:179], v[96:99], v211, v212 op_sel_hi:[0,0,0]
	v_mfma_scale_f32_16x16x128_f8f6f4 v[92:95], v[222:229], v[180:187], v[92:95], v211, v212 op_sel_hi:[0,0,0]
	v_mfma_scale_f32_16x16x128_f8f6f4 v[88:91], v[230:237], v[180:187], v[88:91], v211, v212 op_sel_hi:[0,0,0]
	v_mfma_scale_f32_16x16x128_f8f6f4 v[84:87], v[222:229], v[214:221], v[84:87], v211, v212 op_sel_hi:[0,0,0]
	v_mfma_scale_f32_16x16x128_f8f6f4 v[80:83], v[230:237], v[214:221], v[80:83], v211, v212 op_sel_hi:[0,0,0]
	s_mov_b32 m0, s1
	v_lshl_add_u64 v[164:165], s[30:31], 0, v[148:149]
	s_barrier
	ds_read_b128 v[168:171], v210 offset:16384
	ds_read_b128 v[172:175], v210 offset:17408
	ds_read_b128 v[176:179], v210 offset:18432
	ds_read_b128 v[180:183], v210 offset:19456
	ds_read_b128 v[184:187], v210 offset:20480
	ds_read_b128 v[188:191], v210 offset:21504
	ds_read_b128 v[214:217], v210 offset:22528
	ds_read_b128 v[218:221], v210 offset:23552
	global_load_lds_dwordx4 v[164:165], off
	v_lshl_add_u64 v[166:167], s[30:31], 0, v[150:151]
	s_mov_b32 m0, s40
	s_nop 0
	global_load_lds_dwordx4 v[166:167], off
	s_barrier
	s_waitcnt lgkmcnt(0)
	s_waitcnt lgkmcnt(0)
	v_mfma_scale_f32_16x16x128_f8f6f4 v[76:79], v[0:7], v[168:175], v[76:79], v211, v212 op_sel_hi:[0,0,0]
	v_mfma_scale_f32_16x16x128_f8f6f4 v[72:75], v[8:15], v[168:175], v[72:75], v211, v212 op_sel_hi:[0,0,0]
	v_mfma_scale_f32_16x16x128_f8f6f4 v[68:71], v[0:7], v[176:183], v[68:71], v211, v212 op_sel_hi:[0,0,0]
	v_mfma_scale_f32_16x16x128_f8f6f4 v[64:67], v[8:15], v[176:183], v[64:67], v211, v212 op_sel_hi:[0,0,0]
	v_mfma_scale_f32_16x16x128_f8f6f4 v[60:63], v[0:7], v[184:191], v[60:63], v211, v212 op_sel_hi:[0,0,0]
	v_mfma_scale_f32_16x16x128_f8f6f4 v[56:59], v[8:15], v[184:191], v[56:59], v211, v212 op_sel_hi:[0,0,0]
	v_mfma_scale_f32_16x16x128_f8f6f4 v[52:55], v[0:7], v[214:221], v[52:55], v211, v212 op_sel_hi:[0,0,0]
	v_mfma_scale_f32_16x16x128_f8f6f4 v[48:51], v[8:15], v[214:221], v[48:51], v211, v212 op_sel_hi:[0,0,0]
	s_barrier
	s_add_u32 s60, s28, 0x20000
	s_addc_u32 s61, s29, 0
	s_mov_b32 m0, s41
	v_lshl_add_u64 v[0:1], s[60:61], 0, v[144:145]
	global_load_lds_dwordx4 v[0:1], off
	v_lshl_add_u64 v[0:1], s[60:61], 0, v[146:147]
	s_mov_b32 m0, s42
	s_nop 0
	global_load_lds_dwordx4 v[0:1], off
	s_waitcnt vmcnt(6)
	s_barrier
	v_mfma_scale_f32_16x16x128_f8f6f4 v[44:47], v[222:229], v[168:175], v[44:47], v211, v212 op_sel_hi:[0,0,0]
	v_mfma_scale_f32_16x16x128_f8f6f4 v[40:43], v[230:237], v[168:175], v[40:43], v211, v212 op_sel_hi:[0,0,0]
	v_mfma_scale_f32_16x16x128_f8f6f4 v[36:39], v[222:229], v[176:183], v[36:39], v211, v212 op_sel_hi:[0,0,0]
	v_mfma_scale_f32_16x16x128_f8f6f4 v[32:35], v[230:237], v[176:183], v[32:35], v211, v212 op_sel_hi:[0,0,0]
	v_mfma_scale_f32_16x16x128_f8f6f4 v[28:31], v[222:229], v[184:191], v[28:31], v211, v212 op_sel_hi:[0,0,0]
	v_mfma_scale_f32_16x16x128_f8f6f4 v[24:27], v[230:237], v[184:191], v[24:27], v211, v212 op_sel_hi:[0,0,0]
	v_mfma_scale_f32_16x16x128_f8f6f4 v[20:23], v[222:229], v[214:221], v[20:23], v211, v212 op_sel_hi:[0,0,0]
	v_mfma_scale_f32_16x16x128_f8f6f4 v[16:19], v[230:237], v[214:221], v[16:19], v211, v212 op_sel_hi:[0,0,0]
	s_barrier
	ds_read_b128 v[0:3], v195
	ds_read_b128 v[4:7], v203
	ds_read_b128 v[8:11], v204
	ds_read_b128 v[12:15], v205
	s_mov_b32 m0, s43
	v_lshl_add_u64 v[222:223], s[30:31], 0, v[152:153]
	ds_read_b128 v[168:171], v210 offset:32768
	ds_read_b128 v[172:175], v210 offset:33792
	ds_read_b128 v[176:179], v210 offset:34816
	ds_read_b128 v[180:183], v210 offset:35840
	ds_read_b128 v[184:187], v210 offset:36864
	ds_read_b128 v[188:191], v210 offset:37888
	ds_read_b128 v[214:217], v210 offset:38912
	ds_read_b128 v[218:221], v210 offset:39936
	global_load_lds_dwordx4 v[222:223], off
	v_lshl_add_u64 v[222:223], s[30:31], 0, v[154:155]
	s_mov_b32 m0, s44
	s_nop 0
	global_load_lds_dwordx4 v[222:223], off
	s_waitcnt lgkmcnt(8)
	s_barrier
	s_waitcnt lgkmcnt(0)
	s_waitcnt lgkmcnt(0)
	v_mfma_scale_f32_16x16x128_f8f6f4 v[140:143], v[0:7], v[168:175], v[140:143], v211, v212 op_sel_hi:[0,0,0]
	v_mfma_scale_f32_16x16x128_f8f6f4 v[136:139], v[8:15], v[168:175], v[136:139], v211, v212 op_sel_hi:[0,0,0]
	v_mfma_scale_f32_16x16x128_f8f6f4 v[132:135], v[0:7], v[176:183], v[132:135], v211, v212 op_sel_hi:[0,0,0]
	v_mfma_scale_f32_16x16x128_f8f6f4 v[128:131], v[8:15], v[176:183], v[128:131], v211, v212 op_sel_hi:[0,0,0]
	v_mfma_scale_f32_16x16x128_f8f6f4 v[124:127], v[0:7], v[184:191], v[124:127], v211, v212 op_sel_hi:[0,0,0]
	v_mfma_scale_f32_16x16x128_f8f6f4 v[120:123], v[8:15], v[184:191], v[120:123], v211, v212 op_sel_hi:[0,0,0]
	v_mfma_scale_f32_16x16x128_f8f6f4 v[116:119], v[0:7], v[214:221], v[116:119], v211, v212 op_sel_hi:[0,0,0]
	v_mfma_scale_f32_16x16x128_f8f6f4 v[112:115], v[8:15], v[214:221], v[112:115], v211, v212 op_sel_hi:[0,0,0]
	s_barrier
	s_mov_b32 m0, s46
	v_lshl_add_u64 v[160:161], v[160:161], 0, s[12:13]
	ds_read_b128 v[222:225], v196
	ds_read_b128 v[226:229], v206
	ds_read_b128 v[230:233], v207
	ds_read_b128 v[234:237], v208
	global_load_lds_dwordx4 v[160:161], off
	v_lshl_add_u64 v[160:161], v[162:163], 0, s[12:13]
	s_mov_b32 m0, s47
	s_nop 0
	global_load_lds_dwordx4 v[160:161], off
	s_barrier
	s_waitcnt lgkmcnt(0)
	s_waitcnt lgkmcnt(0)
	v_mfma_scale_f32_16x16x128_f8f6f4 v[108:111], v[222:229], v[168:175], v[108:111], v211, v212 op_sel_hi:[0,0,0]
	v_mfma_scale_f32_16x16x128_f8f6f4 v[104:107], v[230:237], v[168:175], v[104:107], v211, v212 op_sel_hi:[0,0,0]
	v_mfma_scale_f32_16x16x128_f8f6f4 v[100:103], v[222:229], v[176:183], v[100:103], v211, v212 op_sel_hi:[0,0,0]
	v_mfma_scale_f32_16x16x128_f8f6f4 v[96:99], v[230:237], v[176:183], v[96:99], v211, v212 op_sel_hi:[0,0,0]
	v_mfma_scale_f32_16x16x128_f8f6f4 v[92:95], v[222:229], v[184:191], v[92:95], v211, v212 op_sel_hi:[0,0,0]
	v_mfma_scale_f32_16x16x128_f8f6f4 v[88:91], v[230:237], v[184:191], v[88:91], v211, v212 op_sel_hi:[0,0,0]
	v_mfma_scale_f32_16x16x128_f8f6f4 v[84:87], v[222:229], v[214:221], v[84:87], v211, v212 op_sel_hi:[0,0,0]
	v_mfma_scale_f32_16x16x128_f8f6f4 v[80:83], v[230:237], v[214:221], v[80:83], v211, v212 op_sel_hi:[0,0,0]
	s_mov_b32 m0, s48
	v_lshl_add_u64 v[160:161], v[164:165], 0, s[12:13]
	s_barrier
	ds_read_b128 v[168:171], v210 offset:49152
	ds_read_b128 v[172:175], v210 offset:50176
	ds_read_b128 v[176:179], v210 offset:51200
	ds_read_b128 v[180:183], v210 offset:52224
	ds_read_b128 v[184:187], v210 offset:53248
	ds_read_b128 v[188:191], v210 offset:54272
	ds_read_b128 v[214:217], v210 offset:55296
	ds_read_b128 v[218:221], v210 offset:56320
	global_load_lds_dwordx4 v[160:161], off
	v_lshl_add_u64 v[160:161], v[166:167], 0, s[12:13]
	s_mov_b32 m0, s49
	s_nop 0
	global_load_lds_dwordx4 v[160:161], off
	s_barrier
	s_waitcnt lgkmcnt(0)
	s_waitcnt lgkmcnt(0)
	v_mfma_scale_f32_16x16x128_f8f6f4 v[76:79], v[0:7], v[168:175], v[76:79], v211, v212 op_sel_hi:[0,0,0]
	v_mfma_scale_f32_16x16x128_f8f6f4 v[72:75], v[8:15], v[168:175], v[72:75], v211, v212 op_sel_hi:[0,0,0]
	v_mfma_scale_f32_16x16x128_f8f6f4 v[68:71], v[0:7], v[176:183], v[68:71], v211, v212 op_sel_hi:[0,0,0]
	v_mfma_scale_f32_16x16x128_f8f6f4 v[64:67], v[8:15], v[176:183], v[64:67], v211, v212 op_sel_hi:[0,0,0]
	v_mfma_scale_f32_16x16x128_f8f6f4 v[60:63], v[0:7], v[184:191], v[60:63], v211, v212 op_sel_hi:[0,0,0]
	v_mfma_scale_f32_16x16x128_f8f6f4 v[56:59], v[8:15], v[184:191], v[56:59], v211, v212 op_sel_hi:[0,0,0]
	v_mfma_scale_f32_16x16x128_f8f6f4 v[52:55], v[0:7], v[214:221], v[52:55], v211, v212 op_sel_hi:[0,0,0]
	v_mfma_scale_f32_16x16x128_f8f6f4 v[48:51], v[8:15], v[214:221], v[48:51], v211, v212 op_sel_hi:[0,0,0]
	s_barrier
	s_add_u32 s28, s28, 0x20080
	s_addc_u32 s29, s29, 0
	s_mov_b32 m0, s50
	v_lshl_add_u64 v[0:1], s[28:29], 0, v[144:145]
	global_load_lds_dwordx4 v[0:1], off
	v_lshl_add_u64 v[0:1], s[28:29], 0, v[146:147]
	s_mov_b32 m0, s51
	s_nop 0
	global_load_lds_dwordx4 v[0:1], off
	s_waitcnt vmcnt(6)
	s_barrier
	v_mfma_scale_f32_16x16x128_f8f6f4 v[44:47], v[222:229], v[168:175], v[44:47], v211, v212 op_sel_hi:[0,0,0]
	v_mfma_scale_f32_16x16x128_f8f6f4 v[40:43], v[230:237], v[168:175], v[40:43], v211, v212 op_sel_hi:[0,0,0]
	v_mfma_scale_f32_16x16x128_f8f6f4 v[36:39], v[222:229], v[176:183], v[36:39], v211, v212 op_sel_hi:[0,0,0]
	v_mfma_scale_f32_16x16x128_f8f6f4 v[32:35], v[230:237], v[176:183], v[32:35], v211, v212 op_sel_hi:[0,0,0]
	v_mfma_scale_f32_16x16x128_f8f6f4 v[28:31], v[222:229], v[184:191], v[28:31], v211, v212 op_sel_hi:[0,0,0]
	v_mfma_scale_f32_16x16x128_f8f6f4 v[24:27], v[230:237], v[184:191], v[24:27], v211, v212 op_sel_hi:[0,0,0]
	v_mfma_scale_f32_16x16x128_f8f6f4 v[20:23], v[222:229], v[214:221], v[20:23], v211, v212 op_sel_hi:[0,0,0]
	v_mfma_scale_f32_16x16x128_f8f6f4 v[16:19], v[230:237], v[214:221], v[16:19], v211, v212 op_sel_hi:[0,0,0]
	s_add_i32 s59, s59, 2
	s_add_u32 s26, s26, 0x100
	s_addc_u32 s27, s27, 0
	s_add_u32 s57, s57, 0x100
	s_addc_u32 s58, s58, 0
	s_cmp_gt_u32 s59, 5
	s_barrier
	s_cbranch_scc0 .LBB0_1041
	v_lshl_add_u32 v162, s0, 8, v192
	v_lshl_or_b32 v160, s54, 8, v209
	v_mov_b64_e32 v[166:167], s[8:9]
	v_ashrrev_i32_e32 v161, 31, v160
	v_mad_i64_i32 v[0:1], s[26:27], v162, s52, v[166:167]
	v_lshlrev_b64 v[164:165], 1, v[160:161]
	v_lshl_add_u64 v[170:171], v[0:1], 0, s[14:15]
	s_nop 15
	s_nop 15
	v_lshl_add_u64 v[0:1], v[170:171], 0, v[164:165]
	global_load_dwordx4 v[214:217], v[0:1], off
	v_ashrrev_i32_e32 v163, 31, v162
	v_lshl_add_u64 v[168:169], s[6:7], 0, v[164:165]
	v_lshlrev_b64 v[172:173], 12, v[162:163]
	v_lshl_add_u64 v[0:1], v[168:169], 0, v[172:173]
	global_load_dwordx4 v[218:221], v[0:1], off
	v_or_b32_e32 v190, 16, v162
	v_mad_i64_i32 v[0:1], s[26:27], v190, s52, v[166:167]
	v_or_b32_e32 v188, 32, v162
	v_ashrrev_i32_e32 v191, 31, v190
	v_lshl_add_u64 v[178:179], v[0:1], 0, s[14:15]
	v_mad_i64_i32 v[2:3], s[26:27], v188, s52, v[166:167]
	v_lshlrev_b64 v[184:185], 12, v[190:191]
	v_lshl_add_u64 v[0:1], v[178:179], 0, v[164:165]
	v_lshl_add_u64 v[180:181], v[2:3], 0, s[14:15]
	v_lshl_add_u64 v[2:3], v[168:169], 0, v[184:185]
	global_load_dwordx4 v[222:225], v[0:1], off
	global_load_dwordx4 v[226:229], v[2:3], off
	v_or_b32_e32 v186, 48, v162
	v_ashrrev_i32_e32 v189, 31, v188
	v_ashrrev_i32_e32 v187, 31, v186
	v_mad_i64_i32 v[4:5], s[26:27], v186, s52, v[166:167]
	v_lshlrev_b64 v[176:177], 12, v[188:189]
	v_lshl_add_u64 v[174:175], v[4:5], 0, s[14:15]
	v_lshlrev_b64 v[182:183], 12, v[186:187]
	v_lshl_add_u64 v[0:1], v[180:181], 0, v[164:165]
	v_lshl_add_u64 v[2:3], v[168:169], 0, v[176:177]
	v_lshl_add_u64 v[4:5], v[174:175], 0, v[164:165]
	v_lshl_add_u64 v[6:7], v[168:169], 0, v[182:183]
	global_load_dwordx4 v[8:11], v[0:1], off
	global_load_dwordx4 v[12:15], v[2:3], off
	s_nop 0
	global_load_dwordx4 v[0:3], v[4:5], off
	s_nop 0
	global_load_dwordx4 v[4:7], v[6:7], off
	s_and_b64 vcc, exec, s[16:17]
	s_mov_b32 s54, s20
	s_mov_b32 s0, s18
	s_mov_b64 s[28:29], s[24:25]
	s_waitcnt vmcnt(0)
	v_lshlrev_b32_e32 v230, 16, v214
	v_and_b32_e32 v231, 0xffff0000, v214
	v_mul_f32_e32 v230, 0xbfb8aa3b, v230
	v_mul_f32_e32 v231, 0xbfb8aa3b, v231
	v_lshlrev_b32_e32 v234, 16, v216
	v_and_b32_e32 v235, 0xffff0000, v216
	v_exp_f32_e32 v230, v230
	v_exp_f32_e32 v231, v231
	v_mul_f32_e32 v234, 0xbfb8aa3b, v234
	v_mul_f32_e32 v235, 0xbfb8aa3b, v235
	v_lshlrev_b32_e32 v232, 16, v215
	v_and_b32_e32 v233, 0xffff0000, v215
	v_exp_f32_e32 v234, v234
	v_exp_f32_e32 v235, v235
	v_mul_f32_e32 v232, 0xbfb8aa3b, v232
	v_mul_f32_e32 v233, 0xbfb8aa3b, v233
	v_lshlrev_b32_e32 v236, 16, v217
	v_and_b32_e32 v237, 0xffff0000, v217
	v_exp_f32_e32 v232, v232
	v_exp_f32_e32 v233, v233
	v_add_f32_e32 v230, 1.0, v230
	v_add_f32_e32 v231, 1.0, v231
	v_mul_f32_e32 v236, 0xbfb8aa3b, v236
	v_mul_f32_e32 v237, 0xbfb8aa3b, v237
	v_rcp_f32_e32 v230, v230
	v_rcp_f32_e32 v231, v231
	v_exp_f32_e32 v236, v236
	v_exp_f32_e32 v237, v237
	v_add_f32_e32 v234, 1.0, v234
	v_add_f32_e32 v235, 1.0, v235
	v_rcp_f32_e32 v234, v234
	v_rcp_f32_e32 v235, v235
	v_lshlrev_b32_e32 v214, 16, v218
	v_and_b32_e32 v215, 0xffff0000, v218
	v_add_f32_e32 v232, 1.0, v232
	v_add_f32_e32 v233, 1.0, v233
	v_rcp_f32_e32 v232, v232
	v_rcp_f32_e32 v233, v233
	v_pk_fma_f32 v[140:141], v[140:141], v[230:231], v[214:215]
	v_lshlrev_b32_e32 v216, 16, v219
	v_and_b32_e32 v217, 0xffff0000, v219
	v_lshlrev_b32_e32 v218, 16, v220
	v_and_b32_e32 v219, 0xffff0000, v220
	v_add_f32_e32 v236, 1.0, v236
	v_add_f32_e32 v237, 1.0, v237
	v_med3_f32 v141, v141, s53, v213
	v_med3_f32 v214, v140, s53, v213
	v_mov_b32_e32 v140, 0
	v_rcp_f32_e32 v236, v236
	v_rcp_f32_e32 v237, v237
	v_pk_fma_f32 v[136:137], v[136:137], v[234:235], v[218:219]
	v_cvt_pk_fp8_f32 v140, v214, v141
	v_med3_f32 v137, v137, s53, v213
	v_med3_f32 v136, v136, s53, v213
	v_mov_b32_e32 v141, 0
	v_pk_fma_f32 v[142:143], v[142:143], v[232:233], v[216:217]
	v_cvt_pk_fp8_f32 v141, v136, v137
	v_lshlrev_b32_e32 v220, 16, v221
	v_and_b32_e32 v221, 0xffff0000, v221
	v_med3_f32 v143, v143, s53, v213
	v_med3_f32 v142, v142, s53, v213
	v_pk_fma_f32 v[138:139], v[138:139], v[236:237], v[220:221]
	v_cvt_pk_fp8_f32 v140, v142, v143 op_sel:[0,0,1]
	v_lshlrev_b32_e32 v143, 16, v222
	v_and_b32_e32 v216, 0xffff0000, v222
	v_med3_f32 v136, v139, s53, v213
	v_med3_f32 v137, v138, s53, v213
	v_mul_f32_e32 v143, 0xbfb8aa3b, v143
	v_mul_f32_e32 v216, 0xbfb8aa3b, v216
	v_cvt_pk_fp8_f32 v141, v137, v136 op_sel:[0,0,1]
	v_lshlrev_b64 v[136:137], 11, v[162:163]
	v_exp_f32_e32 v163, v143
	v_exp_f32_e32 v217, v216
	v_lshlrev_b32_e32 v216, 16, v223
	v_mul_f32_e32 v216, 0xbfb8aa3b, v216
	v_exp_f32_e32 v218, v216
	v_add_f32_e32 v163, 1.0, v163
	v_rcp_f32_e32 v216, v163
	v_add_f32_e32 v163, 1.0, v217
	v_rcp_f32_e32 v217, v163
	v_add_f32_e32 v163, 1.0, v218
	v_and_b32_e32 v218, 0xffff0000, v223
	v_mul_f32_e32 v218, 0xbfb8aa3b, v218
	v_exp_f32_e32 v219, v218
	v_lshlrev_b32_e32 v218, 16, v224
	v_mul_f32_e32 v218, 0xbfb8aa3b, v218
	v_exp_f32_e32 v220, v218
	v_rcp_f32_e32 v218, v163
	v_add_f32_e32 v163, 1.0, v219
	v_rcp_f32_e32 v219, v163
	v_add_f32_e32 v163, 1.0, v220
	v_lshlrev_b32_e32 v221, 16, v225
	v_rcp_f32_e32 v220, v163
	v_and_b32_e32 v163, 0xffff0000, v224
	v_mul_f32_e32 v221, 0xbfb8aa3b, v221
	v_and_b32_e32 v222, 0xffff0000, v225
	v_mul_f32_e32 v163, 0xbfb8aa3b, v163
	v_exp_f32_e32 v221, v221
	v_mul_f32_e32 v222, 0xbfb8aa3b, v222
	v_exp_f32_e32 v163, v163
	v_exp_f32_e32 v223, v222
	v_add_f32_e32 v221, 1.0, v221
	v_rcp_f32_e32 v222, v221
	v_add_f32_e32 v163, 1.0, v163
	v_add_f32_e32 v221, 1.0, v223
	v_rcp_f32_e32 v223, v221
	v_rcp_f32_e32 v221, v163
	v_lshlrev_b32_e32 v138, 16, v226
	v_and_b32_e32 v139, 0xffff0000, v226
	v_lshlrev_b32_e32 v142, 16, v228
	v_and_b32_e32 v143, 0xffff0000, v228
	v_pk_fma_f32 v[132:133], v[132:133], v[216:217], v[138:139]
	v_pk_fma_f32 v[128:129], v[128:129], v[220:221], v[142:143]
	v_med3_f32 v133, v133, s53, v213
	v_med3_f32 v138, v132, s53, v213
	v_mov_b32_e32 v132, 0
	v_lshl_add_u64 v[136:137], s[10:11], 0, v[136:137]
	v_med3_f32 v129, v129, s53, v213
	v_med3_f32 v128, v128, s53, v213
	v_cvt_pk_fp8_f32 v132, v138, v133
	v_mov_b32_e32 v133, 0
	v_lshl_add_u64 v[136:137], v[136:137], 0, v[160:161]
	v_cvt_pk_fp8_f32 v133, v128, v129
	global_store_dwordx2 v[136:137], v[140:141], off
	v_lshlrev_b32_e32 v140, 16, v227
	v_and_b32_e32 v141, 0xffff0000, v227
	v_lshlrev_b32_e32 v214, 16, v229
	v_and_b32_e32 v215, 0xffff0000, v229
	v_pk_fma_f32 v[134:135], v[134:135], v[218:219], v[140:141]
	v_pk_fma_f32 v[130:131], v[130:131], v[222:223], v[214:215]
	v_med3_f32 v135, v135, s53, v213
	v_med3_f32 v134, v134, s53, v213
	v_med3_f32 v128, v131, s53, v213
	v_med3_f32 v129, v130, s53, v213
	v_cvt_pk_fp8_f32 v132, v134, v135 op_sel:[0,0,1]
	v_cvt_pk_fp8_f32 v133, v129, v128 op_sel:[0,0,1]
	v_lshlrev_b64 v[128:129], 11, v[190:191]
	v_lshl_add_u64 v[128:129], s[10:11], 0, v[128:129]
	v_lshl_add_u64 v[128:129], v[128:129], 0, v[160:161]
	global_store_dwordx2 v[128:129], v[132:133], off
	v_lshlrev_b32_e32 v133, 16, v8
	v_and_b32_e32 v8, 0xffff0000, v8
	v_mul_f32_e32 v8, 0xbfb8aa3b, v8
	v_lshlrev_b32_e32 v135, 16, v9
	v_exp_f32_e32 v8, v8
	v_mul_f32_e32 v135, 0xbfb8aa3b, v135
	v_exp_f32_e32 v138, v135
	v_and_b32_e32 v9, 0xffff0000, v9
	v_add_f32_e32 v8, 1.0, v8
	v_mul_f32_e32 v133, 0xbfb8aa3b, v133
	v_rcp_f32_e32 v135, v8
	v_add_f32_e32 v8, 1.0, v138
	v_mul_f32_e32 v9, 0xbfb8aa3b, v9
	v_lshlrev_b32_e32 v138, 16, v10
	v_and_b32_e32 v10, 0xffff0000, v10
	v_lshlrev_b32_e32 v139, 16, v11
	v_and_b32_e32 v11, 0xffff0000, v11
	v_exp_f32_e32 v134, v133
	v_exp_f32_e32 v9, v9
	v_mul_f32_e32 v138, 0xbfb8aa3b, v138
	v_mul_f32_e32 v10, 0xbfb8aa3b, v10
	v_mul_f32_e32 v139, 0xbfb8aa3b, v139
	v_mul_f32_e32 v11, 0xbfb8aa3b, v11
	v_exp_f32_e32 v138, v138
	v_exp_f32_e32 v10, v10
	v_exp_f32_e32 v139, v139
	v_exp_f32_e32 v11, v11
	v_add_f32_e32 v134, 1.0, v134
	v_add_f32_e32 v9, 1.0, v9
	v_rcp_f32_e32 v134, v134
	v_rcp_f32_e32 v8, v8
	v_rcp_f32_e32 v9, v9
	v_add_f32_e32 v138, 1.0, v138
	v_add_f32_e32 v140, 1.0, v10
	v_add_f32_e32 v10, 1.0, v139
	v_add_f32_e32 v11, 1.0, v11
	v_rcp_f32_e32 v138, v138
	v_rcp_f32_e32 v10, v10
	v_rcp_f32_e32 v11, v11
	v_rcp_f32_e32 v139, v140
	v_lshlrev_b32_e32 v130, 16, v12
	v_and_b32_e32 v131, 0xffff0000, v12
	v_lshlrev_b32_e32 v12, 16, v13
	v_and_b32_e32 v13, 0xffff0000, v13
	v_lshlrev_b32_e32 v132, 16, v14
	v_and_b32_e32 v133, 0xffff0000, v14
	v_lshlrev_b32_e32 v14, 16, v15
	v_and_b32_e32 v15, 0xffff0000, v15
	v_pk_fma_f32 v[8:9], v[126:127], v[8:9], v[12:13]
	v_pk_fma_f32 v[12:13], v[124:125], v[134:135], v[130:131]
	v_pk_fma_f32 v[10:11], v[122:123], v[10:11], v[14:15]
	v_pk_fma_f32 v[14:15], v[120:121], v[138:139], v[132:133]
	v_med3_f32 v120, v9, s53, v213
	v_med3_f32 v121, v8, s53, v213
	v_med3_f32 v9, v13, s53, v213
	v_med3_f32 v12, v12, s53, v213
	v_mov_b32_e32 v8, 0
	v_med3_f32 v13, v15, s53, v213
	v_med3_f32 v14, v14, s53, v213
	v_cvt_pk_fp8_f32 v8, v12, v9
	v_mov_b32_e32 v9, 0
	v_cvt_pk_fp8_f32 v9, v14, v13
	v_med3_f32 v11, v11, s53, v213
	v_med3_f32 v10, v10, s53, v213
	v_lshlrev_b32_e32 v13, 16, v1
	v_cvt_pk_fp8_f32 v9, v10, v11 op_sel:[0,0,1]
	v_lshlrev_b64 v[10:11], 11, v[188:189]
	v_lshl_add_u64 v[10:11], s[10:11], 0, v[10:11]
	v_lshl_add_u64 v[14:15], v[10:11], 0, v[160:161]
	v_lshlrev_b32_e32 v11, 16, v0
	v_and_b32_e32 v0, 0xffff0000, v0
	v_mul_f32_e32 v0, 0xbfb8aa3b, v0
	v_exp_f32_e32 v0, v0
	v_mul_f32_e32 v13, 0xbfb8aa3b, v13
	v_cvt_pk_fp8_f32 v8, v121, v120 op_sel:[0,0,1]
	v_exp_f32_e32 v120, v13
	v_add_f32_e32 v0, 1.0, v0
	v_and_b32_e32 v1, 0xffff0000, v1
	v_mul_f32_e32 v11, 0xbfb8aa3b, v11
	v_rcp_f32_e32 v13, v0
	v_add_f32_e32 v0, 1.0, v120
	v_mul_f32_e32 v1, 0xbfb8aa3b, v1
	v_lshlrev_b32_e32 v120, 16, v2
	v_and_b32_e32 v2, 0xffff0000, v2
	v_lshlrev_b32_e32 v121, 16, v3
	v_and_b32_e32 v3, 0xffff0000, v3
	v_exp_f32_e32 v12, v11
	v_exp_f32_e32 v1, v1
	v_mul_f32_e32 v120, 0xbfb8aa3b, v120
	v_mul_f32_e32 v2, 0xbfb8aa3b, v2
	v_mul_f32_e32 v121, 0xbfb8aa3b, v121
	v_mul_f32_e32 v3, 0xbfb8aa3b, v3
	v_exp_f32_e32 v120, v120
	v_exp_f32_e32 v2, v2
	v_exp_f32_e32 v121, v121
	v_exp_f32_e32 v3, v3
	v_add_f32_e32 v12, 1.0, v12
	v_add_f32_e32 v1, 1.0, v1
	v_rcp_f32_e32 v12, v12
	v_rcp_f32_e32 v0, v0
	v_rcp_f32_e32 v1, v1
	v_add_f32_e32 v120, 1.0, v120
	v_add_f32_e32 v122, 1.0, v2
	v_add_f32_e32 v2, 1.0, v121
	v_add_f32_e32 v3, 1.0, v3
	v_rcp_f32_e32 v120, v120
	v_rcp_f32_e32 v2, v2
	v_rcp_f32_e32 v3, v3
	v_rcp_f32_e32 v121, v122
	global_store_dwordx2 v[14:15], v[8:9], off
	v_lshlrev_b32_e32 v8, 16, v4
	v_and_b32_e32 v9, 0xffff0000, v4
	v_lshlrev_b32_e32 v4, 16, v5
	v_and_b32_e32 v5, 0xffff0000, v5
	v_lshlrev_b32_e32 v10, 16, v6
	v_and_b32_e32 v11, 0xffff0000, v6
	v_lshlrev_b32_e32 v6, 16, v7
	v_and_b32_e32 v7, 0xffff0000, v7
	v_pk_fma_f32 v[0:1], v[118:119], v[0:1], v[4:5]
	v_pk_fma_f32 v[4:5], v[116:117], v[12:13], v[8:9]
	v_pk_fma_f32 v[2:3], v[114:115], v[2:3], v[6:7]
	v_pk_fma_f32 v[6:7], v[112:113], v[120:121], v[10:11]
	v_med3_f32 v8, v1, s53, v213
	v_med3_f32 v9, v0, s53, v213
	v_med3_f32 v1, v5, s53, v213
	v_med3_f32 v4, v4, s53, v213
	v_mov_b32_e32 v0, 0
	v_med3_f32 v5, v7, s53, v213
	v_med3_f32 v6, v6, s53, v213
	v_cvt_pk_fp8_f32 v0, v4, v1
	v_mov_b32_e32 v1, 0
	v_cvt_pk_fp8_f32 v1, v6, v5
	v_med3_f32 v3, v3, s53, v213
	v_med3_f32 v2, v2, s53, v213
	v_cvt_pk_fp8_f32 v0, v9, v8 op_sel:[0,0,1]
	v_cvt_pk_fp8_f32 v1, v2, v3 op_sel:[0,0,1]
	v_lshlrev_b64 v[2:3], 11, v[186:187]
	v_lshl_add_u64 v[2:3], s[10:11], 0, v[2:3]
	v_lshl_add_u64 v[112:113], v[2:3], 0, v[160:161]
	global_store_dwordx2 v[112:113], v[0:1], off
	v_or_b32_e32 v0, 0x80, v160
	v_ashrrev_i32_e32 v1, 31, v0
	v_lshlrev_b64 v[12:13], 1, v[0:1]
	v_lshl_add_u64 v[0:1], s[6:7], 0, v[172:173]
	v_lshl_add_u64 v[0:1], v[0:1], 0, v[12:13]
	global_load_dwordx4 v[114:117], v[0:1], off
	v_lshl_add_u64 v[0:1], v[170:171], 0, v[12:13]
	global_load_dwordx4 v[118:121], v[0:1], off
	v_lshl_add_u64 v[0:1], s[6:7], 0, v[184:185]
	v_lshl_add_u64 v[0:1], v[0:1], 0, v[12:13]
	global_load_dwordx4 v[122:125], v[0:1], off
	v_lshl_add_u64 v[0:1], v[178:179], 0, v[12:13]
	global_load_dwordx4 v[130:133], v[0:1], off
	v_lshl_add_u64 v[0:1], v[180:181], 0, v[12:13]
	v_lshl_add_u64 v[2:3], s[6:7], 0, v[176:177]
	v_lshl_add_u64 v[2:3], v[2:3], 0, v[12:13]
	global_load_dwordx4 v[8:11], v[0:1], off
	global_load_dwordx4 v[138:141], v[2:3], off
	v_lshl_add_u64 v[2:3], s[6:7], 0, v[182:183]
	v_lshl_add_u64 v[0:1], v[174:175], 0, v[12:13]
	v_lshl_add_u64 v[4:5], v[2:3], 0, v[12:13]
	global_load_dwordx4 v[0:3], v[0:1], off
	s_nop 0
	global_load_dwordx4 v[4:7], v[4:5], off
	s_waitcnt vmcnt(0)
	v_lshlrev_b32_e32 v126, 16, v114
	v_and_b32_e32 v127, 0xffff0000, v114
	v_lshlrev_b32_e32 v135, 16, v118
	v_and_b32_e32 v118, 0xffff0000, v118
	v_mul_f32_e32 v118, 0xbfb8aa3b, v118
	v_lshlrev_b32_e32 v143, 16, v119
	v_exp_f32_e32 v118, v118
	v_mul_f32_e32 v143, 0xbfb8aa3b, v143
	v_exp_f32_e32 v163, v143
	v_mul_f32_e32 v135, 0xbfb8aa3b, v135
	v_add_f32_e32 v118, 1.0, v118
	v_rcp_f32_e32 v143, v118
	v_add_f32_e32 v118, 1.0, v163
	v_lshlrev_b32_e32 v163, 16, v120
	v_mul_f32_e32 v163, 0xbfb8aa3b, v163
	v_and_b32_e32 v120, 0xffff0000, v120
	v_and_b32_e32 v119, 0xffff0000, v119
	v_exp_f32_e32 v163, v163
	v_mul_f32_e32 v120, 0xbfb8aa3b, v120
	v_exp_f32_e32 v142, v135
	v_mul_f32_e32 v119, 0xbfb8aa3b, v119
	v_exp_f32_e32 v120, v120
	v_exp_f32_e32 v119, v119
	v_add_f32_e32 v163, 1.0, v163
	v_add_f32_e32 v142, 1.0, v142
	v_rcp_f32_e32 v170, v163
	v_lshlrev_b32_e32 v163, 16, v121
	v_and_b32_e32 v121, 0xffff0000, v121
	v_add_f32_e32 v171, 1.0, v120
	v_rcp_f32_e32 v142, v142
	v_add_f32_e32 v119, 1.0, v119
	v_mul_f32_e32 v163, 0xbfb8aa3b, v163
	v_mul_f32_e32 v121, 0xbfb8aa3b, v121
	v_rcp_f32_e32 v171, v171
	v_rcp_f32_e32 v118, v118
	v_rcp_f32_e32 v119, v119
	v_exp_f32_e32 v163, v163
	v_exp_f32_e32 v121, v121
	v_lshlrev_b32_e32 v134, 16, v116
	v_and_b32_e32 v135, 0xffff0000, v116
	v_lshlrev_b32_e32 v114, 16, v115
	v_and_b32_e32 v115, 0xffff0000, v115
	v_pk_fma_f32 v[108:109], v[108:109], v[142:143], v[126:127]
	v_pk_fma_f32 v[104:105], v[104:105], v[170:171], v[134:135]
	v_add_f32_e32 v120, 1.0, v163
	v_add_f32_e32 v121, 1.0, v121
	v_pk_fma_f32 v[110:111], v[110:111], v[118:119], v[114:115]
	v_med3_f32 v109, v109, s53, v213
	v_med3_f32 v108, v108, s53, v213
	v_med3_f32 v115, v104, s53, v213
	v_mov_b32_e32 v104, 0
	v_rcp_f32_e32 v120, v120
	v_rcp_f32_e32 v121, v121
	v_cvt_pk_fp8_f32 v104, v108, v109
	v_lshlrev_b32_e32 v116, 16, v117
	v_and_b32_e32 v117, 0xffff0000, v117
	v_med3_f32 v111, v111, s53, v213
	v_med3_f32 v110, v110, s53, v213
	v_pk_fma_f32 v[106:107], v[106:107], v[120:121], v[116:117]
	v_cvt_pk_fp8_f32 v104, v110, v111 op_sel:[0,0,1]
	v_lshlrev_b32_e32 v111, 16, v130
	v_and_b32_e32 v117, 0xffff0000, v130
	v_lshlrev_b32_e32 v120, 16, v132
	v_and_b32_e32 v121, 0xffff0000, v132
	v_mul_f32_e32 v111, 0xbfb8aa3b, v111
	v_mul_f32_e32 v117, 0xbfb8aa3b, v117
	v_mul_f32_e32 v120, 0xbfb8aa3b, v120
	v_mul_f32_e32 v121, 0xbfb8aa3b, v121
	v_exp_f32_e32 v116, v111
	v_exp_f32_e32 v117, v117
	v_exp_f32_e32 v120, v120
	v_exp_f32_e32 v121, v121
	v_lshlrev_b32_e32 v118, 16, v131
	v_and_b32_e32 v119, 0xffff0000, v131
	v_med3_f32 v114, v105, s53, v213
	v_mov_b32_e32 v105, 0
	v_mul_f32_e32 v118, 0xbfb8aa3b, v118
	v_mul_f32_e32 v119, 0xbfb8aa3b, v119
	v_cvt_pk_fp8_f32 v105, v115, v114
	v_add_f32_e32 v116, 1.0, v116
	v_exp_f32_e32 v118, v118
	v_add_f32_e32 v117, 1.0, v117
	v_exp_f32_e32 v119, v119
	v_add_f32_e32 v120, 1.0, v120
	v_add_f32_e32 v121, 1.0, v121
	v_rcp_f32_e32 v116, v116
	v_rcp_f32_e32 v117, v117
	v_rcp_f32_e32 v120, v120
	v_rcp_f32_e32 v121, v121
	v_med3_f32 v107, v107, s53, v213
	v_med3_f32 v106, v106, s53, v213
	v_cvt_pk_fp8_f32 v105, v106, v107 op_sel:[0,0,1]
	v_lshlrev_b32_e32 v106, 16, v122
	v_and_b32_e32 v107, 0xffff0000, v122
	v_lshlrev_b32_e32 v110, 16, v124
	v_and_b32_e32 v111, 0xffff0000, v124
	v_add_f32_e32 v118, 1.0, v118
	v_add_f32_e32 v119, 1.0, v119
	v_rcp_f32_e32 v118, v118
	v_rcp_f32_e32 v119, v119
	v_pk_fma_f32 v[100:101], v[100:101], v[116:117], v[106:107]
	v_pk_fma_f32 v[96:97], v[96:97], v[120:121], v[110:111]
	v_med3_f32 v101, v101, s53, v213
	v_med3_f32 v100, v100, s53, v213
	v_med3_f32 v107, v96, s53, v213
	v_mov_b32_e32 v96, 0
	v_cvt_pk_fp8_f32 v96, v100, v101
	v_lshlrev_b32_e32 v108, 16, v123
	v_and_b32_e32 v109, 0xffff0000, v123
	v_pk_fma_f32 v[102:103], v[102:103], v[118:119], v[108:109]
	v_lshlrev_b32_e32 v109, 16, v9
	v_med3_f32 v103, v103, s53, v213
	v_med3_f32 v102, v102, s53, v213
	v_cvt_pk_fp8_f32 v96, v102, v103 op_sel:[0,0,1]
	v_lshlrev_b32_e32 v103, 16, v8
	v_and_b32_e32 v8, 0xffff0000, v8
	v_mul_f32_e32 v8, 0xbfb8aa3b, v8
	v_lshlrev_b32_e32 v122, 16, v133
	v_and_b32_e32 v123, 0xffff0000, v133
	v_exp_f32_e32 v8, v8
	v_mul_f32_e32 v109, 0xbfb8aa3b, v109
	v_mul_f32_e32 v122, 0xbfb8aa3b, v122
	v_mul_f32_e32 v123, 0xbfb8aa3b, v123
	v_exp_f32_e32 v110, v109
	v_exp_f32_e32 v122, v122
	v_exp_f32_e32 v123, v123
	v_add_f32_e32 v8, 1.0, v8
	v_and_b32_e32 v9, 0xffff0000, v9
	v_mul_f32_e32 v103, 0xbfb8aa3b, v103
	v_rcp_f32_e32 v109, v8
	v_add_f32_e32 v8, 1.0, v110
	v_mul_f32_e32 v9, 0xbfb8aa3b, v9
	v_lshlrev_b32_e32 v110, 16, v10
	v_and_b32_e32 v10, 0xffff0000, v10
	v_lshlrev_b32_e32 v111, 16, v11
	v_and_b32_e32 v11, 0xffff0000, v11
	v_add_f32_e32 v122, 1.0, v122
	v_add_f32_e32 v123, 1.0, v123
	v_exp_f32_e32 v108, v103
	v_exp_f32_e32 v9, v9
	v_mul_f32_e32 v10, 0xbfb8aa3b, v10
	v_mul_f32_e32 v111, 0xbfb8aa3b, v111
	v_mul_f32_e32 v11, 0xbfb8aa3b, v11
	v_rcp_f32_e32 v122, v122
	v_rcp_f32_e32 v123, v123
	v_exp_f32_e32 v10, v10
	v_exp_f32_e32 v111, v111
	v_exp_f32_e32 v11, v11
	v_mul_f32_e32 v110, 0xbfb8aa3b, v110
	v_med3_f32 v106, v97, s53, v213
	v_mov_b32_e32 v97, 0
	v_exp_f32_e32 v110, v110
	v_lshlrev_b32_e32 v114, 16, v125
	v_and_b32_e32 v115, 0xffff0000, v125
	v_cvt_pk_fp8_f32 v97, v107, v106
	v_add_f32_e32 v108, 1.0, v108
	v_add_f32_e32 v9, 1.0, v9
	v_pk_fma_f32 v[98:99], v[98:99], v[122:123], v[114:115]
	v_rcp_f32_e32 v108, v108
	v_rcp_f32_e32 v8, v8
	v_rcp_f32_e32 v9, v9
	v_add_f32_e32 v114, 1.0, v10
	v_add_f32_e32 v10, 1.0, v111
	v_add_f32_e32 v11, 1.0, v11
	v_rcp_f32_e32 v10, v10
	v_rcp_f32_e32 v11, v11
	v_med3_f32 v99, v99, s53, v213
	v_med3_f32 v98, v98, s53, v213
	v_add_f32_e32 v110, 1.0, v110
	v_cvt_pk_fp8_f32 v97, v98, v99 op_sel:[0,0,1]
	v_lshlrev_b32_e32 v98, 16, v138
	v_and_b32_e32 v99, 0xffff0000, v138
	v_lshlrev_b32_e32 v100, 16, v139
	v_and_b32_e32 v101, 0xffff0000, v139
	v_rcp_f32_e32 v110, v110
	v_rcp_f32_e32 v111, v114
	v_lshlrev_b32_e32 v106, 16, v141
	v_and_b32_e32 v107, 0xffff0000, v141
	v_pk_fma_f32 v[8:9], v[94:95], v[8:9], v[100:101]
	v_pk_fma_f32 v[92:93], v[92:93], v[108:109], v[98:99]
	v_pk_fma_f32 v[10:11], v[90:91], v[10:11], v[106:107]
	v_med3_f32 v90, v9, s53, v213
	v_med3_f32 v91, v8, s53, v213
	v_med3_f32 v9, v93, s53, v213
	v_med3_f32 v92, v92, s53, v213
	v_mov_b32_e32 v8, 0
	v_lshlrev_b32_e32 v102, 16, v140
	v_and_b32_e32 v103, 0xffff0000, v140
	v_cvt_pk_fp8_f32 v8, v92, v9
	v_pk_fma_f32 v[88:89], v[88:89], v[110:111], v[102:103]
	v_mov_b32_e32 v9, 0
	v_med3_f32 v89, v89, s53, v213
	v_med3_f32 v88, v88, s53, v213
	v_cvt_pk_fp8_f32 v9, v88, v89
	v_lshlrev_b32_e32 v89, 16, v0
	v_and_b32_e32 v0, 0xffff0000, v0
	v_cvt_pk_fp8_f32 v8, v91, v90 op_sel:[0,0,1]
	v_mul_f32_e32 v0, 0xbfb8aa3b, v0
	v_lshlrev_b32_e32 v91, 16, v1
	v_exp_f32_e32 v0, v0
	v_mul_f32_e32 v91, 0xbfb8aa3b, v91
	v_exp_f32_e32 v92, v91
	v_and_b32_e32 v1, 0xffff0000, v1
	v_add_f32_e32 v0, 1.0, v0
	v_mul_f32_e32 v89, 0xbfb8aa3b, v89
	v_rcp_f32_e32 v91, v0
	v_add_f32_e32 v0, 1.0, v92
	v_mul_f32_e32 v1, 0xbfb8aa3b, v1
	v_lshlrev_b32_e32 v92, 16, v2
	v_and_b32_e32 v2, 0xffff0000, v2
	v_lshlrev_b32_e32 v93, 16, v3
	v_and_b32_e32 v3, 0xffff0000, v3
	v_exp_f32_e32 v90, v89
	v_exp_f32_e32 v1, v1
	v_mul_f32_e32 v92, 0xbfb8aa3b, v92
	v_mul_f32_e32 v2, 0xbfb8aa3b, v2
	v_mul_f32_e32 v93, 0xbfb8aa3b, v93
	v_mul_f32_e32 v3, 0xbfb8aa3b, v3
	v_exp_f32_e32 v92, v92
	v_exp_f32_e32 v2, v2
	v_exp_f32_e32 v93, v93
	v_exp_f32_e32 v3, v3
	v_add_f32_e32 v90, 1.0, v90
	v_add_f32_e32 v1, 1.0, v1
	v_rcp_f32_e32 v90, v90
	v_rcp_f32_e32 v0, v0
	v_rcp_f32_e32 v1, v1
	v_add_f32_e32 v92, 1.0, v92
	v_add_f32_e32 v94, 1.0, v2
	v_add_f32_e32 v2, 1.0, v93
	v_add_f32_e32 v3, 1.0, v3
	v_rcp_f32_e32 v92, v92
	v_rcp_f32_e32 v2, v2
	v_rcp_f32_e32 v3, v3
	v_rcp_f32_e32 v93, v94
	v_med3_f32 v11, v11, s53, v213
	v_med3_f32 v10, v10, s53, v213
	v_cvt_pk_fp8_f32 v9, v10, v11 op_sel:[0,0,1]
	v_lshlrev_b32_e32 v10, 16, v4
	v_and_b32_e32 v11, 0xffff0000, v4
	v_lshlrev_b32_e32 v4, 16, v5
	v_and_b32_e32 v5, 0xffff0000, v5
	v_lshlrev_b32_e32 v88, 16, v6
	v_and_b32_e32 v89, 0xffff0000, v6
	v_lshlrev_b32_e32 v6, 16, v7
	v_and_b32_e32 v7, 0xffff0000, v7
	v_pk_fma_f32 v[0:1], v[86:87], v[0:1], v[4:5]
	v_pk_fma_f32 v[4:5], v[84:85], v[90:91], v[10:11]
	v_pk_fma_f32 v[2:3], v[82:83], v[2:3], v[6:7]
	v_pk_fma_f32 v[6:7], v[80:81], v[92:93], v[88:89]
	v_med3_f32 v10, v1, s53, v213
	v_med3_f32 v11, v0, s53, v213
	v_med3_f32 v1, v5, s53, v213
	v_med3_f32 v4, v4, s53, v213
	v_mov_b32_e32 v0, 0
	v_med3_f32 v5, v7, s53, v213
	v_med3_f32 v6, v6, s53, v213
	v_cvt_pk_fp8_f32 v0, v4, v1
	v_mov_b32_e32 v1, 0
	v_cvt_pk_fp8_f32 v1, v6, v5
	v_med3_f32 v3, v3, s53, v213
	v_med3_f32 v2, v2, s53, v213
	v_cvt_pk_fp8_f32 v0, v11, v10 op_sel:[0,0,1]
	v_cvt_pk_fp8_f32 v1, v2, v3 op_sel:[0,0,1]
	global_store_dwordx2 v[136:137], v[104:105], off offset:128
	global_store_dwordx2 v[128:129], v[96:97], off offset:128
	global_store_dwordx2 v[14:15], v[8:9], off offset:128
	global_store_dwordx2 v[112:113], v[0:1], off offset:128
	v_add_u32_e32 v14, 0x80, v162
	v_ashrrev_i32_e32 v15, 31, v14
	v_lshlrev_b64 v[80:81], 12, v[14:15]
	v_lshl_add_u64 v[0:1], v[168:169], 0, v[80:81]
	global_load_dwordx4 v[100:103], v[0:1], off
	v_mad_i64_i32 v[0:1], s[26:27], v14, s52, v[166:167]
	v_lshl_add_u64 v[82:83], v[0:1], 0, s[14:15]
	v_lshl_add_u64 v[0:1], v[82:83], 0, v[164:165]
	global_load_dwordx4 v[104:107], v[0:1], off
	v_add_u32_e32 v120, 0x90, v162
	v_mad_i64_i32 v[0:1], s[26:27], v120, s52, v[166:167]
	v_ashrrev_i32_e32 v121, 31, v120
	v_lshl_add_u64 v[84:85], v[0:1], 0, s[14:15]
	v_lshl_add_u64 v[0:1], v[84:85], 0, v[164:165]
	v_lshlrev_b64 v[86:87], 12, v[120:121]
	v_lshl_add_u64 v[2:3], v[168:169], 0, v[86:87]
	global_load_dwordx4 v[108:111], v[0:1], off
	global_load_dwordx4 v[112:115], v[2:3], off
	v_add_u32_e32 v98, 0xa0, v162
	v_mad_i64_i32 v[0:1], s[26:27], v98, s52, v[166:167]
	v_ashrrev_i32_e32 v99, 31, v98
	v_lshl_add_u64 v[88:89], v[0:1], 0, s[14:15]
	v_lshl_add_u64 v[0:1], v[88:89], 0, v[164:165]
	v_lshlrev_b64 v[90:91], 12, v[98:99]
	v_lshl_add_u64 v[2:3], v[168:169], 0, v[90:91]
	global_load_dwordx4 v[8:11], v[0:1], off
	global_load_dwordx4 v[116:119], v[2:3], off
	v_add_u32_e32 v96, 0xb0, v162
	v_ashrrev_i32_e32 v97, 31, v96
	v_mad_i64_i32 v[0:1], s[26:27], v96, s52, v[166:167]
	v_lshl_add_u64 v[92:93], v[0:1], 0, s[14:15]
	v_lshlrev_b64 v[94:95], 12, v[96:97]
	v_lshl_add_u64 v[0:1], v[92:93], 0, v[164:165]
	v_lshl_add_u64 v[4:5], v[168:169], 0, v[94:95]
	global_load_dwordx4 v[0:3], v[0:1], off
	s_nop 0
	global_load_dwordx4 v[4:7], v[4:5], off
	v_lshlrev_b64 v[14:15], 11, v[14:15]
	v_lshl_add_u64 v[14:15], s[10:11], 0, v[14:15]
	v_lshl_add_u64 v[14:15], v[14:15], 0, v[160:161]
	s_mov_b64 s[26:27], s[22:23]
	s_waitcnt vmcnt(0)
	v_lshlrev_b32_e32 v122, 16, v100
	v_and_b32_e32 v123, 0xffff0000, v100
	v_lshlrev_b32_e32 v124, 16, v102
	v_lshlrev_b32_e32 v100, 16, v101
	v_and_b32_e32 v101, 0xffff0000, v101
	v_lshlrev_b32_e32 v125, 16, v104
	v_and_b32_e32 v104, 0xffff0000, v104
	v_mul_f32_e32 v104, 0xbfb8aa3b, v104
	v_lshlrev_b32_e32 v127, 16, v105
	v_exp_f32_e32 v104, v104
	v_mul_f32_e32 v127, 0xbfb8aa3b, v127
	v_exp_f32_e32 v128, v127
	v_mul_f32_e32 v125, 0xbfb8aa3b, v125
	v_add_f32_e32 v104, 1.0, v104
	v_rcp_f32_e32 v127, v104
	v_add_f32_e32 v104, 1.0, v128
	v_lshlrev_b32_e32 v128, 16, v106
	v_and_b32_e32 v106, 0xffff0000, v106
	v_and_b32_e32 v105, 0xffff0000, v105
	v_mul_f32_e32 v128, 0xbfb8aa3b, v128
	v_mul_f32_e32 v106, 0xbfb8aa3b, v106
	v_lshlrev_b32_e32 v129, 16, v107
	v_exp_f32_e32 v126, v125
	v_mul_f32_e32 v105, 0xbfb8aa3b, v105
	v_exp_f32_e32 v128, v128
	v_exp_f32_e32 v106, v106
	v_mul_f32_e32 v129, 0xbfb8aa3b, v129
	v_exp_f32_e32 v105, v105
	v_exp_f32_e32 v129, v129
	v_add_f32_e32 v126, 1.0, v126
	v_add_f32_e32 v128, 1.0, v128
	v_and_b32_e32 v107, 0xffff0000, v107
	v_add_f32_e32 v130, 1.0, v106
	v_rcp_f32_e32 v126, v126
	v_add_f32_e32 v105, 1.0, v105
	v_rcp_f32_e32 v128, v128
	v_mul_f32_e32 v107, 0xbfb8aa3b, v107
	v_add_f32_e32 v106, 1.0, v129
	v_rcp_f32_e32 v129, v130
	v_rcp_f32_e32 v104, v104
	v_rcp_f32_e32 v105, v105
	v_exp_f32_e32 v107, v107
	v_and_b32_e32 v125, 0xffff0000, v102
	v_pk_fma_f32 v[76:77], v[76:77], v[126:127], v[122:123]
	v_pk_fma_f32 v[72:73], v[72:73], v[128:129], v[124:125]
	v_add_f32_e32 v107, 1.0, v107
	v_pk_fma_f32 v[78:79], v[78:79], v[104:105], v[100:101]
	v_med3_f32 v77, v77, s53, v213
	v_med3_f32 v76, v76, s53, v213
	v_med3_f32 v100, v73, s53, v213
	v_med3_f32 v101, v72, s53, v213
	v_mov_b32_e32 v72, 0
	v_mov_b32_e32 v73, 0
	v_rcp_f32_e32 v106, v106
	v_rcp_f32_e32 v107, v107
	v_cvt_pk_fp8_f32 v72, v76, v77
	v_cvt_pk_fp8_f32 v73, v101, v100
	v_lshlrev_b32_e32 v77, 16, v108
	v_and_b32_e32 v101, 0xffff0000, v108
	v_mul_f32_e32 v77, 0xbfb8aa3b, v77
	v_mul_f32_e32 v101, 0xbfb8aa3b, v101
	v_exp_f32_e32 v100, v77
	v_exp_f32_e32 v101, v101
	v_lshlrev_b32_e32 v102, 16, v103
	v_and_b32_e32 v103, 0xffff0000, v103
	v_pk_fma_f32 v[74:75], v[74:75], v[106:107], v[102:103]
	v_lshlrev_b32_e32 v102, 16, v109
	v_and_b32_e32 v103, 0xffff0000, v109
	v_med3_f32 v79, v79, s53, v213
	v_med3_f32 v78, v78, s53, v213
	v_med3_f32 v75, v75, s53, v213
	v_med3_f32 v74, v74, s53, v213
	v_mul_f32_e32 v102, 0xbfb8aa3b, v102
	v_mul_f32_e32 v103, 0xbfb8aa3b, v103
	v_cvt_pk_fp8_f32 v72, v78, v79 op_sel:[0,0,1]
	v_cvt_pk_fp8_f32 v73, v74, v75 op_sel:[0,0,1]
	v_add_f32_e32 v100, 1.0, v100
	v_exp_f32_e32 v102, v102
	v_add_f32_e32 v101, 1.0, v101
	v_exp_f32_e32 v103, v103
	v_rcp_f32_e32 v100, v100
	v_rcp_f32_e32 v101, v101
	v_lshlrev_b32_e32 v104, 16, v110
	v_and_b32_e32 v105, 0xffff0000, v110
	global_store_dwordx2 v[14:15], v[72:73], off
	v_lshlrev_b32_e32 v72, 16, v112
	v_and_b32_e32 v73, 0xffff0000, v112
	v_add_f32_e32 v102, 1.0, v102
	v_mul_f32_e32 v104, 0xbfb8aa3b, v104
	v_add_f32_e32 v103, 1.0, v103
	v_mul_f32_e32 v105, 0xbfb8aa3b, v105
	v_exp_f32_e32 v104, v104
	v_rcp_f32_e32 v102, v102
	v_rcp_f32_e32 v103, v103
	v_exp_f32_e32 v105, v105
	v_pk_fma_f32 v[68:69], v[68:69], v[100:101], v[72:73]
	v_lshlrev_b32_e32 v74, 16, v113
	v_med3_f32 v69, v69, s53, v213
	v_med3_f32 v72, v68, s53, v213
	v_mov_b32_e32 v68, 0
	v_cvt_pk_fp8_f32 v68, v72, v69
	v_and_b32_e32 v75, 0xffff0000, v113
	v_add_f32_e32 v104, 1.0, v104
	v_add_f32_e32 v105, 1.0, v105
	v_pk_fma_f32 v[70:71], v[70:71], v[102:103], v[74:75]
	v_rcp_f32_e32 v104, v104
	v_lshlrev_b32_e32 v106, 16, v111
	v_and_b32_e32 v107, 0xffff0000, v111
	v_rcp_f32_e32 v105, v105
	v_med3_f32 v71, v71, s53, v213
	v_med3_f32 v70, v70, s53, v213
	v_mul_f32_e32 v106, 0xbfb8aa3b, v106
	v_mul_f32_e32 v107, 0xbfb8aa3b, v107
	v_cvt_pk_fp8_f32 v68, v70, v71 op_sel:[0,0,1]
	v_lshlrev_b32_e32 v71, 16, v8
	v_and_b32_e32 v8, 0xffff0000, v8
	v_exp_f32_e32 v106, v106
	v_exp_f32_e32 v107, v107
	v_mul_f32_e32 v8, 0xbfb8aa3b, v8
	v_lshlrev_b32_e32 v75, 16, v9
	v_lshlrev_b32_e32 v76, 16, v114
	v_and_b32_e32 v77, 0xffff0000, v114
	v_exp_f32_e32 v8, v8
	v_mul_f32_e32 v75, 0xbfb8aa3b, v75
	v_pk_fma_f32 v[64:65], v[64:65], v[104:105], v[76:77]
	v_exp_f32_e32 v76, v75
	v_add_f32_e32 v106, 1.0, v106
	v_add_f32_e32 v107, 1.0, v107
	v_rcp_f32_e32 v106, v106
	v_rcp_f32_e32 v107, v107
	v_add_f32_e32 v8, 1.0, v8
	v_and_b32_e32 v9, 0xffff0000, v9
	v_med3_f32 v65, v65, s53, v213
	v_med3_f32 v64, v64, s53, v213
	v_mov_b32_e32 v69, 0
	v_mul_f32_e32 v71, 0xbfb8aa3b, v71
	v_rcp_f32_e32 v75, v8
	v_add_f32_e32 v8, 1.0, v76
	v_mul_f32_e32 v9, 0xbfb8aa3b, v9
	v_lshlrev_b32_e32 v76, 16, v10
	v_and_b32_e32 v10, 0xffff0000, v10
	v_lshlrev_b32_e32 v77, 16, v11
	v_and_b32_e32 v11, 0xffff0000, v11
	v_cvt_pk_fp8_f32 v69, v64, v65
	v_exp_f32_e32 v74, v71
	v_exp_f32_e32 v9, v9
	v_mul_f32_e32 v76, 0xbfb8aa3b, v76
	v_mul_f32_e32 v10, 0xbfb8aa3b, v10
	v_mul_f32_e32 v77, 0xbfb8aa3b, v77
	v_mul_f32_e32 v11, 0xbfb8aa3b, v11
	v_lshlrev_b32_e32 v78, 16, v115
	v_and_b32_e32 v79, 0xffff0000, v115
	v_exp_f32_e32 v76, v76
	v_exp_f32_e32 v10, v10
	v_exp_f32_e32 v77, v77
	v_exp_f32_e32 v11, v11
	v_pk_fma_f32 v[66:67], v[66:67], v[106:107], v[78:79]
	v_add_f32_e32 v74, 1.0, v74
	v_med3_f32 v64, v67, s53, v213
	v_med3_f32 v65, v66, s53, v213
	v_cvt_pk_fp8_f32 v69, v65, v64 op_sel:[0,0,1]
	v_add_f32_e32 v9, 1.0, v9
	v_lshlrev_b64 v[64:65], 11, v[120:121]
	v_rcp_f32_e32 v74, v74
	v_rcp_f32_e32 v8, v8
	v_rcp_f32_e32 v9, v9
	v_add_f32_e32 v76, 1.0, v76
	v_add_f32_e32 v78, 1.0, v10
	v_add_f32_e32 v10, 1.0, v77
	v_add_f32_e32 v11, 1.0, v11
	v_lshl_add_u64 v[64:65], s[10:11], 0, v[64:65]
	v_rcp_f32_e32 v76, v76
	v_rcp_f32_e32 v10, v10
	v_rcp_f32_e32 v11, v11
	v_rcp_f32_e32 v77, v78
	v_lshl_add_u64 v[64:65], v[64:65], 0, v[160:161]
	global_store_dwordx2 v[64:65], v[68:69], off
	v_lshlrev_b32_e32 v66, 16, v116
	v_and_b32_e32 v67, 0xffff0000, v116
	v_lshlrev_b32_e32 v68, 16, v117
	v_and_b32_e32 v69, 0xffff0000, v117
	v_lshlrev_b32_e32 v70, 16, v118
	v_and_b32_e32 v71, 0xffff0000, v118
	v_lshlrev_b32_e32 v72, 16, v119
	v_and_b32_e32 v73, 0xffff0000, v119
	v_pk_fma_f32 v[8:9], v[62:63], v[8:9], v[68:69]
	v_pk_fma_f32 v[60:61], v[60:61], v[74:75], v[66:67]
	v_pk_fma_f32 v[10:11], v[58:59], v[10:11], v[72:73]
	v_pk_fma_f32 v[56:57], v[56:57], v[76:77], v[70:71]
	v_med3_f32 v58, v9, s53, v213
	v_med3_f32 v59, v8, s53, v213
	v_med3_f32 v9, v61, s53, v213
	v_med3_f32 v60, v60, s53, v213
	v_mov_b32_e32 v8, 0
	v_med3_f32 v57, v57, s53, v213
	v_med3_f32 v56, v56, s53, v213
	v_cvt_pk_fp8_f32 v8, v60, v9
	v_mov_b32_e32 v9, 0
	v_cvt_pk_fp8_f32 v9, v56, v57
	v_med3_f32 v11, v11, s53, v213
	v_med3_f32 v10, v10, s53, v213
	v_cvt_pk_fp8_f32 v8, v59, v58 op_sel:[0,0,1]
	v_cvt_pk_fp8_f32 v9, v10, v11 op_sel:[0,0,1]
	v_lshlrev_b64 v[10:11], 11, v[98:99]
	v_lshl_add_u64 v[10:11], s[10:11], 0, v[10:11]
	v_lshl_add_u64 v[56:57], v[10:11], 0, v[160:161]
	v_lshlrev_b32_e32 v11, 16, v0
	v_and_b32_e32 v0, 0xffff0000, v0
	v_mul_f32_e32 v0, 0xbfb8aa3b, v0
	v_lshlrev_b32_e32 v59, 16, v1
	v_exp_f32_e32 v0, v0
	v_mul_f32_e32 v59, 0xbfb8aa3b, v59
	v_exp_f32_e32 v60, v59
	v_and_b32_e32 v1, 0xffff0000, v1
	v_add_f32_e32 v0, 1.0, v0
	v_mul_f32_e32 v11, 0xbfb8aa3b, v11
	v_rcp_f32_e32 v59, v0
	v_add_f32_e32 v0, 1.0, v60
	v_mul_f32_e32 v1, 0xbfb8aa3b, v1
	v_lshlrev_b32_e32 v60, 16, v2
	v_and_b32_e32 v2, 0xffff0000, v2
	v_lshlrev_b32_e32 v61, 16, v3
	v_and_b32_e32 v3, 0xffff0000, v3
	v_exp_f32_e32 v58, v11
	v_exp_f32_e32 v1, v1
	v_mul_f32_e32 v60, 0xbfb8aa3b, v60
	v_mul_f32_e32 v2, 0xbfb8aa3b, v2
	v_mul_f32_e32 v61, 0xbfb8aa3b, v61
	v_mul_f32_e32 v3, 0xbfb8aa3b, v3
	v_exp_f32_e32 v60, v60
	v_exp_f32_e32 v2, v2
	v_exp_f32_e32 v61, v61
	v_exp_f32_e32 v3, v3
	v_add_f32_e32 v58, 1.0, v58
	v_add_f32_e32 v1, 1.0, v1
	v_rcp_f32_e32 v58, v58
	v_rcp_f32_e32 v0, v0
	v_rcp_f32_e32 v1, v1
	v_add_f32_e32 v60, 1.0, v60
	v_add_f32_e32 v62, 1.0, v2
	v_add_f32_e32 v2, 1.0, v61
	v_add_f32_e32 v3, 1.0, v3
	v_rcp_f32_e32 v60, v60
	v_rcp_f32_e32 v2, v2
	v_rcp_f32_e32 v3, v3
	v_rcp_f32_e32 v61, v62
	global_store_dwordx2 v[56:57], v[8:9], off
	v_lshlrev_b32_e32 v8, 16, v4
	v_and_b32_e32 v9, 0xffff0000, v4
	v_lshlrev_b32_e32 v4, 16, v5
	v_and_b32_e32 v5, 0xffff0000, v5
	v_lshlrev_b32_e32 v10, 16, v6
	v_and_b32_e32 v11, 0xffff0000, v6
	v_lshlrev_b32_e32 v6, 16, v7
	v_and_b32_e32 v7, 0xffff0000, v7
	v_pk_fma_f32 v[0:1], v[54:55], v[0:1], v[4:5]
	v_pk_fma_f32 v[4:5], v[52:53], v[58:59], v[8:9]
	v_pk_fma_f32 v[2:3], v[50:51], v[2:3], v[6:7]
	v_pk_fma_f32 v[6:7], v[48:49], v[60:61], v[10:11]
	v_med3_f32 v8, v1, s53, v213
	v_med3_f32 v9, v0, s53, v213
	v_med3_f32 v1, v5, s53, v213
	v_med3_f32 v4, v4, s53, v213
	v_mov_b32_e32 v0, 0
	v_med3_f32 v5, v7, s53, v213
	v_med3_f32 v6, v6, s53, v213
	v_cvt_pk_fp8_f32 v0, v4, v1
	v_mov_b32_e32 v1, 0
	v_cvt_pk_fp8_f32 v1, v6, v5
	v_med3_f32 v3, v3, s53, v213
	v_med3_f32 v2, v2, s53, v213
	v_cvt_pk_fp8_f32 v0, v9, v8 op_sel:[0,0,1]
	v_cvt_pk_fp8_f32 v1, v2, v3 op_sel:[0,0,1]
	v_lshlrev_b64 v[2:3], 11, v[96:97]
	v_lshl_add_u64 v[2:3], s[10:11], 0, v[2:3]
	v_lshl_add_u64 v[48:49], v[2:3], 0, v[160:161]
	global_store_dwordx2 v[48:49], v[0:1], off
	v_lshl_add_u64 v[0:1], s[6:7], 0, v[80:81]
	v_lshl_add_u64 v[0:1], v[0:1], 0, v[12:13]
	global_load_dwordx4 v[50:53], v[0:1], off
	v_lshl_add_u64 v[0:1], v[82:83], 0, v[12:13]
	global_load_dwordx4 v[58:61], v[0:1], off
	v_lshl_add_u64 v[0:1], s[6:7], 0, v[86:87]
	v_lshl_add_u64 v[0:1], v[0:1], 0, v[12:13]
	global_load_dwordx4 v[66:69], v[0:1], off
	v_lshl_add_u64 v[0:1], v[84:85], 0, v[12:13]
	global_load_dwordx4 v[70:73], v[0:1], off
	v_lshl_add_u64 v[0:1], v[88:89], 0, v[12:13]
	v_lshl_add_u64 v[2:3], s[6:7], 0, v[90:91]
	v_lshl_add_u64 v[2:3], v[2:3], 0, v[12:13]
	global_load_dwordx4 v[8:11], v[0:1], off
	global_load_dwordx4 v[74:77], v[2:3], off
	v_lshl_add_u64 v[2:3], s[6:7], 0, v[94:95]
	v_lshl_add_u64 v[0:1], v[92:93], 0, v[12:13]
	v_lshl_add_u64 v[4:5], v[2:3], 0, v[12:13]
	global_load_dwordx4 v[0:3], v[0:1], off
	s_nop 0
	global_load_dwordx4 v[4:7], v[4:5], off
	s_waitcnt vmcnt(0)
	v_lshlrev_b32_e32 v12, 16, v50
	v_and_b32_e32 v13, 0xffff0000, v50
	v_lshlrev_b32_e32 v55, 16, v58
	v_and_b32_e32 v58, 0xffff0000, v58
	v_mul_f32_e32 v58, 0xbfb8aa3b, v58
	v_lshlrev_b32_e32 v63, 16, v59
	v_and_b32_e32 v59, 0xffff0000, v59
	v_mul_f32_e32 v55, 0xbfb8aa3b, v55
	v_exp_f32_e32 v58, v58
	v_mul_f32_e32 v63, 0xbfb8aa3b, v63
	v_mul_f32_e32 v59, 0xbfb8aa3b, v59
	v_exp_f32_e32 v62, v55
	v_exp_f32_e32 v78, v63
	v_exp_f32_e32 v59, v59
	v_add_f32_e32 v58, 1.0, v58
	v_add_f32_e32 v62, 1.0, v62
	v_rcp_f32_e32 v63, v58
	v_add_f32_e32 v58, 1.0, v78
	v_lshlrev_b32_e32 v78, 16, v60
	v_add_f32_e32 v59, 1.0, v59
	v_and_b32_e32 v60, 0xffff0000, v60
	v_rcp_f32_e32 v62, v62
	v_mul_f32_e32 v78, 0xbfb8aa3b, v78
	v_rcp_f32_e32 v58, v58
	v_rcp_f32_e32 v59, v59
	v_mul_f32_e32 v60, 0xbfb8aa3b, v60
	v_lshlrev_b32_e32 v79, 16, v61
	v_exp_f32_e32 v78, v78
	v_exp_f32_e32 v60, v60
	v_mul_f32_e32 v79, 0xbfb8aa3b, v79
	v_exp_f32_e32 v79, v79
	v_lshlrev_b32_e32 v50, 16, v51
	v_and_b32_e32 v51, 0xffff0000, v51
	v_and_b32_e32 v61, 0xffff0000, v61
	v_mul_f32_e32 v61, 0xbfb8aa3b, v61
	v_pk_fma_f32 v[46:47], v[46:47], v[58:59], v[50:51]
	v_pk_fma_f32 v[12:13], v[44:45], v[62:63], v[12:13]
	v_add_f32_e32 v78, 1.0, v78
	v_exp_f32_e32 v61, v61
	v_add_f32_e32 v80, 1.0, v60
	v_med3_f32 v45, v46, s53, v213
	v_med3_f32 v13, v13, s53, v213
	v_med3_f32 v46, v12, s53, v213
	v_mov_b32_e32 v12, 0
	v_rcp_f32_e32 v78, v78
	v_add_f32_e32 v60, 1.0, v79
	v_rcp_f32_e32 v79, v80
	v_cvt_pk_fp8_f32 v12, v46, v13
	v_lshlrev_b32_e32 v54, 16, v52
	v_and_b32_e32 v55, 0xffff0000, v52
	v_add_f32_e32 v61, 1.0, v61
	v_med3_f32 v44, v47, s53, v213
	v_rcp_f32_e32 v60, v60
	v_rcp_f32_e32 v61, v61
	v_pk_fma_f32 v[40:41], v[40:41], v[78:79], v[54:55]
	v_cvt_pk_fp8_f32 v12, v45, v44 op_sel:[0,0,1]
	v_lshlrev_b32_e32 v45, 16, v70
	v_and_b32_e32 v51, 0xffff0000, v70
	v_lshlrev_b32_e32 v54, 16, v72
	v_and_b32_e32 v55, 0xffff0000, v72
	v_mul_f32_e32 v45, 0xbfb8aa3b, v45
	v_mul_f32_e32 v51, 0xbfb8aa3b, v51
	v_mul_f32_e32 v54, 0xbfb8aa3b, v54
	v_mul_f32_e32 v55, 0xbfb8aa3b, v55
	v_exp_f32_e32 v50, v45
	v_exp_f32_e32 v51, v51
	v_exp_f32_e32 v54, v54
	v_exp_f32_e32 v55, v55
	v_lshlrev_b32_e32 v52, 16, v53
	v_and_b32_e32 v53, 0xffff0000, v53
	v_pk_fma_f32 v[42:43], v[42:43], v[60:61], v[52:53]
	v_lshlrev_b32_e32 v52, 16, v71
	v_and_b32_e32 v53, 0xffff0000, v71
	v_med3_f32 v41, v41, s53, v213
	v_med3_f32 v40, v40, s53, v213
	v_mov_b32_e32 v13, 0
	v_mul_f32_e32 v52, 0xbfb8aa3b, v52
	v_mul_f32_e32 v53, 0xbfb8aa3b, v53
	v_cvt_pk_fp8_f32 v13, v40, v41
	v_add_f32_e32 v50, 1.0, v50
	v_exp_f32_e32 v52, v52
	v_add_f32_e32 v51, 1.0, v51
	v_exp_f32_e32 v53, v53
	v_add_f32_e32 v54, 1.0, v54
	v_add_f32_e32 v55, 1.0, v55
	v_rcp_f32_e32 v50, v50
	v_rcp_f32_e32 v51, v51
	v_rcp_f32_e32 v54, v54
	v_rcp_f32_e32 v55, v55
	v_med3_f32 v40, v43, s53, v213
	v_med3_f32 v41, v42, s53, v213
	v_cvt_pk_fp8_f32 v13, v41, v40 op_sel:[0,0,1]
	v_lshlrev_b32_e32 v40, 16, v66
	v_and_b32_e32 v41, 0xffff0000, v66
	v_lshlrev_b32_e32 v44, 16, v68
	v_and_b32_e32 v45, 0xffff0000, v68
	v_add_f32_e32 v52, 1.0, v52
	v_add_f32_e32 v53, 1.0, v53
	v_rcp_f32_e32 v52, v52
	v_rcp_f32_e32 v53, v53
	v_pk_fma_f32 v[36:37], v[36:37], v[50:51], v[40:41]
	v_pk_fma_f32 v[32:33], v[32:33], v[54:55], v[44:45]
	v_med3_f32 v37, v37, s53, v213
	v_med3_f32 v36, v36, s53, v213
	v_med3_f32 v41, v32, s53, v213
	v_mov_b32_e32 v32, 0
	v_cvt_pk_fp8_f32 v32, v36, v37
	v_lshlrev_b32_e32 v42, 16, v67
	v_and_b32_e32 v43, 0xffff0000, v67
	v_pk_fma_f32 v[38:39], v[38:39], v[52:53], v[42:43]
	v_lshlrev_b32_e32 v43, 16, v9
	v_med3_f32 v39, v39, s53, v213
	v_med3_f32 v38, v38, s53, v213
	v_cvt_pk_fp8_f32 v32, v38, v39 op_sel:[0,0,1]
	v_lshlrev_b32_e32 v39, 16, v8
	v_and_b32_e32 v8, 0xffff0000, v8
	v_mul_f32_e32 v8, 0xbfb8aa3b, v8
	v_lshlrev_b32_e32 v58, 16, v73
	v_and_b32_e32 v59, 0xffff0000, v73
	v_exp_f32_e32 v8, v8
	v_mul_f32_e32 v43, 0xbfb8aa3b, v43
	v_mul_f32_e32 v58, 0xbfb8aa3b, v58
	v_mul_f32_e32 v59, 0xbfb8aa3b, v59
	v_exp_f32_e32 v44, v43
	v_exp_f32_e32 v58, v58
	v_exp_f32_e32 v59, v59
	v_add_f32_e32 v8, 1.0, v8
	v_and_b32_e32 v9, 0xffff0000, v9
	v_mul_f32_e32 v39, 0xbfb8aa3b, v39
	v_rcp_f32_e32 v43, v8
	v_add_f32_e32 v8, 1.0, v44
	v_mul_f32_e32 v9, 0xbfb8aa3b, v9
	v_lshlrev_b32_e32 v44, 16, v10
	v_and_b32_e32 v10, 0xffff0000, v10
	v_lshlrev_b32_e32 v45, 16, v11
	v_and_b32_e32 v11, 0xffff0000, v11
	v_add_f32_e32 v58, 1.0, v58
	v_add_f32_e32 v59, 1.0, v59
	v_exp_f32_e32 v42, v39
	v_exp_f32_e32 v9, v9
	v_mul_f32_e32 v10, 0xbfb8aa3b, v10
	v_mul_f32_e32 v45, 0xbfb8aa3b, v45
	v_mul_f32_e32 v11, 0xbfb8aa3b, v11
	v_rcp_f32_e32 v58, v58
	v_rcp_f32_e32 v59, v59
	v_exp_f32_e32 v10, v10
	v_exp_f32_e32 v45, v45
	v_exp_f32_e32 v11, v11
	v_mul_f32_e32 v44, 0xbfb8aa3b, v44
	v_med3_f32 v40, v33, s53, v213
	v_mov_b32_e32 v33, 0
	v_exp_f32_e32 v44, v44
	v_lshlrev_b32_e32 v46, 16, v69
	v_and_b32_e32 v47, 0xffff0000, v69
	v_cvt_pk_fp8_f32 v33, v41, v40
	v_add_f32_e32 v42, 1.0, v42
	v_add_f32_e32 v9, 1.0, v9
	v_pk_fma_f32 v[34:35], v[34:35], v[58:59], v[46:47]
	v_rcp_f32_e32 v42, v42
	v_rcp_f32_e32 v8, v8
	v_rcp_f32_e32 v9, v9
	v_add_f32_e32 v46, 1.0, v10
	v_add_f32_e32 v10, 1.0, v45
	v_add_f32_e32 v11, 1.0, v11
	v_rcp_f32_e32 v10, v10
	v_rcp_f32_e32 v11, v11
	v_med3_f32 v35, v35, s53, v213
	v_med3_f32 v34, v34, s53, v213
	v_add_f32_e32 v44, 1.0, v44
	v_cvt_pk_fp8_f32 v33, v34, v35 op_sel:[0,0,1]
	v_lshlrev_b32_e32 v34, 16, v74
	v_and_b32_e32 v35, 0xffff0000, v74
	v_lshlrev_b32_e32 v36, 16, v75
	v_and_b32_e32 v37, 0xffff0000, v75
	v_rcp_f32_e32 v44, v44
	v_rcp_f32_e32 v45, v46
	v_lshlrev_b32_e32 v40, 16, v77
	v_and_b32_e32 v41, 0xffff0000, v77
	v_pk_fma_f32 v[8:9], v[30:31], v[8:9], v[36:37]
	v_pk_fma_f32 v[28:29], v[28:29], v[42:43], v[34:35]
	v_pk_fma_f32 v[10:11], v[26:27], v[10:11], v[40:41]
	v_med3_f32 v26, v9, s53, v213
	v_med3_f32 v27, v8, s53, v213
	v_med3_f32 v9, v29, s53, v213
	v_med3_f32 v28, v28, s53, v213
	v_mov_b32_e32 v8, 0
	v_lshlrev_b32_e32 v38, 16, v76
	v_and_b32_e32 v39, 0xffff0000, v76
	v_cvt_pk_fp8_f32 v8, v28, v9
	v_pk_fma_f32 v[24:25], v[24:25], v[44:45], v[38:39]
	v_mov_b32_e32 v9, 0
	v_med3_f32 v25, v25, s53, v213
	v_med3_f32 v24, v24, s53, v213
	v_cvt_pk_fp8_f32 v9, v24, v25
	v_lshlrev_b32_e32 v25, 16, v0
	v_and_b32_e32 v0, 0xffff0000, v0
	v_cvt_pk_fp8_f32 v8, v27, v26 op_sel:[0,0,1]
	v_mul_f32_e32 v0, 0xbfb8aa3b, v0
	v_lshlrev_b32_e32 v27, 16, v1
	v_exp_f32_e32 v0, v0
	v_mul_f32_e32 v27, 0xbfb8aa3b, v27
	v_exp_f32_e32 v28, v27
	v_and_b32_e32 v1, 0xffff0000, v1
	v_add_f32_e32 v0, 1.0, v0
	v_mul_f32_e32 v25, 0xbfb8aa3b, v25
	v_rcp_f32_e32 v27, v0
	v_add_f32_e32 v0, 1.0, v28
	v_mul_f32_e32 v1, 0xbfb8aa3b, v1
	v_lshlrev_b32_e32 v28, 16, v2
	v_and_b32_e32 v2, 0xffff0000, v2
	v_lshlrev_b32_e32 v29, 16, v3
	v_and_b32_e32 v3, 0xffff0000, v3
	v_exp_f32_e32 v26, v25
	v_exp_f32_e32 v1, v1
	v_mul_f32_e32 v28, 0xbfb8aa3b, v28
	v_mul_f32_e32 v2, 0xbfb8aa3b, v2
	v_mul_f32_e32 v29, 0xbfb8aa3b, v29
	v_mul_f32_e32 v3, 0xbfb8aa3b, v3
	v_exp_f32_e32 v28, v28
	v_exp_f32_e32 v2, v2
	v_exp_f32_e32 v29, v29
	v_exp_f32_e32 v3, v3
	v_add_f32_e32 v26, 1.0, v26
	v_add_f32_e32 v1, 1.0, v1
	v_rcp_f32_e32 v26, v26
	v_rcp_f32_e32 v0, v0
	v_rcp_f32_e32 v1, v1
	v_add_f32_e32 v28, 1.0, v28
	v_add_f32_e32 v30, 1.0, v2
	v_add_f32_e32 v2, 1.0, v29
	v_add_f32_e32 v3, 1.0, v3
	v_rcp_f32_e32 v28, v28
	v_rcp_f32_e32 v2, v2
	v_rcp_f32_e32 v3, v3
	v_rcp_f32_e32 v29, v30
	v_med3_f32 v11, v11, s53, v213
	v_med3_f32 v10, v10, s53, v213
	v_cvt_pk_fp8_f32 v9, v10, v11 op_sel:[0,0,1]
	v_lshlrev_b32_e32 v10, 16, v4
	v_and_b32_e32 v11, 0xffff0000, v4
	v_lshlrev_b32_e32 v4, 16, v5
	v_and_b32_e32 v5, 0xffff0000, v5
	v_lshlrev_b32_e32 v24, 16, v6
	v_and_b32_e32 v25, 0xffff0000, v6
	v_lshlrev_b32_e32 v6, 16, v7
	v_and_b32_e32 v7, 0xffff0000, v7
	v_pk_fma_f32 v[0:1], v[22:23], v[0:1], v[4:5]
	v_pk_fma_f32 v[4:5], v[20:21], v[26:27], v[10:11]
	v_pk_fma_f32 v[2:3], v[18:19], v[2:3], v[6:7]
	v_pk_fma_f32 v[6:7], v[16:17], v[28:29], v[24:25]
	v_med3_f32 v10, v1, s53, v213
	v_med3_f32 v11, v0, s53, v213
	v_med3_f32 v1, v5, s53, v213
	v_med3_f32 v4, v4, s53, v213
	v_mov_b32_e32 v0, 0
	v_med3_f32 v5, v7, s53, v213
	v_med3_f32 v6, v6, s53, v213
	v_cvt_pk_fp8_f32 v0, v4, v1
	v_mov_b32_e32 v1, 0
	v_cvt_pk_fp8_f32 v1, v6, v5
	v_med3_f32 v3, v3, s53, v213
	v_med3_f32 v2, v2, s53, v213
	v_cvt_pk_fp8_f32 v0, v11, v10 op_sel:[0,0,1]
	v_cvt_pk_fp8_f32 v1, v2, v3 op_sel:[0,0,1]
	global_store_dwordx2 v[14:15], v[12:13], off offset:128
	global_store_dwordx2 v[64:65], v[32:33], off offset:128
	global_store_dwordx2 v[56:57], v[8:9], off offset:128
	global_store_dwordx2 v[48:49], v[0:1], off offset:128
	s_cbranch_vccz .LBB0_1034
	s_waitcnt vmcnt(0)
	s_cmpk_gt_u32 s33, 0xff
	s_cbranch_scc1 .LBB0_1045
	s_barrier

.LBB0_1112:
	ds_read_b128 v[0:3], v191
	ds_read_b128 v[4:7], v195
	ds_read_b128 v[8:11], v196
	ds_read_b128 v[12:15], v197
	s_add_u32 s36, s34, 0x80
	s_addc_u32 s37, s35, 0
	s_cmp_eq_u32 s62, 12
	s_cselect_b32 s39, s21, s37
	s_cselect_b32 s38, s58, s36
	s_cselect_b32 s37, s23, s61
	s_cselect_b32 s36, s59, s60
	v_lshl_add_u64 v[144:145], s[34:35], 0, v[166:167]
	s_add_i32 m0, s43, 0xc000
	ds_read_b128 v[168:171], v208
	ds_read_b128 v[172:175], v208 offset:1024
	ds_read_b128 v[176:179], v208 offset:2048
	ds_read_b128 v[180:183], v208 offset:3072
	ds_read_b128 v[212:215], v208 offset:4096
	ds_read_b128 v[216:219], v208 offset:5120
	ds_read_b128 v[220:223], v208 offset:6144
	ds_read_b128 v[224:227], v208 offset:7168
	global_load_lds_dwordx4 v[144:145], off
	v_lshl_add_u64 v[144:145], s[34:35], 0, v[164:165]
	s_add_i32 m0, s43, 0xe000
	s_nop 0
	global_load_lds_dwordx4 v[144:145], off
	s_waitcnt lgkmcnt(8)
	s_barrier
	s_waitcnt lgkmcnt(0)
	s_waitcnt lgkmcnt(0)
	v_mfma_scale_f32_16x16x128_f8f6f4 v[140:143], v[0:7], v[168:175], v[140:143], v209, v210 op_sel_hi:[0,0,0]
	v_mfma_scale_f32_16x16x128_f8f6f4 v[136:139], v[8:15], v[168:175], v[136:139], v209, v210 op_sel_hi:[0,0,0]
	v_mfma_scale_f32_16x16x128_f8f6f4 v[132:135], v[0:7], v[176:183], v[132:135], v209, v210 op_sel_hi:[0,0,0]
	v_mfma_scale_f32_16x16x128_f8f6f4 v[128:131], v[8:15], v[176:183], v[128:131], v209, v210 op_sel_hi:[0,0,0]
	v_mfma_scale_f32_16x16x128_f8f6f4 v[124:127], v[0:7], v[212:219], v[124:127], v209, v210 op_sel_hi:[0,0,0]
	v_mfma_scale_f32_16x16x128_f8f6f4 v[120:123], v[8:15], v[212:219], v[120:123], v209, v210 op_sel_hi:[0,0,0]
	v_mfma_scale_f32_16x16x128_f8f6f4 v[116:119], v[0:7], v[220:227], v[116:119], v209, v210 op_sel_hi:[0,0,0]
	v_mfma_scale_f32_16x16x128_f8f6f4 v[112:115], v[8:15], v[220:227], v[112:115], v209, v210 op_sel_hi:[0,0,0]
	s_barrier
	s_mov_b32 m0, s44
	v_lshl_add_u64 v[144:145], s[36:37], 0, v[152:153]
	ds_read_b128 v[228:231], v192
	ds_read_b128 v[232:235], v198
	ds_read_b128 v[236:239], v199
	ds_read_b128 v[240:243], v200
	global_load_lds_dwordx4 v[144:145], off
	v_lshl_add_u64 v[146:147], s[36:37], 0, v[154:155]
	s_mov_b32 m0, s45
	s_nop 0
	global_load_lds_dwordx4 v[146:147], off
	s_barrier
	s_waitcnt lgkmcnt(0)
	s_waitcnt lgkmcnt(0)
	v_mfma_scale_f32_16x16x128_f8f6f4 v[76:79], v[228:235], v[168:175], v[76:79], v209, v210 op_sel_hi:[0,0,0]
	v_mfma_scale_f32_16x16x128_f8f6f4 v[72:75], v[236:243], v[168:175], v[72:75], v209, v210 op_sel_hi:[0,0,0]
	v_mfma_scale_f32_16x16x128_f8f6f4 v[68:71], v[228:235], v[176:183], v[68:71], v209, v210 op_sel_hi:[0,0,0]
	v_mfma_scale_f32_16x16x128_f8f6f4 v[64:67], v[236:243], v[176:183], v[64:67], v209, v210 op_sel_hi:[0,0,0]
	v_mfma_scale_f32_16x16x128_f8f6f4 v[60:63], v[228:235], v[212:219], v[60:63], v209, v210 op_sel_hi:[0,0,0]
	v_mfma_scale_f32_16x16x128_f8f6f4 v[56:59], v[236:243], v[212:219], v[56:59], v209, v210 op_sel_hi:[0,0,0]
	v_mfma_scale_f32_16x16x128_f8f6f4 v[52:55], v[228:235], v[220:227], v[52:55], v209, v210 op_sel_hi:[0,0,0]
	v_mfma_scale_f32_16x16x128_f8f6f4 v[48:51], v[236:243], v[220:227], v[48:51], v209, v210 op_sel_hi:[0,0,0]
	s_mov_b32 m0, s43
	v_lshl_add_u64 v[148:149], s[38:39], 0, v[156:157]
	s_barrier
	ds_read_b128 v[168:171], v208 offset:16384
	ds_read_b128 v[172:175], v208 offset:17408
	ds_read_b128 v[176:179], v208 offset:18432
	ds_read_b128 v[180:183], v208 offset:19456
	ds_read_b128 v[212:215], v208 offset:20480
	ds_read_b128 v[216:219], v208 offset:21504
	ds_read_b128 v[220:223], v208 offset:22528
	ds_read_b128 v[224:227], v208 offset:23552
	global_load_lds_dwordx4 v[148:149], off
	v_lshl_add_u64 v[150:151], s[38:39], 0, v[158:159]
	s_mov_b32 m0, s46
	s_nop 0
	global_load_lds_dwordx4 v[150:151], off
	s_barrier
	s_waitcnt lgkmcnt(0)
	s_waitcnt lgkmcnt(0)
	v_mfma_scale_f32_16x16x128_f8f6f4 v[108:111], v[0:7], v[168:175], v[108:111], v209, v210 op_sel_hi:[0,0,0]
	v_mfma_scale_f32_16x16x128_f8f6f4 v[104:107], v[8:15], v[168:175], v[104:107], v209, v210 op_sel_hi:[0,0,0]
	v_mfma_scale_f32_16x16x128_f8f6f4 v[100:103], v[0:7], v[176:183], v[100:103], v209, v210 op_sel_hi:[0,0,0]
	v_mfma_scale_f32_16x16x128_f8f6f4 v[96:99], v[8:15], v[176:183], v[96:99], v209, v210 op_sel_hi:[0,0,0]
	v_mfma_scale_f32_16x16x128_f8f6f4 v[92:95], v[0:7], v[212:219], v[92:95], v209, v210 op_sel_hi:[0,0,0]
	v_mfma_scale_f32_16x16x128_f8f6f4 v[88:91], v[8:15], v[212:219], v[88:91], v209, v210 op_sel_hi:[0,0,0]
	v_mfma_scale_f32_16x16x128_f8f6f4 v[84:87], v[0:7], v[220:227], v[84:87], v209, v210 op_sel_hi:[0,0,0]
	v_mfma_scale_f32_16x16x128_f8f6f4 v[80:83], v[8:15], v[220:227], v[80:83], v209, v210 op_sel_hi:[0,0,0]
	s_barrier
	s_add_u32 s64, s36, 0x40000
	s_addc_u32 s65, s37, 0
	s_mov_b32 m0, s47
	v_lshl_add_u64 v[0:1], s[64:65], 0, v[152:153]
	global_load_lds_dwordx4 v[0:1], off
	v_lshl_add_u64 v[0:1], s[64:65], 0, v[154:155]
	s_mov_b32 m0, s48
	s_nop 0
	global_load_lds_dwordx4 v[0:1], off
	s_waitcnt vmcnt(6)
	s_barrier
	v_mfma_scale_f32_16x16x128_f8f6f4 v[44:47], v[228:235], v[168:175], v[44:47], v209, v210 op_sel_hi:[0,0,0]
	v_mfma_scale_f32_16x16x128_f8f6f4 v[40:43], v[236:243], v[168:175], v[40:43], v209, v210 op_sel_hi:[0,0,0]
	v_mfma_scale_f32_16x16x128_f8f6f4 v[36:39], v[228:235], v[176:183], v[36:39], v209, v210 op_sel_hi:[0,0,0]
	v_mfma_scale_f32_16x16x128_f8f6f4 v[32:35], v[236:243], v[176:183], v[32:35], v209, v210 op_sel_hi:[0,0,0]
	v_mfma_scale_f32_16x16x128_f8f6f4 v[28:31], v[228:235], v[212:219], v[28:31], v209, v210 op_sel_hi:[0,0,0]
	v_mfma_scale_f32_16x16x128_f8f6f4 v[24:27], v[236:243], v[212:219], v[24:27], v209, v210 op_sel_hi:[0,0,0]
	v_mfma_scale_f32_16x16x128_f8f6f4 v[20:23], v[228:235], v[220:227], v[20:23], v209, v210 op_sel_hi:[0,0,0]
	v_mfma_scale_f32_16x16x128_f8f6f4 v[16:19], v[236:243], v[220:227], v[16:19], v209, v210 op_sel_hi:[0,0,0]
	s_barrier
	ds_read_b128 v[0:3], v193
	ds_read_b128 v[4:7], v201
	ds_read_b128 v[8:11], v202
	ds_read_b128 v[12:15], v203
	s_mov_b32 m0, s49
	v_lshl_add_u64 v[184:185], s[38:39], 0, v[160:161]
	ds_read_b128 v[168:171], v208 offset:32768
	ds_read_b128 v[172:175], v208 offset:33792
	ds_read_b128 v[176:179], v208 offset:34816
	ds_read_b128 v[180:183], v208 offset:35840
	ds_read_b128 v[212:215], v208 offset:36864
	ds_read_b128 v[216:219], v208 offset:37888
	ds_read_b128 v[220:223], v208 offset:38912
	ds_read_b128 v[224:227], v208 offset:39936
	global_load_lds_dwordx4 v[184:185], off
	v_lshl_add_u64 v[184:185], s[38:39], 0, v[162:163]
	s_mov_b32 m0, s50
	s_nop 0
	global_load_lds_dwordx4 v[184:185], off
	s_waitcnt lgkmcnt(8)
	s_barrier
	s_waitcnt lgkmcnt(0)
	s_waitcnt lgkmcnt(0)
	v_mfma_scale_f32_16x16x128_f8f6f4 v[140:143], v[0:7], v[168:175], v[140:143], v209, v210 op_sel_hi:[0,0,0]
	v_mfma_scale_f32_16x16x128_f8f6f4 v[136:139], v[8:15], v[168:175], v[136:139], v209, v210 op_sel_hi:[0,0,0]
	v_mfma_scale_f32_16x16x128_f8f6f4 v[132:135], v[0:7], v[176:183], v[132:135], v209, v210 op_sel_hi:[0,0,0]
	v_mfma_scale_f32_16x16x128_f8f6f4 v[128:131], v[8:15], v[176:183], v[128:131], v209, v210 op_sel_hi:[0,0,0]
	v_mfma_scale_f32_16x16x128_f8f6f4 v[124:127], v[0:7], v[212:219], v[124:127], v209, v210 op_sel_hi:[0,0,0]
	v_mfma_scale_f32_16x16x128_f8f6f4 v[120:123], v[8:15], v[212:219], v[120:123], v209, v210 op_sel_hi:[0,0,0]
	v_mfma_scale_f32_16x16x128_f8f6f4 v[116:119], v[0:7], v[220:227], v[116:119], v209, v210 op_sel_hi:[0,0,0]
	v_mfma_scale_f32_16x16x128_f8f6f4 v[112:115], v[8:15], v[220:227], v[112:115], v209, v210 op_sel_hi:[0,0,0]
	s_barrier
	s_mov_b32 m0, s52
	v_lshl_add_u64 v[144:145], v[144:145], 0, s[16:17]
	ds_read_b128 v[228:231], v194
	ds_read_b128 v[232:235], v204
	ds_read_b128 v[236:239], v205
	ds_read_b128 v[240:243], v206
	global_load_lds_dwordx4 v[144:145], off
	v_lshl_add_u64 v[144:145], v[146:147], 0, s[16:17]
	s_mov_b32 m0, s53
	s_nop 0
	global_load_lds_dwordx4 v[144:145], off
	s_barrier
	s_waitcnt lgkmcnt(0)
	s_waitcnt lgkmcnt(0)
	v_mfma_scale_f32_16x16x128_f8f6f4 v[76:79], v[228:235], v[168:175], v[76:79], v209, v210 op_sel_hi:[0,0,0]
	v_mfma_scale_f32_16x16x128_f8f6f4 v[72:75], v[236:243], v[168:175], v[72:75], v209, v210 op_sel_hi:[0,0,0]
	v_mfma_scale_f32_16x16x128_f8f6f4 v[68:71], v[228:235], v[176:183], v[68:71], v209, v210 op_sel_hi:[0,0,0]
	v_mfma_scale_f32_16x16x128_f8f6f4 v[64:67], v[236:243], v[176:183], v[64:67], v209, v210 op_sel_hi:[0,0,0]
	v_mfma_scale_f32_16x16x128_f8f6f4 v[60:63], v[228:235], v[212:219], v[60:63], v209, v210 op_sel_hi:[0,0,0]
	v_mfma_scale_f32_16x16x128_f8f6f4 v[56:59], v[236:243], v[212:219], v[56:59], v209, v210 op_sel_hi:[0,0,0]
	v_mfma_scale_f32_16x16x128_f8f6f4 v[52:55], v[228:235], v[220:227], v[52:55], v209, v210 op_sel_hi:[0,0,0]
	v_mfma_scale_f32_16x16x128_f8f6f4 v[48:51], v[236:243], v[220:227], v[48:51], v209, v210 op_sel_hi:[0,0,0]
	s_mov_b32 m0, s54
	v_lshl_add_u64 v[144:145], v[148:149], 0, s[16:17]
	s_barrier
	ds_read_b128 v[168:171], v208 offset:49152
	ds_read_b128 v[172:175], v208 offset:50176
	ds_read_b128 v[176:179], v208 offset:51200
	ds_read_b128 v[180:183], v208 offset:52224
	ds_read_b128 v[212:215], v208 offset:53248
	ds_read_b128 v[216:219], v208 offset:54272
	ds_read_b128 v[220:223], v208 offset:55296
	ds_read_b128 v[224:227], v208 offset:56320
	global_load_lds_dwordx4 v[144:145], off
	v_lshl_add_u64 v[144:145], v[150:151], 0, s[16:17]
	s_mov_b32 m0, s55
	s_nop 0
	global_load_lds_dwordx4 v[144:145], off
	s_barrier
	s_waitcnt lgkmcnt(0)
	s_waitcnt lgkmcnt(0)
	v_mfma_scale_f32_16x16x128_f8f6f4 v[108:111], v[0:7], v[168:175], v[108:111], v209, v210 op_sel_hi:[0,0,0]
	v_mfma_scale_f32_16x16x128_f8f6f4 v[104:107], v[8:15], v[168:175], v[104:107], v209, v210 op_sel_hi:[0,0,0]
	v_mfma_scale_f32_16x16x128_f8f6f4 v[100:103], v[0:7], v[176:183], v[100:103], v209, v210 op_sel_hi:[0,0,0]
	v_mfma_scale_f32_16x16x128_f8f6f4 v[96:99], v[8:15], v[176:183], v[96:99], v209, v210 op_sel_hi:[0,0,0]
	v_mfma_scale_f32_16x16x128_f8f6f4 v[92:95], v[0:7], v[212:219], v[92:95], v209, v210 op_sel_hi:[0,0,0]
	v_mfma_scale_f32_16x16x128_f8f6f4 v[88:91], v[8:15], v[212:219], v[88:91], v209, v210 op_sel_hi:[0,0,0]
	v_mfma_scale_f32_16x16x128_f8f6f4 v[84:87], v[0:7], v[220:227], v[84:87], v209, v210 op_sel_hi:[0,0,0]
	v_mfma_scale_f32_16x16x128_f8f6f4 v[80:83], v[8:15], v[220:227], v[80:83], v209, v210 op_sel_hi:[0,0,0]
	s_barrier
	s_add_u32 s36, s36, 0x40080
	s_addc_u32 s37, s37, 0
	s_mov_b32 m0, s56
	v_lshl_add_u64 v[0:1], s[36:37], 0, v[152:153]
	global_load_lds_dwordx4 v[0:1], off
	v_lshl_add_u64 v[0:1], s[36:37], 0, v[154:155]
	s_mov_b32 m0, s57
	s_nop 0
	global_load_lds_dwordx4 v[0:1], off
	s_waitcnt vmcnt(6)
	s_barrier
	v_mfma_scale_f32_16x16x128_f8f6f4 v[44:47], v[228:235], v[168:175], v[44:47], v209, v210 op_sel_hi:[0,0,0]
	v_mfma_scale_f32_16x16x128_f8f6f4 v[40:43], v[236:243], v[168:175], v[40:43], v209, v210 op_sel_hi:[0,0,0]
	v_mfma_scale_f32_16x16x128_f8f6f4 v[36:39], v[228:235], v[176:183], v[36:39], v209, v210 op_sel_hi:[0,0,0]
	v_mfma_scale_f32_16x16x128_f8f6f4 v[32:35], v[236:243], v[176:183], v[32:35], v209, v210 op_sel_hi:[0,0,0]
	v_mfma_scale_f32_16x16x128_f8f6f4 v[28:31], v[228:235], v[212:219], v[28:31], v209, v210 op_sel_hi:[0,0,0]
	v_mfma_scale_f32_16x16x128_f8f6f4 v[24:27], v[236:243], v[212:219], v[24:27], v209, v210 op_sel_hi:[0,0,0]
	v_mfma_scale_f32_16x16x128_f8f6f4 v[20:23], v[228:235], v[220:227], v[20:23], v209, v210 op_sel_hi:[0,0,0]
	v_mfma_scale_f32_16x16x128_f8f6f4 v[16:19], v[236:243], v[220:227], v[16:19], v209, v210 op_sel_hi:[0,0,0]
	s_add_i32 s62, s62, 2
	s_add_u32 s34, s34, 0x100
	s_addc_u32 s35, s35, 0
	s_add_u32 s60, s60, 0x100
	s_addc_u32 s61, s61, 0
	s_cmp_gt_u32 s62, 13
	s_barrier
	s_cbranch_scc0 .LBB0_1112
	v_lshl_or_b32 v168, s31, 8, v207
	v_lshl_add_u32 v184, s30, 8, v190
	v_ashrrev_i32_e32 v169, 31, v168
	v_lshlrev_b64 v[0:1], 2, v[168:169]
	v_ashrrev_i32_e32 v185, 31, v184
	v_or_b32_e32 v230, 16, v184
	s_ashr_i32 s21, s30, 3
	v_lshl_add_u64 v[188:189], s[0:1], 0, v[0:1]
	v_lshlrev_b64 v[2:3], 13, v[184:185]
	v_ashrrev_i32_e32 v231, 31, v230
	s_mul_hi_i32 s23, s21, 0xc000
	s_mul_i32 s21, s21, 0xc000
	s_nop 15
	s_nop 15
	v_lshl_add_u64 v[172:173], v[188:189], 0, v[2:3]
	v_lshl_add_u64 v[174:175], v[184:185], 3, s[14:15]
	v_lshlrev_b64 v[2:3], 13, v[230:231]
	v_lshl_add_u64 v[182:183], v[230:231], 3, s[14:15]
	s_add_u32 s21, s10, s21
	global_load_dwordx2 v[228:229], v[174:175], off
	global_load_dwordx4 v[212:215], v[172:173], off
	global_load_dwordx4 v[216:219], v[172:173], off offset:16
	v_lshl_add_u64 v[176:177], v[188:189], 0, v[2:3]
	global_load_dwordx2 v[232:233], v[182:183], off
	global_load_dwordx4 v[220:223], v[176:177], off
	global_load_dwordx4 v[224:227], v[176:177], off offset:16
	s_addc_u32 s23, s11, s23
	v_lshl_add_u64 v[180:181], s[6:7], 0, v[0:1]
	s_add_u32 s30, s21, 0x904000
	v_lshl_add_u64 v[178:179], s[4:5], 0, v[0:1]
	global_load_dwordx4 v[12:15], v[180:181], off
	global_load_dwordx4 v[144:147], v[178:179], off
	global_load_dwordx4 v[8:11], v[178:179], off offset:16
	global_load_dwordx4 v[148:151], v[180:181], off offset:16
	s_addc_u32 s31, s23, 0
	v_lshl_add_u64 v[0:1], s[30:31], 0, v[0:1]
	global_load_dwordx4 v[4:7], v[0:1], off
	s_nop 0
	global_load_dwordx4 v[0:3], v[0:1], off offset:16
	v_lshlrev_b64 v[170:171], 12, v[184:185]
	v_lshlrev_b64 v[186:187], 1, v[168:169]
	v_lshl_add_u64 v[170:171], s[12:13], 0, v[170:171]
	v_lshl_add_u64 v[170:171], v[170:171], 0, v[186:187]
	s_and_b64 vcc, exec, s[24:25]
	s_mov_b64 s[36:37], s[28:29]
	s_mov_b64 s[34:35], s[26:27]
	s_waitcnt vmcnt(0)
	v_sub_f32_e32 v215, v215, v228
	v_sub_f32_e32 v214, v214, v228
	v_sub_f32_e32 v213, v213, v228
	v_sub_f32_e32 v212, v212, v228
	v_sub_f32_e32 v219, v219, v228
	v_sub_f32_e32 v218, v218, v228
	v_sub_f32_e32 v217, v217, v228
	v_sub_f32_e32 v216, v216, v228
	v_sub_f32_e32 v223, v223, v232
	v_sub_f32_e32 v222, v222, v232
	v_sub_f32_e32 v221, v221, v232
	v_sub_f32_e32 v220, v220, v232
	v_sub_f32_e32 v225, v225, v232
	v_sub_f32_e32 v224, v224, v232
	v_sub_f32_e32 v227, v227, v232
	v_sub_f32_e32 v226, v226, v232
	v_pk_mul_f32 v[212:213], v[228:229], v[212:213] op_sel:[1,0]
	v_pk_mul_f32 v[214:215], v[228:229], v[214:215] op_sel:[1,0]
	v_pk_mul_f32 v[216:217], v[228:229], v[216:217] op_sel:[1,0]
	v_pk_mul_f32 v[218:219], v[228:229], v[218:219] op_sel:[1,0]
	v_pk_mul_f32 v[220:221], v[232:233], v[220:221] op_sel:[1,0]
	v_pk_mul_f32 v[222:223], v[232:233], v[222:223] op_sel:[1,0]
	v_pk_mul_f32 v[224:225], v[232:233], v[224:225] op_sel:[1,0]
	v_pk_mul_f32 v[226:227], v[232:233], v[226:227] op_sel:[1,0]
	v_pk_fma_f32 v[214:215], v[146:147], v[214:215], v[14:15]
	v_pk_fma_f32 v[212:213], v[144:145], v[212:213], v[12:13]
	v_pk_fma_f32 v[218:219], v[10:11], v[218:219], v[150:151]
	v_pk_fma_f32 v[216:217], v[8:9], v[216:217], v[148:149]
	v_pk_fma_f32 v[222:223], v[146:147], v[222:223], v[14:15]
	v_pk_fma_f32 v[220:221], v[144:145], v[220:221], v[12:13]
	v_pk_fma_f32 v[224:225], v[8:9], v[224:225], v[148:149]
	v_pk_fma_f32 v[226:227], v[10:11], v[226:227], v[150:151]
	v_pk_mul_f32 v[212:213], v[212:213], s[18:19] op_sel_hi:[1,0]
	v_pk_mul_f32 v[214:215], v[214:215], s[18:19] op_sel_hi:[1,0]
	v_pk_mul_f32 v[216:217], v[216:217], s[18:19] op_sel_hi:[1,0]
	v_pk_mul_f32 v[218:219], v[218:219], s[18:19] op_sel_hi:[1,0]
	v_pk_mul_f32 v[220:221], v[220:221], s[18:19] op_sel_hi:[1,0]
	v_pk_mul_f32 v[222:223], v[222:223], s[18:19] op_sel_hi:[1,0]
	v_pk_mul_f32 v[224:225], v[224:225], s[18:19] op_sel_hi:[1,0]
	v_pk_mul_f32 v[226:227], v[226:227], s[18:19] op_sel_hi:[1,0]
	v_pk_fma_f32 v[142:143], v[142:143], v[6:7], v[214:215]
	v_pk_fma_f32 v[140:141], v[140:141], v[4:5], v[212:213]
	v_pk_fma_f32 v[138:139], v[138:139], v[2:3], v[218:219]
	v_pk_fma_f32 v[136:137], v[136:137], v[0:1], v[216:217]
	v_pk_fma_f32 v[212:213], v[134:135], v[6:7], v[222:223]
	v_pk_fma_f32 v[214:215], v[132:133], v[4:5], v[220:221]
	v_cvt_pk_bf16_f32 v132, v140, v141
	v_cvt_pk_bf16_f32 v133, v142, v143
	v_cvt_pk_bf16_f32 v134, v136, v137
	v_cvt_pk_bf16_f32 v135, v138, v139
	v_pk_fma_f32 v[128:129], v[128:129], v[0:1], v[224:225]
	global_store_dwordx4 v[170:171], v[132:135], off
	v_or_b32_e32 v136, 32, v184
	v_ashrrev_i32_e32 v137, 31, v136
	v_pk_fma_f32 v[134:135], v[130:131], v[2:3], v[226:227]
	v_cvt_pk_bf16_f32 v130, v214, v215
	v_cvt_pk_bf16_f32 v131, v212, v213
	v_cvt_pk_bf16_f32 v132, v128, v129
	v_lshlrev_b64 v[128:129], 12, v[230:231]
	v_lshl_add_u64 v[128:129], s[12:13], 0, v[128:129]
	v_lshl_add_u64 v[128:129], v[128:129], 0, v[186:187]
	v_or_b32_e32 v226, 48, v184
	v_cvt_pk_bf16_f32 v133, v134, v135
	global_store_dwordx4 v[128:129], v[130:133], off
	v_ashrrev_i32_e32 v227, 31, v226
	v_lshlrev_b64 v[134:135], 13, v[226:227]
	v_lshlrev_b64 v[130:131], 13, v[136:137]
	v_lshl_add_u64 v[132:133], v[136:137], 3, s[14:15]
	v_lshl_add_u64 v[138:139], v[226:227], 3, s[14:15]
	v_lshl_add_u64 v[130:131], v[188:189], 0, v[130:131]
	global_load_dwordx2 v[224:225], v[132:133], off
	global_load_dwordx4 v[140:143], v[130:131], off
	global_load_dwordx4 v[212:215], v[130:131], off offset:16
	v_lshl_add_u64 v[134:135], v[188:189], 0, v[134:135]
	global_load_dwordx2 v[228:229], v[138:139], off
	global_load_dwordx4 v[216:219], v[134:135], off
	global_load_dwordx4 v[220:223], v[134:135], off offset:16
	v_lshlrev_b64 v[136:137], 12, v[136:137]
	v_lshl_add_u64 v[136:137], s[12:13], 0, v[136:137]
	v_lshlrev_b64 v[226:227], 12, v[226:227]
	v_lshl_add_u64 v[136:137], v[136:137], 0, v[186:187]
	v_add_u32_e32 v230, 0x80, v184
	v_ashrrev_i32_e32 v231, 31, v230
	v_add_u32_e32 v232, 0xa0, v184
	v_ashrrev_i32_e32 v233, 31, v232
	s_waitcnt vmcnt(0)
	v_sub_f32_e32 v143, v143, v224
	v_sub_f32_e32 v142, v142, v224
	v_sub_f32_e32 v141, v141, v224
	v_sub_f32_e32 v140, v140, v224
	v_sub_f32_e32 v217, v217, v228
	v_sub_f32_e32 v216, v216, v228
	v_sub_f32_e32 v221, v221, v228
	v_sub_f32_e32 v220, v220, v228
	v_sub_f32_e32 v215, v215, v224
	v_sub_f32_e32 v214, v214, v224
	v_sub_f32_e32 v213, v213, v224
	v_sub_f32_e32 v212, v212, v224
	v_sub_f32_e32 v223, v223, v228
	v_sub_f32_e32 v222, v222, v228
	v_pk_mul_f32 v[140:141], v[224:225], v[140:141] op_sel:[1,0]
	v_pk_mul_f32 v[142:143], v[224:225], v[142:143] op_sel:[1,0]
	v_pk_mul_f32 v[216:217], v[228:229], v[216:217] op_sel:[1,0]
	v_pk_mul_f32 v[220:221], v[228:229], v[220:221] op_sel:[1,0]
	v_sub_f32_e32 v219, v219, v228
	v_sub_f32_e32 v218, v218, v228
	v_pk_mul_f32 v[212:213], v[224:225], v[212:213] op_sel:[1,0]
	v_pk_mul_f32 v[214:215], v[224:225], v[214:215] op_sel:[1,0]
	v_pk_mul_f32 v[222:223], v[228:229], v[222:223] op_sel:[1,0]
	v_pk_fma_f32 v[142:143], v[146:147], v[142:143], v[14:15]
	v_pk_fma_f32 v[140:141], v[144:145], v[140:141], v[12:13]
	v_pk_fma_f32 v[216:217], v[144:145], v[216:217], v[12:13]
	v_pk_fma_f32 v[220:221], v[8:9], v[220:221], v[148:149]
	v_pk_mul_f32 v[218:219], v[228:229], v[218:219] op_sel:[1,0]
	v_pk_fma_f32 v[214:215], v[10:11], v[214:215], v[150:151]
	v_pk_fma_f32 v[212:213], v[8:9], v[212:213], v[148:149]
	v_pk_fma_f32 v[222:223], v[10:11], v[222:223], v[150:151]
	v_pk_mul_f32 v[140:141], v[140:141], s[18:19] op_sel_hi:[1,0]
	v_pk_mul_f32 v[142:143], v[142:143], s[18:19] op_sel_hi:[1,0]
	v_pk_mul_f32 v[216:217], v[216:217], s[18:19] op_sel_hi:[1,0]
	v_pk_mul_f32 v[220:221], v[220:221], s[18:19] op_sel_hi:[1,0]
	v_pk_fma_f32 v[218:219], v[146:147], v[218:219], v[14:15]
	v_pk_mul_f32 v[212:213], v[212:213], s[18:19] op_sel_hi:[1,0]
	v_pk_mul_f32 v[214:215], v[214:215], s[18:19] op_sel_hi:[1,0]
	v_pk_mul_f32 v[222:223], v[222:223], s[18:19] op_sel_hi:[1,0]
	v_pk_fma_f32 v[126:127], v[126:127], v[6:7], v[142:143]
	v_pk_fma_f32 v[124:125], v[124:125], v[4:5], v[140:141]
	v_pk_fma_f32 v[116:117], v[116:117], v[4:5], v[216:217]
	v_pk_fma_f32 v[142:143], v[112:113], v[0:1], v[220:221]
	v_cvt_pk_bf16_f32 v112, v124, v125
	v_pk_mul_f32 v[218:219], v[218:219], s[18:19] op_sel_hi:[1,0]
	v_pk_fma_f32 v[122:123], v[122:123], v[2:3], v[214:215]
	v_pk_fma_f32 v[120:121], v[120:121], v[0:1], v[212:213]
	v_pk_fma_f32 v[140:141], v[114:115], v[2:3], v[222:223]
	v_cvt_pk_bf16_f32 v113, v126, v127
	v_cvt_pk_bf16_f32 v114, v120, v121
	v_cvt_pk_bf16_f32 v115, v122, v123
	global_store_dwordx4 v[136:137], v[112:115], off
	v_pk_fma_f32 v[118:119], v[118:119], v[6:7], v[218:219]
	v_lshl_add_u64 v[122:123], v[230:231], 3, s[14:15]
	v_cvt_pk_bf16_f32 v112, v116, v117
	v_lshl_add_u64 v[116:117], s[12:13], 0, v[226:227]
	v_cvt_pk_bf16_f32 v113, v118, v119
	v_lshl_add_u64 v[116:117], v[116:117], 0, v[186:187]
	v_cvt_pk_bf16_f32 v114, v142, v143
	v_cvt_pk_bf16_f32 v115, v140, v141
	global_store_dwordx4 v[116:117], v[112:115], off
	v_lshlrev_b64 v[140:141], 13, v[232:233]
	s_nop 0
	v_lshlrev_b64 v[112:113], 13, v[230:231]
	v_lshl_add_u64 v[118:119], v[188:189], 0, v[112:113]
	v_add_u32_e32 v112, 0x90, v184
	v_ashrrev_i32_e32 v113, 31, v112
	v_lshlrev_b64 v[114:115], 13, v[112:113]
	v_lshl_add_u64 v[126:127], v[112:113], 3, s[14:15]
	global_load_dwordx2 v[142:143], v[122:123], off
	global_load_dwordx4 v[212:215], v[118:119], off
	global_load_dwordx4 v[216:219], v[118:119], off offset:16
	v_lshl_add_u64 v[124:125], v[188:189], 0, v[114:115]
	global_load_dwordx2 v[228:229], v[126:127], off
	global_load_dwordx4 v[220:223], v[124:125], off
	global_load_dwordx4 v[224:227], v[124:125], off offset:16
	v_lshlrev_b64 v[114:115], 12, v[230:231]
	v_lshlrev_b64 v[120:121], 12, v[112:113]
	v_lshl_add_u64 v[230:231], s[12:13], 0, v[114:115]
	v_lshl_add_u64 v[120:121], s[12:13], 0, v[120:121]
	v_lshl_add_u64 v[114:115], v[188:189], 0, v[140:141]
	v_lshl_add_u64 v[140:141], v[230:231], 0, v[186:187]
	v_lshl_add_u64 v[120:121], v[120:121], 0, v[186:187]
	v_lshl_add_u64 v[112:113], v[232:233], 3, s[14:15]
	s_waitcnt vmcnt(0)
	v_sub_f32_e32 v215, v215, v142
	v_sub_f32_e32 v214, v214, v142
	v_sub_f32_e32 v213, v213, v142
	v_sub_f32_e32 v212, v212, v142
	v_sub_f32_e32 v219, v219, v142
	v_sub_f32_e32 v218, v218, v142
	v_sub_f32_e32 v217, v217, v142
	v_sub_f32_e32 v216, v216, v142
	v_sub_f32_e32 v223, v223, v228
	v_sub_f32_e32 v222, v222, v228
	v_sub_f32_e32 v221, v221, v228
	v_sub_f32_e32 v220, v220, v228
	v_sub_f32_e32 v225, v225, v228
	v_sub_f32_e32 v224, v224, v228
	v_sub_f32_e32 v227, v227, v228
	v_sub_f32_e32 v226, v226, v228
	v_pk_mul_f32 v[212:213], v[142:143], v[212:213] op_sel:[1,0]
	v_pk_mul_f32 v[214:215], v[142:143], v[214:215] op_sel:[1,0]
	v_pk_mul_f32 v[216:217], v[142:143], v[216:217] op_sel:[1,0]
	v_pk_mul_f32 v[142:143], v[142:143], v[218:219] op_sel:[1,0]
	v_pk_mul_f32 v[218:219], v[228:229], v[220:221] op_sel:[1,0]
	v_pk_mul_f32 v[220:221], v[228:229], v[222:223] op_sel:[1,0]
	v_pk_mul_f32 v[222:223], v[228:229], v[224:225] op_sel:[1,0]
	v_pk_mul_f32 v[224:225], v[228:229], v[226:227] op_sel:[1,0]
	v_pk_fma_f32 v[212:213], v[144:145], v[212:213], v[12:13]
	v_pk_fma_f32 v[222:223], v[8:9], v[222:223], v[148:149]
	v_pk_fma_f32 v[214:215], v[146:147], v[214:215], v[14:15]
	v_pk_fma_f32 v[142:143], v[10:11], v[142:143], v[150:151]
	v_pk_fma_f32 v[216:217], v[8:9], v[216:217], v[148:149]
	v_pk_fma_f32 v[218:219], v[144:145], v[218:219], v[12:13]
	v_pk_fma_f32 v[224:225], v[10:11], v[224:225], v[150:151]
	v_pk_mul_f32 v[212:213], v[212:213], s[18:19] op_sel_hi:[1,0]
	v_pk_mul_f32 v[222:223], v[222:223], s[18:19] op_sel_hi:[1,0]
	v_pk_fma_f32 v[220:221], v[146:147], v[220:221], v[14:15]
	v_pk_mul_f32 v[214:215], v[214:215], s[18:19] op_sel_hi:[1,0]
	v_pk_mul_f32 v[216:217], v[216:217], s[18:19] op_sel_hi:[1,0]
	v_pk_mul_f32 v[142:143], v[142:143], s[18:19] op_sel_hi:[1,0]
	v_pk_mul_f32 v[218:219], v[218:219], s[18:19] op_sel_hi:[1,0]
	v_pk_mul_f32 v[224:225], v[224:225], s[18:19] op_sel_hi:[1,0]
	v_pk_fma_f32 v[108:109], v[108:109], v[4:5], v[212:213]
	v_pk_fma_f32 v[212:213], v[96:97], v[0:1], v[222:223]
	v_cvt_pk_bf16_f32 v96, v108, v109
	v_pk_mul_f32 v[220:221], v[220:221], s[18:19] op_sel_hi:[1,0]
	v_pk_fma_f32 v[110:111], v[110:111], v[6:7], v[214:215]
	v_pk_fma_f32 v[106:107], v[106:107], v[2:3], v[142:143]
	v_pk_fma_f32 v[104:105], v[104:105], v[0:1], v[216:217]
	v_pk_fma_f32 v[100:101], v[100:101], v[4:5], v[218:219]
	v_pk_fma_f32 v[142:143], v[98:99], v[2:3], v[224:225]
	v_cvt_pk_bf16_f32 v97, v110, v111
	v_cvt_pk_bf16_f32 v98, v104, v105
	v_cvt_pk_bf16_f32 v99, v106, v107
	global_store_dwordx4 v[140:141], v[96:99], off
	v_pk_fma_f32 v[102:103], v[102:103], v[6:7], v[220:221]
	s_nop 0
	v_cvt_pk_bf16_f32 v96, v100, v101
	v_cvt_pk_bf16_f32 v97, v102, v103
	v_cvt_pk_bf16_f32 v98, v212, v213
	v_cvt_pk_bf16_f32 v99, v142, v143
	global_store_dwordx4 v[120:121], v[96:99], off
	global_load_dwordx2 v[142:143], v[112:113], off
	global_load_dwordx4 v[104:107], v[114:115], off
	global_load_dwordx4 v[108:111], v[114:115], off offset:16
	v_add_u32_e32 v96, 0xb0, v184
	v_ashrrev_i32_e32 v97, 31, v96
	v_lshlrev_b64 v[98:99], 13, v[96:97]
	v_lshl_add_u64 v[102:103], v[96:97], 3, s[14:15]
	v_lshl_add_u64 v[100:101], v[188:189], 0, v[98:99]
	global_load_dwordx2 v[184:185], v[102:103], off
	global_load_dwordx4 v[212:215], v[100:101], off
	global_load_dwordx4 v[216:219], v[100:101], off offset:16
	v_lshlrev_b64 v[98:99], 12, v[232:233]
	v_lshlrev_b64 v[96:97], 12, v[96:97]
	v_lshl_add_u64 v[98:99], s[12:13], 0, v[98:99]
	v_lshl_add_u64 v[96:97], s[12:13], 0, v[96:97]
	v_lshl_add_u64 v[98:99], v[98:99], 0, v[186:187]
	v_lshl_add_u64 v[96:97], v[96:97], 0, v[186:187]
	s_waitcnt vmcnt(0)
	v_sub_f32_e32 v107, v107, v142
	v_sub_f32_e32 v106, v106, v142
	v_sub_f32_e32 v105, v105, v142
	v_sub_f32_e32 v104, v104, v142
	v_sub_f32_e32 v111, v111, v142
	v_sub_f32_e32 v110, v110, v142
	v_sub_f32_e32 v109, v109, v142
	v_sub_f32_e32 v108, v108, v142
	v_sub_f32_e32 v187, v215, v184
	v_sub_f32_e32 v186, v214, v184
	v_sub_f32_e32 v189, v213, v184
	v_sub_f32_e32 v188, v212, v184
	v_sub_f32_e32 v213, v219, v184
	v_sub_f32_e32 v212, v218, v184
	v_sub_f32_e32 v215, v217, v184
	v_sub_f32_e32 v214, v216, v184
	v_pk_mul_f32 v[104:105], v[142:143], v[104:105] op_sel:[1,0]
	v_pk_mul_f32 v[106:107], v[142:143], v[106:107] op_sel:[1,0]
	v_pk_mul_f32 v[108:109], v[142:143], v[108:109] op_sel:[1,0]
	v_pk_mul_f32 v[110:111], v[142:143], v[110:111] op_sel:[1,0]
	v_pk_mul_f32 v[142:143], v[184:185], v[188:189] op_sel:[1,0]
	v_pk_mul_f32 v[186:187], v[184:185], v[186:187] op_sel:[1,0]
	v_pk_mul_f32 v[188:189], v[184:185], v[214:215] op_sel:[1,0]
	v_pk_mul_f32 v[184:185], v[184:185], v[212:213] op_sel:[1,0]
	v_pk_fma_f32 v[106:107], v[146:147], v[106:107], v[14:15]
	v_pk_fma_f32 v[104:105], v[144:145], v[104:105], v[12:13]
	v_pk_fma_f32 v[110:111], v[10:11], v[110:111], v[150:151]
	v_pk_fma_f32 v[108:109], v[8:9], v[108:109], v[148:149]
	v_pk_fma_f32 v[10:11], v[10:11], v[184:185], v[150:151]
	v_pk_fma_f32 v[8:9], v[8:9], v[188:189], v[148:149]
	v_pk_fma_f32 v[14:15], v[146:147], v[186:187], v[14:15]
	v_pk_fma_f32 v[12:13], v[144:145], v[142:143], v[12:13]
	v_pk_mul_f32 v[104:105], v[104:105], s[18:19] op_sel_hi:[1,0]
	v_pk_mul_f32 v[106:107], v[106:107], s[18:19] op_sel_hi:[1,0]
	v_pk_mul_f32 v[108:109], v[108:109], s[18:19] op_sel_hi:[1,0]
	v_pk_mul_f32 v[110:111], v[110:111], s[18:19] op_sel_hi:[1,0]
	v_pk_mul_f32 v[8:9], v[8:9], s[18:19] op_sel_hi:[1,0]
	v_pk_mul_f32 v[10:11], v[10:11], s[18:19] op_sel_hi:[1,0]
	v_pk_mul_f32 v[12:13], v[12:13], s[18:19] op_sel_hi:[1,0]
	v_pk_mul_f32 v[14:15], v[14:15], s[18:19] op_sel_hi:[1,0]
	v_pk_fma_f32 v[94:95], v[94:95], v[6:7], v[106:107]
	v_pk_fma_f32 v[92:93], v[92:93], v[4:5], v[104:105]
	v_pk_fma_f32 v[90:91], v[90:91], v[2:3], v[110:111]
	v_pk_fma_f32 v[88:89], v[88:89], v[0:1], v[108:109]
	v_pk_fma_f32 v[10:11], v[82:83], v[2:3], v[10:11]
	v_pk_fma_f32 v[8:9], v[80:81], v[0:1], v[8:9]
	v_cvt_pk_bf16_f32 v0, v92, v93
	v_cvt_pk_bf16_f32 v1, v94, v95
	v_cvt_pk_bf16_f32 v2, v88, v89
	v_cvt_pk_bf16_f32 v3, v90, v91
	v_pk_fma_f32 v[6:7], v[86:87], v[6:7], v[14:15]
	v_pk_fma_f32 v[4:5], v[84:85], v[4:5], v[12:13]
	global_store_dwordx4 v[98:99], v[0:3], off
	s_nop 1
	v_cvt_pk_bf16_f32 v0, v4, v5
	v_cvt_pk_bf16_f32 v1, v6, v7
	v_cvt_pk_bf16_f32 v2, v8, v9
	v_cvt_pk_bf16_f32 v3, v10, v11
	global_store_dwordx4 v[96:97], v[0:3], off
	global_load_dwordx2 v[142:143], v[174:175], off
	global_load_dwordx4 v[88:91], v[172:173], off offset:512
	global_load_dwordx4 v[92:95], v[172:173], off offset:528
	global_load_dwordx2 v[144:145], v[182:183], off
	global_load_dwordx4 v[104:107], v[176:177], off offset:512
	global_load_dwordx4 v[108:111], v[176:177], off offset:528
	global_load_dwordx4 v[12:15], v[180:181], off offset:512
	global_load_dwordx4 v[80:83], v[178:179], off offset:512
	global_load_dwordx4 v[8:11], v[178:179], off offset:528
	global_load_dwordx4 v[84:87], v[180:181], off offset:528
	v_or_b32_e32 v0, 0x80, v168
	v_ashrrev_i32_e32 v1, 31, v0
	v_lshl_add_u64 v[0:1], v[0:1], 2, s[30:31]
	global_load_dwordx4 v[4:7], v[0:1], off
	s_nop 0
	global_load_dwordx4 v[0:3], v[0:1], off offset:16
	s_mov_b32 s31, s22
	s_mov_b32 s30, s20
	s_waitcnt vmcnt(0)
	v_sub_f32_e32 v91, v91, v142
	v_sub_f32_e32 v90, v90, v142
	v_sub_f32_e32 v89, v89, v142
	v_sub_f32_e32 v88, v88, v142
	v_sub_f32_e32 v95, v95, v142
	v_sub_f32_e32 v94, v94, v142
	v_sub_f32_e32 v93, v93, v142
	v_sub_f32_e32 v92, v92, v142
	v_sub_f32_e32 v111, v111, v144
	v_sub_f32_e32 v110, v110, v144
	v_sub_f32_e32 v109, v109, v144
	v_sub_f32_e32 v108, v108, v144
	v_sub_f32_e32 v107, v107, v144
	v_sub_f32_e32 v106, v106, v144
	v_sub_f32_e32 v105, v105, v144
	v_sub_f32_e32 v104, v104, v144
	v_pk_mul_f32 v[88:89], v[142:143], v[88:89] op_sel:[1,0]
	v_pk_mul_f32 v[90:91], v[142:143], v[90:91] op_sel:[1,0]
	v_pk_mul_f32 v[92:93], v[142:143], v[92:93] op_sel:[1,0]
	v_pk_mul_f32 v[94:95], v[142:143], v[94:95] op_sel:[1,0]
	v_pk_mul_f32 v[108:109], v[144:145], v[108:109] op_sel:[1,0]
	v_pk_mul_f32 v[110:111], v[144:145], v[110:111] op_sel:[1,0]
	v_pk_mul_f32 v[104:105], v[144:145], v[104:105] op_sel:[1,0]
	v_pk_mul_f32 v[106:107], v[144:145], v[106:107] op_sel:[1,0]
	v_pk_fma_f32 v[90:91], v[82:83], v[90:91], v[14:15]
	v_pk_fma_f32 v[88:89], v[80:81], v[88:89], v[12:13]
	v_pk_fma_f32 v[94:95], v[10:11], v[94:95], v[86:87]
	v_pk_fma_f32 v[92:93], v[8:9], v[92:93], v[84:85]
	v_pk_fma_f32 v[110:111], v[10:11], v[110:111], v[86:87]
	v_pk_fma_f32 v[108:109], v[8:9], v[108:109], v[84:85]
	v_pk_fma_f32 v[106:107], v[82:83], v[106:107], v[14:15]
	v_pk_fma_f32 v[104:105], v[80:81], v[104:105], v[12:13]
	v_pk_mul_f32 v[88:89], v[88:89], s[18:19] op_sel_hi:[1,0]
	v_pk_mul_f32 v[90:91], v[90:91], s[18:19] op_sel_hi:[1,0]
	v_pk_mul_f32 v[92:93], v[92:93], s[18:19] op_sel_hi:[1,0]
	v_pk_mul_f32 v[94:95], v[94:95], s[18:19] op_sel_hi:[1,0]
	v_pk_mul_f32 v[108:109], v[108:109], s[18:19] op_sel_hi:[1,0]
	v_pk_mul_f32 v[110:111], v[110:111], s[18:19] op_sel_hi:[1,0]
	v_pk_mul_f32 v[104:105], v[104:105], s[18:19] op_sel_hi:[1,0]
	v_pk_mul_f32 v[106:107], v[106:107], s[18:19] op_sel_hi:[1,0]
	v_pk_fma_f32 v[78:79], v[78:79], v[6:7], v[90:91]
	v_pk_fma_f32 v[76:77], v[76:77], v[4:5], v[88:89]
	v_pk_fma_f32 v[74:75], v[74:75], v[2:3], v[94:95]
	v_pk_fma_f32 v[72:73], v[72:73], v[0:1], v[92:93]
	v_pk_fma_f32 v[88:89], v[66:67], v[2:3], v[110:111]
	v_pk_fma_f32 v[90:91], v[64:65], v[0:1], v[108:109]
	v_cvt_pk_bf16_f32 v64, v76, v77
	v_cvt_pk_bf16_f32 v65, v78, v79
	v_cvt_pk_bf16_f32 v66, v72, v73
	v_cvt_pk_bf16_f32 v67, v74, v75
	v_pk_fma_f32 v[70:71], v[70:71], v[6:7], v[106:107]
	v_pk_fma_f32 v[68:69], v[68:69], v[4:5], v[104:105]
	global_store_dwordx4 v[170:171], v[64:67], off offset:256
	s_nop 1
	v_cvt_pk_bf16_f32 v64, v68, v69
	v_cvt_pk_bf16_f32 v65, v70, v71
	v_cvt_pk_bf16_f32 v66, v90, v91
	v_cvt_pk_bf16_f32 v67, v88, v89
	global_store_dwordx4 v[128:129], v[64:67], off offset:256
	global_load_dwordx2 v[88:89], v[132:133], off
	global_load_dwordx4 v[64:67], v[130:131], off offset:512
	global_load_dwordx4 v[68:71], v[130:131], off offset:528
	global_load_dwordx2 v[90:91], v[138:139], off
	global_load_dwordx4 v[72:75], v[134:135], off offset:512
	global_load_dwordx4 v[76:79], v[134:135], off offset:528
	s_waitcnt vmcnt(0)
	v_sub_f32_e32 v67, v67, v88
	v_sub_f32_e32 v66, v66, v88
	v_sub_f32_e32 v65, v65, v88
	v_sub_f32_e32 v64, v64, v88
	v_sub_f32_e32 v71, v71, v88
	v_sub_f32_e32 v70, v70, v88
	v_sub_f32_e32 v69, v69, v88
	v_sub_f32_e32 v68, v68, v88
	v_sub_f32_e32 v79, v79, v90
	v_sub_f32_e32 v78, v78, v90
	v_sub_f32_e32 v77, v77, v90
	v_sub_f32_e32 v76, v76, v90
	v_sub_f32_e32 v75, v75, v90
	v_sub_f32_e32 v74, v74, v90
	v_sub_f32_e32 v73, v73, v90
	v_sub_f32_e32 v72, v72, v90
	v_pk_mul_f32 v[64:65], v[88:89], v[64:65] op_sel:[1,0]
	v_pk_mul_f32 v[66:67], v[88:89], v[66:67] op_sel:[1,0]
	v_pk_mul_f32 v[68:69], v[88:89], v[68:69] op_sel:[1,0]
	v_pk_mul_f32 v[70:71], v[88:89], v[70:71] op_sel:[1,0]
	v_pk_mul_f32 v[76:77], v[90:91], v[76:77] op_sel:[1,0]
	v_pk_mul_f32 v[78:79], v[90:91], v[78:79] op_sel:[1,0]
	v_pk_mul_f32 v[72:73], v[90:91], v[72:73] op_sel:[1,0]
	v_pk_mul_f32 v[74:75], v[90:91], v[74:75] op_sel:[1,0]
	v_pk_fma_f32 v[66:67], v[82:83], v[66:67], v[14:15]
	v_pk_fma_f32 v[64:65], v[80:81], v[64:65], v[12:13]
	v_pk_fma_f32 v[70:71], v[10:11], v[70:71], v[86:87]
	v_pk_fma_f32 v[68:69], v[8:9], v[68:69], v[84:85]
	v_pk_fma_f32 v[78:79], v[10:11], v[78:79], v[86:87]
	v_pk_fma_f32 v[76:77], v[8:9], v[76:77], v[84:85]
	v_pk_fma_f32 v[74:75], v[82:83], v[74:75], v[14:15]
	v_pk_fma_f32 v[72:73], v[80:81], v[72:73], v[12:13]
	v_pk_mul_f32 v[64:65], v[64:65], s[18:19] op_sel_hi:[1,0]
	v_pk_mul_f32 v[66:67], v[66:67], s[18:19] op_sel_hi:[1,0]
	v_pk_mul_f32 v[68:69], v[68:69], s[18:19] op_sel_hi:[1,0]
	v_pk_mul_f32 v[70:71], v[70:71], s[18:19] op_sel_hi:[1,0]
	v_pk_mul_f32 v[76:77], v[76:77], s[18:19] op_sel_hi:[1,0]
	v_pk_mul_f32 v[78:79], v[78:79], s[18:19] op_sel_hi:[1,0]
	v_pk_mul_f32 v[72:73], v[72:73], s[18:19] op_sel_hi:[1,0]
	v_pk_mul_f32 v[74:75], v[74:75], s[18:19] op_sel_hi:[1,0]
	v_pk_fma_f32 v[62:63], v[62:63], v[6:7], v[66:67]
	v_pk_fma_f32 v[60:61], v[60:61], v[4:5], v[64:65]
	v_pk_fma_f32 v[58:59], v[58:59], v[2:3], v[70:71]
	v_pk_fma_f32 v[56:57], v[56:57], v[0:1], v[68:69]
	v_pk_fma_f32 v[64:65], v[50:51], v[2:3], v[78:79]
	v_pk_fma_f32 v[66:67], v[48:49], v[0:1], v[76:77]
	v_cvt_pk_bf16_f32 v48, v60, v61
	v_cvt_pk_bf16_f32 v49, v62, v63
	v_cvt_pk_bf16_f32 v50, v56, v57
	v_cvt_pk_bf16_f32 v51, v58, v59
	v_pk_fma_f32 v[54:55], v[54:55], v[6:7], v[74:75]
	v_pk_fma_f32 v[52:53], v[52:53], v[4:5], v[72:73]
	global_store_dwordx4 v[136:137], v[48:51], off offset:256
	s_nop 1
	v_cvt_pk_bf16_f32 v48, v52, v53
	v_cvt_pk_bf16_f32 v49, v54, v55
	v_cvt_pk_bf16_f32 v50, v66, v67
	v_cvt_pk_bf16_f32 v51, v64, v65
	global_store_dwordx4 v[116:117], v[48:51], off offset:256
	global_load_dwordx2 v[64:65], v[122:123], off
	global_load_dwordx4 v[48:51], v[118:119], off offset:512
	global_load_dwordx4 v[52:55], v[118:119], off offset:528
	global_load_dwordx2 v[66:67], v[126:127], off
	global_load_dwordx4 v[56:59], v[124:125], off offset:512
	global_load_dwordx4 v[60:63], v[124:125], off offset:528
	s_waitcnt vmcnt(0)
	v_sub_f32_e32 v51, v51, v64
	v_sub_f32_e32 v50, v50, v64
	v_sub_f32_e32 v49, v49, v64
	v_sub_f32_e32 v48, v48, v64
	v_sub_f32_e32 v55, v55, v64
	v_sub_f32_e32 v54, v54, v64
	v_sub_f32_e32 v53, v53, v64
	v_sub_f32_e32 v52, v52, v64
	v_sub_f32_e32 v63, v63, v66
	v_sub_f32_e32 v62, v62, v66
	v_sub_f32_e32 v61, v61, v66
	v_sub_f32_e32 v60, v60, v66
	v_sub_f32_e32 v59, v59, v66
	v_sub_f32_e32 v58, v58, v66
	v_sub_f32_e32 v57, v57, v66
	v_sub_f32_e32 v56, v56, v66
	v_pk_mul_f32 v[48:49], v[64:65], v[48:49] op_sel:[1,0]
	v_pk_mul_f32 v[50:51], v[64:65], v[50:51] op_sel:[1,0]
	v_pk_mul_f32 v[52:53], v[64:65], v[52:53] op_sel:[1,0]
	v_pk_mul_f32 v[54:55], v[64:65], v[54:55] op_sel:[1,0]
	v_pk_mul_f32 v[60:61], v[66:67], v[60:61] op_sel:[1,0]
	v_pk_mul_f32 v[62:63], v[66:67], v[62:63] op_sel:[1,0]
	v_pk_mul_f32 v[56:57], v[66:67], v[56:57] op_sel:[1,0]
	v_pk_mul_f32 v[58:59], v[66:67], v[58:59] op_sel:[1,0]
	v_pk_fma_f32 v[50:51], v[82:83], v[50:51], v[14:15]
	v_pk_fma_f32 v[48:49], v[80:81], v[48:49], v[12:13]
	v_pk_fma_f32 v[54:55], v[10:11], v[54:55], v[86:87]
	v_pk_fma_f32 v[52:53], v[8:9], v[52:53], v[84:85]
	v_pk_fma_f32 v[62:63], v[10:11], v[62:63], v[86:87]
	v_pk_fma_f32 v[60:61], v[8:9], v[60:61], v[84:85]
	v_pk_fma_f32 v[58:59], v[82:83], v[58:59], v[14:15]
	v_pk_fma_f32 v[56:57], v[80:81], v[56:57], v[12:13]
	v_pk_mul_f32 v[48:49], v[48:49], s[18:19] op_sel_hi:[1,0]
	v_pk_mul_f32 v[50:51], v[50:51], s[18:19] op_sel_hi:[1,0]
	v_pk_mul_f32 v[52:53], v[52:53], s[18:19] op_sel_hi:[1,0]
	v_pk_mul_f32 v[54:55], v[54:55], s[18:19] op_sel_hi:[1,0]
	v_pk_mul_f32 v[60:61], v[60:61], s[18:19] op_sel_hi:[1,0]
	v_pk_mul_f32 v[62:63], v[62:63], s[18:19] op_sel_hi:[1,0]
	v_pk_mul_f32 v[56:57], v[56:57], s[18:19] op_sel_hi:[1,0]
	v_pk_mul_f32 v[58:59], v[58:59], s[18:19] op_sel_hi:[1,0]
	v_pk_fma_f32 v[46:47], v[46:47], v[6:7], v[50:51]
	v_pk_fma_f32 v[44:45], v[44:45], v[4:5], v[48:49]
	v_pk_fma_f32 v[42:43], v[42:43], v[2:3], v[54:55]
	v_pk_fma_f32 v[40:41], v[40:41], v[0:1], v[52:53]
	v_pk_fma_f32 v[48:49], v[34:35], v[2:3], v[62:63]
	v_pk_fma_f32 v[50:51], v[32:33], v[0:1], v[60:61]
	v_cvt_pk_bf16_f32 v32, v44, v45
	v_cvt_pk_bf16_f32 v33, v46, v47
	v_cvt_pk_bf16_f32 v34, v40, v41
	v_cvt_pk_bf16_f32 v35, v42, v43
	v_pk_fma_f32 v[38:39], v[38:39], v[6:7], v[58:59]
	v_pk_fma_f32 v[36:37], v[36:37], v[4:5], v[56:57]
	global_store_dwordx4 v[140:141], v[32:35], off offset:256
	s_nop 1
	v_cvt_pk_bf16_f32 v32, v36, v37
	v_cvt_pk_bf16_f32 v33, v38, v39
	v_cvt_pk_bf16_f32 v34, v50, v51
	v_cvt_pk_bf16_f32 v35, v48, v49
	global_store_dwordx4 v[120:121], v[32:35], off offset:256
	global_load_dwordx2 v[48:49], v[112:113], off
	global_load_dwordx4 v[32:35], v[114:115], off offset:512
	global_load_dwordx4 v[36:39], v[114:115], off offset:528
	global_load_dwordx2 v[50:51], v[102:103], off
	global_load_dwordx4 v[40:43], v[100:101], off offset:512
	global_load_dwordx4 v[44:47], v[100:101], off offset:528
	s_waitcnt vmcnt(0)
	v_sub_f32_e32 v35, v35, v48
	v_sub_f32_e32 v34, v34, v48
	v_sub_f32_e32 v33, v33, v48
	v_sub_f32_e32 v32, v32, v48
	v_sub_f32_e32 v39, v39, v48
	v_sub_f32_e32 v38, v38, v48
	v_sub_f32_e32 v37, v37, v48
	v_sub_f32_e32 v36, v36, v48
	v_sub_f32_e32 v47, v47, v50
	v_sub_f32_e32 v46, v46, v50
	v_sub_f32_e32 v45, v45, v50
	v_sub_f32_e32 v44, v44, v50
	v_sub_f32_e32 v43, v43, v50
	v_sub_f32_e32 v42, v42, v50
	v_sub_f32_e32 v41, v41, v50
	v_sub_f32_e32 v40, v40, v50
	v_pk_mul_f32 v[32:33], v[48:49], v[32:33] op_sel:[1,0]
	v_pk_mul_f32 v[34:35], v[48:49], v[34:35] op_sel:[1,0]
	v_pk_mul_f32 v[36:37], v[48:49], v[36:37] op_sel:[1,0]
	v_pk_mul_f32 v[38:39], v[48:49], v[38:39] op_sel:[1,0]
	v_pk_mul_f32 v[44:45], v[50:51], v[44:45] op_sel:[1,0]
	v_pk_mul_f32 v[46:47], v[50:51], v[46:47] op_sel:[1,0]
	v_pk_mul_f32 v[40:41], v[50:51], v[40:41] op_sel:[1,0]
	v_pk_mul_f32 v[42:43], v[50:51], v[42:43] op_sel:[1,0]
	v_pk_fma_f32 v[34:35], v[82:83], v[34:35], v[14:15]
	v_pk_fma_f32 v[32:33], v[80:81], v[32:33], v[12:13]
	v_pk_fma_f32 v[38:39], v[10:11], v[38:39], v[86:87]
	v_pk_fma_f32 v[36:37], v[8:9], v[36:37], v[84:85]
	v_pk_fma_f32 v[10:11], v[10:11], v[46:47], v[86:87]
	v_pk_fma_f32 v[8:9], v[8:9], v[44:45], v[84:85]
	v_pk_fma_f32 v[14:15], v[82:83], v[42:43], v[14:15]
	v_pk_fma_f32 v[12:13], v[80:81], v[40:41], v[12:13]
	v_pk_mul_f32 v[32:33], v[32:33], s[18:19] op_sel_hi:[1,0]
	v_pk_mul_f32 v[34:35], v[34:35], s[18:19] op_sel_hi:[1,0]
	v_pk_mul_f32 v[36:37], v[36:37], s[18:19] op_sel_hi:[1,0]
	v_pk_mul_f32 v[38:39], v[38:39], s[18:19] op_sel_hi:[1,0]
	v_pk_mul_f32 v[8:9], v[8:9], s[18:19] op_sel_hi:[1,0]
	v_pk_mul_f32 v[10:11], v[10:11], s[18:19] op_sel_hi:[1,0]
	v_pk_mul_f32 v[12:13], v[12:13], s[18:19] op_sel_hi:[1,0]
	v_pk_mul_f32 v[14:15], v[14:15], s[18:19] op_sel_hi:[1,0]
	v_pk_fma_f32 v[30:31], v[30:31], v[6:7], v[34:35]
	v_pk_fma_f32 v[28:29], v[28:29], v[4:5], v[32:33]
	v_pk_fma_f32 v[26:27], v[26:27], v[2:3], v[38:39]
	v_pk_fma_f32 v[24:25], v[24:25], v[0:1], v[36:37]
	v_pk_fma_f32 v[10:11], v[18:19], v[2:3], v[10:11]
	v_pk_fma_f32 v[8:9], v[16:17], v[0:1], v[8:9]
	v_cvt_pk_bf16_f32 v0, v28, v29
	v_cvt_pk_bf16_f32 v1, v30, v31
	v_cvt_pk_bf16_f32 v2, v24, v25
	v_cvt_pk_bf16_f32 v3, v26, v27
	v_pk_fma_f32 v[6:7], v[22:23], v[6:7], v[14:15]
	v_pk_fma_f32 v[4:5], v[20:21], v[4:5], v[12:13]
	global_store_dwordx4 v[98:99], v[0:3], off offset:256
	s_nop 1
	v_cvt_pk_bf16_f32 v0, v4, v5
	v_cvt_pk_bf16_f32 v1, v6, v7
	v_cvt_pk_bf16_f32 v2, v8, v9
	v_cvt_pk_bf16_f32 v3, v10, v11
	global_store_dwordx4 v[96:97], v[0:3], off offset:256
	s_cbranch_vccz .LBB0_1105
	s_waitcnt vmcnt(0)
	s_cmpk_gt_u32 s19, 0xff
	s_cbranch_scc1 .LBB0_1116
	s_barrier

.LBB0_1171:
	s_setprio 0
	s_mov_b64 s[4:5], s[86:87]
	s_mov_b32 s8, 0
	s_cmp_lt_i32 s82, 10
	s_cselect_b64 s[6:7], -1, 0
	v_mbcnt_lo_u32_b32 v0, -1, s8
	v_mbcnt_hi_u32_b32 v0, -1, v0
	v_or_b32_e32 v162, s92, v0
	s_and_b64 s[14:15], s[6:7], s[0:1]
	s_andn2_b64 vcc, exec, s[14:15]
	v_readfirstlane_b32 s12, v162
	s_cbranch_vccnz .LBB0_1245
	s_load_dwordx2 s[18:19], s[4:5], 0x138
	s_ashr_i32 s33, s12, 6
	v_and_b32_e32 v65, 63, v162
	s_mov_b64 s[16:17], s[86:87]
	s_cmp_lt_i32 s33, 4
	s_mov_b64 s[0:1], -1
	s_cbranch_scc0 .LBB0_1223
	s_mul_i32 s0, s33, s3
	s_add_i32 s20, s0, s2
	s_cmpk_gt_i32 s20, 0x3ff
	s_cbranch_scc1 .LBB0_1222
	s_waitcnt lgkmcnt(0)
	s_add_u32 s42, s18, 0x900000
	s_mul_i32 s0, s33, 0x5000
	s_addc_u32 s43, s19, 0
	s_add_i32 s13, s0, 0
	s_add_u32 s0, s18, 0x68700000
	v_mov_b32_e32 v67, 0
	v_lshrrev_b32_e32 v8, 4, v65
	s_addc_u32 s1, s19, 0
	v_lshlrev_b32_e32 v0, 3, v65
	v_mov_b32_e32 v1, v67
	v_and_b32_e32 v64, 15, v162
	v_lshl_add_u64 v[68:69], s[0:1], 0, v[0:1]
	v_lshlrev_b32_e32 v0, 10, v8
	v_lshl_add_u64 v[70:71], s[0:1], 0, v[0:1]
	v_lshl_or_b32 v0, v8, 5, v64
	v_mul_u32_u24_e32 v9, 0x110, v0
	v_mov_b32_e32 v0, s13
	s_movk_i32 s0, 0x84
	v_mad_u32_u24 v164, v65, s0, v0
	s_add_i32 s44, 0, 0x18800
	s_add_i32 s0, 0, 0x18880
	s_cmpk_lg_i32 s3, 0x100
	s_cselect_b64 s[26:27], -1, 0
	s_add_u32 s28, s18, 0x10000
	s_addc_u32 s29, s19, 0
	v_lshlrev_b32_e32 v66, 2, v65
	s_cmp_lt_u32 s12, 64
	v_cmp_gt_u32_e32 vcc, 32, v65
	v_add_u32_e32 v168, s0, v66
	s_cselect_b64 s[0:1], -1, 0
	s_and_b64 s[30:31], s[0:1], vcc
	v_or_b32_e32 v6, 0x400, v66
	v_mov_b32_e32 v7, v67
	s_add_u32 s34, s18, 0xb40000
	v_lshlrev_b64 v[78:79], 2, v[6:7]
	v_or_b32_e32 v6, 0x500, v66
	s_addc_u32 s35, s19, 0
	v_lshlrev_b64 v[84:85], 2, v[6:7]
	v_or_b32_e32 v6, 0x600, v66
	s_add_u32 s36, s18, 0xb80000
	s_load_dwordx4 s[8:11], s[16:17], 0xd0
	s_load_dwordx2 s[22:23], s[16:17], 0xe0
	v_lshlrev_b32_e32 v0, 7, v65
	v_lshlrev_b64 v[90:91], 2, v[6:7]
	v_or_b32_e32 v6, 0x700, v66
	s_addc_u32 s37, s19, 0
	v_sub_u32_e32 v165, v164, v0
	v_or_b32_e32 v0, 0x100, v66
	v_lshlrev_b64 v[96:97], 2, v[6:7]
	v_mul_u32_u24_e32 v6, 0x210, v8
	v_lshlrev_b32_e32 v7, 2, v64
	s_add_u32 s38, s18, 0xbc0000
	v_add3_u32 v170, s13, v6, v7
	v_lshlrev_b32_e32 v6, 8, v65
	v_mov_b32_e32 v7, v67
	s_addc_u32 s39, s19, 0
	v_lshlrev_b64 v[106:107], 2, v[0:1]
	v_add_u32_e32 v0, 0, v9
	v_lshlrev_b64 v[72:73], 2, v[66:67]
	v_mul_u32_u24_e32 v10, 12, v65
	v_or_b32_e32 v2, 0x200, v66
	v_mov_b32_e32 v3, v67
	v_or_b32_e32 v4, 0x300, v66
	v_mov_b32_e32 v5, v67
	v_lshl_add_u64 v[102:103], s[28:29], 0, v[6:7]
	s_add_u32 s40, s18, 0xc00000
	v_lshl_add_u64 v[6:7], s[18:19], 0, v[66:67]
	s_mov_b64 s[0:1], 0x70700000
	v_add_u32_e32 v176, 0x18800, v0
	v_mbcnt_lo_u32_b32 v0, -1, 0
	s_mov_b32 s25, 0
	v_cmp_eq_u32_e64 s[6:7], 0, v65
	v_lshl_add_u32 v163, v8, 11, s13
	v_cmp_gt_u32_e64 s[4:5], 16, v65
	v_lshrrev_b32_e32 v166, 2, v65
	v_add_u32_e32 v167, s44, v66
	v_and_b32_e32 v169, 3, v162
	s_waitcnt lgkmcnt(0)
	v_lshl_add_u64 v[74:75], s[8:9], 0, v[72:73]
	v_lshl_add_u64 v[76:77], s[10:11], 0, v[72:73]
	s_movk_i32 s45, 0x100
	s_movk_i32 s46, 0x200
	s_movk_i32 s47, 0x400
	v_lshl_add_u64 v[80:81], s[8:9], 0, v[78:79]
	v_lshl_add_u64 v[82:83], s[10:11], 0, v[78:79]
	v_lshl_add_u64 v[86:87], s[8:9], 0, v[84:85]
	v_lshl_add_u64 v[88:89], s[10:11], 0, v[84:85]
	v_lshl_add_u64 v[92:93], s[8:9], 0, v[90:91]
	v_lshl_add_u64 v[94:95], s[10:11], 0, v[90:91]
	v_lshl_add_u64 v[98:99], s[8:9], 0, v[96:97]
	v_lshl_add_u64 v[100:101], s[10:11], 0, v[96:97]
	v_lshl_add_u32 v171, v65, 4, s13
	s_addc_u32 s41, s19, 0
	s_lshl_b32 s48, s3, 2
	v_lshl_add_u64 v[104:105], v[6:7], 0, s[0:1]
	s_lshl_b32 s49, s20, 4
	s_lshl_b32 s50, s3, 6
	v_lshlrev_b32_e32 v172, 11, v64
	v_add_u32_e32 v173, v165, v10
	v_lshlrev_b64 v[108:109], 2, v[2:3]
	v_lshlrev_b64 v[110:111], 2, v[4:5]
	s_movk_i32 s51, 0x800
	v_mov_b32_e32 v174, 0x3727c5ac
	s_mov_b32 s52, 0xf800000
	v_mov_b32_e32 v175, 0x260
	s_mov_b32 s53, 0x8000
	s_movk_i32 s54, 0x1000
	s_mov_b32 s55, 0x10000
	s_mov_b32 s56, 0x11000
	s_mov_b32 s57, 0x20000
	s_mov_b32 s58, 0x21000
	s_mov_b32 s59, 0x30000
	s_mov_b32 s60, 0x31000
	s_add_i32 s61, 0, 0x27440
	v_lshlrev_b32_e32 v177, 2, v64
	s_movk_i32 s62, 0x4000
	s_mov_b32 s63, 0xff7fc99e
	s_movk_i32 s64, 0x80
	s_movk_i32 s65, 0x2000
	s_mov_b32 s66, 0x40000
	s_mov_b32 s67, 0x80000
	s_mov_b32 s68, 0x100000
	s_mov_b32 s69, 0x200000
	s_mov_b32 s70, 0x400000
	s_mov_b32 s71, 0x800000
	s_mov_b32 s72, 0x1000000
	s_brev_b32 s73, 64
	s_brev_b32 s74, 32
	s_brev_b32 s75, 16
	s_brev_b32 s76, 8
	s_brev_b32 s77, 4
	v_mov_b32_e32 v178, 1
	v_mbcnt_hi_u32_b32 v179, -1, v0
	v_mov_b32_e32 v180, 0xff7fc99e
	s_mov_b32 s78, 0
	s_branch .LBB0_1177

.LBB0_1335:
	ds_read_b128 v[0:3], v184
	ds_read_b128 v[4:7], v189
	ds_read_b128 v[8:11], v190
	ds_read_b128 v[12:15], v191
	s_add_u32 s54, s18, 0x80
	s_addc_u32 s55, s19, 0
	s_and_b64 s[22:23], exec, s[22:23]
	s_cselect_b32 s23, s1, s55
	s_cselect_b32 s22, s0, s54
	v_lshl_add_u64 v[16:17], s[18:19], 0, v[164:165]
	s_add_i32 m0, s27, 0xc000
	ds_read_b128 v[210:213], v202
	ds_read_b128 v[214:217], v202 offset:1024
	ds_read_b128 v[218:221], v202 offset:2048
	ds_read_b128 v[222:225], v202 offset:3072
	ds_read_b128 v[226:229], v202 offset:4096
	ds_read_b128 v[230:233], v202 offset:5120
	ds_read_b128 v[234:237], v202 offset:6144
	ds_read_b128 v[238:241], v202 offset:7168
	global_load_lds_dwordx4 v[16:17], off
	v_lshl_add_u64 v[16:17], s[18:19], 0, v[162:163]
	s_add_i32 m0, s27, 0xe000
	s_nop 0
	global_load_lds_dwordx4 v[16:17], off
	s_waitcnt lgkmcnt(8)
	s_barrier
	s_waitcnt lgkmcnt(0)
	s_waitcnt lgkmcnt(0)
	v_mfma_scale_f32_16x16x128_f8f6f4 v[148:151], v[0:7], v[210:217], v[148:151], v203, v204 op_sel_hi:[0,0,0]
	v_mfma_scale_f32_16x16x128_f8f6f4 v[140:143], v[8:15], v[210:217], v[140:143], v203, v204 op_sel_hi:[0,0,0]
	v_mfma_scale_f32_16x16x128_f8f6f4 v[132:135], v[0:7], v[218:225], v[132:135], v203, v204 op_sel_hi:[0,0,0]
	v_mfma_scale_f32_16x16x128_f8f6f4 v[124:127], v[8:15], v[218:225], v[124:127], v203, v204 op_sel_hi:[0,0,0]
	v_mfma_scale_f32_16x16x128_f8f6f4 v[116:119], v[0:7], v[226:233], v[116:119], v203, v204 op_sel_hi:[0,0,0]
	v_mfma_scale_f32_16x16x128_f8f6f4 v[108:111], v[8:15], v[226:233], v[108:111], v203, v204 op_sel_hi:[0,0,0]
	v_mfma_scale_f32_16x16x128_f8f6f4 v[100:103], v[0:7], v[234:241], v[100:103], v203, v204 op_sel_hi:[0,0,0]
	v_mfma_scale_f32_16x16x128_f8f6f4 v[92:95], v[8:15], v[234:241], v[92:95], v203, v204 op_sel_hi:[0,0,0]
	s_barrier
	s_mov_b32 m0, s28
	v_lshl_add_u64 v[172:173], s[20:21], 0, v[154:155]
	ds_read_b128 v[16:19], v185
	ds_read_b128 v[20:23], v192
	ds_read_b128 v[242:245], v193
	ds_read_b128 v[246:249], v194
	global_load_lds_dwordx4 v[172:173], off
	v_lshl_add_u64 v[174:175], s[20:21], 0, v[152:153]
	s_mov_b32 m0, s29
	s_nop 0
	global_load_lds_dwordx4 v[174:175], off
	s_barrier
	s_waitcnt lgkmcnt(0)
	s_waitcnt lgkmcnt(0)
	v_mfma_scale_f32_16x16x128_f8f6f4 v[144:147], v[16:23], v[210:217], v[144:147], v209, v204 op_sel_hi:[0,0,0]
	v_mfma_scale_f32_16x16x128_f8f6f4 v[136:139], v[242:249], v[210:217], v[136:139], v209, v204 op_sel_hi:[0,0,0]
	v_mfma_scale_f32_16x16x128_f8f6f4 v[128:131], v[16:23], v[218:225], v[128:131], v209, v204 op_sel_hi:[0,0,0]
	v_mfma_scale_f32_16x16x128_f8f6f4 v[120:123], v[242:249], v[218:225], v[120:123], v209, v204 op_sel_hi:[0,0,0]
	v_mfma_scale_f32_16x16x128_f8f6f4 v[112:115], v[16:23], v[226:233], v[112:115], v209, v204 op_sel_hi:[0,0,0]
	v_mfma_scale_f32_16x16x128_f8f6f4 v[104:107], v[242:249], v[226:233], v[104:107], v209, v204 op_sel_hi:[0,0,0]
	v_mfma_scale_f32_16x16x128_f8f6f4 v[96:99], v[16:23], v[234:241], v[96:99], v209, v204 op_sel_hi:[0,0,0]
	v_mfma_scale_f32_16x16x128_f8f6f4 v[88:91], v[242:249], v[234:241], v[88:91], v209, v204 op_sel_hi:[0,0,0]
	s_mov_b32 m0, s27
	s_barrier
	ds_read_b128 v[210:213], v202 offset:16384
	ds_read_b128 v[214:217], v202 offset:17408
	ds_read_b128 v[218:221], v202 offset:18432
	ds_read_b128 v[222:225], v202 offset:19456
	ds_read_b128 v[226:229], v202 offset:20480
	ds_read_b128 v[230:233], v202 offset:21504
	ds_read_b128 v[234:237], v202 offset:22528
	ds_read_b128 v[238:241], v202 offset:23552
	global_load_lds_dwordx4 v156, s[22:23]
	s_mov_b32 m0, s30
	v_mov_b32_e32 v177, v157
	global_load_lds_dwordx4 v176, s[22:23]
	s_barrier
	s_waitcnt lgkmcnt(0)
	v_lshl_add_u64 v[178:179], s[22:23], 0, v[156:157]
	v_lshl_add_u64 v[176:177], s[22:23], 0, v[176:177]
	s_waitcnt lgkmcnt(0)
	v_mfma_scale_f32_16x16x128_f8f6f4 v[84:87], v[0:7], v[210:217], v[84:87], v203, v204 op_sel_hi:[0,0,0]
	v_mfma_scale_f32_16x16x128_f8f6f4 v[76:79], v[8:15], v[210:217], v[76:79], v203, v204 op_sel_hi:[0,0,0]
	v_mfma_scale_f32_16x16x128_f8f6f4 v[68:71], v[0:7], v[218:225], v[68:71], v203, v204 op_sel_hi:[0,0,0]
	v_mfma_scale_f32_16x16x128_f8f6f4 v[60:63], v[8:15], v[218:225], v[60:63], v203, v204 op_sel_hi:[0,0,0]
	v_mfma_scale_f32_16x16x128_f8f6f4 v[52:55], v[0:7], v[226:233], v[52:55], v203, v204 op_sel_hi:[0,0,0]
	v_mfma_scale_f32_16x16x128_f8f6f4 v[44:47], v[8:15], v[226:233], v[44:47], v203, v204 op_sel_hi:[0,0,0]
	v_mfma_scale_f32_16x16x128_f8f6f4 v[36:39], v[0:7], v[234:241], v[36:39], v203, v204 op_sel_hi:[0,0,0]
	v_mfma_scale_f32_16x16x128_f8f6f4 v[28:31], v[8:15], v[234:241], v[28:31], v203, v204 op_sel_hi:[0,0,0]
	s_barrier
	s_add_u32 s54, s20, 0x40000
	s_addc_u32 s55, s21, 0
	s_mov_b32 m0, s31
	v_lshl_add_u64 v[0:1], s[54:55], 0, v[154:155]
	global_load_lds_dwordx4 v[0:1], off
	v_lshl_add_u64 v[0:1], s[54:55], 0, v[152:153]
	s_mov_b32 m0, s33
	s_nop 0
	global_load_lds_dwordx4 v[0:1], off
	s_waitcnt vmcnt(6)
	s_barrier
	v_mfma_scale_f32_16x16x128_f8f6f4 v[80:83], v[16:23], v[210:217], v[80:83], v209, v204 op_sel_hi:[0,0,0]
	v_mfma_scale_f32_16x16x128_f8f6f4 v[72:75], v[242:249], v[210:217], v[72:75], v209, v204 op_sel_hi:[0,0,0]
	v_mfma_scale_f32_16x16x128_f8f6f4 v[64:67], v[16:23], v[218:225], v[64:67], v209, v204 op_sel_hi:[0,0,0]
	v_mfma_scale_f32_16x16x128_f8f6f4 v[56:59], v[242:249], v[218:225], v[56:59], v209, v204 op_sel_hi:[0,0,0]
	v_mfma_scale_f32_16x16x128_f8f6f4 v[48:51], v[16:23], v[226:233], v[48:51], v209, v204 op_sel_hi:[0,0,0]
	v_mfma_scale_f32_16x16x128_f8f6f4 v[40:43], v[242:249], v[226:233], v[40:43], v209, v204 op_sel_hi:[0,0,0]
	v_mfma_scale_f32_16x16x128_f8f6f4 v[32:35], v[16:23], v[234:241], v[32:35], v209, v204 op_sel_hi:[0,0,0]
	v_mfma_scale_f32_16x16x128_f8f6f4 v[24:27], v[242:249], v[234:241], v[24:27], v209, v204 op_sel_hi:[0,0,0]
	s_barrier
	ds_read_b128 v[0:3], v186
	ds_read_b128 v[4:7], v195
	ds_read_b128 v[8:11], v196
	ds_read_b128 v[12:15], v197
	s_mov_b32 m0, s34
	v_lshl_add_u64 v[170:171], s[22:23], 0, v[170:171]
	ds_read_b128 v[16:19], v202 offset:32768
	ds_read_b128 v[20:23], v202 offset:33792
	ds_read_b128 v[210:213], v202 offset:34816
	ds_read_b128 v[214:217], v202 offset:35840
	ds_read_b128 v[218:221], v202 offset:36864
	ds_read_b128 v[222:225], v202 offset:37888
	ds_read_b128 v[226:229], v202 offset:38912
	ds_read_b128 v[230:233], v202 offset:39936
	global_load_lds_dwordx4 v[170:171], off
	v_lshl_add_u64 v[168:169], s[22:23], 0, v[168:169]
	s_mov_b32 m0, s35
	s_nop 0
	global_load_lds_dwordx4 v[168:169], off
	s_waitcnt lgkmcnt(8)
	s_barrier
	s_waitcnt lgkmcnt(0)
	s_waitcnt lgkmcnt(0)
	v_mfma_scale_f32_16x16x128_f8f6f4 v[148:151], v[0:7], v[16:23], v[148:151], v203, v204 op_sel_hi:[0,0,0]
	v_mfma_scale_f32_16x16x128_f8f6f4 v[140:143], v[8:15], v[16:23], v[140:143], v203, v204 op_sel_hi:[0,0,0]
	v_mfma_scale_f32_16x16x128_f8f6f4 v[132:135], v[0:7], v[210:217], v[132:135], v203, v204 op_sel_hi:[0,0,0]
	v_mfma_scale_f32_16x16x128_f8f6f4 v[124:127], v[8:15], v[210:217], v[124:127], v203, v204 op_sel_hi:[0,0,0]
	v_mfma_scale_f32_16x16x128_f8f6f4 v[116:119], v[0:7], v[218:225], v[116:119], v203, v204 op_sel_hi:[0,0,0]
	v_mfma_scale_f32_16x16x128_f8f6f4 v[108:111], v[8:15], v[218:225], v[108:111], v203, v204 op_sel_hi:[0,0,0]
	v_mfma_scale_f32_16x16x128_f8f6f4 v[100:103], v[0:7], v[226:233], v[100:103], v203, v204 op_sel_hi:[0,0,0]
	v_mfma_scale_f32_16x16x128_f8f6f4 v[92:95], v[8:15], v[226:233], v[92:95], v203, v204 op_sel_hi:[0,0,0]
	s_barrier
	s_mov_b32 m0, s36
	v_lshl_add_u64 v[168:169], v[172:173], 0, s[10:11]
	ds_read_b128 v[234:237], v187
	ds_read_b128 v[238:241], v198
	ds_read_b128 v[242:245], v199
	ds_read_b128 v[246:249], v200
	global_load_lds_dwordx4 v[168:169], off
	v_lshl_add_u64 v[168:169], v[174:175], 0, s[10:11]
	s_mov_b32 m0, s37
	s_nop 0
	global_load_lds_dwordx4 v[168:169], off
	s_barrier
	s_waitcnt lgkmcnt(0)
	s_waitcnt lgkmcnt(0)
	v_mfma_scale_f32_16x16x128_f8f6f4 v[144:147], v[234:241], v[16:23], v[144:147], v209, v204 op_sel_hi:[0,0,0]
	v_mfma_scale_f32_16x16x128_f8f6f4 v[136:139], v[242:249], v[16:23], v[136:139], v209, v204 op_sel_hi:[0,0,0]
	v_mfma_scale_f32_16x16x128_f8f6f4 v[128:131], v[234:241], v[210:217], v[128:131], v209, v204 op_sel_hi:[0,0,0]
	v_mfma_scale_f32_16x16x128_f8f6f4 v[120:123], v[242:249], v[210:217], v[120:123], v209, v204 op_sel_hi:[0,0,0]
	v_mfma_scale_f32_16x16x128_f8f6f4 v[112:115], v[234:241], v[218:225], v[112:115], v209, v204 op_sel_hi:[0,0,0]
	v_mfma_scale_f32_16x16x128_f8f6f4 v[104:107], v[242:249], v[218:225], v[104:107], v209, v204 op_sel_hi:[0,0,0]
	v_mfma_scale_f32_16x16x128_f8f6f4 v[96:99], v[234:241], v[226:233], v[96:99], v209, v204 op_sel_hi:[0,0,0]
	v_mfma_scale_f32_16x16x128_f8f6f4 v[88:91], v[242:249], v[226:233], v[88:91], v209, v204 op_sel_hi:[0,0,0]
	s_mov_b32 m0, s38
	v_lshl_add_u64 v[178:179], v[178:179], 0, s[10:11]
	s_barrier
	ds_read_b128 v[16:19], v202 offset:49152
	ds_read_b128 v[20:23], v202 offset:50176
	ds_read_b128 v[168:171], v202 offset:51200
	ds_read_b128 v[172:175], v202 offset:52224
	ds_read_b128 v[210:213], v202 offset:53248
	ds_read_b128 v[214:217], v202 offset:54272
	ds_read_b128 v[218:221], v202 offset:55296
	ds_read_b128 v[222:225], v202 offset:56320
	global_load_lds_dwordx4 v[178:179], off
	v_lshl_add_u64 v[176:177], v[176:177], 0, s[10:11]
	s_mov_b32 m0, s39
	s_nop 0
	global_load_lds_dwordx4 v[176:177], off
	s_barrier
	s_waitcnt lgkmcnt(0)
	s_waitcnt lgkmcnt(0)
	v_mfma_scale_f32_16x16x128_f8f6f4 v[84:87], v[0:7], v[16:23], v[84:87], v203, v204 op_sel_hi:[0,0,0]
	v_mfma_scale_f32_16x16x128_f8f6f4 v[76:79], v[8:15], v[16:23], v[76:79], v203, v204 op_sel_hi:[0,0,0]
	v_mfma_scale_f32_16x16x128_f8f6f4 v[68:71], v[0:7], v[168:175], v[68:71], v203, v204 op_sel_hi:[0,0,0]
	v_mfma_scale_f32_16x16x128_f8f6f4 v[60:63], v[8:15], v[168:175], v[60:63], v203, v204 op_sel_hi:[0,0,0]
	v_mfma_scale_f32_16x16x128_f8f6f4 v[52:55], v[0:7], v[210:217], v[52:55], v203, v204 op_sel_hi:[0,0,0]
	v_mfma_scale_f32_16x16x128_f8f6f4 v[44:47], v[8:15], v[210:217], v[44:47], v203, v204 op_sel_hi:[0,0,0]
	v_mfma_scale_f32_16x16x128_f8f6f4 v[36:39], v[0:7], v[218:225], v[36:39], v203, v204 op_sel_hi:[0,0,0]
	v_mfma_scale_f32_16x16x128_f8f6f4 v[28:31], v[8:15], v[218:225], v[28:31], v203, v204 op_sel_hi:[0,0,0]
	s_barrier
	s_add_u32 s20, s20, 0x40080
	s_addc_u32 s21, s21, 0
	s_mov_b32 m0, s40
	v_lshl_add_u64 v[0:1], s[20:21], 0, v[154:155]
	global_load_lds_dwordx4 v[0:1], off
	v_lshl_add_u64 v[0:1], s[20:21], 0, v[152:153]
	s_mov_b32 m0, s41
	s_nop 0
	global_load_lds_dwordx4 v[0:1], off
	s_waitcnt vmcnt(6)
	s_barrier
	v_mfma_scale_f32_16x16x128_f8f6f4 v[80:83], v[234:241], v[16:23], v[80:83], v209, v204 op_sel_hi:[0,0,0]
	v_mfma_scale_f32_16x16x128_f8f6f4 v[72:75], v[242:249], v[16:23], v[72:75], v209, v204 op_sel_hi:[0,0,0]
	v_mfma_scale_f32_16x16x128_f8f6f4 v[64:67], v[234:241], v[168:175], v[64:67], v209, v204 op_sel_hi:[0,0,0]
	v_mfma_scale_f32_16x16x128_f8f6f4 v[56:59], v[242:249], v[168:175], v[56:59], v209, v204 op_sel_hi:[0,0,0]
	v_mfma_scale_f32_16x16x128_f8f6f4 v[48:51], v[234:241], v[210:217], v[48:51], v209, v204 op_sel_hi:[0,0,0]
	v_mfma_scale_f32_16x16x128_f8f6f4 v[40:43], v[242:249], v[210:217], v[40:43], v209, v204 op_sel_hi:[0,0,0]
	v_mfma_scale_f32_16x16x128_f8f6f4 v[32:35], v[234:241], v[218:225], v[32:35], v209, v204 op_sel_hi:[0,0,0]
	v_mfma_scale_f32_16x16x128_f8f6f4 v[24:27], v[242:249], v[218:225], v[24:27], v209, v204 op_sel_hi:[0,0,0]
	s_add_i32 s53, s53, 2
	s_add_u32 s18, s18, 0x100
	s_addc_u32 s19, s19, 0
	s_add_u32 s16, s16, 0x100
	s_addc_u32 s17, s17, 0
	s_cmp_gt_u32 s53, 13
	s_barrier
	s_cbranch_scc1 .LBB0_1326

.LBB0_1419:
	ds_read_b128 v[0:3], v170
	ds_read_b128 v[4:7], v175
	ds_read_b128 v[8:11], v176
	ds_read_b128 v[12:15], v177
	s_add_u32 s20, s18, 0x80
	s_addc_u32 s21, s19, 0
	s_cmp_eq_u32 s58, 12
	s_cselect_b32 s23, s9, s21
	s_cselect_b32 s22, s55, s20
	s_cselect_b32 s21, s13, s57
	s_cselect_b32 s20, s12, s56
	v_lshl_add_u64 v[162:163], s[18:19], 0, v[160:161]
	s_add_i32 m0, s29, 0xc000
	ds_read_b128 v[192:195], v188
	ds_read_b128 v[196:199], v188 offset:1024
	ds_read_b128 v[200:203], v188 offset:2048
	ds_read_b128 v[204:207], v188 offset:3072
	ds_read_b128 v[208:211], v188 offset:4096
	ds_read_b128 v[212:215], v188 offset:5120
	ds_read_b128 v[216:219], v188 offset:6144
	ds_read_b128 v[220:223], v188 offset:7168
	global_load_lds_dwordx4 v[162:163], off
	v_lshl_add_u64 v[162:163], s[18:19], 0, v[158:159]
	s_add_i32 m0, s29, 0xe000
	s_nop 0
	global_load_lds_dwordx4 v[162:163], off
	s_waitcnt lgkmcnt(8)
	s_barrier
	s_waitcnt lgkmcnt(0)
	s_waitcnt lgkmcnt(0)
	v_mfma_scale_f32_16x16x128_f8f6f4 v[140:143], v[0:7], v[192:199], v[140:143], v189, v190 op_sel_hi:[0,0,0]
	v_mfma_scale_f32_16x16x128_f8f6f4 v[136:139], v[8:15], v[192:199], v[136:139], v189, v190 op_sel_hi:[0,0,0]
	v_mfma_scale_f32_16x16x128_f8f6f4 v[132:135], v[0:7], v[200:207], v[132:135], v189, v190 op_sel_hi:[0,0,0]
	v_mfma_scale_f32_16x16x128_f8f6f4 v[128:131], v[8:15], v[200:207], v[128:131], v189, v190 op_sel_hi:[0,0,0]
	v_mfma_scale_f32_16x16x128_f8f6f4 v[124:127], v[0:7], v[208:215], v[124:127], v189, v190 op_sel_hi:[0,0,0]
	v_mfma_scale_f32_16x16x128_f8f6f4 v[120:123], v[8:15], v[208:215], v[120:123], v189, v190 op_sel_hi:[0,0,0]
	v_mfma_scale_f32_16x16x128_f8f6f4 v[116:119], v[0:7], v[216:223], v[116:119], v189, v190 op_sel_hi:[0,0,0]
	v_mfma_scale_f32_16x16x128_f8f6f4 v[112:115], v[8:15], v[216:223], v[112:115], v189, v190 op_sel_hi:[0,0,0]
	s_barrier
	s_mov_b32 m0, s30
	v_lshl_add_u64 v[162:163], s[20:21], 0, v[146:147]
	ds_read_b128 v[224:227], v171
	ds_read_b128 v[228:231], v178
	ds_read_b128 v[232:235], v179
	ds_read_b128 v[236:239], v180
	global_load_lds_dwordx4 v[162:163], off
	v_lshl_add_u64 v[164:165], s[20:21], 0, v[144:145]
	s_mov_b32 m0, s31
	s_nop 0
	global_load_lds_dwordx4 v[164:165], off
	s_barrier
	s_waitcnt lgkmcnt(0)
	s_waitcnt lgkmcnt(0)
	v_mfma_scale_f32_16x16x128_f8f6f4 v[84:87], v[224:231], v[192:199], v[84:87], v189, v190 op_sel_hi:[0,0,0]
	v_mfma_scale_f32_16x16x128_f8f6f4 v[76:79], v[232:239], v[192:199], v[76:79], v189, v190 op_sel_hi:[0,0,0]
	v_mfma_scale_f32_16x16x128_f8f6f4 v[68:71], v[224:231], v[200:207], v[68:71], v189, v190 op_sel_hi:[0,0,0]
	v_mfma_scale_f32_16x16x128_f8f6f4 v[64:67], v[232:239], v[200:207], v[64:67], v189, v190 op_sel_hi:[0,0,0]
	v_mfma_scale_f32_16x16x128_f8f6f4 v[60:63], v[224:231], v[208:215], v[60:63], v189, v190 op_sel_hi:[0,0,0]
	v_mfma_scale_f32_16x16x128_f8f6f4 v[56:59], v[232:239], v[208:215], v[56:59], v189, v190 op_sel_hi:[0,0,0]
	v_mfma_scale_f32_16x16x128_f8f6f4 v[52:55], v[224:231], v[216:223], v[52:55], v189, v190 op_sel_hi:[0,0,0]
	v_mfma_scale_f32_16x16x128_f8f6f4 v[48:51], v[232:239], v[216:223], v[48:51], v189, v190 op_sel_hi:[0,0,0]
	s_mov_b32 m0, s29
	v_lshl_add_u64 v[166:167], s[22:23], 0, v[148:149]
	s_barrier
	ds_read_b128 v[192:195], v188 offset:16384
	ds_read_b128 v[196:199], v188 offset:17408
	ds_read_b128 v[200:203], v188 offset:18432
	ds_read_b128 v[204:207], v188 offset:19456
	ds_read_b128 v[208:211], v188 offset:20480
	ds_read_b128 v[212:215], v188 offset:21504
	ds_read_b128 v[216:219], v188 offset:22528
	ds_read_b128 v[220:223], v188 offset:23552
	global_load_lds_dwordx4 v[166:167], off
	v_lshl_add_u64 v[168:169], s[22:23], 0, v[150:151]
	s_mov_b32 m0, s33
	s_nop 0
	global_load_lds_dwordx4 v[168:169], off
	s_barrier
	s_waitcnt lgkmcnt(0)
	s_waitcnt lgkmcnt(0)
	v_mfma_scale_f32_16x16x128_f8f6f4 v[108:111], v[0:7], v[192:199], v[108:111], v189, v190 op_sel_hi:[0,0,0]
	v_mfma_scale_f32_16x16x128_f8f6f4 v[104:107], v[8:15], v[192:199], v[104:107], v189, v190 op_sel_hi:[0,0,0]
	v_mfma_scale_f32_16x16x128_f8f6f4 v[100:103], v[0:7], v[200:207], v[100:103], v189, v190 op_sel_hi:[0,0,0]
	v_mfma_scale_f32_16x16x128_f8f6f4 v[96:99], v[8:15], v[200:207], v[96:99], v189, v190 op_sel_hi:[0,0,0]
	v_mfma_scale_f32_16x16x128_f8f6f4 v[92:95], v[0:7], v[208:215], v[92:95], v189, v190 op_sel_hi:[0,0,0]
	v_mfma_scale_f32_16x16x128_f8f6f4 v[88:91], v[8:15], v[208:215], v[88:91], v189, v190 op_sel_hi:[0,0,0]
	v_mfma_scale_f32_16x16x128_f8f6f4 v[80:83], v[0:7], v[216:223], v[80:83], v189, v190 op_sel_hi:[0,0,0]
	v_mfma_scale_f32_16x16x128_f8f6f4 v[72:75], v[8:15], v[216:223], v[72:75], v189, v190 op_sel_hi:[0,0,0]
	s_barrier
	s_add_u32 s60, s20, 0x40000
	s_addc_u32 s61, s21, 0
	s_mov_b32 m0, s34
	v_lshl_add_u64 v[0:1], s[60:61], 0, v[146:147]
	global_load_lds_dwordx4 v[0:1], off
	v_lshl_add_u64 v[0:1], s[60:61], 0, v[144:145]
	s_mov_b32 m0, s35
	s_nop 0
	global_load_lds_dwordx4 v[0:1], off
	s_waitcnt vmcnt(6)
	s_barrier
	v_mfma_scale_f32_16x16x128_f8f6f4 v[44:47], v[224:231], v[192:199], v[44:47], v189, v190 op_sel_hi:[0,0,0]
	v_mfma_scale_f32_16x16x128_f8f6f4 v[40:43], v[232:239], v[192:199], v[40:43], v189, v190 op_sel_hi:[0,0,0]
	v_mfma_scale_f32_16x16x128_f8f6f4 v[36:39], v[224:231], v[200:207], v[36:39], v189, v190 op_sel_hi:[0,0,0]
	v_mfma_scale_f32_16x16x128_f8f6f4 v[32:35], v[232:239], v[200:207], v[32:35], v189, v190 op_sel_hi:[0,0,0]
	v_mfma_scale_f32_16x16x128_f8f6f4 v[28:31], v[224:231], v[208:215], v[28:31], v189, v190 op_sel_hi:[0,0,0]
	v_mfma_scale_f32_16x16x128_f8f6f4 v[24:27], v[232:239], v[208:215], v[24:27], v189, v190 op_sel_hi:[0,0,0]
	v_mfma_scale_f32_16x16x128_f8f6f4 v[20:23], v[224:231], v[216:223], v[20:23], v189, v190 op_sel_hi:[0,0,0]
	v_mfma_scale_f32_16x16x128_f8f6f4 v[16:19], v[232:239], v[216:223], v[16:19], v189, v190 op_sel_hi:[0,0,0]
	s_barrier
	ds_read_b128 v[0:3], v172
	ds_read_b128 v[4:7], v181
	ds_read_b128 v[8:11], v182
	ds_read_b128 v[12:15], v183
	s_mov_b32 m0, s36
	v_lshl_add_u64 v[224:225], s[22:23], 0, v[152:153]
	ds_read_b128 v[192:195], v188 offset:32768
	ds_read_b128 v[196:199], v188 offset:33792
	ds_read_b128 v[200:203], v188 offset:34816
	ds_read_b128 v[204:207], v188 offset:35840
	ds_read_b128 v[208:211], v188 offset:36864
	ds_read_b128 v[212:215], v188 offset:37888
	ds_read_b128 v[216:219], v188 offset:38912
	ds_read_b128 v[220:223], v188 offset:39936
	global_load_lds_dwordx4 v[224:225], off
	v_lshl_add_u64 v[224:225], s[22:23], 0, v[154:155]
	s_mov_b32 m0, s37
	s_nop 0
	global_load_lds_dwordx4 v[224:225], off
	s_waitcnt lgkmcnt(8)
	s_barrier
	s_waitcnt lgkmcnt(0)
	s_waitcnt lgkmcnt(0)
	v_mfma_scale_f32_16x16x128_f8f6f4 v[140:143], v[0:7], v[192:199], v[140:143], v189, v190 op_sel_hi:[0,0,0]
	v_mfma_scale_f32_16x16x128_f8f6f4 v[136:139], v[8:15], v[192:199], v[136:139], v189, v190 op_sel_hi:[0,0,0]
	v_mfma_scale_f32_16x16x128_f8f6f4 v[132:135], v[0:7], v[200:207], v[132:135], v189, v190 op_sel_hi:[0,0,0]
	v_mfma_scale_f32_16x16x128_f8f6f4 v[128:131], v[8:15], v[200:207], v[128:131], v189, v190 op_sel_hi:[0,0,0]
	v_mfma_scale_f32_16x16x128_f8f6f4 v[124:127], v[0:7], v[208:215], v[124:127], v189, v190 op_sel_hi:[0,0,0]
	v_mfma_scale_f32_16x16x128_f8f6f4 v[120:123], v[8:15], v[208:215], v[120:123], v189, v190 op_sel_hi:[0,0,0]
	v_mfma_scale_f32_16x16x128_f8f6f4 v[116:119], v[0:7], v[216:223], v[116:119], v189, v190 op_sel_hi:[0,0,0]
	v_mfma_scale_f32_16x16x128_f8f6f4 v[112:115], v[8:15], v[216:223], v[112:115], v189, v190 op_sel_hi:[0,0,0]
	s_barrier
	s_mov_b32 m0, s40
	v_lshl_add_u64 v[162:163], v[162:163], 0, s[4:5]
	ds_read_b128 v[224:227], v173
	ds_read_b128 v[228:231], v184
	ds_read_b128 v[232:235], v185
	ds_read_b128 v[236:239], v186
	global_load_lds_dwordx4 v[162:163], off
	v_lshl_add_u64 v[162:163], v[164:165], 0, s[4:5]
	s_mov_b32 m0, s41
	s_nop 0
	global_load_lds_dwordx4 v[162:163], off
	s_barrier
	s_waitcnt lgkmcnt(0)
	s_waitcnt lgkmcnt(0)
	v_mfma_scale_f32_16x16x128_f8f6f4 v[84:87], v[224:231], v[192:199], v[84:87], v189, v190 op_sel_hi:[0,0,0]
	v_mfma_scale_f32_16x16x128_f8f6f4 v[76:79], v[232:239], v[192:199], v[76:79], v189, v190 op_sel_hi:[0,0,0]
	v_mfma_scale_f32_16x16x128_f8f6f4 v[68:71], v[224:231], v[200:207], v[68:71], v189, v190 op_sel_hi:[0,0,0]
	v_mfma_scale_f32_16x16x128_f8f6f4 v[64:67], v[232:239], v[200:207], v[64:67], v189, v190 op_sel_hi:[0,0,0]
	v_mfma_scale_f32_16x16x128_f8f6f4 v[60:63], v[224:231], v[208:215], v[60:63], v189, v190 op_sel_hi:[0,0,0]
	v_mfma_scale_f32_16x16x128_f8f6f4 v[56:59], v[232:239], v[208:215], v[56:59], v189, v190 op_sel_hi:[0,0,0]
	v_mfma_scale_f32_16x16x128_f8f6f4 v[52:55], v[224:231], v[216:223], v[52:55], v189, v190 op_sel_hi:[0,0,0]
	v_mfma_scale_f32_16x16x128_f8f6f4 v[48:51], v[232:239], v[216:223], v[48:51], v189, v190 op_sel_hi:[0,0,0]
	s_mov_b32 m0, s42
	v_lshl_add_u64 v[162:163], v[166:167], 0, s[4:5]
	s_barrier
	ds_read_b128 v[192:195], v188 offset:49152
	ds_read_b128 v[196:199], v188 offset:50176
	ds_read_b128 v[200:203], v188 offset:51200
	ds_read_b128 v[204:207], v188 offset:52224
	ds_read_b128 v[208:211], v188 offset:53248
	ds_read_b128 v[212:215], v188 offset:54272
	ds_read_b128 v[216:219], v188 offset:55296
	ds_read_b128 v[220:223], v188 offset:56320
	global_load_lds_dwordx4 v[162:163], off
	v_lshl_add_u64 v[162:163], v[168:169], 0, s[4:5]
	s_mov_b32 m0, s43
	s_nop 0
	global_load_lds_dwordx4 v[162:163], off
	s_barrier
	s_waitcnt lgkmcnt(0)
	s_waitcnt lgkmcnt(0)
	v_mfma_scale_f32_16x16x128_f8f6f4 v[108:111], v[0:7], v[192:199], v[108:111], v189, v190 op_sel_hi:[0,0,0]
	v_mfma_scale_f32_16x16x128_f8f6f4 v[104:107], v[8:15], v[192:199], v[104:107], v189, v190 op_sel_hi:[0,0,0]
	v_mfma_scale_f32_16x16x128_f8f6f4 v[100:103], v[0:7], v[200:207], v[100:103], v189, v190 op_sel_hi:[0,0,0]
	v_mfma_scale_f32_16x16x128_f8f6f4 v[96:99], v[8:15], v[200:207], v[96:99], v189, v190 op_sel_hi:[0,0,0]
	v_mfma_scale_f32_16x16x128_f8f6f4 v[92:95], v[0:7], v[208:215], v[92:95], v189, v190 op_sel_hi:[0,0,0]
	v_mfma_scale_f32_16x16x128_f8f6f4 v[88:91], v[8:15], v[208:215], v[88:91], v189, v190 op_sel_hi:[0,0,0]
	v_mfma_scale_f32_16x16x128_f8f6f4 v[80:83], v[0:7], v[216:223], v[80:83], v189, v190 op_sel_hi:[0,0,0]
	v_mfma_scale_f32_16x16x128_f8f6f4 v[72:75], v[8:15], v[216:223], v[72:75], v189, v190 op_sel_hi:[0,0,0]
	s_barrier
	s_add_u32 s20, s20, 0x40080
	s_addc_u32 s21, s21, 0
	s_mov_b32 m0, s44
	v_lshl_add_u64 v[0:1], s[20:21], 0, v[146:147]
	global_load_lds_dwordx4 v[0:1], off
	v_lshl_add_u64 v[0:1], s[20:21], 0, v[144:145]
	s_mov_b32 m0, s45
	s_nop 0
	global_load_lds_dwordx4 v[0:1], off
	s_waitcnt vmcnt(6)
	s_barrier
	v_mfma_scale_f32_16x16x128_f8f6f4 v[44:47], v[224:231], v[192:199], v[44:47], v189, v190 op_sel_hi:[0,0,0]
	v_mfma_scale_f32_16x16x128_f8f6f4 v[40:43], v[232:239], v[192:199], v[40:43], v189, v190 op_sel_hi:[0,0,0]
	v_mfma_scale_f32_16x16x128_f8f6f4 v[36:39], v[224:231], v[200:207], v[36:39], v189, v190 op_sel_hi:[0,0,0]
	v_mfma_scale_f32_16x16x128_f8f6f4 v[32:35], v[232:239], v[200:207], v[32:35], v189, v190 op_sel_hi:[0,0,0]
	v_mfma_scale_f32_16x16x128_f8f6f4 v[28:31], v[224:231], v[208:215], v[28:31], v189, v190 op_sel_hi:[0,0,0]
	v_mfma_scale_f32_16x16x128_f8f6f4 v[24:27], v[232:239], v[208:215], v[24:27], v189, v190 op_sel_hi:[0,0,0]
	v_mfma_scale_f32_16x16x128_f8f6f4 v[20:23], v[224:231], v[216:223], v[20:23], v189, v190 op_sel_hi:[0,0,0]
	v_mfma_scale_f32_16x16x128_f8f6f4 v[16:19], v[232:239], v[216:223], v[16:19], v189, v190 op_sel_hi:[0,0,0]
	s_add_i32 s58, s58, 2
	s_add_u32 s18, s18, 0x100
	s_addc_u32 s19, s19, 0
	s_add_u32 s56, s56, 0x100
	s_addc_u32 s57, s57, 0
	s_cmp_gt_u32 s58, 13
	s_barrier
	s_cbranch_scc0 .LBB0_1419
	v_lshl_or_b32 v8, s54, 8, v187
	s_ashr_i32 s17, s16, 31
	s_lshl_b64 s[16:17], s[16:17], 19
	v_lshl_add_u64 v[10:11], v[156:157], 0, s[16:17]
	v_ashrrev_i32_e32 v9, 31, v8
	v_lshl_add_u64 v[8:9], v[10:11], 0, v[8:9]
	v_mbcnt_lo_u32_b32 v10, -1, 0
	v_mbcnt_hi_u32_b32 v10, -1, v10
	v_and_b32_e32 v10, 16, v10
	v_mov_b32_e32 v12, 0x8000
	v_cmp_eq_u32_e32 vcc, 0, v10
	s_nop 1
	v_cndmask_b32_e32 v12, -8, v12, vcc
	v_ashrrev_i32_e32 v13, 31, v12
	v_lshl_add_u64 v[8:9], v[8:9], 0, v[12:13]
	v_med3_f32 v132, v132, s7, v191
	v_med3_f32 v133, v133, s7, v191
	v_med3_f32 v134, v134, s7, v191
	v_med3_f32 v135, v135, s7, v191
	v_med3_f32 v128, v128, s7, v191
	v_med3_f32 v129, v129, s7, v191
	v_med3_f32 v130, v130, s7, v191
	v_med3_f32 v131, v131, s7, v191
	v_cvt_pk_fp8_f32 v224, v132, v133
	v_cvt_pk_fp8_f32 v225, v128, v129
	v_cvt_pk_fp8_f32 v224, v134, v135 op_sel:[0,0,1]
	v_cvt_pk_fp8_f32 v225, v130, v131 op_sel:[0,0,1]
	v_med3_f32 v140, v140, s7, v191
	v_med3_f32 v141, v141, s7, v191
	v_med3_f32 v142, v142, s7, v191
	v_med3_f32 v143, v143, s7, v191
	v_med3_f32 v136, v136, s7, v191
	v_med3_f32 v137, v137, s7, v191
	v_med3_f32 v138, v138, s7, v191
	v_med3_f32 v139, v139, s7, v191
	v_cvt_pk_fp8_f32 v226, v140, v141
	v_cvt_pk_fp8_f32 v227, v136, v137
	v_cvt_pk_fp8_f32 v226, v142, v143 op_sel:[0,0,1]
	v_cvt_pk_fp8_f32 v227, v138, v139 op_sel:[0,0,1]
	s_nop 1
	v_permlane16_swap_b32_e32 v224, v226
	v_permlane16_swap_b32_e32 v225, v227
	global_store_dwordx4 v[8:9], v[224:227], off
	v_med3_f32 v68, v68, s7, v191
	v_med3_f32 v69, v69, s7, v191
	v_med3_f32 v70, v70, s7, v191
	v_med3_f32 v71, v71, s7, v191
	v_med3_f32 v64, v64, s7, v191
	v_med3_f32 v65, v65, s7, v191
	v_med3_f32 v66, v66, s7, v191
	v_med3_f32 v67, v67, s7, v191
	v_cvt_pk_fp8_f32 v228, v68, v69
	v_cvt_pk_fp8_f32 v229, v64, v65
	v_cvt_pk_fp8_f32 v228, v70, v71 op_sel:[0,0,1]
	v_cvt_pk_fp8_f32 v229, v66, v67 op_sel:[0,0,1]
	v_med3_f32 v84, v84, s7, v191
	v_med3_f32 v85, v85, s7, v191
	v_med3_f32 v86, v86, s7, v191
	v_med3_f32 v87, v87, s7, v191
	v_med3_f32 v76, v76, s7, v191
	v_med3_f32 v77, v77, s7, v191
	v_med3_f32 v78, v78, s7, v191
	v_med3_f32 v79, v79, s7, v191
	v_cvt_pk_fp8_f32 v230, v84, v85
	v_cvt_pk_fp8_f32 v231, v76, v77
	v_cvt_pk_fp8_f32 v230, v86, v87 op_sel:[0,0,1]
	v_cvt_pk_fp8_f32 v231, v78, v79 op_sel:[0,0,1]
	s_nop 1
	v_permlane16_swap_b32_e32 v228, v230
	v_permlane16_swap_b32_e32 v229, v231
	global_store_dwordx4 v[8:9], v[228:231], off offset:128
	v_lshl_add_u64 v[8:9], v[8:9], 0, s[62:63]
	v_med3_f32 v116, v116, s7, v191
	v_med3_f32 v117, v117, s7, v191
	v_med3_f32 v118, v118, s7, v191
	v_med3_f32 v119, v119, s7, v191
	v_med3_f32 v112, v112, s7, v191
	v_med3_f32 v113, v113, s7, v191
	v_med3_f32 v114, v114, s7, v191
	v_med3_f32 v115, v115, s7, v191
	v_cvt_pk_fp8_f32 v232, v116, v117
	v_cvt_pk_fp8_f32 v233, v112, v113
	v_cvt_pk_fp8_f32 v232, v118, v119 op_sel:[0,0,1]
	v_cvt_pk_fp8_f32 v233, v114, v115 op_sel:[0,0,1]
	v_med3_f32 v124, v124, s7, v191
	v_med3_f32 v125, v125, s7, v191
	v_med3_f32 v126, v126, s7, v191
	v_med3_f32 v127, v127, s7, v191
	v_med3_f32 v120, v120, s7, v191
	v_med3_f32 v121, v121, s7, v191
	v_med3_f32 v122, v122, s7, v191
	v_med3_f32 v123, v123, s7, v191
	v_cvt_pk_fp8_f32 v234, v124, v125
	v_cvt_pk_fp8_f32 v235, v120, v121
	v_cvt_pk_fp8_f32 v234, v126, v127 op_sel:[0,0,1]
	v_cvt_pk_fp8_f32 v235, v122, v123 op_sel:[0,0,1]
	s_nop 1
	v_permlane16_swap_b32_e32 v232, v234
	v_permlane16_swap_b32_e32 v233, v235
	global_store_dwordx4 v[8:9], v[232:235], off
	v_med3_f32 v52, v52, s7, v191
	v_med3_f32 v53, v53, s7, v191
	v_med3_f32 v54, v54, s7, v191
	v_med3_f32 v55, v55, s7, v191
	v_med3_f32 v48, v48, s7, v191
	v_med3_f32 v49, v49, s7, v191
	v_med3_f32 v50, v50, s7, v191
	v_med3_f32 v51, v51, s7, v191
	v_cvt_pk_fp8_f32 v236, v52, v53
	v_cvt_pk_fp8_f32 v237, v48, v49
	v_cvt_pk_fp8_f32 v236, v54, v55 op_sel:[0,0,1]
	v_cvt_pk_fp8_f32 v237, v50, v51 op_sel:[0,0,1]
	v_med3_f32 v60, v60, s7, v191
	v_med3_f32 v61, v61, s7, v191
	v_med3_f32 v62, v62, s7, v191
	v_med3_f32 v63, v63, s7, v191
	v_med3_f32 v56, v56, s7, v191
	v_med3_f32 v57, v57, s7, v191
	v_med3_f32 v58, v58, s7, v191
	v_med3_f32 v59, v59, s7, v191
	v_cvt_pk_fp8_f32 v238, v60, v61
	v_cvt_pk_fp8_f32 v239, v56, v57
	v_cvt_pk_fp8_f32 v238, v62, v63 op_sel:[0,0,1]
	v_cvt_pk_fp8_f32 v239, v58, v59 op_sel:[0,0,1]
	s_nop 1
	v_permlane16_swap_b32_e32 v236, v238
	v_permlane16_swap_b32_e32 v237, v239
	global_store_dwordx4 v[8:9], v[236:239], off offset:128
	v_lshl_add_u64 v[8:9], v[8:9], 0, s[64:65]
	v_med3_f32 v100, v100, s7, v191
	v_med3_f32 v101, v101, s7, v191
	v_med3_f32 v102, v102, s7, v191
	v_med3_f32 v103, v103, s7, v191
	v_med3_f32 v96, v96, s7, v191
	v_med3_f32 v97, v97, s7, v191
	v_med3_f32 v98, v98, s7, v191
	v_med3_f32 v99, v99, s7, v191
	v_cvt_pk_fp8_f32 v224, v100, v101
	v_cvt_pk_fp8_f32 v225, v96, v97
	v_cvt_pk_fp8_f32 v224, v102, v103 op_sel:[0,0,1]
	v_cvt_pk_fp8_f32 v225, v98, v99 op_sel:[0,0,1]
	v_med3_f32 v108, v108, s7, v191
	v_med3_f32 v109, v109, s7, v191
	v_med3_f32 v110, v110, s7, v191
	v_med3_f32 v111, v111, s7, v191
	v_med3_f32 v104, v104, s7, v191
	v_med3_f32 v105, v105, s7, v191
	v_med3_f32 v106, v106, s7, v191
	v_med3_f32 v107, v107, s7, v191
	v_cvt_pk_fp8_f32 v226, v108, v109
	v_cvt_pk_fp8_f32 v227, v104, v105
	v_cvt_pk_fp8_f32 v226, v110, v111 op_sel:[0,0,1]
	v_cvt_pk_fp8_f32 v227, v106, v107 op_sel:[0,0,1]
	s_nop 1
	v_permlane16_swap_b32_e32 v224, v226
	v_permlane16_swap_b32_e32 v225, v227
	global_store_dwordx4 v[8:9], v[224:227], off
	v_med3_f32 v36, v36, s7, v191
	v_med3_f32 v37, v37, s7, v191
	v_med3_f32 v38, v38, s7, v191
	v_med3_f32 v39, v39, s7, v191
	v_med3_f32 v32, v32, s7, v191
	v_med3_f32 v33, v33, s7, v191
	v_med3_f32 v34, v34, s7, v191
	v_med3_f32 v35, v35, s7, v191
	v_cvt_pk_fp8_f32 v228, v36, v37
	v_cvt_pk_fp8_f32 v229, v32, v33
	v_cvt_pk_fp8_f32 v228, v38, v39 op_sel:[0,0,1]
	v_cvt_pk_fp8_f32 v229, v34, v35 op_sel:[0,0,1]
	v_med3_f32 v44, v44, s7, v191
	v_med3_f32 v45, v45, s7, v191
	v_med3_f32 v46, v46, s7, v191
	v_med3_f32 v47, v47, s7, v191
	v_med3_f32 v40, v40, s7, v191
	v_med3_f32 v41, v41, s7, v191
	v_med3_f32 v42, v42, s7, v191
	v_med3_f32 v43, v43, s7, v191
	v_cvt_pk_fp8_f32 v230, v44, v45
	v_cvt_pk_fp8_f32 v231, v40, v41
	v_cvt_pk_fp8_f32 v230, v46, v47 op_sel:[0,0,1]
	v_cvt_pk_fp8_f32 v231, v42, v43 op_sel:[0,0,1]
	s_nop 1
	v_permlane16_swap_b32_e32 v228, v230
	v_permlane16_swap_b32_e32 v229, v231
	global_store_dwordx4 v[8:9], v[228:231], off offset:128
	v_lshl_add_u64 v[8:9], v[8:9], 0, s[62:63]
	v_med3_f32 v80, v80, s7, v191
	v_med3_f32 v81, v81, s7, v191
	v_med3_f32 v82, v82, s7, v191
	v_med3_f32 v83, v83, s7, v191
	v_med3_f32 v72, v72, s7, v191
	v_med3_f32 v73, v73, s7, v191
	v_med3_f32 v74, v74, s7, v191
	v_med3_f32 v75, v75, s7, v191
	v_cvt_pk_fp8_f32 v232, v80, v81
	v_cvt_pk_fp8_f32 v233, v72, v73
	v_cvt_pk_fp8_f32 v232, v82, v83 op_sel:[0,0,1]
	v_cvt_pk_fp8_f32 v233, v74, v75 op_sel:[0,0,1]
	v_med3_f32 v92, v92, s7, v191
	v_med3_f32 v93, v93, s7, v191
	v_med3_f32 v94, v94, s7, v191
	v_med3_f32 v95, v95, s7, v191
	v_med3_f32 v88, v88, s7, v191
	v_med3_f32 v89, v89, s7, v191
	v_med3_f32 v90, v90, s7, v191
	v_med3_f32 v91, v91, s7, v191
	v_cvt_pk_fp8_f32 v234, v92, v93
	v_cvt_pk_fp8_f32 v235, v88, v89
	v_cvt_pk_fp8_f32 v234, v94, v95 op_sel:[0,0,1]
	v_cvt_pk_fp8_f32 v235, v90, v91 op_sel:[0,0,1]
	s_nop 1
	v_permlane16_swap_b32_e32 v232, v234
	v_permlane16_swap_b32_e32 v233, v235
	global_store_dwordx4 v[8:9], v[232:235], off
	v_med3_f32 v20, v20, s7, v191
	v_med3_f32 v21, v21, s7, v191
	v_med3_f32 v22, v22, s7, v191
	v_med3_f32 v23, v23, s7, v191
	v_med3_f32 v16, v16, s7, v191
	v_med3_f32 v17, v17, s7, v191
	v_med3_f32 v18, v18, s7, v191
	v_med3_f32 v19, v19, s7, v191
	v_cvt_pk_fp8_f32 v236, v20, v21
	v_cvt_pk_fp8_f32 v237, v16, v17
	v_cvt_pk_fp8_f32 v236, v22, v23 op_sel:[0,0,1]
	v_cvt_pk_fp8_f32 v237, v18, v19 op_sel:[0,0,1]
	v_med3_f32 v28, v28, s7, v191
	v_med3_f32 v29, v29, s7, v191
	v_med3_f32 v30, v30, s7, v191
	v_med3_f32 v31, v31, s7, v191
	v_med3_f32 v24, v24, s7, v191
	v_med3_f32 v25, v25, s7, v191
	v_med3_f32 v26, v26, s7, v191
	v_med3_f32 v27, v27, s7, v191
	v_cvt_pk_fp8_f32 v238, v28, v29
	v_cvt_pk_fp8_f32 v239, v24, v25
	v_cvt_pk_fp8_f32 v238, v30, v31 op_sel:[0,0,1]
	v_cvt_pk_fp8_f32 v239, v26, v27 op_sel:[0,0,1]
	s_nop 1
	v_permlane16_swap_b32_e32 v236, v238
	v_permlane16_swap_b32_e32 v237, v239
	global_store_dwordx4 v[8:9], v[236:239], off offset:128
	s_and_b64 vcc, exec, s[10:11]
	s_mov_b32 s17, s53
	s_mov_b32 s54, s52
	s_mov_b32 s16, s8
	s_mov_b64 s[20:21], s[12:13]
	s_mov_b64 s[18:19], s[14:15]
	s_cbranch_vccz .LBB0_1413
	s_waitcnt vmcnt(0)
	s_cmpk_gt_u32 s24, 0xff
	s_cbranch_scc1 .LBB0_1423
	s_barrier

.LBB0_1478:
	s_setprio 0
	s_mov_b64 s[0:1], s[86:87]
	s_mov_b32 s8, 0
	s_cmp_lt_i32 s82, 13
	s_cselect_b64 s[6:7], -1, 0
	v_mbcnt_lo_u32_b32 v0, -1, s8
	v_mbcnt_hi_u32_b32 v0, -1, v0
	v_or_b32_e32 v0, s92, v0
	s_and_b64 s[4:5], s[6:7], s[4:5]
	s_andn2_b64 vcc, exec, s[4:5]
	v_readfirstlane_b32 s26, v0
	s_cbranch_vccnz .LBB0_1517
	s_load_dwordx4 s[8:11], s[0:1], 0x130
	v_cmp_gt_i32_e32 vcc, 64, v0
	v_and_b32_e32 v86, 31, v0
	v_mbcnt_lo_u32_b32 v10, -1, 0
	s_waitcnt vmcnt(0) lgkmcnt(0)
	s_barrier
	s_and_saveexec_b64 s[0:1], vcc
	s_cbranch_execz .LBB0_1483
	v_lshlrev_b32_e32 v2, 8, v86
	v_mov_b32_e32 v3, 0
	v_lshl_add_u64 v[2:3], s[10:11], 0, v[2:3]
	v_add_co_u32_e32 v2, vcc, 0x10000, v2
	s_nop 1
	v_addc_co_u32_e32 v3, vcc, 0, v3, vcc
	global_load_dword v1, v[2:3], off sc1
	v_mbcnt_hi_u32_b32 v3, -1, v10
	v_and_b32_e32 v4, 64, v3
	v_add_u32_e32 v2, -1, v3
	v_cmp_lt_i32_e32 vcc, v2, v4
	v_add_u32_e32 v5, -2, v3
	v_add_u32_e32 v6, -4, v3
	v_cndmask_b32_e32 v2, v2, v3, vcc
	v_lshlrev_b32_e32 v8, 2, v2
	v_cmp_lt_i32_e32 vcc, v5, v4
	v_add_u32_e32 v7, -8, v3
	s_waitcnt vmcnt(0)
	v_add_u32_e32 v2, 0xff, v1
	v_ashrrev_i32_e32 v2, 8, v2
	ds_bpermute_b32 v8, v8, v2
	v_cndmask_b32_e32 v5, v5, v3, vcc
	v_cmp_ne_u32_e32 vcc, 0, v86
	v_lshlrev_b32_e32 v5, 2, v5
	s_waitcnt lgkmcnt(0)
	v_cndmask_b32_e32 v8, 0, v8, vcc
	v_add_u32_e32 v8, v8, v2
	ds_bpermute_b32 v5, v5, v8
	v_cmp_lt_i32_e32 vcc, v6, v4
	s_nop 1
	v_cndmask_b32_e32 v6, v6, v3, vcc
	v_cmp_lt_u32_e32 vcc, 1, v86
	v_lshlrev_b32_e32 v6, 2, v6
	s_waitcnt lgkmcnt(0)
	v_cndmask_b32_e32 v5, 0, v5, vcc
	v_add_u32_e32 v5, v5, v8
	ds_bpermute_b32 v6, v6, v5
	v_cmp_lt_i32_e32 vcc, v7, v4
	s_nop 1
	v_cndmask_b32_e32 v7, v7, v3, vcc
	v_cmp_lt_u32_e32 vcc, 3, v86
	v_lshlrev_b32_e32 v7, 2, v7
	s_waitcnt lgkmcnt(0)
	v_cndmask_b32_e32 v6, 0, v6, vcc
	v_add_u32_e32 v5, v6, v5
	ds_bpermute_b32 v6, v7, v5
	v_add_u32_e32 v7, -16, v3
	v_cmp_lt_i32_e32 vcc, v7, v4
	s_nop 1
	v_cndmask_b32_e32 v4, v7, v3, vcc
	v_cmp_lt_u32_e32 vcc, 7, v86
	v_lshlrev_b32_e32 v4, 2, v4
	s_waitcnt lgkmcnt(0)
	v_cndmask_b32_e32 v3, 0, v6, vcc
	v_add_u32_e32 v3, v3, v5
	ds_bpermute_b32 v4, v4, v3
	v_cmp_gt_i32_e32 vcc, 32, v0
	s_and_b64 exec, exec, vcc
	s_cbranch_execz .LBB0_1483
	v_cmp_lt_u32_e32 vcc, 15, v86
	s_waitcnt lgkmcnt(0)
	s_nop 0
	v_cndmask_b32_e32 v4, 0, v4, vcc
	v_add_u32_e32 v3, v4, v3
	v_lshl_add_u32 v4, v86, 2, 0
	v_add_u32_e32 v5, 0x20100, v4
	v_add_u32_e32 v4, 0x20000, v4
	v_cmp_eq_u32_e32 vcc, 31, v86
	ds_write_b32 v5, v1
	v_sub_u32_e32 v1, v3, v2
	ds_write_b32 v4, v1
	s_and_b64 exec, exec, vcc
	s_add_i32 s4, 0, 0x20080
	v_mov_b32_e32 v1, s4
	ds_write_b32 v1, v3
